# stack3: rotary-epilogue table prefetch, out-proj residual prefetch, pipelined compression-bias loop, no setprio raise in fp6 moe-up loop, dead M0 save/restore removed
# speedup vs baseline: 1.0012x; 1.0002x over previous
; #define PG8_STAGE(bufoff, gbase, voff) do { _Pragma("unroll") for (int _i = 0; _i < 2; ++_i) \
;         glds16((const void*)(gbase), (voff)[_i], ldsbase + (unsigned)(bufoff) + ldsw + (unsigned)_i * 8192u); } while (0)
; #define PG8_WAIT_V(n) asm volatile("s_waitcnt vmcnt(" #n ")" ::: "memory")
; #define PG8_BAR __builtin_amdgcn_s_barrier()
; __device__ __forceinline__ void glds16(const void* sbase, unsigned voff, unsigned lds_dst) {
;     unsigned keep;
;     asm volatile("s_mov_b32 %0, m0\n\ts_mov_b32 m0, %3\n\ts_nop 0\n\tglobal_load_lds_dwordx4 %1, %2\n\ts_mov_b32 m0, %0" : "=&s"(keep) : "v"(voff), "s"(sbase), "s"(lds_dst) : "memory");
; }
;     ...
;     PG8_STAGE(PG8_SB(0, 0), cB, voffB); PG8_STAGE(PG8_SB(0, 1), cB + hstepB, voffB); PG8_STAGE(PG8_SA(0, 0), cA, voffA); PG8_STAGE(PG8_SA(0, 1), cA + hstepA, voffA);
;     if (wr == 1) PG8_BAR;
;     PG8_WAIT_V(2); PG8_BAR;
;     PG8_STAGE(PG8_SB(1, 0), cB + kstep, voffB); PG8_STAGE(PG8_SA(1, 0), cA + kstep, voffA); PG8_STAGE(PG8_SB(1, 1), cB + hstepB + kstep, voffB);
;     PG8_WAIT_V(6); PG8_BAR;
.LBB0_1941:
	s_and_b64 vcc, exec, s[2:3]
	s_cbranch_vccnz .LBB0_2045
	v_bfe_i32 v4, v0, 27, 1
	v_lshlrev_b32_e32 v2, 4, v0
	v_lshrrev_b32_e32 v4, 22, v4
	v_add_u32_e32 v4, v2, v4
	v_and_b32_e32 v4, 0xfffffc00, v4
	v_sub_u32_e32 v4, v2, v4
	v_ashrrev_i32_e32 v1, 31, v0
	v_lshrrev_b32_e32 v5, 4, v4
	v_lshrrev_b32_e32 v1, 26, v1
	v_bitop3_b32 v4, v5, v4, 32 bitop3:0x6c
	v_add_u32_e32 v1, v0, v1
	v_ashrrev_i32_e32 v6, 31, v4
	v_ashrrev_i32_e32 v1, 6, v1
	v_lshrrev_b32_e32 v6, 26, v6
	v_lshlrev_b32_e32 v5, 3, v1
	v_add_u32_e32 v6, v4, v6
	v_and_b32_e32 v5, -16, v5
	v_ashrrev_i32_e32 v7, 6, v6
	v_and_b32_e32 v6, 0xc0, v6
	v_add_u32_e32 v5, v7, v5
	v_sub_u32_e32 v4, v4, v6
	v_lshlrev_b32_e32 v1, 5, v1
	v_ashrrev_i16_sdwa v4, v188, sext(v4) dst_sel:DWORD dst_unused:UNUSED_PAD src0_sel:DWORD src1_sel:BYTE_0
	v_lshlrev_b32_e32 v6, 1, v5
	v_lshrrev_b32_e32 v8, 2, v5
	v_and_b32_e32 v7, 3, v7
	s_mov_b32 s3, 0x1fffe0
	v_and_b32_e32 v1, 32, v1
	v_bfe_i32 v4, v4, 0, 16
	v_and_b32_e32 v6, 24, v6
	v_and_b32_e32 v8, 4, v8
	v_and_or_b32 v7, v5, s3, v7
	v_or3_b32 v6, v7, v8, v6
	v_add_lshl_u32 v4, v1, v4, 1
	v_add_u32_e32 v2, 0x2000, v2
	v_lshl_add_u32 v1, v5, 11, v4
	v_lshl_add_u32 v180, v6, 11, v4
	v_ashrrev_i32_e32 v4, 31, v2
	v_lshrrev_b32_e32 v4, 22, v4
	v_add_u32_e32 v4, v2, v4
	v_ashrrev_i32_e32 v4, 10, v4
	v_mul_i32_i24_e32 v5, 0x400, v4
	v_sub_u32_e32 v2, v2, v5
	v_lshrrev_b32_e32 v5, 4, v2
	v_bitop3_b32 v2, v5, v2, 32 bitop3:0x6c
	v_ashrrev_i32_e32 v6, 31, v2
	v_lshrrev_b32_e32 v6, 26, v6
	v_lshlrev_b32_e32 v5, 3, v4
	v_add_u32_e32 v6, v2, v6
	v_and_b32_e32 v5, -16, v5
	v_ashrrev_i32_e32 v7, 6, v6
	v_and_b32_e32 v6, 0xc0, v6
	s_ashr_i32 s2, s14, 6
	v_add_u32_e32 v5, v7, v5
	v_sub_u32_e32 v2, v2, v6
	v_lshlrev_b32_e32 v4, 5, v4
	v_ashrrev_i16_sdwa v2, v188, sext(v2) dst_sel:DWORD dst_unused:UNUSED_PAD src0_sel:DWORD src1_sel:BYTE_0
	v_lshlrev_b32_e32 v6, 1, v5
	v_lshrrev_b32_e32 v8, 2, v5
	v_and_b32_e32 v7, 3, v7
	s_lshl_b32 s8, s2, 10
	v_and_b32_e32 v4, 32, v4
	v_bfe_i32 v2, v2, 0, 16
	v_and_b32_e32 v6, 24, v6
	v_and_b32_e32 v8, 4, v8
	v_and_or_b32 v7, v5, s3, v7
	s_add_i32 s37, s8, 0
	v_or3_b32 v6, v7, v8, v6
	v_add_lshl_u32 v2, v4, v2, 1
	s_add_i32 s38, s37, 0x10000
	s_mov_b32 m0, s38
	s_nop 0
	global_load_lds_dwordx4 v180, s[24:25]
	v_lshl_add_u32 v182, v6, 11, v2
	s_ashr_i32 s3, s14, 8
	s_add_i32 s39, s37, 0x12000
	s_mov_b32 m0, s39
	s_nop 0
	global_load_lds_dwordx4 v182, s[24:25]
	s_add_u32 s8, s24, 0x40000
	s_addc_u32 s9, s25, 0
	s_add_i32 s40, s37, 0x14000
	s_mov_b32 m0, s40
	s_nop 0
	global_load_lds_dwordx4 v180, s[8:9]
	s_add_i32 s41, s37, 0x16000
	s_mov_b32 m0, s41
	s_nop 0
	global_load_lds_dwordx4 v182, s[8:9]
	s_mov_b32 m0, s37
	s_nop 0
	global_load_lds_dwordx4 v1, s[4:5]
	v_lshl_add_u32 v181, v5, 11, v2
	s_add_i32 s42, s37, 0x2000
	s_mov_b32 m0, s42
	s_nop 0
	global_load_lds_dwordx4 v181, s[4:5]
	s_add_u32 s8, s4, 0x40000
	s_addc_u32 s9, s5, 0
	s_add_i32 s43, s37, 0x4000
	s_mov_b32 m0, s43
	s_nop 0
	global_load_lds_dwordx4 v1, s[8:9]
	s_add_i32 s44, s37, 0x6000
	s_mov_b32 m0, s44
	s_nop 0
	global_load_lds_dwordx4 v181, s[8:9]
	s_cmp_eq_u32 s3, 1
	s_cselect_b64 s[8:9], -1, 0
	s_cmp_lg_u32 s3, 1
	s_cbranch_scc1 .LBB0_1944
	s_barrier
.LBB0_1944:
	s_add_u32 s10, s16, 0x41892000
	s_addc_u32 s11, s17, 0
	s_add_u32 s45, s16, 0x43892000
	s_addc_u32 s46, s17, 0
	s_add_u32 s12, s16, 0x32882000
	s_addc_u32 s13, s17, 0
	s_and_b64 s[6:7], s[6:7], exec
	v_bfe_u32 v4, v0, 4, 2
	s_movk_i32 s6, 0x7f
	v_and_b32_e32 v183, 15, v0
	v_lshlrev_b32_e32 v2, 4, v4
	v_lshlrev_b32_e32 v0, 2, v0
	s_cselect_b32 s47, 0x7c, s6
	s_and_b32 s18, s2, 3
	v_lshl_or_b32 v5, v183, 6, v2
	s_lshl_b32 s2, s3, 13
	v_and_b32_e32 v0, 32, v0
	s_lshl_b32 s48, s3, 6
	v_bitop3_b32 v7, v5, s2, v0 bitop3:0xde
	s_lshl_b32 s2, s18, 12
	s_add_u32 s6, s16, 0x3a892000
	s_addc_u32 s7, s17, 0
	v_bitop3_b32 v8, v5, s2, v0 bitop3:0xde
	s_add_u32 s2, s24, 0x80
	s_waitcnt vmcnt(2)
	s_barrier
	s_addc_u32 s3, s25, 0
	s_add_i32 s49, s37, 0x18000
	s_mov_b32 m0, s49
	s_nop 0
	global_load_lds_dwordx4 v180, s[2:3]
	s_add_i32 s50, s37, 0x1a000
	s_mov_b32 m0, s50
	s_nop 0
	global_load_lds_dwordx4 v182, s[2:3]
	s_add_u32 s2, s4, 0x80
	s_addc_u32 s3, s5, 0
	s_add_i32 s51, s37, 0x8000
	s_mov_b32 m0, s51
	s_nop 0
	global_load_lds_dwordx4 v1, s[2:3]
	s_add_i32 s52, s37, 0xa000
	s_mov_b32 m0, s52
	s_nop 0
	global_load_lds_dwordx4 v181, s[2:3]
	s_add_u32 s2, s24, 0x40080
	s_addc_u32 s3, s25, 0
	s_add_i32 s53, s37, 0x1c000
	s_mov_b32 m0, s53
	s_nop 0
	global_load_lds_dwordx4 v180, s[2:3]
	s_add_i32 s54, s37, 0x1e000
	s_add_i32 s55, s37, 0xc000
	s_mov_b32 m0, s54
	s_nop 0
	global_load_lds_dwordx4 v182, s[2:3]
	s_cmpk_lt_u32 s14, 0x100
	s_cselect_b64 s[14:15], -1, 0
	s_add_i32 s56, s37, 0xe000
	s_lshl_b32 s2, s18, 6
	v_lshlrev_b32_e32 v0, 2, v4
	s_add_u32 s2, s45, s2
	v_lshl_or_b32 v0, s18, 4, v0
	s_addc_u32 s3, s46, 0
	v_lshl_add_u64 v[164:165], s[2:3], 0, v[2:3]
	v_lshlrev_b32_e32 v2, 2, v0
	v_lshlrev_b32_e32 v6, 3, v4
	s_waitcnt vmcnt(6)
	v_lshl_add_u64 v[4:5], s[16:17], 0, v[2:3]
	s_mov_b64 s[2:3], 0x32500000
	v_lshl_add_u64 v[166:167], v[4:5], 0, s[2:3]
	s_mov_b64 s[2:3], 0x32580000
	v_lshl_or_b32 v2, s18, 5, v6
	v_lshl_add_u64 v[168:169], v[4:5], 0, s[2:3]
	s_mov_b32 s57, 0
	v_add_u32_e32 v184, 0, v8
	v_add_u32_e32 v185, 0, v7
	v_lshlrev_b32_e32 v205, 1, v2
	s_mov_b64 s[22:23], s[24:25]
	s_mov_b64 s[20:21], s[4:5]
	s_barrier
	s_branch .LBB0_1947

; #define PG8_STAGE(bufoff, gbase, voff) do { _Pragma("unroll") for (int _i = 0; _i < 2; ++_i) \
;         glds16((const void*)(gbase), (voff)[_i], ldsbase + (unsigned)(bufoff) + ldsw + (unsigned)_i * 8192u); } while (0)
; #define PG8_LDA(dst, b, h) do { _Pragma("unroll") for (int m = 0; m < 4; ++m) _Pragma("unroll") for (int k = 0; k < 2; ++k) dst[m][k] = *(const LAS bf16x8*)(lds + PG8_SA(b, h) + aoff + m * 2048 + k * 1024); } while (0)
; #define PG8_LDB(dst, b, h) do { _Pragma("unroll") for (int n = 0; n < 2; ++n) _Pragma("unroll") for (int k = 0; k < 2; ++k) dst[n][k] = *(const LAS bf16x8*)(lds + PG8_SB(b, h) + boff + n * 2048 + k * 1024); } while (0)
; #define PG8_WAIT_V(n) asm volatile("s_waitcnt vmcnt(" #n ")" ::: "memory")
; #define PG8_WAIT_L(n) asm volatile("s_waitcnt lgkmcnt(" #n ")" ::: "memory")
; #define PG8_BAR __builtin_amdgcn_s_barrier()
; #define PG8_SCHED __builtin_amdgcn_sched_barrier(0)
; __device__ __forceinline__ void glds16(const void* sbase, unsigned voff, unsigned lds_dst) {
;     ...
;     asm volatile("s_mov_b32 %0, m0\n\ts_mov_b32 m0, %3\n\ts_nop 0\n\tglobal_load_lds_dwordx4 %1, %2\n\ts_mov_b32 m0, %0" : "=&s"(keep) : "v"(voff), "s"(sbase), "s"(lds_dst) : "memory");
;     ...
;             PG8_LDB(B0, 0, 0); PG8_LDB(B1, 0, 1); PG8_SCHED; PG8_LDA(At, 0, 0); PG8_STAGE(PG8_SA(1, 1), a1 + hstepA, voffA);
;             PG8_WAIT_V(8); PG8_WAIT_L(0); PG8_BAR; PG8_MMA(0, 0, At, B0); PG8_MMA(0, 1, At, B1); PG8_BAR; PG8_SCHED;
;             PG8_LDA(At, 0, 1); PG8_STAGE(PG8_SB(0, 0), b2, voffB); PG8_STAGE(PG8_SB(0, 1), b2 + hstepB, voffB); PG8_STAGE(PG8_SA(0, 0), a2, voffA);
;             PG8_WAIT_V(8); PG8_WAIT_L(0); PG8_BAR; PG8_MMA(1, 0, At, B0); PG8_MMA(1, 1, At, B1); PG8_BAR; PG8_SCHED;
.LBB0_1950:
	v_add_u32_e32 v2, 0x10000, v184
	ds_read_b128 v[28:31], v2
	ds_read_b128 v[32:35], v2 offset:1024
	ds_read_b128 v[20:23], v2 offset:2048
	ds_read_b128 v[24:27], v2 offset:3072
	v_add_u32_e32 v2, 0x14000, v184
	s_waitcnt lgkmcnt(4)
	ds_read_b128 v[12:15], v2
	ds_read_b128 v[16:19], v2 offset:1024
	ds_read_b128 v[4:7], v2 offset:2048
	ds_read_b128 v[8:11], v2 offset:3072
	s_add_u32 s24, s4, 0xfffc0080
	s_addc_u32 s25, s5, -1
	s_cmp_eq_u32 s31, 12
	s_cselect_b32 s28, s20, s24
	s_cselect_b32 s29, s21, s25
	s_cselect_b32 s26, s22, s17
	s_cselect_b32 s27, s23, s19
	s_add_u32 s24, s28, 0x80
	s_addc_u32 s25, s29, 0
	ds_read_b128 v[206:209], v185
	ds_read_b128 v[210:213], v185 offset:1024
	ds_read_b128 v[214:217], v185 offset:2048
	ds_read_b128 v[218:221], v185 offset:3072
	ds_read_b128 v[222:225], v185 offset:4096
	ds_read_b128 v[226:229], v185 offset:5120
	ds_read_b128 v[230:233], v185 offset:6144
	ds_read_b128 v[234:237], v185 offset:7168
	s_mov_b32 m0, s55
	s_nop 0
	global_load_lds_dwordx4 v1, s[4:5]
	s_nop 0
	s_mov_b32 m0, s56
	s_nop 0
	global_load_lds_dwordx4 v181, s[4:5]
	s_waitcnt vmcnt(8)
	s_waitcnt lgkmcnt(0)
	s_barrier
	s_setprio 1
	v_mov_b32_e32 v2, s47
	s_waitcnt lgkmcnt(6)
	v_mfma_scale_f32_16x16x128_f8f6f4 v[160:163], v[28:35], v[206:213], v[160:163], v189, v2 op_sel_hi:[0,0,0]
	v_mfma_scale_f32_16x16x128_f8f6f4 v[156:159], v[20:27], v[206:213], v[156:159], v189, v2 op_sel_hi:[0,0,0]
	s_waitcnt lgkmcnt(4)
	v_mfma_scale_f32_16x16x128_f8f6f4 v[148:151], v[28:35], v[214:221], v[148:151], v189, v2 op_sel_hi:[0,0,0]
	v_mfma_scale_f32_16x16x128_f8f6f4 v[140:143], v[20:27], v[214:221], v[140:143], v189, v2 op_sel_hi:[0,0,0]
	s_waitcnt lgkmcnt(2)
	v_mfma_scale_f32_16x16x128_f8f6f4 v[132:135], v[28:35], v[222:229], v[132:135], v189, v2 op_sel_hi:[0,0,0]
	v_mfma_scale_f32_16x16x128_f8f6f4 v[124:127], v[20:27], v[222:229], v[124:127], v189, v2 op_sel_hi:[0,0,0]
	s_waitcnt lgkmcnt(0)
	v_mfma_scale_f32_16x16x128_f8f6f4 v[116:119], v[28:35], v[230:237], v[116:119], v189, v2 op_sel_hi:[0,0,0]
	v_mfma_scale_f32_16x16x128_f8f6f4 v[108:111], v[20:27], v[230:237], v[108:111], v189, v2 op_sel_hi:[0,0,0]
	s_setprio 0
	s_setprio 1
	v_mfma_scale_f32_16x16x128_f8f6f4 v[152:155], v[12:19], v[206:213], v[152:155], v189, v2 op_sel_hi:[0,0,0]
	v_mfma_scale_f32_16x16x128_f8f6f4 v[144:147], v[4:11], v[206:213], v[144:147], v189, v2 op_sel_hi:[0,0,0]
	v_mfma_scale_f32_16x16x128_f8f6f4 v[136:139], v[12:19], v[214:221], v[136:139], v189, v2 op_sel_hi:[0,0,0]
	v_mfma_scale_f32_16x16x128_f8f6f4 v[128:131], v[4:11], v[214:221], v[128:131], v189, v2 op_sel_hi:[0,0,0]
	v_mfma_scale_f32_16x16x128_f8f6f4 v[120:123], v[12:19], v[222:229], v[120:123], v189, v2 op_sel_hi:[0,0,0]
	v_mfma_scale_f32_16x16x128_f8f6f4 v[112:115], v[4:11], v[222:229], v[112:115], v189, v2 op_sel_hi:[0,0,0]
	v_mfma_scale_f32_16x16x128_f8f6f4 v[104:107], v[12:19], v[230:237], v[104:107], v189, v2 op_sel_hi:[0,0,0]
	v_mfma_scale_f32_16x16x128_f8f6f4 v[100:103], v[4:11], v[230:237], v[100:103], v189, v2 op_sel_hi:[0,0,0]
	s_setprio 0
	s_barrier
	ds_read_b128 v[206:209], v185 offset:16384
	ds_read_b128 v[210:213], v185 offset:17408
	ds_read_b128 v[214:217], v185 offset:18432
	ds_read_b128 v[218:221], v185 offset:19456
	ds_read_b128 v[222:225], v185 offset:20480
	ds_read_b128 v[226:229], v185 offset:21504
	ds_read_b128 v[230:233], v185 offset:22528
	ds_read_b128 v[234:237], v185 offset:23552
	s_mov_b32 m0, s38
	s_nop 0
	global_load_lds_dwordx4 v180, s[26:27]
	s_add_u32 s60, s26, 0x40000
	s_mov_b32 m0, s39
	s_nop 0
	global_load_lds_dwordx4 v182, s[26:27]
	s_addc_u32 s61, s27, 0
	s_mov_b32 m0, s40
	s_nop 0
	global_load_lds_dwordx4 v180, s[60:61]
	s_nop 0
	s_mov_b32 m0, s41
	s_nop 0
	global_load_lds_dwordx4 v182, s[60:61]
	s_nop 0
	s_mov_b32 m0, s37
	s_nop 0
	global_load_lds_dwordx4 v1, s[28:29]
	s_nop 0
	s_mov_b32 m0, s42
	s_nop 0
	global_load_lds_dwordx4 v181, s[28:29]
	s_waitcnt vmcnt(8)
	s_waitcnt lgkmcnt(0)
	s_barrier
	s_setprio 1
	s_waitcnt lgkmcnt(6)
	v_mfma_scale_f32_16x16x128_f8f6f4 v[96:99], v[28:35], v[206:213], v[96:99], v189, v2 op_sel_hi:[0,0,0]
	v_mfma_scale_f32_16x16x128_f8f6f4 v[92:95], v[20:27], v[206:213], v[92:95], v189, v2 op_sel_hi:[0,0,0]
	s_waitcnt lgkmcnt(4)
	v_mfma_scale_f32_16x16x128_f8f6f4 v[84:87], v[28:35], v[214:221], v[84:87], v189, v2 op_sel_hi:[0,0,0]
	v_mfma_scale_f32_16x16x128_f8f6f4 v[76:79], v[20:27], v[214:221], v[76:79], v189, v2 op_sel_hi:[0,0,0]
	s_waitcnt lgkmcnt(2)
	v_mfma_scale_f32_16x16x128_f8f6f4 v[68:71], v[28:35], v[222:229], v[68:71], v189, v2 op_sel_hi:[0,0,0]
	v_mfma_scale_f32_16x16x128_f8f6f4 v[60:63], v[20:27], v[222:229], v[60:63], v189, v2 op_sel_hi:[0,0,0]
	s_waitcnt lgkmcnt(0)
	v_mfma_scale_f32_16x16x128_f8f6f4 v[52:55], v[28:35], v[230:237], v[52:55], v189, v2 op_sel_hi:[0,0,0]
	v_mfma_scale_f32_16x16x128_f8f6f4 v[44:47], v[20:27], v[230:237], v[44:47], v189, v2 op_sel_hi:[0,0,0]
	s_setprio 0
	s_setprio 1
	v_mfma_scale_f32_16x16x128_f8f6f4 v[88:91], v[12:19], v[206:213], v[88:91], v189, v2 op_sel_hi:[0,0,0]
	v_mfma_scale_f32_16x16x128_f8f6f4 v[80:83], v[4:11], v[206:213], v[80:83], v189, v2 op_sel_hi:[0,0,0]
	v_mfma_scale_f32_16x16x128_f8f6f4 v[72:75], v[12:19], v[214:221], v[72:75], v189, v2 op_sel_hi:[0,0,0]
	v_mfma_scale_f32_16x16x128_f8f6f4 v[64:67], v[4:11], v[214:221], v[64:67], v189, v2 op_sel_hi:[0,0,0]
	v_mfma_scale_f32_16x16x128_f8f6f4 v[56:59], v[12:19], v[222:229], v[56:59], v189, v2 op_sel_hi:[0,0,0]
	v_mfma_scale_f32_16x16x128_f8f6f4 v[48:51], v[4:11], v[222:229], v[48:51], v189, v2 op_sel_hi:[0,0,0]
	v_mfma_scale_f32_16x16x128_f8f6f4 v[40:43], v[12:19], v[230:237], v[40:43], v189, v2 op_sel_hi:[0,0,0]
	v_mfma_scale_f32_16x16x128_f8f6f4 v[36:39], v[4:11], v[230:237], v[36:39], v189, v2 op_sel_hi:[0,0,0]
	s_setprio 0
	s_barrier
; #define PG8_STAGE(bufoff, gbase, voff) do { _Pragma("unroll") for (int _i = 0; _i < 2; ++_i) \
;         glds16((const void*)(gbase), (voff)[_i], ldsbase + (unsigned)(bufoff) + ldsw + (unsigned)_i * 8192u); } while (0)
; #define PG8_LDA(dst, b, h) do { _Pragma("unroll") for (int m = 0; m < 4; ++m) _Pragma("unroll") for (int k = 0; k < 2; ++k) dst[m][k] = *(const LAS bf16x8*)(lds + PG8_SA(b, h) + aoff + m * 2048 + k * 1024); } while (0)
; #define PG8_LDB(dst, b, h) do { _Pragma("unroll") for (int n = 0; n < 2; ++n) _Pragma("unroll") for (int k = 0; k < 2; ++k) dst[n][k] = *(const LAS bf16x8*)(lds + PG8_SB(b, h) + boff + n * 2048 + k * 1024); } while (0)
; #define PG8_WAIT_V(n) asm volatile("s_waitcnt vmcnt(" #n ")" ::: "memory")
; #define PG8_WAIT_L(n) asm volatile("s_waitcnt lgkmcnt(" #n ")" ::: "memory")
; #define PG8_BAR __builtin_amdgcn_s_barrier()
; #define PG8_SCHED __builtin_amdgcn_sched_barrier(0)
; __device__ __forceinline__ void glds16(const void* sbase, unsigned voff, unsigned lds_dst) {
;     ...
;     asm volatile("s_mov_b32 %0, m0\n\ts_mov_b32 m0, %3\n\ts_nop 0\n\tglobal_load_lds_dwordx4 %1, %2\n\ts_mov_b32 m0, %0" : "=&s"(keep) : "v"(voff), "s"(sbase), "s"(lds_dst) : "memory");
;     ...
;             PG8_LDB(B0, 1, 0); PG8_LDB(B1, 1, 1); PG8_SCHED; PG8_LDA(At, 1, 0); PG8_STAGE(PG8_SA(0, 1), a2 + hstepA, voffA);
;             PG8_WAIT_V(8); PG8_WAIT_L(0); PG8_BAR; PG8_MMA(0, 0, At, B0); PG8_MMA(0, 1, At, B1); PG8_BAR; PG8_SCHED;
;             PG8_LDA(At, 1, 1); PG8_STAGE(PG8_SB(1, 0), b3, voffB); PG8_STAGE(PG8_SB(1, 1), b3 + hstepB, voffB); PG8_STAGE(PG8_SA(1, 0), a3, voffA);
;             PG8_WAIT_V(8); PG8_WAIT_L(0); PG8_BAR; PG8_MMA(1, 0, At, B0); PG8_MMA(1, 1, At, B1); PG8_BAR; PG8_SCHED;
	v_add_u32_e32 v4, 0x18000, v184
	v_add_u32_e32 v8, 0x1c000, v184
	ds_read_b128 v[20:23], v4
	ds_read_b128 v[24:27], v4 offset:1024
	ds_read_b128 v[28:31], v4 offset:2048
	ds_read_b128 v[32:35], v4 offset:3072
	ds_read_b128 v[12:15], v8
	ds_read_b128 v[16:19], v8 offset:1024
	ds_read_b128 v[4:7], v8 offset:2048
	ds_read_b128 v[8:11], v8 offset:3072
	ds_read_b128 v[206:209], v185 offset:32768
	ds_read_b128 v[210:213], v185 offset:33792
	ds_read_b128 v[214:217], v185 offset:34816
	ds_read_b128 v[218:221], v185 offset:35840
	ds_read_b128 v[222:225], v185 offset:36864
	ds_read_b128 v[226:229], v185 offset:37888
	ds_read_b128 v[230:233], v185 offset:38912
	ds_read_b128 v[234:237], v185 offset:39936
	s_add_u32 s28, s28, 0x40000
	s_addc_u32 s29, s29, 0
	s_mov_b32 m0, s43
	s_nop 0
	global_load_lds_dwordx4 v1, s[28:29]
	s_nop 0
	s_mov_b32 m0, s44
	s_nop 0
	global_load_lds_dwordx4 v181, s[28:29]
	s_waitcnt vmcnt(8)
	s_waitcnt lgkmcnt(0)
	s_barrier
	s_setprio 1
	s_waitcnt lgkmcnt(6)
	v_mfma_scale_f32_16x16x128_f8f6f4 v[160:163], v[20:27], v[206:213], v[160:163], v189, v2 op_sel_hi:[0,0,0]
	v_mfma_scale_f32_16x16x128_f8f6f4 v[156:159], v[28:35], v[206:213], v[156:159], v189, v2 op_sel_hi:[0,0,0]
	s_waitcnt lgkmcnt(4)
	v_mfma_scale_f32_16x16x128_f8f6f4 v[148:151], v[20:27], v[214:221], v[148:151], v189, v2 op_sel_hi:[0,0,0]
	v_mfma_scale_f32_16x16x128_f8f6f4 v[140:143], v[28:35], v[214:221], v[140:143], v189, v2 op_sel_hi:[0,0,0]
	s_waitcnt lgkmcnt(2)
	v_mfma_scale_f32_16x16x128_f8f6f4 v[132:135], v[20:27], v[222:229], v[132:135], v189, v2 op_sel_hi:[0,0,0]
	v_mfma_scale_f32_16x16x128_f8f6f4 v[124:127], v[28:35], v[222:229], v[124:127], v189, v2 op_sel_hi:[0,0,0]
	s_waitcnt lgkmcnt(0)
	v_mfma_scale_f32_16x16x128_f8f6f4 v[116:119], v[20:27], v[230:237], v[116:119], v189, v2 op_sel_hi:[0,0,0]
	v_mfma_scale_f32_16x16x128_f8f6f4 v[108:111], v[28:35], v[230:237], v[108:111], v189, v2 op_sel_hi:[0,0,0]
	s_setprio 0
	s_setprio 1
	v_mfma_scale_f32_16x16x128_f8f6f4 v[152:155], v[12:19], v[206:213], v[152:155], v189, v2 op_sel_hi:[0,0,0]
	v_mfma_scale_f32_16x16x128_f8f6f4 v[144:147], v[4:11], v[206:213], v[144:147], v189, v2 op_sel_hi:[0,0,0]
	v_mfma_scale_f32_16x16x128_f8f6f4 v[136:139], v[12:19], v[214:221], v[136:139], v189, v2 op_sel_hi:[0,0,0]
	v_mfma_scale_f32_16x16x128_f8f6f4 v[128:131], v[4:11], v[214:221], v[128:131], v189, v2 op_sel_hi:[0,0,0]
	v_mfma_scale_f32_16x16x128_f8f6f4 v[120:123], v[12:19], v[222:229], v[120:123], v189, v2 op_sel_hi:[0,0,0]
	v_mfma_scale_f32_16x16x128_f8f6f4 v[112:115], v[4:11], v[222:229], v[112:115], v189, v2 op_sel_hi:[0,0,0]
	v_mfma_scale_f32_16x16x128_f8f6f4 v[104:107], v[12:19], v[230:237], v[104:107], v189, v2 op_sel_hi:[0,0,0]
	v_mfma_scale_f32_16x16x128_f8f6f4 v[100:103], v[4:11], v[230:237], v[100:103], v189, v2 op_sel_hi:[0,0,0]
	s_setprio 0
	s_barrier
	ds_read_b128 v[206:209], v185 offset:49152
	ds_read_b128 v[210:213], v185 offset:50176
	ds_read_b128 v[214:217], v185 offset:51200
	ds_read_b128 v[218:221], v185 offset:52224
	ds_read_b128 v[222:225], v185 offset:53248
	ds_read_b128 v[226:229], v185 offset:54272
	ds_read_b128 v[230:233], v185 offset:55296
	ds_read_b128 v[234:237], v185 offset:56320
	s_add_u32 s28, s26, 0x80
	s_addc_u32 s29, s27, 0
	s_mov_b32 m0, s49
	s_nop 0
	global_load_lds_dwordx4 v180, s[28:29]
	s_add_u32 s26, s26, 0x40080
	s_mov_b32 m0, s50
	s_nop 0
	global_load_lds_dwordx4 v182, s[28:29]
	s_addc_u32 s27, s27, 0
	s_mov_b32 m0, s53
	s_nop 0
	global_load_lds_dwordx4 v180, s[26:27]
	s_nop 0
	s_mov_b32 m0, s54
	s_nop 0
	global_load_lds_dwordx4 v182, s[26:27]
	s_mov_b32 m0, s51
	s_nop 0
	global_load_lds_dwordx4 v1, s[24:25]
	s_nop 0
	s_mov_b32 m0, s52
	s_nop 0
	global_load_lds_dwordx4 v181, s[24:25]
	s_waitcnt vmcnt(8)
	s_waitcnt lgkmcnt(0)
	s_barrier
	s_setprio 1
	s_waitcnt lgkmcnt(6)
	v_mfma_scale_f32_16x16x128_f8f6f4 v[96:99], v[20:27], v[206:213], v[96:99], v189, v2 op_sel_hi:[0,0,0]
	v_mfma_scale_f32_16x16x128_f8f6f4 v[92:95], v[28:35], v[206:213], v[92:95], v189, v2 op_sel_hi:[0,0,0]
	s_waitcnt lgkmcnt(4)
	v_mfma_scale_f32_16x16x128_f8f6f4 v[84:87], v[20:27], v[214:221], v[84:87], v189, v2 op_sel_hi:[0,0,0]
	v_mfma_scale_f32_16x16x128_f8f6f4 v[76:79], v[28:35], v[214:221], v[76:79], v189, v2 op_sel_hi:[0,0,0]
	s_waitcnt lgkmcnt(2)
	v_mfma_scale_f32_16x16x128_f8f6f4 v[68:71], v[20:27], v[222:229], v[68:71], v189, v2 op_sel_hi:[0,0,0]
	v_mfma_scale_f32_16x16x128_f8f6f4 v[60:63], v[28:35], v[222:229], v[60:63], v189, v2 op_sel_hi:[0,0,0]
	s_waitcnt lgkmcnt(0)
	v_mfma_scale_f32_16x16x128_f8f6f4 v[52:55], v[20:27], v[230:237], v[52:55], v189, v2 op_sel_hi:[0,0,0]
	v_mfma_scale_f32_16x16x128_f8f6f4 v[44:47], v[28:35], v[230:237], v[44:47], v189, v2 op_sel_hi:[0,0,0]
	s_setprio 0
	s_setprio 1
	v_mfma_scale_f32_16x16x128_f8f6f4 v[88:91], v[12:19], v[206:213], v[88:91], v189, v2 op_sel_hi:[0,0,0]
	v_mfma_scale_f32_16x16x128_f8f6f4 v[80:83], v[4:11], v[206:213], v[80:83], v189, v2 op_sel_hi:[0,0,0]
	v_mfma_scale_f32_16x16x128_f8f6f4 v[72:75], v[12:19], v[214:221], v[72:75], v189, v2 op_sel_hi:[0,0,0]
	v_mfma_scale_f32_16x16x128_f8f6f4 v[64:67], v[4:11], v[214:221], v[64:67], v189, v2 op_sel_hi:[0,0,0]
	v_mfma_scale_f32_16x16x128_f8f6f4 v[56:59], v[12:19], v[222:229], v[56:59], v189, v2 op_sel_hi:[0,0,0]
	v_mfma_scale_f32_16x16x128_f8f6f4 v[48:51], v[4:11], v[222:229], v[48:51], v189, v2 op_sel_hi:[0,0,0]
	v_mfma_scale_f32_16x16x128_f8f6f4 v[40:43], v[12:19], v[230:237], v[40:43], v189, v2 op_sel_hi:[0,0,0]
	v_mfma_scale_f32_16x16x128_f8f6f4 v[36:39], v[4:11], v[230:237], v[36:39], v189, v2 op_sel_hi:[0,0,0]
	s_setprio 0
	s_barrier
	s_add_i32 s31, s31, 2
	s_add_u32 s17, s17, 0x100
	s_addc_u32 s19, s19, 0
	s_add_u32 s4, s4, 0x100
	s_addc_u32 s5, s5, 0
	s_cmp_gt_u32 s31, 13
	s_cbranch_scc0 .LBB0_1950
	s_and_b64 vcc, exec, s[14:15]
	s_cbranch_vccz .LBB0_1953
	s_barrier

;     __device__ __forceinline__ void operator()(const f32x4 (&acc)[2][2][4][2], const Unit& u, int wr, int wc, int fr, int fq) const {
;     ...
;                 for (int m = 0; m < 4; ++m) { const int t = row0 + ai * HALF + m * 16, b = t >> 11, s = t & 2047;
;                     const float rsc = scale * rr8[ai][m];
;                     const f32x4 c = *(const f32x4*)(cosN + s * 64 + 4 * uu) * rsc, sn = *(const f32x4*)(sinN + s * 64 + 4 * uu) * rsc;
.LBB0_1968:
	s_andn2_b64 vcc, exec, s[24:25]
	s_cbranch_vccnz .LBB0_2034
	v_and_b32_e32 v13, 0x7cf, v12
	v_lshlrev_b32_e32 v2, 8, v13
	v_lshl_add_u64 v[4:5], v[166:167], 0, v[2:3]
	v_lshl_add_u64 v[8:9], v[168:169], 0, v[2:3]
	global_load_dwordx4 v[4:7], v[4:5], off
	v_lshlrev_b32_e32 v2, 7, v13
	global_load_dwordx4 v[8:11], v[8:9], off
	v_lshlrev_b32_e32 v248, 8, v13
	v_mov_b32_e32 v249, v3
	v_lshl_add_u64 v[246:247], v[166:167], 0, v[248:249]
	v_lshl_add_u64 v[248:249], v[168:169], 0, v[248:249]
	s_mov_b64 s[66:67], 0x1000
	v_lshl_add_u64 v[198:199], s[66:67], 0, v[246:247]
	global_load_dwordx4 v[210:213], v[198:199], off
	v_lshl_add_u64 v[198:199], s[66:67], 0, v[248:249]
	global_load_dwordx4 v[206:209], v[198:199], off
	s_mov_b64 s[66:67], 0x2000
	v_lshl_add_u64 v[198:199], s[66:67], 0, v[246:247]
	global_load_dwordx4 v[218:221], v[198:199], off
	v_lshl_add_u64 v[198:199], s[66:67], 0, v[248:249]
	global_load_dwordx4 v[214:217], v[198:199], off
	s_mov_b64 s[66:67], 0x3000
	v_lshl_add_u64 v[198:199], s[66:67], 0, v[246:247]
	global_load_dwordx4 v[226:229], v[198:199], off
	v_lshl_add_u64 v[198:199], s[66:67], 0, v[248:249]
	global_load_dwordx4 v[222:225], v[198:199], off
	s_mov_b64 s[66:67], 0x8000
	v_lshl_add_u64 v[198:199], s[66:67], 0, v[246:247]
	global_load_dwordx4 v[234:237], v[198:199], off
	v_lshl_add_u64 v[198:199], s[66:67], 0, v[248:249]
	global_load_dwordx4 v[230:233], v[198:199], off
	s_mov_b64 s[66:67], 0x9000
	v_lshl_add_u64 v[198:199], s[66:67], 0, v[246:247]
	global_load_dwordx4 v[242:245], v[198:199], off
	v_lshl_add_u64 v[198:199], s[66:67], 0, v[248:249]
	global_load_dwordx4 v[238:241], v[198:199], off
	s_mov_b64 s[30:31], -1
	s_and_b64 vcc, exec, s[28:29]
	s_mul_hi_u32 s17, s19, 0x802000
	s_mul_i32 s19, s19, 0x802000
	v_lshlrev_b32_e32 v170, 1, v2
	s_cbranch_vccz .LBB0_1971
	s_add_u32 s30, s45, s19
	s_addc_u32 s31, s46, s17
	s_ashr_i32 s27, s26, 31
	s_lshl_b64 s[24:25], s[26:27], 19
	s_add_u32 s24, s30, s24
	s_addc_u32 s25, s31, s25
	v_mov_b32_e32 v171, v3
	v_lshl_add_u64 v[178:179], s[24:25], 0, v[170:171]
	s_mov_b64 s[30:31], 0

; __device__ __forceinline__ unsigned cvtpk(float lo, float hi) { unsigned r; asm volatile("v_cvt_pk_bf16_f32 %0, %1, %2" : "=v"(r) : "v"(lo), "v"(hi)); return r; }
;     __device__ __forceinline__ void operator()(const f32x4 (&acc)[2][2][4][2], const Unit& u, int wr, int wc, int fr, int fq) const {
;     ...
;                     const f32x4 c = *(const f32x4*)(cosN + s * 64 + 4 * uu) * rsc, sn = *(const f32x4*)(sinN + s * 64 + 4 * uu) * rsc;
; #pragma unroll
;                     for (int bj = 0; bj < 2; ++bj) { const f32x4 x1 = acc[ai][bj][m][0], x2 = acc[ai][bj][m][1];
;                         const f32x4 o1 = x1 * c - x2 * sn, o2 = x1 * sn + x2 * c;
;                         bf16_t* dst = isq ? (QN + (size_t)t * 1024 + (2 * pn + bj) * 128 + 4 * uu) : (KV6 + (size_t)(pn - 4) * kvstride + ((size_t)(b * 2 + bj) * 2048 + s) * 128 + 4 * uu);
;                         u32x2 w1, w2; w1.x = cvtpk(o1[0], o1[1]); w1.y = cvtpk(o1[2], o1[3]); w2.x = cvtpk(o2[0], o2[1]); w2.y = cvtpk(o2[2], o2[3]);
;                         *(u32x2*)dst = w1; *(u32x2*)(dst + 64) = w2; } }
.LBB0_1985:
	v_pk_mul_f32 v[172:173], v[128:129], v[206:207]
	v_pk_mul_f32 v[206:207], v[136:137], v[206:207]
	v_pk_mul_f32 v[170:171], v[130:131], v[208:209]
	v_pk_mul_f32 v[208:209], v[138:139], v[208:209]
	v_pk_fma_f32 v[206:207], v[128:129], v[210:211], v[206:207]
	s_movk_i32 s25, 0x7ef
	v_pk_fma_f32 v[170:171], v[138:139], v[212:213], v[170:171] neg_lo:[0,0,1] neg_hi:[0,0,1]
	v_pk_fma_f32 v[172:173], v[136:137], v[210:211], v[172:173] neg_lo:[0,0,1] neg_hi:[0,0,1]
	v_pk_fma_f32 v[208:209], v[130:131], v[212:213], v[208:209]
	v_lshl_add_u64 v[210:211], v[178:179], 0, v[2:3]
	v_cvt_pk_bf16_f32 v212, v172, v173
	v_cvt_pk_bf16_f32 v213, v170, v171
	v_cvt_pk_bf16_f32 v206, v206, v207
	v_cvt_pk_bf16_f32 v207, v208, v209
	v_bitop3_b32 v15, v12, s25, 32 bitop3:0xc8
	global_store_dwordx2 v[210:211], v[212:213], off
	global_store_dwordx2 v[210:211], v[206:207], off offset:128
	s_mov_b64 s[66:67], 0xa000
	v_lshl_add_u64 v[198:199], s[66:67], 0, v[246:247]
	global_load_dwordx4 v[210:213], v[198:199], off
	v_lshl_add_u64 v[198:199], s[66:67], 0, v[248:249]
	global_load_dwordx4 v[206:209], v[198:199], off
	v_lshlrev_b32_e32 v4, 8, v15
	v_mov_b32_e32 v5, v3
	v_lshl_add_u64 v[6:7], v[166:167], 0, v[4:5]
	v_lshl_add_u64 v[4:5], v[168:169], 0, v[4:5]
	s_nop 0
	v_lshlrev_b32_e32 v15, 7, v15
	s_mov_b64 s[28:29], -1
	s_and_b64 vcc, exec, s[4:5]
	v_lshlrev_b32_e32 v170, 1, v15
	s_cbranch_vccnz .LBB0_1987
	s_add_u32 s25, s45, s19
	s_addc_u32 s30, s46, s17
	s_ashr_i32 s27, s26, 31
	s_lshl_b64 s[28:29], s[26:27], 19
	s_add_u32 s28, s25, s28
	s_addc_u32 s29, s30, s29
	v_mov_b32_e32 v171, v3
	v_lshl_add_u64 v[178:179], s[28:29], 0, v[170:171]
	s_mov_b64 s[28:29], 0

; __device__ __forceinline__ unsigned cvtpk(float lo, float hi) { unsigned r; asm volatile("v_cvt_pk_bf16_f32 %0, %1, %2" : "=v"(r) : "v"(lo), "v"(hi)); return r; }
;     __device__ __forceinline__ void operator()(const f32x4 (&acc)[2][2][4][2], const Unit& u, int wr, int wc, int fr, int fq) const {
;     ...
;                     const f32x4 c = *(const f32x4*)(cosN + s * 64 + 4 * uu) * rsc, sn = *(const f32x4*)(sinN + s * 64 + 4 * uu) * rsc;
; #pragma unroll
;                     for (int bj = 0; bj < 2; ++bj) { const f32x4 x1 = acc[ai][bj][m][0], x2 = acc[ai][bj][m][1];
;                         const f32x4 o1 = x1 * c - x2 * sn, o2 = x1 * sn + x2 * c;
;                         bf16_t* dst = isq ? (QN + (size_t)t * 1024 + (2 * pn + bj) * 128 + 4 * uu) : (KV6 + (size_t)(pn - 4) * kvstride + ((size_t)(b * 2 + bj) * 2048 + s) * 128 + 4 * uu);
;                         u32x2 w1, w2; w1.x = cvtpk(o1[0], o1[1]); w1.y = cvtpk(o1[2], o1[3]); w2.x = cvtpk(o2[0], o2[1]); w2.y = cvtpk(o2[2], o2[3]);
;                         *(u32x2*)dst = w1; *(u32x2*)(dst + 64) = w2; } }
.LBB0_1993:
	v_pk_mul_f32 v[172:173], v[112:113], v[214:215]
	v_pk_mul_f32 v[214:215], v[120:121], v[214:215]
	v_pk_mul_f32 v[170:171], v[114:115], v[216:217]
	v_pk_mul_f32 v[216:217], v[122:123], v[216:217]
	v_pk_fma_f32 v[214:215], v[112:113], v[218:219], v[214:215]
	s_movk_i32 s25, 0x7ff
	v_pk_fma_f32 v[170:171], v[122:123], v[220:221], v[170:171] neg_lo:[0,0,1] neg_hi:[0,0,1]
	v_pk_fma_f32 v[172:173], v[120:121], v[218:219], v[172:173] neg_lo:[0,0,1] neg_hi:[0,0,1]
	v_pk_fma_f32 v[216:217], v[114:115], v[220:221], v[216:217]
	v_lshl_add_u64 v[218:219], v[178:179], 0, v[2:3]
	v_cvt_pk_bf16_f32 v220, v172, v173
	v_cvt_pk_bf16_f32 v221, v170, v171
	v_cvt_pk_bf16_f32 v214, v214, v215
	v_cvt_pk_bf16_f32 v215, v216, v217
	v_bitop3_b32 v15, v12, s25, 48 bitop3:0xc8
	global_store_dwordx2 v[218:219], v[220:221], off
	global_store_dwordx2 v[218:219], v[214:215], off offset:128
	s_mov_b64 s[66:67], 0xb000
	v_lshl_add_u64 v[198:199], s[66:67], 0, v[246:247]
	global_load_dwordx4 v[218:221], v[198:199], off
	v_lshl_add_u64 v[198:199], s[66:67], 0, v[248:249]
	global_load_dwordx4 v[214:217], v[198:199], off
	v_lshlrev_b32_e32 v4, 8, v15
	v_mov_b32_e32 v5, v3
	v_lshl_add_u64 v[6:7], v[166:167], 0, v[4:5]
	v_lshl_add_u64 v[4:5], v[168:169], 0, v[4:5]
	s_nop 0
	v_lshlrev_b32_e32 v15, 7, v15
	s_mov_b64 s[28:29], -1
	s_and_b64 vcc, exec, s[4:5]
	v_lshlrev_b32_e32 v170, 1, v15
	s_cbranch_vccnz .LBB0_1995
	s_add_u32 s25, s45, s19
	s_addc_u32 s28, s46, s17
	s_ashr_i32 s27, s26, 31
	s_lshl_b64 s[26:27], s[26:27], 19
	s_add_u32 s26, s25, s26
	s_addc_u32 s27, s28, s27
	v_mov_b32_e32 v171, v3
	v_lshl_add_u64 v[178:179], s[26:27], 0, v[170:171]
	s_mov_b64 s[28:29], 0

; #define PG8_STAGE(bufoff, gbase, voff) do { _Pragma("unroll") for (int _i = 0; _i < 2; ++_i) \
;         glds16((const void*)(gbase), (voff)[_i], ldsbase + (unsigned)(bufoff) + ldsw + (unsigned)_i * 8192u); } while (0)
; #define PG8_WAIT_V(n) asm volatile("s_waitcnt vmcnt(" #n ")" ::: "memory")
; #define PG8_BAR __builtin_amdgcn_s_barrier()
; #define PHASE_LOCALS() unsigned long long wz_ = 0; asm volatile("" : "+s"(wz_)); unsigned char* ws = args.ws + wz_; int tid = w0 * 64 + lane_id(); asm volatile("" : "+v"(tid)); \
;     const int wid = __builtin_amdgcn_readfirstlane(tid >> 6), lane = tid & 63; unsigned char* act = ws + WS_ACT; (void)wid; (void)lane; (void)act
;     ...
;     PG8_STAGE(PG8_SB(0, 0), cB, voffB); PG8_STAGE(PG8_SB(0, 1), cB + hstepB, voffB); PG8_STAGE(PG8_SA(0, 0), cA, voffA); PG8_STAGE(PG8_SA(0, 1), cA + hstepA, voffA);
;     if (wr == 1) PG8_BAR;
;     PG8_WAIT_V(2); PG8_BAR;
;     PG8_STAGE(PG8_SB(1, 0), cB + kstep, voffB); PG8_STAGE(PG8_SA(1, 0), cA + kstep, voffA); PG8_STAGE(PG8_SB(1, 1), cB + hstepB + kstep, voffB);
;     PG8_WAIT_V(6); PG8_BAR;
; __global__ void __launch_bounds__(512, 2) fwd(Args args) {
;     ...
;             { PHASE_LOCALS(); pg8::SplitPairSched S; S.o.init(16, 8, G, bx); S.A0 = (const char*)(act + A_KV6); S.A1 = (const char*)(act + A_KV6 + SZ_KV); S.Bt = (const char*)(ws + WS_CW1 + (size_t)(l * 2) * SZ_CW1);
;               S.astep = (size_t)256 * 2048 * 2; S.bstep = (size_t)256 * 4096 * 2; S.bset = SZ_CW1; S.kslice = 1024 * 2;
;               pg8::EpiF32Part E{(float*)(act + A_CPART), 512, (size_t)4096 * 512};
;               for (int rep = 0; rep < REP_CMP1; ++rep) pg8::gemm_phase<false>(lds, 4096 * 2, 2048 * 2, S, E, w0, 127, 127, 16); }
.LBB0_2099:
	s_andn2_b64 vcc, exec, s[2:3]
	s_cbranch_vccnz .LBB0_2205
	s_mov_b64 s[2:3], 0
	v_mbcnt_lo_u32_b32 v0, -1, 0
	v_mbcnt_hi_u32_b32 v0, -1, v0
	v_readlane_b32 s0, v250, 60
	v_readlane_b32 s4, v252, 30
	v_readlane_b32 s5, v252, 31
	v_add_u32_e32 v0, s0, v0
	s_andn2_b64 vcc, exec, s[4:5]
	v_mbcnt_lo_u32_b32 v0, -1, 0
	v_mbcnt_hi_u32_b32 v0, -1, v0
	s_nop 0
	v_add_u32_e32 v4, s0, v0
	s_nop 0
	v_readfirstlane_b32 s6, v4
	s_cbranch_vccnz .LBB0_2120
	s_waitcnt lgkmcnt(0)
	v_bfe_i32 v1, v4, 27, 1
	v_lshlrev_b32_e32 v2, 4, v4
	v_lshrrev_b32_e32 v1, 22, v1
	v_add_u32_e32 v1, v2, v1
	v_and_b32_e32 v1, 0xfffffc00, v1
	s_add_u32 s2, s80, s2
	v_sub_u32_e32 v1, v2, v1
	s_addc_u32 s3, s81, s3
	v_lshrrev_b32_e32 v5, 4, v1
	s_add_u32 s0, s2, 0x43892000
	v_bitop3_b32 v1, v5, v1, 32 bitop3:0x6c
	s_addc_u32 s24, s3, 0
	v_ashrrev_i32_e32 v0, 31, v4
	v_ashrrev_i32_e32 v6, 31, v1
	s_add_u32 s25, s2, 0x44094000
	v_lshrrev_b32_e32 v0, 26, v0
	v_lshrrev_b32_e32 v6, 26, v6
	s_addc_u32 s26, s3, 0
	s_lshl_b32 s4, s27, 23
	v_add_u32_e32 v0, v4, v0
	v_add_u32_e32 v6, v1, v6
	s_add_u32 s4, s2, s4
	v_ashrrev_i32_e32 v0, 6, v0
	v_lshrrev_b32_e32 v7, 6, v6
	v_and_b32_e32 v6, 0xc0, v6
	s_addc_u32 s5, s3, 0
	v_lshlrev_b32_e32 v5, 3, v0
	v_lshlrev_b32_e32 v0, 5, v0
	v_sub_u32_e32 v1, v1, v6
	s_add_u32 s27, s4, 0x2d00000
	v_and_b32_e32 v5, 0xffff0, v5
	v_and_b32_e32 v0, 32, v0
	v_ashrrev_i16_sdwa v1, v188, sext(v1) dst_sel:DWORD dst_unused:UNUSED_PAD src0_sel:DWORD src1_sel:BYTE_0
	v_add_u32_e32 v2, 0x2000, v2
	s_addc_u32 s28, s5, 0
	v_add_u32_sdwa v0, v0, sext(v1) dst_sel:DWORD dst_unused:UNUSED_PAD src0_sel:DWORD src1_sel:WORD_0
	v_add_lshl_u32 v1, v7, v5, 12
	v_ashrrev_i32_e32 v5, 31, v2
	s_ashr_i32 s8, s6, 6
	s_ashr_i32 s7, s6, 8
	v_lshrrev_b32_e32 v5, 22, v5
	s_lshl_b32 s9, s8, 10
	v_readlane_b32 s4, v253, 0
	v_add_u32_e32 v5, v2, v5
	v_readlane_b32 s5, v253, 1
	s_add_u32 s4, s27, s4
	v_ashrrev_i32_e32 v5, 10, v5
	s_addc_u32 s5, s28, s5
	v_readlane_b32 s10, v253, 3
	v_mul_i32_i24_e32 v6, 0x400, v5
	s_add_u32 s4, s4, s10
	v_sub_u32_e32 v2, v2, v6
	s_addc_u32 s5, s5, 0
	v_readlane_b32 s10, v253, 6
	v_lshrrev_b32_e32 v6, 4, v2
	v_readlane_b32 s11, v253, 7
	s_add_u32 s16, s4, s10
	v_bitop3_b32 v2, v6, v2, 32 bitop3:0x6c
	s_addc_u32 s17, s5, s11
	v_readlane_b32 s4, v253, 9
	v_ashrrev_i32_e32 v7, 31, v2
	v_readlane_b32 s5, v253, 10
	v_lshrrev_b32_e32 v7, 26, v7
	s_and_b64 s[4:5], s[4:5], exec
	v_add_u32_e32 v7, v2, v7
	s_cselect_b32 s5, s0, s25
	v_readlane_b32 s12, v253, 11
	v_lshrrev_b32_e32 v8, 6, v7
	v_and_b32_e32 v7, 0xc0, v7
	s_cselect_b32 s4, s24, s26
	s_add_u32 s5, s5, s12
	v_lshlrev_b32_e32 v6, 3, v5
	v_lshlrev_b32_e32 v5, 5, v5
	v_sub_u32_e32 v2, v2, v7
	s_addc_u32 s4, s4, 0
	v_and_b32_e32 v6, 0xffff0, v6
	v_and_b32_e32 v5, 32, v5
	v_ashrrev_i16_sdwa v2, v188, sext(v2) dst_sel:DWORD dst_unused:UNUSED_PAD src0_sel:DWORD src1_sel:BYTE_0
	s_add_u32 s18, s5, s10
	v_lshl_add_u32 v0, v0, 1, v1
	v_add_u32_sdwa v2, v5, sext(v2) dst_sel:DWORD dst_unused:UNUSED_PAD src0_sel:DWORD src1_sel:WORD_0
	v_add_lshl_u32 v5, v8, v6, 12
	s_addc_u32 s19, s4, s11
	s_add_i32 s29, s9, 0
	v_add_u32_e32 v1, v0, v1
	v_lshl_add_u32 v2, v2, 1, v5
	s_add_i32 s30, s29, 0x10000
	s_mov_b32 m0, s30
	s_nop 0
	global_load_lds_dwordx4 v1, s[16:17]
	s_waitcnt vmcnt(0)
	v_add_u32_e32 v132, v2, v5
	s_add_i32 s31, s29, 0x12000
	s_mov_b32 m0, s31
	s_nop 0
	global_load_lds_dwordx4 v132, s[16:17]
	s_add_u32 s4, s16, 0x100000
	s_addc_u32 s5, s17, 0
	s_add_i32 s34, s29, 0x14000
	s_mov_b32 m0, s34
	s_nop 0
	global_load_lds_dwordx4 v1, s[4:5]
	s_add_i32 s35, s29, 0x16000
	s_mov_b32 m0, s35
	s_nop 0
	global_load_lds_dwordx4 v132, s[4:5]
	s_mov_b32 m0, s29
	s_nop 0
	global_load_lds_dwordx4 v0, s[18:19]
	s_add_i32 s36, s29, 0x2000
	s_mov_b32 m0, s36
	s_nop 0
	global_load_lds_dwordx4 v2, s[18:19]
	s_add_u32 s4, s18, 0x80000
	s_addc_u32 s5, s19, 0
	s_add_i32 s37, s29, 0x4000
	s_mov_b32 m0, s37
	s_nop 0
	global_load_lds_dwordx4 v0, s[4:5]
	s_add_i32 s38, s29, 0x6000
	s_mov_b32 m0, s38
	s_nop 0
	global_load_lds_dwordx4 v2, s[4:5]
	s_cmp_eq_u32 s7, 1
	s_cselect_b64 s[4:5], -1, 0
	s_cmp_lg_u32 s7, 1
	s_cbranch_scc1 .LBB0_2103
	s_barrier
.LBB0_2103:
	v_bfe_u32 v6, v4, 4, 2
	s_add_u32 s39, s2, 0x53a1e000
	v_and_b32_e32 v5, 15, v4
	v_lshlrev_b32_e32 v7, 4, v6
	v_lshlrev_b32_e32 v4, 2, v4
	s_addc_u32 s40, s3, 0
	v_lshl_or_b32 v133, s7, 6, v5
	v_lshl_or_b32 v5, v5, 6, v7
	s_lshl_b32 s2, s7, 13
	v_and_b32_e32 v4, 32, v4
	v_bitop3_b32 v7, v5, s2, v4 bitop3:0xde
	s_lshl_b32 s2, s8, 5
	s_and_b32 s8, s2, 0x60
	s_lshl_b32 s2, s8, 7
	v_bitop3_b32 v4, v5, s2, v4 bitop3:0xde
	s_add_u32 s2, s16, 0x80
	s_waitcnt vmcnt(2)
	s_barrier
	s_addc_u32 s3, s17, 0
	s_add_i32 s41, s29, 0x18000
	s_mov_b32 m0, s41
	s_nop 0
	global_load_lds_dwordx4 v1, s[2:3]
	s_add_i32 s42, s29, 0x1a000
	s_mov_b32 m0, s42
	s_nop 0
	global_load_lds_dwordx4 v132, s[2:3]
	s_add_u32 s2, s18, 0x80
	s_addc_u32 s3, s19, 0
	s_add_i32 s43, s29, 0x8000
	s_mov_b32 m0, s43
	s_nop 0
	global_load_lds_dwordx4 v0, s[2:3]
	s_add_i32 s44, s29, 0xa000
	s_mov_b32 m0, s44
	s_nop 0
	global_load_lds_dwordx4 v2, s[2:3]
	s_add_u32 s2, s16, 0x100080
	s_addc_u32 s3, s17, 0
	s_add_i32 s45, s29, 0x1c000
	s_mov_b32 m0, s45
	s_nop 0
	global_load_lds_dwordx4 v1, s[2:3]
	s_add_i32 s46, s29, 0x1e000
	s_mov_b32 m0, s46
	s_nop 0
	global_load_lds_dwordx4 v132, s[2:3]
	s_waitcnt vmcnt(6)
	s_add_i32 s47, s29, 0xc000
	v_readlane_b32 s14, v253, 4
	s_cmpk_lt_u32 s6, 0x100
	v_readlane_b32 s15, v253, 5
	s_cselect_b64 s[6:7], -1, 0
	s_add_i32 s48, s29, 0xe000
	v_lshl_or_b32 v134, v6, 2, s8
	s_mov_b32 s49, 0
	v_add_u32_e32 v135, 0, v4
	v_add_u32_e32 v136, 0, v7
	v_readlane_b32 s15, v253, 2
	v_readlane_b32 s52, v253, 8
	s_mov_b64 s[10:11], s[18:19]
	s_mov_b64 s[12:13], s[16:17]
	s_barrier
	s_branch .LBB0_2106

; #define PG8_STAGE(bufoff, gbase, voff) do { _Pragma("unroll") for (int _i = 0; _i < 2; ++_i) \
;         glds16((const void*)(gbase), (voff)[_i], ldsbase + (unsigned)(bufoff) + ldsw + (unsigned)_i * 8192u); } while (0)
; #define PG8_LDA(dst, b, h) do { _Pragma("unroll") for (int m = 0; m < 4; ++m) _Pragma("unroll") for (int k = 0; k < 2; ++k) dst[m][k] = *(const LAS bf16x8*)(lds + PG8_SA(b, h) + aoff + m * 2048 + k * 1024); } while (0)
; #define PG8_LDB(dst, b, h) do { _Pragma("unroll") for (int n = 0; n < 2; ++n) _Pragma("unroll") for (int k = 0; k < 2; ++k) dst[n][k] = *(const LAS bf16x8*)(lds + PG8_SB(b, h) + boff + n * 2048 + k * 1024); } while (0)
; #define PG8_WAIT_V(n) asm volatile("s_waitcnt vmcnt(" #n ")" ::: "memory")
; #define PG8_WAIT_L(n) asm volatile("s_waitcnt lgkmcnt(" #n ")" ::: "memory")
; #define PG8_BAR __builtin_amdgcn_s_barrier()
; #define PG8_SCHED __builtin_amdgcn_sched_barrier(0)
; __device__ __forceinline__ void glds16(const void* sbase, unsigned voff, unsigned lds_dst) {
;     ...
;     asm volatile("s_mov_b32 %0, m0\n\ts_mov_b32 m0, %3\n\ts_nop 0\n\tglobal_load_lds_dwordx4 %1, %2\n\ts_mov_b32 m0, %0" : "=&s"(keep) : "v"(voff), "s"(sbase), "s"(lds_dst) : "memory");
;     ...
;             PG8_LDB(B0, 0, 0); PG8_LDB(B1, 0, 1); PG8_SCHED; PG8_LDA(At, 0, 0); PG8_STAGE(PG8_SA(1, 1), a1 + hstepA, voffA);
;             PG8_WAIT_V(8); PG8_WAIT_L(0); PG8_BAR; PG8_MMA(0, 0, At, B0); PG8_MMA(0, 1, At, B1); PG8_BAR; PG8_SCHED;
;             PG8_LDA(At, 0, 1); PG8_STAGE(PG8_SB(0, 0), b2, voffB); PG8_STAGE(PG8_SB(0, 1), b2 + hstepB, voffB); PG8_STAGE(PG8_SA(0, 0), a2, voffA);
;             PG8_WAIT_V(8); PG8_WAIT_L(0); PG8_BAR; PG8_MMA(1, 0, At, B0); PG8_MMA(1, 1, At, B1); PG8_BAR; PG8_SCHED;
.LBB0_2113:
	v_add_u32_e32 v137, 0x10000, v135
	ds_read_b128 v[138:141], v137
	ds_read_b128 v[142:145], v137 offset:1024
	ds_read_b128 v[146:149], v137 offset:2048
	ds_read_b128 v[150:153], v137 offset:3072
	v_add_u32_e32 v137, 0x14000, v135
	ds_read_b128 v[154:157], v137
	ds_read_b128 v[158:161], v137 offset:1024
	ds_read_b128 v[162:165], v137 offset:2048
	ds_read_b128 v[166:169], v137 offset:3072
	s_add_u32 s18, s16, 0xfff80080
	s_addc_u32 s19, s17, -1
	s_cmp_eq_u32 s54, 12
	s_cselect_b32 s22, s10, s18
	s_cselect_b32 s23, s11, s19
	s_cselect_b32 s20, s12, s9
	s_cselect_b32 s21, s13, s53
	s_add_u32 s18, s22, 0x80
	s_addc_u32 s19, s23, 0
	ds_read_b128 v[176:179], v136
	ds_read_b128 v[180:183], v136 offset:1024
	ds_read_b128 v[206:209], v136 offset:2048
	ds_read_b128 v[210:213], v136 offset:3072
	ds_read_b128 v[214:217], v136 offset:4096
	ds_read_b128 v[218:221], v136 offset:5120
	ds_read_b128 v[222:225], v136 offset:6144
	ds_read_b128 v[226:229], v136 offset:7168
	s_mov_b32 m0, s47
	s_nop 0
	global_load_lds_dwordx4 v0, s[16:17]
	s_nop 0
	s_mov_b32 m0, s48
	s_nop 0
	global_load_lds_dwordx4 v2, s[16:17]
	s_waitcnt vmcnt(8)
	s_waitcnt lgkmcnt(0)
	s_barrier
	s_setprio 1
	s_waitcnt lgkmcnt(7)
	v_mfma_f32_16x16x32_bf16 v[128:131], v[138:141], v[176:179], v[128:131]
	v_mfma_f32_16x16x32_bf16 v[124:127], v[146:149], v[176:179], v[124:127]
	s_waitcnt lgkmcnt(5)
	v_mfma_f32_16x16x32_bf16 v[120:123], v[138:141], v[206:209], v[120:123]
	v_mfma_f32_16x16x32_bf16 v[116:119], v[146:149], v[206:209], v[116:119]
	s_waitcnt lgkmcnt(3)
	v_mfma_f32_16x16x32_bf16 v[108:111], v[138:141], v[214:217], v[108:111]
	v_mfma_f32_16x16x32_bf16 v[100:103], v[146:149], v[214:217], v[100:103]
	s_waitcnt lgkmcnt(1)
	v_mfma_f32_16x16x32_bf16 v[92:95], v[138:141], v[222:225], v[92:95]
	v_mfma_f32_16x16x32_bf16 v[84:87], v[146:149], v[222:225], v[84:87]
	v_mfma_f32_16x16x32_bf16 v[128:131], v[142:145], v[180:183], v[128:131]
	v_mfma_f32_16x16x32_bf16 v[124:127], v[150:153], v[180:183], v[124:127]
	v_mfma_f32_16x16x32_bf16 v[120:123], v[142:145], v[210:213], v[120:123]
	v_mfma_f32_16x16x32_bf16 v[116:119], v[150:153], v[210:213], v[116:119]
	v_mfma_f32_16x16x32_bf16 v[108:111], v[142:145], v[218:221], v[108:111]
	v_mfma_f32_16x16x32_bf16 v[100:103], v[150:153], v[218:221], v[100:103]
	s_waitcnt lgkmcnt(0)
	v_mfma_f32_16x16x32_bf16 v[92:95], v[142:145], v[226:229], v[92:95]
	v_mfma_f32_16x16x32_bf16 v[84:87], v[150:153], v[226:229], v[84:87]
	s_setprio 0
	s_setprio 1
	v_mfma_f32_16x16x32_bf16 v[112:115], v[154:157], v[176:179], v[112:115]
	v_mfma_f32_16x16x32_bf16 v[104:107], v[162:165], v[176:179], v[104:107]
	v_mfma_f32_16x16x32_bf16 v[96:99], v[154:157], v[206:209], v[96:99]
	v_mfma_f32_16x16x32_bf16 v[88:91], v[162:165], v[206:209], v[88:91]
	v_mfma_f32_16x16x32_bf16 v[80:83], v[154:157], v[214:217], v[80:83]
	v_mfma_f32_16x16x32_bf16 v[76:79], v[162:165], v[214:217], v[76:79]
	v_mfma_f32_16x16x32_bf16 v[72:75], v[154:157], v[222:225], v[72:75]
	v_mfma_f32_16x16x32_bf16 v[68:71], v[162:165], v[222:225], v[68:71]
	v_mfma_f32_16x16x32_bf16 v[112:115], v[158:161], v[180:183], v[112:115]
	v_mfma_f32_16x16x32_bf16 v[104:107], v[166:169], v[180:183], v[104:107]
	v_mfma_f32_16x16x32_bf16 v[96:99], v[158:161], v[210:213], v[96:99]
	v_mfma_f32_16x16x32_bf16 v[88:91], v[166:169], v[210:213], v[88:91]
	v_mfma_f32_16x16x32_bf16 v[80:83], v[158:161], v[218:221], v[80:83]
	v_mfma_f32_16x16x32_bf16 v[76:79], v[166:169], v[218:221], v[76:79]
	v_mfma_f32_16x16x32_bf16 v[72:75], v[158:161], v[226:229], v[72:75]
	v_mfma_f32_16x16x32_bf16 v[68:71], v[166:169], v[226:229], v[68:71]
	s_setprio 0
	s_barrier
	ds_read_b128 v[176:179], v136 offset:16384
	ds_read_b128 v[180:183], v136 offset:17408
	ds_read_b128 v[206:209], v136 offset:18432
	ds_read_b128 v[210:213], v136 offset:19456
	ds_read_b128 v[214:217], v136 offset:20480
	ds_read_b128 v[218:221], v136 offset:21504
	ds_read_b128 v[222:225], v136 offset:22528
	ds_read_b128 v[226:229], v136 offset:23552
	s_mov_b32 m0, s30
	s_nop 0
	global_load_lds_dwordx4 v1, s[20:21]
	s_add_u32 s56, s20, 0x100000
	s_mov_b32 m0, s31
	s_nop 0
	global_load_lds_dwordx4 v132, s[20:21]
	s_addc_u32 s57, s21, 0
	s_mov_b32 m0, s34
	s_nop 0
	global_load_lds_dwordx4 v1, s[56:57]
	s_nop 0
	s_mov_b32 m0, s35
	s_nop 0
	global_load_lds_dwordx4 v132, s[56:57]
	s_nop 0
	s_mov_b32 m0, s29
	s_nop 0
	global_load_lds_dwordx4 v0, s[22:23]
	s_nop 0
	s_mov_b32 m0, s36
	s_nop 0
	global_load_lds_dwordx4 v2, s[22:23]
	s_waitcnt vmcnt(8)
	s_waitcnt lgkmcnt(0)
	s_barrier
; #define PG8_STAGE(bufoff, gbase, voff) do { _Pragma("unroll") for (int _i = 0; _i < 2; ++_i) \
;         glds16((const void*)(gbase), (voff)[_i], ldsbase + (unsigned)(bufoff) + ldsw + (unsigned)_i * 8192u); } while (0)
; #define PG8_LDA(dst, b, h) do { _Pragma("unroll") for (int m = 0; m < 4; ++m) _Pragma("unroll") for (int k = 0; k < 2; ++k) dst[m][k] = *(const LAS bf16x8*)(lds + PG8_SA(b, h) + aoff + m * 2048 + k * 1024); } while (0)
; #define PG8_LDB(dst, b, h) do { _Pragma("unroll") for (int n = 0; n < 2; ++n) _Pragma("unroll") for (int k = 0; k < 2; ++k) dst[n][k] = *(const LAS bf16x8*)(lds + PG8_SB(b, h) + boff + n * 2048 + k * 1024); } while (0)
; #define PG8_WAIT_V(n) asm volatile("s_waitcnt vmcnt(" #n ")" ::: "memory")
; #define PG8_WAIT_L(n) asm volatile("s_waitcnt lgkmcnt(" #n ")" ::: "memory")
; #define PG8_BAR __builtin_amdgcn_s_barrier()
; #define PG8_SCHED __builtin_amdgcn_sched_barrier(0)
; __device__ __forceinline__ void glds16(const void* sbase, unsigned voff, unsigned lds_dst) {
;     ...
;     asm volatile("s_mov_b32 %0, m0\n\ts_mov_b32 m0, %3\n\ts_nop 0\n\tglobal_load_lds_dwordx4 %1, %2\n\ts_mov_b32 m0, %0" : "=&s"(keep) : "v"(voff), "s"(sbase), "s"(lds_dst) : "memory");
;     ...
;             PG8_WAIT_V(8); PG8_WAIT_L(0); PG8_BAR; PG8_MMA(1, 0, At, B0); PG8_MMA(1, 1, At, B1); PG8_BAR; PG8_SCHED;
;             PG8_LDB(B0, 1, 0); PG8_LDB(B1, 1, 1); PG8_SCHED; PG8_LDA(At, 1, 0); PG8_STAGE(PG8_SA(0, 1), a2 + hstepA, voffA);
;             PG8_WAIT_V(8); PG8_WAIT_L(0); PG8_BAR; PG8_MMA(0, 0, At, B0); PG8_MMA(0, 1, At, B1); PG8_BAR; PG8_SCHED;
;             PG8_LDA(At, 1, 1); PG8_STAGE(PG8_SB(1, 0), b3, voffB); PG8_STAGE(PG8_SB(1, 1), b3 + hstepB, voffB); PG8_STAGE(PG8_SA(1, 0), a3, voffA);
	s_setprio 1
	s_waitcnt lgkmcnt(7)
	v_mfma_f32_16x16x32_bf16 v[64:67], v[138:141], v[176:179], v[64:67]
	v_mfma_f32_16x16x32_bf16 v[60:63], v[146:149], v[176:179], v[60:63]
	s_waitcnt lgkmcnt(5)
	v_mfma_f32_16x16x32_bf16 v[56:59], v[138:141], v[206:209], v[56:59]
	v_mfma_f32_16x16x32_bf16 v[52:55], v[146:149], v[206:209], v[52:55]
	s_waitcnt lgkmcnt(3)
	v_mfma_f32_16x16x32_bf16 v[40:43], v[138:141], v[214:217], v[40:43]
	v_mfma_f32_16x16x32_bf16 v[36:39], v[146:149], v[214:217], v[36:39]
	s_waitcnt lgkmcnt(1)
	v_mfma_f32_16x16x32_bf16 v[24:27], v[138:141], v[222:225], v[24:27]
	v_mfma_f32_16x16x32_bf16 v[20:23], v[146:149], v[222:225], v[20:23]
	v_mfma_f32_16x16x32_bf16 v[64:67], v[142:145], v[180:183], v[64:67]
	v_mfma_f32_16x16x32_bf16 v[60:63], v[150:153], v[180:183], v[60:63]
	v_mfma_f32_16x16x32_bf16 v[56:59], v[142:145], v[210:213], v[56:59]
	v_mfma_f32_16x16x32_bf16 v[52:55], v[150:153], v[210:213], v[52:55]
	v_mfma_f32_16x16x32_bf16 v[40:43], v[142:145], v[218:221], v[40:43]
	v_mfma_f32_16x16x32_bf16 v[36:39], v[150:153], v[218:221], v[36:39]
	s_waitcnt lgkmcnt(0)
	v_mfma_f32_16x16x32_bf16 v[24:27], v[142:145], v[226:229], v[24:27]
	v_mfma_f32_16x16x32_bf16 v[20:23], v[150:153], v[226:229], v[20:23]
	s_setprio 0
	s_setprio 1
	v_mfma_f32_16x16x32_bf16 v[48:51], v[154:157], v[176:179], v[48:51]
	v_mfma_f32_16x16x32_bf16 v[44:47], v[162:165], v[176:179], v[44:47]
	v_mfma_f32_16x16x32_bf16 v[32:35], v[154:157], v[206:209], v[32:35]
	v_mfma_f32_16x16x32_bf16 v[28:31], v[162:165], v[206:209], v[28:31]
	v_mfma_f32_16x16x32_bf16 v[16:19], v[154:157], v[214:217], v[16:19]
	v_mfma_f32_16x16x32_bf16 v[12:15], v[162:165], v[214:217], v[12:15]
	v_mfma_f32_16x16x32_bf16 v[8:11], v[154:157], v[222:225], v[8:11]
	v_mfma_f32_16x16x32_bf16 v[4:7], v[162:165], v[222:225], v[4:7]
	v_mfma_f32_16x16x32_bf16 v[48:51], v[158:161], v[180:183], v[48:51]
	v_mfma_f32_16x16x32_bf16 v[44:47], v[166:169], v[180:183], v[44:47]
	v_mfma_f32_16x16x32_bf16 v[32:35], v[158:161], v[210:213], v[32:35]
	v_mfma_f32_16x16x32_bf16 v[28:31], v[166:169], v[210:213], v[28:31]
	v_mfma_f32_16x16x32_bf16 v[16:19], v[158:161], v[218:221], v[16:19]
	v_mfma_f32_16x16x32_bf16 v[12:15], v[166:169], v[218:221], v[12:15]
	v_mfma_f32_16x16x32_bf16 v[8:11], v[158:161], v[226:229], v[8:11]
	v_mfma_f32_16x16x32_bf16 v[4:7], v[166:169], v[226:229], v[4:7]
	s_setprio 0
	s_barrier
	v_add_u32_e32 v137, 0x18000, v135
	ds_read_b128 v[138:141], v137
	ds_read_b128 v[142:145], v137 offset:1024
	ds_read_b128 v[146:149], v137 offset:2048
	ds_read_b128 v[150:153], v137 offset:3072
	v_add_u32_e32 v137, 0x1c000, v135
	ds_read_b128 v[154:157], v137
	ds_read_b128 v[158:161], v137 offset:1024
	ds_read_b128 v[162:165], v137 offset:2048
	ds_read_b128 v[166:169], v137 offset:3072
	ds_read_b128 v[176:179], v136 offset:32768
	ds_read_b128 v[180:183], v136 offset:33792
	ds_read_b128 v[206:209], v136 offset:34816
	ds_read_b128 v[210:213], v136 offset:35840
	ds_read_b128 v[214:217], v136 offset:36864
	ds_read_b128 v[218:221], v136 offset:37888
	ds_read_b128 v[222:225], v136 offset:38912
	ds_read_b128 v[226:229], v136 offset:39936
	s_add_u32 s22, s22, 0x80000
	s_addc_u32 s23, s23, 0
	s_mov_b32 m0, s37
	s_nop 0
	global_load_lds_dwordx4 v0, s[22:23]
	s_nop 0
	s_mov_b32 m0, s38
	s_nop 0
	global_load_lds_dwordx4 v2, s[22:23]
	s_waitcnt vmcnt(8)
	s_waitcnt lgkmcnt(0)
	s_barrier
	s_setprio 1
	s_waitcnt lgkmcnt(7)
	v_mfma_f32_16x16x32_bf16 v[128:131], v[138:141], v[176:179], v[128:131]
	v_mfma_f32_16x16x32_bf16 v[124:127], v[146:149], v[176:179], v[124:127]
	s_waitcnt lgkmcnt(5)
	v_mfma_f32_16x16x32_bf16 v[120:123], v[138:141], v[206:209], v[120:123]
	v_mfma_f32_16x16x32_bf16 v[116:119], v[146:149], v[206:209], v[116:119]
	s_waitcnt lgkmcnt(3)
	v_mfma_f32_16x16x32_bf16 v[108:111], v[138:141], v[214:217], v[108:111]
	v_mfma_f32_16x16x32_bf16 v[100:103], v[146:149], v[214:217], v[100:103]
	s_waitcnt lgkmcnt(1)
	v_mfma_f32_16x16x32_bf16 v[92:95], v[138:141], v[222:225], v[92:95]
	v_mfma_f32_16x16x32_bf16 v[84:87], v[146:149], v[222:225], v[84:87]
	v_mfma_f32_16x16x32_bf16 v[128:131], v[142:145], v[180:183], v[128:131]
	v_mfma_f32_16x16x32_bf16 v[124:127], v[150:153], v[180:183], v[124:127]
	v_mfma_f32_16x16x32_bf16 v[120:123], v[142:145], v[210:213], v[120:123]
	v_mfma_f32_16x16x32_bf16 v[116:119], v[150:153], v[210:213], v[116:119]
	v_mfma_f32_16x16x32_bf16 v[108:111], v[142:145], v[218:221], v[108:111]
	v_mfma_f32_16x16x32_bf16 v[100:103], v[150:153], v[218:221], v[100:103]
	s_waitcnt lgkmcnt(0)
	v_mfma_f32_16x16x32_bf16 v[92:95], v[142:145], v[226:229], v[92:95]
	v_mfma_f32_16x16x32_bf16 v[84:87], v[150:153], v[226:229], v[84:87]
	s_setprio 0
	s_setprio 1
	v_mfma_f32_16x16x32_bf16 v[112:115], v[154:157], v[176:179], v[112:115]
	v_mfma_f32_16x16x32_bf16 v[104:107], v[162:165], v[176:179], v[104:107]
	v_mfma_f32_16x16x32_bf16 v[96:99], v[154:157], v[206:209], v[96:99]
	v_mfma_f32_16x16x32_bf16 v[88:91], v[162:165], v[206:209], v[88:91]
	v_mfma_f32_16x16x32_bf16 v[80:83], v[154:157], v[214:217], v[80:83]
	v_mfma_f32_16x16x32_bf16 v[76:79], v[162:165], v[214:217], v[76:79]
	v_mfma_f32_16x16x32_bf16 v[72:75], v[154:157], v[222:225], v[72:75]
	v_mfma_f32_16x16x32_bf16 v[68:71], v[162:165], v[222:225], v[68:71]
	v_mfma_f32_16x16x32_bf16 v[112:115], v[158:161], v[180:183], v[112:115]
	v_mfma_f32_16x16x32_bf16 v[104:107], v[166:169], v[180:183], v[104:107]
	v_mfma_f32_16x16x32_bf16 v[96:99], v[158:161], v[210:213], v[96:99]
	v_mfma_f32_16x16x32_bf16 v[88:91], v[166:169], v[210:213], v[88:91]
	v_mfma_f32_16x16x32_bf16 v[80:83], v[158:161], v[218:221], v[80:83]
	v_mfma_f32_16x16x32_bf16 v[76:79], v[166:169], v[218:221], v[76:79]
	v_mfma_f32_16x16x32_bf16 v[72:75], v[158:161], v[226:229], v[72:75]
	v_mfma_f32_16x16x32_bf16 v[68:71], v[166:169], v[226:229], v[68:71]
	s_setprio 0
	s_barrier
; #define PG8_STAGE(bufoff, gbase, voff) do { _Pragma("unroll") for (int _i = 0; _i < 2; ++_i) \
;         glds16((const void*)(gbase), (voff)[_i], ldsbase + (unsigned)(bufoff) + ldsw + (unsigned)_i * 8192u); } while (0)
; #define PG8_LDA(dst, b, h) do { _Pragma("unroll") for (int m = 0; m < 4; ++m) _Pragma("unroll") for (int k = 0; k < 2; ++k) dst[m][k] = *(const LAS bf16x8*)(lds + PG8_SA(b, h) + aoff + m * 2048 + k * 1024); } while (0)
; #define PG8_WAIT_V(n) asm volatile("s_waitcnt vmcnt(" #n ")" ::: "memory")
; #define PG8_WAIT_L(n) asm volatile("s_waitcnt lgkmcnt(" #n ")" ::: "memory")
; #define PG8_BAR __builtin_amdgcn_s_barrier()
; #define PG8_SCHED __builtin_amdgcn_sched_barrier(0)
; __device__ __forceinline__ void glds16(const void* sbase, unsigned voff, unsigned lds_dst) {
;     ...
;     asm volatile("s_mov_b32 %0, m0\n\ts_mov_b32 m0, %3\n\ts_nop 0\n\tglobal_load_lds_dwordx4 %1, %2\n\ts_mov_b32 m0, %0" : "=&s"(keep) : "v"(voff), "s"(sbase), "s"(lds_dst) : "memory");
;     ...
;             PG8_LDA(At, 1, 1); PG8_STAGE(PG8_SB(1, 0), b3, voffB); PG8_STAGE(PG8_SB(1, 1), b3 + hstepB, voffB); PG8_STAGE(PG8_SA(1, 0), a3, voffA);
;             PG8_WAIT_V(8); PG8_WAIT_L(0); PG8_BAR; PG8_MMA(1, 0, At, B0); PG8_MMA(1, 1, At, B1); PG8_BAR; PG8_SCHED;
	ds_read_b128 v[176:179], v136 offset:49152
	ds_read_b128 v[180:183], v136 offset:50176
	ds_read_b128 v[206:209], v136 offset:51200
	ds_read_b128 v[210:213], v136 offset:52224
	ds_read_b128 v[214:217], v136 offset:53248
	ds_read_b128 v[218:221], v136 offset:54272
	ds_read_b128 v[222:225], v136 offset:55296
	ds_read_b128 v[226:229], v136 offset:56320
	s_add_u32 s22, s20, 0x80
	s_addc_u32 s23, s21, 0
	s_mov_b32 m0, s41
	s_nop 0
	global_load_lds_dwordx4 v1, s[22:23]
	s_add_u32 s20, s20, 0x100080
	s_mov_b32 m0, s42
	s_nop 0
	global_load_lds_dwordx4 v132, s[22:23]
	s_addc_u32 s21, s21, 0
	s_mov_b32 m0, s45
	s_nop 0
	global_load_lds_dwordx4 v1, s[20:21]
	s_nop 0
	s_mov_b32 m0, s46
	s_nop 0
	global_load_lds_dwordx4 v132, s[20:21]
	s_mov_b32 m0, s43
	s_nop 0
	global_load_lds_dwordx4 v0, s[18:19]
	s_nop 0
	s_mov_b32 m0, s44
	s_nop 0
	global_load_lds_dwordx4 v2, s[18:19]
	s_waitcnt vmcnt(8)
	s_waitcnt lgkmcnt(0)
	s_barrier
	s_setprio 1
	s_waitcnt lgkmcnt(7)
	v_mfma_f32_16x16x32_bf16 v[64:67], v[138:141], v[176:179], v[64:67]
	v_mfma_f32_16x16x32_bf16 v[60:63], v[146:149], v[176:179], v[60:63]
	s_waitcnt lgkmcnt(5)
	v_mfma_f32_16x16x32_bf16 v[56:59], v[138:141], v[206:209], v[56:59]
	v_mfma_f32_16x16x32_bf16 v[52:55], v[146:149], v[206:209], v[52:55]
	s_waitcnt lgkmcnt(3)
	v_mfma_f32_16x16x32_bf16 v[40:43], v[138:141], v[214:217], v[40:43]
	v_mfma_f32_16x16x32_bf16 v[36:39], v[146:149], v[214:217], v[36:39]
	s_waitcnt lgkmcnt(1)
	v_mfma_f32_16x16x32_bf16 v[24:27], v[138:141], v[222:225], v[24:27]
	v_mfma_f32_16x16x32_bf16 v[20:23], v[146:149], v[222:225], v[20:23]
	v_mfma_f32_16x16x32_bf16 v[64:67], v[142:145], v[180:183], v[64:67]
	v_mfma_f32_16x16x32_bf16 v[60:63], v[150:153], v[180:183], v[60:63]
	v_mfma_f32_16x16x32_bf16 v[56:59], v[142:145], v[210:213], v[56:59]
	v_mfma_f32_16x16x32_bf16 v[52:55], v[150:153], v[210:213], v[52:55]
	v_mfma_f32_16x16x32_bf16 v[40:43], v[142:145], v[218:221], v[40:43]
	v_mfma_f32_16x16x32_bf16 v[36:39], v[150:153], v[218:221], v[36:39]
	s_waitcnt lgkmcnt(0)
	v_mfma_f32_16x16x32_bf16 v[24:27], v[142:145], v[226:229], v[24:27]
	v_mfma_f32_16x16x32_bf16 v[20:23], v[150:153], v[226:229], v[20:23]
	s_setprio 0
	s_setprio 1
	v_mfma_f32_16x16x32_bf16 v[48:51], v[154:157], v[176:179], v[48:51]
	v_mfma_f32_16x16x32_bf16 v[44:47], v[162:165], v[176:179], v[44:47]
	v_mfma_f32_16x16x32_bf16 v[32:35], v[154:157], v[206:209], v[32:35]
	v_mfma_f32_16x16x32_bf16 v[28:31], v[162:165], v[206:209], v[28:31]
	v_mfma_f32_16x16x32_bf16 v[16:19], v[154:157], v[214:217], v[16:19]
	v_mfma_f32_16x16x32_bf16 v[12:15], v[162:165], v[214:217], v[12:15]
	v_mfma_f32_16x16x32_bf16 v[8:11], v[154:157], v[222:225], v[8:11]
	v_mfma_f32_16x16x32_bf16 v[4:7], v[162:165], v[222:225], v[4:7]
	v_mfma_f32_16x16x32_bf16 v[48:51], v[158:161], v[180:183], v[48:51]
	v_mfma_f32_16x16x32_bf16 v[44:47], v[166:169], v[180:183], v[44:47]
	v_mfma_f32_16x16x32_bf16 v[32:35], v[158:161], v[210:213], v[32:35]
	v_mfma_f32_16x16x32_bf16 v[28:31], v[166:169], v[210:213], v[28:31]
	v_mfma_f32_16x16x32_bf16 v[16:19], v[158:161], v[218:221], v[16:19]
	v_mfma_f32_16x16x32_bf16 v[12:15], v[166:169], v[218:221], v[12:15]
	v_mfma_f32_16x16x32_bf16 v[8:11], v[158:161], v[226:229], v[8:11]
	v_mfma_f32_16x16x32_bf16 v[4:7], v[166:169], v[226:229], v[4:7]
	s_setprio 0
	s_barrier
	s_add_i32 s54, s54, 2
	s_add_u32 s9, s9, 0x100
	s_addc_u32 s53, s53, 0
	s_add_u32 s16, s16, 0x100
	s_addc_u32 s17, s17, 0
	s_cmp_gt_u32 s54, 13
	s_cbranch_scc0 .LBB0_2113
	s_and_b64 vcc, exec, s[6:7]
	s_cbranch_vccz .LBB0_2116
	s_barrier

; __device__ __forceinline__ int lane_id() { int l_; asm volatile("v_mbcnt_lo_u32_b32 %0, -1, 0\n\tv_mbcnt_hi_u32_b32 %0, -1, %0" : "=v"(l_)); return l_; }
; #define PG8_STAGE(bufoff, gbase, voff) do { _Pragma("unroll") for (int _i = 0; _i < 2; ++_i) \
;         glds16((const void*)(gbase), (voff)[_i], ldsbase + (unsigned)(bufoff) + ldsw + (unsigned)_i * 8192u); } while (0)
; #define PG8_WAIT_V(n) asm volatile("s_waitcnt vmcnt(" #n ")" ::: "memory")
; #define PG8_BAR __builtin_amdgcn_s_barrier()
;     ...
;     int tid = w0_ * 64 + lane_id(); asm volatile("" : "+v"(tid));
;     const int wid = __builtin_amdgcn_readfirstlane(tid >> 6), lane = tid & 63, wr = wid >> 2, wc = wid & 3, fr = lane & 15, fq = lane >> 4;
;     const int nt = nt_ ? nt_ : Kb / 128;
;     unsigned voffA[2], voffB[2];
; #pragma unroll
;     for (int i = 0; i < 2; ++i) { int R, C; stage_rc(tid * 16 + i * 8192, R, C); const int Rb = Epi::PERM ? ((R & ~31) + perm32(R & 31)) : R;
;         voffA[i] = (unsigned)(R * ldab + C * 2); voffB[i] = (unsigned)(Rb * Kb + C * 2); }
;     const size_t kstep = (size_t)(BK * 2);
;     const size_t hstepA = (size_t)HALF * ldab, hstepB = (size_t)HALF * Kb;
;     const unsigned ldsw = (unsigned)wid * 1024u, ldsbase = (unsigned)(size_t)lds;
;     const int aoff = lds_byte(wr * 64 + fr, fq * 8), boff = lds_byte(wc * 32 + fr, fq * 8);
;     ...
;     Unit cur, nxt; int ui = 0;
;     if (!S.next(0, cur)) return;
;     f32x4 acc[2][2][4][2];
; #pragma unroll
;     for (int a = 0; a < 2; ++a)
; #pragma unroll
;         for (int b = 0; b < 2; ++b)
; #pragma unroll
;             for (int m = 0; m < 4; ++m)
; #pragma unroll
;                 for (int n = 0; n < 2; ++n) acc[a][b][m][n] = (f32x4){0.f, 0.f, 0.f, 0.f};
;     bf16x8 At[4][2], B0[2][2], B1[2][2];
;     const char* cA = uniform_ptr(cur.a); const char* cB = uniform_ptr(cur.b);
;     PG8_STAGE(PG8_SB(0, 0), cB, voffB); PG8_STAGE(PG8_SB(0, 1), cB + hstepB, voffB); PG8_STAGE(PG8_SA(0, 0), cA, voffA); PG8_STAGE(PG8_SA(0, 1), cA + hstepA, voffA);
;     if (wr == 1) PG8_BAR;
;     PG8_WAIT_V(2); PG8_BAR;
;     PG8_STAGE(PG8_SB(1, 0), cB + kstep, voffB); PG8_STAGE(PG8_SA(1, 0), cA + kstep, voffA); PG8_STAGE(PG8_SB(1, 1), cB + hstepB + kstep, voffB);
;     PG8_WAIT_V(6); PG8_BAR;
.LBB0_2263:
	v_mbcnt_lo_u32_b32 v0, -1, 0
	v_mbcnt_hi_u32_b32 v0, -1, v0
	v_readlane_b32 s0, v250, 60
	v_readlane_b32 s4, v252, 37
	v_readlane_b32 s5, v252, 38
	v_add_u32_e32 v0, s0, v0
	s_andn2_b64 vcc, exec, s[4:5]
	v_readfirstlane_b32 s8, v0
	s_cbranch_vccnz .LBB0_2283
	v_bfe_i32 v4, v0, 27, 1
	v_lshlrev_b32_e32 v1, 4, v0
	v_lshrrev_b32_e32 v4, 22, v4
	v_add_u32_e32 v4, v1, v4
	v_and_b32_e32 v4, 0xfffffc00, v4
	v_sub_u32_e32 v4, v1, v4
	v_ashrrev_i32_e32 v2, 31, v0
	v_lshrrev_b32_e32 v5, 4, v4
	v_lshrrev_b32_e32 v2, 26, v2
	v_bitop3_b32 v4, v5, v4, 32 bitop3:0x6c
	v_add_u32_e32 v2, v0, v2
	v_ashrrev_i32_e32 v6, 31, v4
	s_add_u32 s0, s20, 0x4861e000
	v_ashrrev_i32_e32 v2, 6, v2
	v_lshrrev_b32_e32 v6, 26, v6
	s_addc_u32 s24, s21, 0
	s_lshl_b32 s4, s27, 19
	v_lshlrev_b32_e32 v5, 3, v2
	v_add_u32_e32 v6, v4, v6
	s_add_u32 s4, s20, s4
	v_and_b32_e32 v5, -16, v5
	v_ashrrev_i32_e32 v7, 6, v6
	v_and_b32_e32 v6, 0xc0, v6
	s_addc_u32 s5, s21, 0
	v_add_u32_e32 v5, v7, v5
	v_sub_u32_e32 v4, v4, v6
	s_add_u32 s25, s4, 0x3d00000
	v_lshlrev_b32_e32 v2, 5, v2
	v_ashrrev_i16_sdwa v4, v188, sext(v4) dst_sel:DWORD dst_unused:UNUSED_PAD src0_sel:DWORD src1_sel:BYTE_0
	v_lshlrev_b32_e32 v6, 1, v5
	v_lshrrev_b32_e32 v8, 2, v5
	v_and_b32_e32 v7, 3, v7
	s_mov_b32 s4, 0x3fffe0
	v_and_b32_e32 v2, 32, v2
	v_bfe_i32 v4, v4, 0, 16
	v_and_b32_e32 v6, 24, v6
	v_and_b32_e32 v8, 4, v8
	v_and_or_b32 v7, v5, s4, v7
	v_or3_b32 v6, v7, v8, v6
	v_add_lshl_u32 v4, v2, v4, 1
	v_add_u32_e32 v1, 0x2000, v1
	v_lshl_add_u32 v2, v5, 10, v4
	s_waitcnt vmcnt(0)
	v_lshl_add_u32 v132, v6, 10, v4
	v_ashrrev_i32_e32 v4, 31, v1
	v_lshrrev_b32_e32 v4, 22, v4
	v_add_u32_e32 v4, v1, v4
	v_ashrrev_i32_e32 v4, 10, v4
	v_mul_i32_i24_e32 v5, 0x400, v4
	v_sub_u32_e32 v1, v1, v5
	v_lshrrev_b32_e32 v5, 4, v1
	v_bitop3_b32 v1, v5, v1, 32 bitop3:0x6c
	v_ashrrev_i32_e32 v6, 31, v1
	v_lshrrev_b32_e32 v6, 26, v6
	v_lshlrev_b32_e32 v5, 3, v4
	v_add_u32_e32 v6, v1, v6
	v_and_b32_e32 v5, -16, v5
	v_ashrrev_i32_e32 v7, 6, v6
	s_addc_u32 s26, s5, 0
	v_add_u32_e32 v5, v7, v5
	v_and_b32_e32 v7, 3, v7
	s_ashr_i32 s10, s8, 6
	s_ashr_i32 s9, s8, 8
	v_and_or_b32 v7, v5, s4, v7
	s_lshl_b32 s6, s10, 10
	v_readlane_b32 s4, v253, 12
	v_readlane_b32 s5, v253, 13
	s_add_u32 s16, s25, s4
	s_addc_u32 s17, s26, s5
	v_readlane_b32 s4, v253, 14
	v_readlane_b32 s5, v253, 15
	v_and_b32_e32 v6, 0xc0, v6
	s_and_b64 s[4:5], s[4:5], exec
	v_sub_u32_e32 v1, v1, v6
	s_cselect_b32 s5, s2, s0
	v_readlane_b32 s7, v253, 19
	v_lshlrev_b32_e32 v4, 5, v4
	v_ashrrev_i16_sdwa v1, v188, sext(v1) dst_sel:DWORD dst_unused:UNUSED_PAD src0_sel:DWORD src1_sel:BYTE_0
	v_lshlrev_b32_e32 v6, 1, v5
	v_lshrrev_b32_e32 v8, 2, v5
	s_cselect_b32 s4, s3, s24
	s_add_u32 s18, s5, s7
	v_and_b32_e32 v4, 32, v4
	v_bfe_i32 v1, v1, 0, 16
	v_and_b32_e32 v6, 24, v6
	v_and_b32_e32 v8, 4, v8
	s_addc_u32 s19, s4, 0
	s_add_i32 s27, s6, 0
	v_or3_b32 v6, v7, v8, v6
	v_add_lshl_u32 v1, v4, v1, 1
	s_add_i32 s28, s27, 0x10000
	s_mov_b32 m0, s28
	s_nop 0
	global_load_lds_dwordx4 v132, s[16:17]
	v_lshl_add_u32 v134, v6, 10, v1
	s_add_i32 s29, s27, 0x12000
	s_mov_b32 m0, s29
	s_nop 0
	global_load_lds_dwordx4 v134, s[16:17]
	s_add_u32 s4, s16, 0x20000
	s_addc_u32 s5, s17, 0
	s_add_i32 s30, s27, 0x14000
	s_mov_b32 m0, s30
	s_nop 0
	global_load_lds_dwordx4 v132, s[4:5]
	s_add_i32 s31, s27, 0x16000
	s_mov_b32 m0, s31
	s_nop 0
	global_load_lds_dwordx4 v134, s[4:5]
	s_mov_b32 m0, s27
	s_nop 0
	global_load_lds_dwordx4 v2, s[18:19]
	v_lshl_add_u32 v133, v5, 10, v1
	s_add_i32 s34, s27, 0x2000
	s_mov_b32 m0, s34
	s_nop 0
	global_load_lds_dwordx4 v133, s[18:19]
	s_add_u32 s4, s18, 0x20000
	s_addc_u32 s5, s19, 0
	s_add_i32 s35, s27, 0x4000
	s_mov_b32 m0, s35
	s_nop 0
	global_load_lds_dwordx4 v2, s[4:5]
	s_add_i32 s36, s27, 0x6000
	s_mov_b32 m0, s36
	s_nop 0
	global_load_lds_dwordx4 v133, s[4:5]
	s_cmp_eq_u32 s9, 1
	s_cselect_b64 s[4:5], -1, 0
	s_cmp_lg_u32 s9, 1
	s_cbranch_scc1 .LBB0_2266
	s_barrier
.LBB0_2266:
	v_lshrrev_b32_e32 v4, 1, v0
	v_and_b32_e32 v4, 24, v4
	s_add_u32 s6, s20, 0x4881e000
	v_and_b32_e32 v1, 15, v0
	v_lshlrev_b32_e32 v5, 1, v4
	v_lshlrev_b32_e32 v0, 2, v0
	s_addc_u32 s7, s21, 0
	v_lshl_or_b32 v135, s9, 6, v1
	v_lshl_or_b32 v1, v1, 6, v5
	s_lshl_b32 s9, s9, 13
	v_and_b32_e32 v0, 32, v0
	v_bitop3_b32 v5, v1, s9, v0 bitop3:0xde
	s_lshl_b32 s9, s10, 5
	s_and_b32 s12, s9, 0x60
	s_lshl_b32 s9, s12, 7
	s_add_u32 s10, s16, 0x80
	v_bitop3_b32 v0, v1, s9, v0 bitop3:0xde
	s_waitcnt vmcnt(2)
	s_barrier
	s_addc_u32 s11, s17, 0
	s_add_i32 s37, s27, 0x18000
	s_mov_b32 m0, s37
	s_nop 0
	global_load_lds_dwordx4 v132, s[10:11]
	s_add_i32 s38, s27, 0x1a000
	s_mov_b32 m0, s38
	s_nop 0
	global_load_lds_dwordx4 v134, s[10:11]
	s_add_u32 s10, s18, 0x80
	s_addc_u32 s11, s19, 0
	s_add_i32 s39, s27, 0x8000
	s_mov_b32 m0, s39
	s_nop 0
	global_load_lds_dwordx4 v2, s[10:11]
	s_add_i32 s40, s27, 0xa000
	s_mov_b32 m0, s40
	s_nop 0
	global_load_lds_dwordx4 v133, s[10:11]
	s_add_u32 s10, s16, 0x20080
	s_addc_u32 s11, s17, 0
	s_add_i32 s41, s27, 0x1c000
	s_mov_b32 m0, s41
	s_nop 0
	global_load_lds_dwordx4 v132, s[10:11]
	s_add_i32 s42, s27, 0x1e000
	s_mov_b32 m0, s42
	s_nop 0
	global_load_lds_dwordx4 v134, s[10:11]
	s_waitcnt vmcnt(6)
	s_add_i32 s43, s27, 0xc000
	s_cmpk_lt_u32 s8, 0x100
	s_cselect_b64 s[8:9], -1, 0
	s_add_i32 s44, s27, 0xe000
	v_or_b32_e32 v136, s12, v4
	s_mov_b32 s48, 0
	v_add_u32_e32 v137, 0, v0
	v_add_u32_e32 v138, 0, v5
	v_readlane_b32 s49, v253, 18
	s_mov_b32 s45, 0
	s_mov_b64 s[12:13], s[18:19]
	s_mov_b64 s[14:15], s[16:17]
	s_barrier
	s_branch .LBB0_2269

; #define PG8_STAGE(bufoff, gbase, voff) do { _Pragma("unroll") for (int _i = 0; _i < 2; ++_i) \
;         glds16((const void*)(gbase), (voff)[_i], ldsbase + (unsigned)(bufoff) + ldsw + (unsigned)_i * 8192u); } while (0)
; #define PG8_LDA(dst, b, h) do { _Pragma("unroll") for (int m = 0; m < 4; ++m) _Pragma("unroll") for (int k = 0; k < 2; ++k) dst[m][k] = *(const LAS bf16x8*)(lds + PG8_SA(b, h) + aoff + m * 2048 + k * 1024); } while (0)
; #define PG8_LDB(dst, b, h) do { _Pragma("unroll") for (int n = 0; n < 2; ++n) _Pragma("unroll") for (int k = 0; k < 2; ++k) dst[n][k] = *(const LAS bf16x8*)(lds + PG8_SB(b, h) + boff + n * 2048 + k * 1024); } while (0)
; #define PG8_WAIT_V(n) asm volatile("s_waitcnt vmcnt(" #n ")" ::: "memory")
; #define PG8_WAIT_L(n) asm volatile("s_waitcnt lgkmcnt(" #n ")" ::: "memory")
; #define PG8_BAR __builtin_amdgcn_s_barrier()
; #define PG8_SCHED __builtin_amdgcn_sched_barrier(0)
;     ...
;             const char* a1 = cA + (size_t)(t + 1) * kstep;
;             const char* a2 = last ? nA : cA + (size_t)(t + 2) * kstep; const char* b2 = last ? nB : cB + (size_t)(t + 2) * kstep;
;             const char* a3 = a2 + kstep; const char* b3 = b2 + kstep;
;             PG8_LDB(B0, 0, 0); PG8_LDB(B1, 0, 1); PG8_SCHED; PG8_LDA(At, 0, 0); PG8_STAGE(PG8_SA(1, 1), a1 + hstepA, voffA);
;             PG8_WAIT_V(8); PG8_WAIT_L(0); PG8_BAR; PG8_MMA(0, 0, At, B0); PG8_MMA(0, 1, At, B1); PG8_BAR; PG8_SCHED;
;             PG8_LDA(At, 0, 1); PG8_STAGE(PG8_SB(0, 0), b2, voffB); PG8_STAGE(PG8_SB(0, 1), b2 + hstepB, voffB); PG8_STAGE(PG8_SA(0, 0), a2, voffA);
;             PG8_WAIT_V(8); PG8_WAIT_L(0); PG8_BAR; PG8_MMA(1, 0, At, B0); PG8_MMA(1, 1, At, B1); PG8_BAR; PG8_SCHED;
.LBB0_2276:
	v_add_u32_e32 v0, 0x10000, v137
	ds_read_b128 v[140:143], v0
	ds_read_b128 v[144:147], v0 offset:1024
	ds_read_b128 v[148:151], v0 offset:2048
	ds_read_b128 v[152:155], v0 offset:3072
	v_add_u32_e32 v0, 0x14000, v137
	ds_read_b128 v[156:159], v0
	ds_read_b128 v[160:163], v0 offset:1024
	ds_read_b128 v[164:167], v0 offset:2048
	ds_read_b128 v[168:171], v0 offset:3072
	s_add_u32 s18, s16, 0xfffe0080
	s_addc_u32 s19, s17, -1
	s_cmp_eq_u32 s52, 4
	s_cselect_b32 s22, s12, s18
	s_cselect_b32 s23, s13, s19
	s_cselect_b32 s20, s14, s50
	s_cselect_b32 s21, s15, s51
	s_add_u32 s18, s22, 0x80
	s_addc_u32 s19, s23, 0
	ds_read_b128 v[176:179], v138
	ds_read_b128 v[180:183], v138 offset:1024
	ds_read_b128 v[206:209], v138 offset:2048
	ds_read_b128 v[210:213], v138 offset:3072
	ds_read_b128 v[214:217], v138 offset:4096
	ds_read_b128 v[218:221], v138 offset:5120
	ds_read_b128 v[222:225], v138 offset:6144
	ds_read_b128 v[226:229], v138 offset:7168
	s_mov_b32 m0, s43
	s_nop 0
	global_load_lds_dwordx4 v2, s[16:17]
	s_nop 0
	s_mov_b32 m0, s44
	s_nop 0
	global_load_lds_dwordx4 v133, s[16:17]
	s_waitcnt vmcnt(8)
	s_waitcnt lgkmcnt(0)
	s_barrier
	s_setprio 1
	s_waitcnt lgkmcnt(7)
	v_mfma_f32_16x16x32_bf16 v[128:131], v[140:143], v[176:179], v[128:131]
	v_mfma_f32_16x16x32_bf16 v[124:127], v[148:151], v[176:179], v[124:127]
	s_waitcnt lgkmcnt(5)
	v_mfma_f32_16x16x32_bf16 v[120:123], v[140:143], v[206:209], v[120:123]
	v_mfma_f32_16x16x32_bf16 v[112:115], v[148:151], v[206:209], v[112:115]
	s_waitcnt lgkmcnt(3)
	v_mfma_f32_16x16x32_bf16 v[104:107], v[140:143], v[214:217], v[104:107]
	v_mfma_f32_16x16x32_bf16 v[96:99], v[148:151], v[214:217], v[96:99]
	s_waitcnt lgkmcnt(1)
	v_mfma_f32_16x16x32_bf16 v[88:91], v[140:143], v[222:225], v[88:91]
	v_mfma_f32_16x16x32_bf16 v[80:83], v[148:151], v[222:225], v[80:83]
	v_mfma_f32_16x16x32_bf16 v[128:131], v[144:147], v[180:183], v[128:131]
	v_mfma_f32_16x16x32_bf16 v[124:127], v[152:155], v[180:183], v[124:127]
	v_mfma_f32_16x16x32_bf16 v[120:123], v[144:147], v[210:213], v[120:123]
	v_mfma_f32_16x16x32_bf16 v[112:115], v[152:155], v[210:213], v[112:115]
	v_mfma_f32_16x16x32_bf16 v[104:107], v[144:147], v[218:221], v[104:107]
	v_mfma_f32_16x16x32_bf16 v[96:99], v[152:155], v[218:221], v[96:99]
	s_waitcnt lgkmcnt(0)
	v_mfma_f32_16x16x32_bf16 v[88:91], v[144:147], v[226:229], v[88:91]
	v_mfma_f32_16x16x32_bf16 v[80:83], v[152:155], v[226:229], v[80:83]
	s_setprio 0
	s_setprio 1
	v_mfma_f32_16x16x32_bf16 v[116:119], v[156:159], v[176:179], v[116:119]
	v_mfma_f32_16x16x32_bf16 v[108:111], v[164:167], v[176:179], v[108:111]
	v_mfma_f32_16x16x32_bf16 v[100:103], v[156:159], v[206:209], v[100:103]
	v_mfma_f32_16x16x32_bf16 v[92:95], v[164:167], v[206:209], v[92:95]
	v_mfma_f32_16x16x32_bf16 v[84:87], v[156:159], v[214:217], v[84:87]
	v_mfma_f32_16x16x32_bf16 v[76:79], v[164:167], v[214:217], v[76:79]
	v_mfma_f32_16x16x32_bf16 v[72:75], v[156:159], v[222:225], v[72:75]
	v_mfma_f32_16x16x32_bf16 v[68:71], v[164:167], v[222:225], v[68:71]
	v_mfma_f32_16x16x32_bf16 v[116:119], v[160:163], v[180:183], v[116:119]
	v_mfma_f32_16x16x32_bf16 v[108:111], v[168:171], v[180:183], v[108:111]
	v_mfma_f32_16x16x32_bf16 v[100:103], v[160:163], v[210:213], v[100:103]
	v_mfma_f32_16x16x32_bf16 v[92:95], v[168:171], v[210:213], v[92:95]
	v_mfma_f32_16x16x32_bf16 v[84:87], v[160:163], v[218:221], v[84:87]
	v_mfma_f32_16x16x32_bf16 v[76:79], v[168:171], v[218:221], v[76:79]
	v_mfma_f32_16x16x32_bf16 v[72:75], v[160:163], v[226:229], v[72:75]
	v_mfma_f32_16x16x32_bf16 v[68:71], v[168:171], v[226:229], v[68:71]
	s_setprio 0
	s_barrier
	ds_read_b128 v[176:179], v138 offset:16384
	ds_read_b128 v[180:183], v138 offset:17408
	ds_read_b128 v[206:209], v138 offset:18432
	ds_read_b128 v[210:213], v138 offset:19456
	ds_read_b128 v[214:217], v138 offset:20480
	ds_read_b128 v[218:221], v138 offset:21504
	ds_read_b128 v[222:225], v138 offset:22528
	ds_read_b128 v[226:229], v138 offset:23552
	s_mov_b32 m0, s28
	s_nop 0
	global_load_lds_dwordx4 v132, s[20:21]
	s_add_u32 s54, s20, 0x20000
	s_mov_b32 m0, s29
	s_nop 0
	global_load_lds_dwordx4 v134, s[20:21]
	s_addc_u32 s55, s21, 0
	s_mov_b32 m0, s30
	s_nop 0
	global_load_lds_dwordx4 v132, s[54:55]
	s_nop 0
	s_mov_b32 m0, s31
	s_nop 0
	global_load_lds_dwordx4 v134, s[54:55]
	s_nop 0
	s_mov_b32 m0, s27
	s_nop 0
	global_load_lds_dwordx4 v2, s[22:23]
	s_nop 0
	s_mov_b32 m0, s34
	s_nop 0
	global_load_lds_dwordx4 v133, s[22:23]
	s_waitcnt vmcnt(8)
	s_waitcnt lgkmcnt(0)
	s_barrier
; #define PG8_STAGE(bufoff, gbase, voff) do { _Pragma("unroll") for (int _i = 0; _i < 2; ++_i) \
;         glds16((const void*)(gbase), (voff)[_i], ldsbase + (unsigned)(bufoff) + ldsw + (unsigned)_i * 8192u); } while (0)
; #define PG8_LDA(dst, b, h) do { _Pragma("unroll") for (int m = 0; m < 4; ++m) _Pragma("unroll") for (int k = 0; k < 2; ++k) dst[m][k] = *(const LAS bf16x8*)(lds + PG8_SA(b, h) + aoff + m * 2048 + k * 1024); } while (0)
; #define PG8_LDB(dst, b, h) do { _Pragma("unroll") for (int n = 0; n < 2; ++n) _Pragma("unroll") for (int k = 0; k < 2; ++k) dst[n][k] = *(const LAS bf16x8*)(lds + PG8_SB(b, h) + boff + n * 2048 + k * 1024); } while (0)
; #define PG8_WAIT_V(n) asm volatile("s_waitcnt vmcnt(" #n ")" ::: "memory")
; #define PG8_WAIT_L(n) asm volatile("s_waitcnt lgkmcnt(" #n ")" ::: "memory")
; #define PG8_BAR __builtin_amdgcn_s_barrier()
; #define PG8_SCHED __builtin_amdgcn_sched_barrier(0)
;     ...
;             PG8_WAIT_V(8); PG8_WAIT_L(0); PG8_BAR; PG8_MMA(1, 0, At, B0); PG8_MMA(1, 1, At, B1); PG8_BAR; PG8_SCHED;
;             PG8_LDB(B0, 1, 0); PG8_LDB(B1, 1, 1); PG8_SCHED; PG8_LDA(At, 1, 0); PG8_STAGE(PG8_SA(0, 1), a2 + hstepA, voffA);
;             PG8_WAIT_V(8); PG8_WAIT_L(0); PG8_BAR; PG8_MMA(0, 0, At, B0); PG8_MMA(0, 1, At, B1); PG8_BAR; PG8_SCHED;
;             PG8_LDA(At, 1, 1); PG8_STAGE(PG8_SB(1, 0), b3, voffB); PG8_STAGE(PG8_SB(1, 1), b3 + hstepB, voffB); PG8_STAGE(PG8_SA(1, 0), a3, voffA);
;             PG8_WAIT_V(8); PG8_WAIT_L(0); PG8_BAR; PG8_MMA(1, 0, At, B0); PG8_MMA(1, 1, At, B1); PG8_BAR; PG8_SCHED;
	s_setprio 1
	s_waitcnt lgkmcnt(7)
	v_mfma_f32_16x16x32_bf16 v[64:67], v[140:143], v[176:179], v[64:67]
	v_mfma_f32_16x16x32_bf16 v[60:63], v[148:151], v[176:179], v[60:63]
	s_waitcnt lgkmcnt(5)
	v_mfma_f32_16x16x32_bf16 v[56:59], v[140:143], v[206:209], v[56:59]
	v_mfma_f32_16x16x32_bf16 v[48:51], v[148:151], v[206:209], v[48:51]
	s_waitcnt lgkmcnt(3)
	v_mfma_f32_16x16x32_bf16 v[40:43], v[140:143], v[214:217], v[40:43]
	v_mfma_f32_16x16x32_bf16 v[32:35], v[148:151], v[214:217], v[32:35]
	s_waitcnt lgkmcnt(1)
	v_mfma_f32_16x16x32_bf16 v[24:27], v[140:143], v[222:225], v[24:27]
	v_mfma_f32_16x16x32_bf16 v[16:19], v[148:151], v[222:225], v[16:19]
	v_mfma_f32_16x16x32_bf16 v[64:67], v[144:147], v[180:183], v[64:67]
	v_mfma_f32_16x16x32_bf16 v[60:63], v[152:155], v[180:183], v[60:63]
	v_mfma_f32_16x16x32_bf16 v[56:59], v[144:147], v[210:213], v[56:59]
	v_mfma_f32_16x16x32_bf16 v[48:51], v[152:155], v[210:213], v[48:51]
	v_mfma_f32_16x16x32_bf16 v[40:43], v[144:147], v[218:221], v[40:43]
	v_mfma_f32_16x16x32_bf16 v[32:35], v[152:155], v[218:221], v[32:35]
	s_waitcnt lgkmcnt(0)
	v_mfma_f32_16x16x32_bf16 v[24:27], v[144:147], v[226:229], v[24:27]
	v_mfma_f32_16x16x32_bf16 v[16:19], v[152:155], v[226:229], v[16:19]
	s_setprio 0
	s_setprio 1
	v_mfma_f32_16x16x32_bf16 v[52:55], v[156:159], v[176:179], v[52:55]
	v_mfma_f32_16x16x32_bf16 v[44:47], v[164:167], v[176:179], v[44:47]
	v_mfma_f32_16x16x32_bf16 v[36:39], v[156:159], v[206:209], v[36:39]
	v_mfma_f32_16x16x32_bf16 v[28:31], v[164:167], v[206:209], v[28:31]
	v_mfma_f32_16x16x32_bf16 v[20:23], v[156:159], v[214:217], v[20:23]
	v_mfma_f32_16x16x32_bf16 v[12:15], v[164:167], v[214:217], v[12:15]
	v_mfma_f32_16x16x32_bf16 v[8:11], v[156:159], v[222:225], v[8:11]
	v_mfma_f32_16x16x32_bf16 v[4:7], v[164:167], v[222:225], v[4:7]
	v_mfma_f32_16x16x32_bf16 v[52:55], v[160:163], v[180:183], v[52:55]
	v_mfma_f32_16x16x32_bf16 v[44:47], v[168:171], v[180:183], v[44:47]
	v_mfma_f32_16x16x32_bf16 v[36:39], v[160:163], v[210:213], v[36:39]
	v_mfma_f32_16x16x32_bf16 v[28:31], v[168:171], v[210:213], v[28:31]
	v_mfma_f32_16x16x32_bf16 v[20:23], v[160:163], v[218:221], v[20:23]
	v_mfma_f32_16x16x32_bf16 v[12:15], v[168:171], v[218:221], v[12:15]
	v_mfma_f32_16x16x32_bf16 v[8:11], v[160:163], v[226:229], v[8:11]
	v_mfma_f32_16x16x32_bf16 v[4:7], v[168:171], v[226:229], v[4:7]
	s_setprio 0
	s_barrier
	v_add_u32_e32 v0, 0x18000, v137
	ds_read_b128 v[140:143], v0
	ds_read_b128 v[144:147], v0 offset:1024
	ds_read_b128 v[148:151], v0 offset:2048
	ds_read_b128 v[152:155], v0 offset:3072
	v_add_u32_e32 v0, 0x1c000, v137
	ds_read_b128 v[156:159], v0
	ds_read_b128 v[160:163], v0 offset:1024
	ds_read_b128 v[164:167], v0 offset:2048
	ds_read_b128 v[168:171], v0 offset:3072
	ds_read_b128 v[176:179], v138 offset:32768
	ds_read_b128 v[180:183], v138 offset:33792
	ds_read_b128 v[206:209], v138 offset:34816
	ds_read_b128 v[210:213], v138 offset:35840
	ds_read_b128 v[214:217], v138 offset:36864
	ds_read_b128 v[218:221], v138 offset:37888
	ds_read_b128 v[222:225], v138 offset:38912
	ds_read_b128 v[226:229], v138 offset:39936
	s_add_u32 s22, s22, 0x20000
	s_addc_u32 s23, s23, 0
	s_mov_b32 m0, s35
	s_nop 0
	global_load_lds_dwordx4 v2, s[22:23]
	s_nop 0
	s_mov_b32 m0, s36
	s_nop 0
	global_load_lds_dwordx4 v133, s[22:23]
	s_waitcnt vmcnt(8)
	s_waitcnt lgkmcnt(0)
	s_barrier
	s_setprio 1
	s_waitcnt lgkmcnt(7)
	v_mfma_f32_16x16x32_bf16 v[128:131], v[140:143], v[176:179], v[128:131]
	v_mfma_f32_16x16x32_bf16 v[124:127], v[148:151], v[176:179], v[124:127]
	s_waitcnt lgkmcnt(5)
	v_mfma_f32_16x16x32_bf16 v[120:123], v[140:143], v[206:209], v[120:123]
	v_mfma_f32_16x16x32_bf16 v[112:115], v[148:151], v[206:209], v[112:115]
	s_waitcnt lgkmcnt(3)
	v_mfma_f32_16x16x32_bf16 v[104:107], v[140:143], v[214:217], v[104:107]
	v_mfma_f32_16x16x32_bf16 v[96:99], v[148:151], v[214:217], v[96:99]
	s_waitcnt lgkmcnt(1)
	v_mfma_f32_16x16x32_bf16 v[88:91], v[140:143], v[222:225], v[88:91]
	v_mfma_f32_16x16x32_bf16 v[80:83], v[148:151], v[222:225], v[80:83]
	v_mfma_f32_16x16x32_bf16 v[128:131], v[144:147], v[180:183], v[128:131]
	v_mfma_f32_16x16x32_bf16 v[124:127], v[152:155], v[180:183], v[124:127]
	v_mfma_f32_16x16x32_bf16 v[120:123], v[144:147], v[210:213], v[120:123]
	v_mfma_f32_16x16x32_bf16 v[112:115], v[152:155], v[210:213], v[112:115]
	v_mfma_f32_16x16x32_bf16 v[104:107], v[144:147], v[218:221], v[104:107]
	v_mfma_f32_16x16x32_bf16 v[96:99], v[152:155], v[218:221], v[96:99]
	s_waitcnt lgkmcnt(0)
	v_mfma_f32_16x16x32_bf16 v[88:91], v[144:147], v[226:229], v[88:91]
	v_mfma_f32_16x16x32_bf16 v[80:83], v[152:155], v[226:229], v[80:83]
	s_setprio 0
	s_setprio 1
	v_mfma_f32_16x16x32_bf16 v[116:119], v[156:159], v[176:179], v[116:119]
	v_mfma_f32_16x16x32_bf16 v[108:111], v[164:167], v[176:179], v[108:111]
	v_mfma_f32_16x16x32_bf16 v[100:103], v[156:159], v[206:209], v[100:103]
	v_mfma_f32_16x16x32_bf16 v[92:95], v[164:167], v[206:209], v[92:95]
	v_mfma_f32_16x16x32_bf16 v[84:87], v[156:159], v[214:217], v[84:87]
	v_mfma_f32_16x16x32_bf16 v[76:79], v[164:167], v[214:217], v[76:79]
	v_mfma_f32_16x16x32_bf16 v[72:75], v[156:159], v[222:225], v[72:75]
	v_mfma_f32_16x16x32_bf16 v[68:71], v[164:167], v[222:225], v[68:71]
	v_mfma_f32_16x16x32_bf16 v[116:119], v[160:163], v[180:183], v[116:119]
	v_mfma_f32_16x16x32_bf16 v[108:111], v[168:171], v[180:183], v[108:111]
	v_mfma_f32_16x16x32_bf16 v[100:103], v[160:163], v[210:213], v[100:103]
	v_mfma_f32_16x16x32_bf16 v[92:95], v[168:171], v[210:213], v[92:95]
	v_mfma_f32_16x16x32_bf16 v[84:87], v[160:163], v[218:221], v[84:87]
	v_mfma_f32_16x16x32_bf16 v[76:79], v[168:171], v[218:221], v[76:79]
	v_mfma_f32_16x16x32_bf16 v[72:75], v[160:163], v[226:229], v[72:75]
	v_mfma_f32_16x16x32_bf16 v[68:71], v[168:171], v[226:229], v[68:71]
	s_setprio 0
	s_barrier
; #define PG8_STAGE(bufoff, gbase, voff) do { _Pragma("unroll") for (int _i = 0; _i < 2; ++_i) \
;         glds16((const void*)(gbase), (voff)[_i], ldsbase + (unsigned)(bufoff) + ldsw + (unsigned)_i * 8192u); } while (0)
; #define PG8_LDA(dst, b, h) do { _Pragma("unroll") for (int m = 0; m < 4; ++m) _Pragma("unroll") for (int k = 0; k < 2; ++k) dst[m][k] = *(const LAS bf16x8*)(lds + PG8_SA(b, h) + aoff + m * 2048 + k * 1024); } while (0)
; #define PG8_WAIT_V(n) asm volatile("s_waitcnt vmcnt(" #n ")" ::: "memory")
; #define PG8_WAIT_L(n) asm volatile("s_waitcnt lgkmcnt(" #n ")" ::: "memory")
; #define PG8_BAR __builtin_amdgcn_s_barrier()
; #define PG8_SCHED __builtin_amdgcn_sched_barrier(0)
;     ...
;             PG8_LDA(At, 1, 1); PG8_STAGE(PG8_SB(1, 0), b3, voffB); PG8_STAGE(PG8_SB(1, 1), b3 + hstepB, voffB); PG8_STAGE(PG8_SA(1, 0), a3, voffA);
;             PG8_WAIT_V(8); PG8_WAIT_L(0); PG8_BAR; PG8_MMA(1, 0, At, B0); PG8_MMA(1, 1, At, B1); PG8_BAR; PG8_SCHED;
;         }
;         if (wr == 0) PG8_BAR;
	ds_read_b128 v[176:179], v138 offset:49152
	ds_read_b128 v[180:183], v138 offset:50176
	ds_read_b128 v[206:209], v138 offset:51200
	ds_read_b128 v[210:213], v138 offset:52224
	ds_read_b128 v[214:217], v138 offset:53248
	ds_read_b128 v[218:221], v138 offset:54272
	ds_read_b128 v[222:225], v138 offset:55296
	ds_read_b128 v[226:229], v138 offset:56320
	s_add_u32 s22, s20, 0x80
	s_addc_u32 s23, s21, 0
	s_mov_b32 m0, s37
	s_nop 0
	global_load_lds_dwordx4 v132, s[22:23]
	s_add_u32 s20, s20, 0x20080
	s_mov_b32 m0, s38
	s_nop 0
	global_load_lds_dwordx4 v134, s[22:23]
	s_addc_u32 s21, s21, 0
	s_mov_b32 m0, s41
	s_nop 0
	global_load_lds_dwordx4 v132, s[20:21]
	s_nop 0
	s_mov_b32 m0, s42
	s_nop 0
	global_load_lds_dwordx4 v134, s[20:21]
	s_mov_b32 m0, s39
	s_nop 0
	global_load_lds_dwordx4 v2, s[18:19]
	s_nop 0
	s_mov_b32 m0, s40
	s_nop 0
	global_load_lds_dwordx4 v133, s[18:19]
	s_waitcnt vmcnt(8)
	s_waitcnt lgkmcnt(0)
	s_barrier
	s_setprio 1
	s_waitcnt lgkmcnt(7)
	v_mfma_f32_16x16x32_bf16 v[64:67], v[140:143], v[176:179], v[64:67]
	v_mfma_f32_16x16x32_bf16 v[60:63], v[148:151], v[176:179], v[60:63]
	s_waitcnt lgkmcnt(5)
	v_mfma_f32_16x16x32_bf16 v[56:59], v[140:143], v[206:209], v[56:59]
	v_mfma_f32_16x16x32_bf16 v[48:51], v[148:151], v[206:209], v[48:51]
	s_waitcnt lgkmcnt(3)
	v_mfma_f32_16x16x32_bf16 v[40:43], v[140:143], v[214:217], v[40:43]
	v_mfma_f32_16x16x32_bf16 v[32:35], v[148:151], v[214:217], v[32:35]
	s_waitcnt lgkmcnt(1)
	v_mfma_f32_16x16x32_bf16 v[24:27], v[140:143], v[222:225], v[24:27]
	v_mfma_f32_16x16x32_bf16 v[16:19], v[148:151], v[222:225], v[16:19]
	v_mfma_f32_16x16x32_bf16 v[64:67], v[144:147], v[180:183], v[64:67]
	v_mfma_f32_16x16x32_bf16 v[60:63], v[152:155], v[180:183], v[60:63]
	v_mfma_f32_16x16x32_bf16 v[56:59], v[144:147], v[210:213], v[56:59]
	v_mfma_f32_16x16x32_bf16 v[48:51], v[152:155], v[210:213], v[48:51]
	v_mfma_f32_16x16x32_bf16 v[40:43], v[144:147], v[218:221], v[40:43]
	v_mfma_f32_16x16x32_bf16 v[32:35], v[152:155], v[218:221], v[32:35]
	s_waitcnt lgkmcnt(0)
	v_mfma_f32_16x16x32_bf16 v[24:27], v[144:147], v[226:229], v[24:27]
	v_mfma_f32_16x16x32_bf16 v[16:19], v[152:155], v[226:229], v[16:19]
	s_setprio 0
	s_setprio 1
	v_mfma_f32_16x16x32_bf16 v[52:55], v[156:159], v[176:179], v[52:55]
	v_mfma_f32_16x16x32_bf16 v[44:47], v[164:167], v[176:179], v[44:47]
	v_mfma_f32_16x16x32_bf16 v[36:39], v[156:159], v[206:209], v[36:39]
	v_mfma_f32_16x16x32_bf16 v[28:31], v[164:167], v[206:209], v[28:31]
	v_mfma_f32_16x16x32_bf16 v[20:23], v[156:159], v[214:217], v[20:23]
	v_mfma_f32_16x16x32_bf16 v[12:15], v[164:167], v[214:217], v[12:15]
	v_mfma_f32_16x16x32_bf16 v[8:11], v[156:159], v[222:225], v[8:11]
	v_mfma_f32_16x16x32_bf16 v[4:7], v[164:167], v[222:225], v[4:7]
	v_mfma_f32_16x16x32_bf16 v[52:55], v[160:163], v[180:183], v[52:55]
	v_mfma_f32_16x16x32_bf16 v[44:47], v[168:171], v[180:183], v[44:47]
	v_mfma_f32_16x16x32_bf16 v[36:39], v[160:163], v[210:213], v[36:39]
	v_mfma_f32_16x16x32_bf16 v[28:31], v[168:171], v[210:213], v[28:31]
	v_mfma_f32_16x16x32_bf16 v[20:23], v[160:163], v[218:221], v[20:23]
	v_mfma_f32_16x16x32_bf16 v[12:15], v[168:171], v[218:221], v[12:15]
	v_mfma_f32_16x16x32_bf16 v[8:11], v[160:163], v[226:229], v[8:11]
	v_mfma_f32_16x16x32_bf16 v[4:7], v[168:171], v[226:229], v[4:7]
	s_setprio 0
	s_barrier
	s_add_i32 s52, s52, 2
	s_add_u32 s50, s50, 0x100
	s_addc_u32 s51, s51, 0
	s_add_u32 s16, s16, 0x100
	s_addc_u32 s17, s17, 0
	s_cmp_gt_u32 s52, 5
	s_cbranch_scc0 .LBB0_2276
	s_and_b64 vcc, exec, s[8:9]
	s_cbranch_vccz .LBB0_2279
	s_barrier

; __device__ __forceinline__ int lane_id() { int l_; asm volatile("v_mbcnt_lo_u32_b32 %0, -1, 0\n\tv_mbcnt_hi_u32_b32 %0, -1, %0" : "=v"(l_)); return l_; }
; #define PG8_WAIT_V(n) asm volatile("s_waitcnt vmcnt(" #n ")" ::: "memory")
; #define PG8_BAR __builtin_amdgcn_s_barrier()
;     __device__ __forceinline__ bool idx(int i, int& pm, int& pn) const {
;         const long L = (long)i * G + c; if (L >= nwg) return false;
;         int wgid = (int)L; { const int q = nwg / 8, r = nwg % 8, xcd = wgid % 8, off = wgid / 8; wgid = (xcd < r ? xcd * (q + 1) : r * (q + 1) + (xcd - r) * q) + off; }
;         const int nig = 8 * nN, gid = wgid / nig, fm = gid * 8, gsz = (nM - fm) < 8 ? (nM - fm) : 8;
;         pm = fm + ((wgid % nig) % gsz); pn = (wgid % nig) / gsz; return true;
;     ...
;     int tid = w0_ * 64 + lane_id(); asm volatile("" : "+v"(tid));
;     const int wid = __builtin_amdgcn_readfirstlane(tid >> 6), lane = tid & 63, wr = wid >> 2, wc = wid & 3, fr = lane & 15, fq = lane >> 4;
;     const int nt = nt_ ? nt_ : Kb / 128;
;     unsigned voffA[2], voffB[2];
; #pragma unroll
;     for (int i = 0; i < 2; ++i) { int R, C; stage_rc(tid * 16 + i * 8192, R, C); const int Rb = Epi::PERM ? ((R & ~31) + perm32(R & 31)) : R;
;         voffA[i] = (unsigned)(R * ldab + C * 2); voffB[i] = (unsigned)(Rb * Kb + C * 2); }
;     const size_t kstep = (size_t)(BK * 2);
;     const size_t hstepA = (size_t)HALF * ldab, hstepB = (size_t)HALF * Kb;
;     const unsigned ldsw = (unsigned)wid * 1024u, ldsbase = (unsigned)(size_t)lds;
;     const int aoff = lds_byte(wr * 64 + fr, fq * 8), boff = lds_byte(wc * 32 + fr, fq * 8);
;     ...
;     Unit cur, nxt; int ui = 0;
;     if (!S.next(0, cur)) return;
;     f32x4 acc[2][2][4][2];
; #pragma unroll
;     for (int a = 0; a < 2; ++a)
; #pragma unroll
;         for (int b = 0; b < 2; ++b)
; #pragma unroll
;             for (int m = 0; m < 4; ++m)
; #pragma unroll
;                 for (int n = 0; n < 2; ++n) acc[a][b][m][n] = (f32x4){0.f, 0.f, 0.f, 0.f};
;     bf16x8 At[4][2], B0[2][2], B1[2][2];
;     const char* cA = uniform_ptr(cur.a); const char* cB = uniform_ptr(cur.b);
;     PG8_STAGE(PG8_SB(0, 0), cB, voffB); PG8_STAGE(PG8_SB(0, 1), cB + hstepB, voffB); PG8_STAGE(PG8_SA(0, 0), cA, voffA); PG8_STAGE(PG8_SA(0, 1), cA + hstepA, voffA);
;     if (wr == 1) PG8_BAR;
;     PG8_WAIT_V(2); PG8_BAR;
.LBB0_2286:
	s_mov_b64 s[6:7], 0
	v_mbcnt_lo_u32_b32 v0, -1, 0
	v_mbcnt_hi_u32_b32 v0, -1, v0
	v_readlane_b32 s11, v250, 60
	v_readlane_b32 s10, v253, 35
	v_readlane_b32 s12, v253, 34
	v_add_u32_e32 v0, s11, v0
	s_cmp_eq_u32 s0, 0
	s_cselect_b64 s[2:3], -1, 0
	s_and_b64 s[8:9], s[2:3], exec
	s_cselect_b32 s0, 16, 0x90
	s_mul_hi_u32 s9, s0, s10
	s_mul_i32 s9, s9, s12
	s_cselect_b32 s8, 6, 8
	s_sub_i32 s0, s0, s9
	s_sub_i32 s9, s0, s12
	s_cmp_ge_u32 s0, s12
	s_cselect_b32 s0, s9, s0
	s_sub_i32 s9, s0, s12
	s_cmp_ge_u32 s0, s12
	s_cselect_b32 s0, s9, s0
	v_readlane_b32 s9, v252, 39
	s_sub_i32 s0, s9, s0
	s_ashr_i32 s9, s0, 31
	s_abs_i32 s0, s0
	s_mul_hi_u32 s10, s0, s10
	s_mul_i32 s10, s10, s12
	s_sub_i32 s0, s0, s10
	s_sub_i32 s10, s0, s12
	s_cmp_ge_u32 s0, s12
	s_cselect_b32 s0, s10, s0
	s_sub_i32 s10, s0, s12
	s_cmp_ge_u32 s0, s12
	s_cselect_b32 s0, s10, s0
	s_xor_b32 s0, s0, s9
	v_mbcnt_lo_u32_b32 v0, -1, 0
	v_mbcnt_hi_u32_b32 v0, -1, v0
	s_sub_i32 s34, s0, s9
	s_lshl_b32 s0, s8, 6
	v_add_u32_e32 v0, s11, v0
	s_cmp_ge_i32 s34, s0
	s_nop 0
	v_readfirstlane_b32 s12, v0
	s_cbranch_scc1 .LBB0_2285
	s_add_u32 s9, s80, s6
	s_addc_u32 s10, s81, s7
	s_add_u32 s14, s9, 0x3a892000
	s_addc_u32 s15, s10, 0
	s_and_b64 s[6:7], s[2:3], exec
	s_movk_i32 s6, 0x200
	s_cselect_b32 s13, s6, 0x100
	s_mov_b32 s6, 0xc18c000
	v_bfe_i32 v4, v0, 27, 1
	s_cselect_b32 s6, s6, 0xd18c000
	v_lshlrev_b32_e32 v1, 4, v0
	v_lshrrev_b32_e32 v4, 22, v4
	s_add_u32 s35, s14, s6
	v_add_u32_e32 v4, v1, v4
	s_addc_u32 s36, s15, 0
	v_and_b32_e32 v4, 0xfffffc00, v4
	s_and_b64 s[6:7], s[2:3], exec
	v_sub_u32_e32 v4, v1, v4
	s_cselect_b32 s6, s31, s30
	v_ashrrev_i32_e32 v2, 31, v0
	v_lshrrev_b32_e32 v5, 4, v4
	s_add_u32 s37, s9, s6
	v_lshrrev_b32_e32 v2, 26, v2
	v_bitop3_b32 v4, v5, v4, 32 bitop3:0x6c
	s_addc_u32 s38, s10, 0
	s_lshl_b32 s39, s13, 8
	v_add_u32_e32 v2, v0, v2
	v_ashrrev_i32_e32 v6, 31, v4
	s_and_b64 s[6:7], s[2:3], exec
	v_ashrrev_i32_e32 v2, 6, v2
	v_lshrrev_b32_e32 v6, 26, v6
	s_cselect_b32 s9, 10, 9
	s_lshl_b32 s40, s8, 3
	v_lshlrev_b32_e32 v5, 3, v2
	v_add_u32_e32 v6, v4, v6
	s_or_b32 s41, s40, 1
	s_ashr_i32 s42, s34, 31
	v_and_b32_e32 v5, -16, v5
	v_ashrrev_i32_e32 v7, 6, v6
	v_and_b32_e32 v6, 0xc0, v6
	s_and_b64 s[6:7], s[2:3], exec
	v_add_u32_e32 v5, v7, v5
	v_sub_u32_e32 v4, v4, v6
	v_lshlrev_b32_e32 v2, 5, v2
	v_ashrrev_i16_sdwa v4, v188, sext(v4) dst_sel:DWORD dst_unused:UNUSED_PAD src0_sel:DWORD src1_sel:BYTE_0
	v_lshlrev_b32_e32 v6, 1, v5
	v_lshrrev_b32_e32 v8, 2, v5
	v_and_b32_e32 v7, 3, v7
	s_movk_i32 s6, 0xffe0
	v_and_b32_e32 v2, 32, v2
	v_bfe_i32 v4, v4, 0, 16
	v_and_b32_e32 v6, 24, v6
	v_and_b32_e32 v8, 4, v8
	v_and_or_b32 v7, v5, s6, v7
	v_or3_b32 v6, v7, v8, v6
	v_add_lshl_u32 v4, v2, v4, 1
	v_add_u32_e32 v1, 0x2000, v1
	v_lshl_add_u32 v2, v5, s9, v4
	v_lshl_add_u32 v132, v6, s9, v4
	v_ashrrev_i32_e32 v4, 31, v1
	v_lshrrev_b32_e32 v4, 22, v4
	v_add_u32_e32 v4, v1, v4
	v_ashrrev_i32_e32 v4, 10, v4
	v_mul_i32_i24_e32 v5, 0x400, v4
	v_sub_u32_e32 v1, v1, v5
	v_lshrrev_b32_e32 v5, 4, v1
	v_bitop3_b32 v1, v5, v1, 32 bitop3:0x6c
	v_ashrrev_i32_e32 v6, 31, v1
	v_lshrrev_b32_e32 v6, 26, v6
	v_lshlrev_b32_e32 v5, 3, v4
	v_add_u32_e32 v6, v1, v6
	v_and_b32_e32 v5, -16, v5
	v_ashrrev_i32_e32 v7, 6, v6
	v_add_u32_e32 v5, v7, v5
	v_and_b32_e32 v7, 3, v7
	s_cselect_b32 s43, 18, 17
	v_and_b32_e32 v6, 0xc0, v6
	v_and_or_b32 v7, v5, s6, v7
	s_lshr_b32 s6, s42, 29
	v_sub_u32_e32 v1, v1, v6
	s_add_i32 s6, s34, s6
	s_ashr_i32 s16, s12, 6
	v_lshlrev_b32_e32 v4, 5, v4
	v_ashrrev_i16_sdwa v1, v188, sext(v1) dst_sel:DWORD dst_unused:UNUSED_PAD src0_sel:DWORD src1_sel:BYTE_0
	v_lshlrev_b32_e32 v6, 1, v5
	v_lshrrev_b32_e32 v8, 2, v5
	s_ashr_i32 s7, s6, 3
	s_and_b32 s6, s6, -8
	v_and_b32_e32 v4, 32, v4
	v_bfe_i32 v1, v1, 0, 16
	v_and_b32_e32 v6, 24, v6
	v_and_b32_e32 v8, 4, v8
	s_ashr_i32 s17, s12, 8
	s_lshl_b32 s10, s16, 10
	s_sub_i32 s6, s34, s6
	v_or3_b32 v6, v7, v8, v6
	v_add_lshl_u32 v1, v4, v1, 1
	s_cmp_lt_i32 s6, 0
	v_lshl_add_u32 v133, v5, s9, v1
	v_lshl_add_u32 v134, v6, s9, v1
	s_cselect_b32 s9, s41, s40
	s_abs_i32 s45, s40
	v_cvt_f32_u32_e32 v1, s45
	s_mul_i32 s6, s9, s6
	s_sub_i32 s9, 0, s45
	s_add_i32 s6, s6, s7
	v_rcp_iflag_f32_e32 v1, v1
	s_bfe_i32 s44, s8, 0x1001c
	s_abs_i32 s8, s6
	s_ashr_i32 s7, s6, 31
	v_mul_f32_e32 v1, 0x4f7ffffe, v1
	v_cvt_u32_f32_e32 v1, v1
	s_xor_b32 s7, s7, s44
	v_readfirstlane_b32 s46, v1
	s_mul_i32 s9, s9, s46
	s_mul_hi_u32 s9, s46, s9
	s_add_i32 s46, s46, s9
	s_mul_hi_u32 s9, s8, s46
	s_mul_i32 s11, s9, s45
	s_sub_i32 s8, s8, s11
	s_add_i32 s11, s9, 1
	s_sub_i32 s18, s8, s45
	s_cmp_ge_u32 s8, s45
	s_cselect_b32 s9, s11, s9
	s_cselect_b32 s8, s18, s8
	s_add_i32 s11, s9, 1
	s_cmp_ge_u32 s8, s45
	s_cselect_b32 s8, s11, s9
	s_xor_b32 s8, s8, s7
	s_sub_i32 s7, s8, s7
	s_lshl_b32 s8, s7, 3
	s_sub_i32 s9, 64, s8
	s_min_i32 s9, s9, 8
	s_mul_i32 s7, s7, s40
	s_sub_i32 s11, s6, s7
	s_sext_i32_i8 s7, s9
	v_cvt_f32_i32_e32 v4, s7
	s_sext_i32_i8 s6, s11
	v_cvt_f32_i32_e32 v1, s6
	s_xor_b32 s18, s6, s7
	v_rcp_iflag_f32_e32 v5, v4
	s_ashr_i32 s18, s18, 30
	s_or_b32 s18, s18, 1
	v_mul_f32_e32 v5, v1, v5
	v_trunc_f32_e32 v5, v5
	v_fma_f32 v1, -v5, v4, v1
	v_cvt_i32_f32_e32 v5, v5
	v_cmp_ge_f32_e64 s[6:7], |v1|, |v4|
	s_and_b64 s[6:7], s[6:7], exec
	s_cselect_b32 s6, s18, 0
	v_readfirstlane_b32 s7, v5
	s_add_i32 s6, s7, s6
	s_mul_i32 s7, s6, s9
	s_sub_i32 s7, s11, s7
	s_sext_i32_i8 s7, s7
	s_add_i32 s20, s8, s7
	s_sext_i32_i8 s8, s6
	s_ashr_i32 s9, s8, 31
	s_lshl_b64 s[6:7], s[8:9], s43
	s_add_u32 s22, s37, s6
	s_addc_u32 s23, s38, s7
	s_ashr_i32 s21, s20, 31
	s_lshl_b64 s[6:7], s[20:21], s43
	s_add_u32 s24, s35, s6
	s_addc_u32 s25, s36, s7
	s_add_i32 s21, s10, 0
	s_add_i32 s47, s21, 0x10000
	s_mov_b32 m0, s47
	s_nop 0
	global_load_lds_dwordx4 v132, s[22:23]
	s_add_i32 s48, s21, 0x12000
	s_mov_b32 m0, s48
	s_nop 0
	global_load_lds_dwordx4 v134, s[22:23]
	s_add_u32 s10, s22, s39
	s_addc_u32 s11, s23, 0
	s_add_i32 s49, s21, 0x14000
	s_mov_b32 m0, s49
	s_nop 0
	global_load_lds_dwordx4 v132, s[10:11]
	s_add_i32 s50, s21, 0x16000
	s_mov_b32 m0, s50
	s_nop 0
	global_load_lds_dwordx4 v134, s[10:11]
	s_add_i32 s51, s21, 0x2000
	s_mov_b32 m0, s21
	s_nop 0
	global_load_lds_dwordx4 v2, s[24:25]
	s_nop 0
	s_mov_b32 m0, s51
	s_nop 0
	global_load_lds_dwordx4 v133, s[24:25]
	s_add_u32 s6, s24, s39
	s_addc_u32 s7, s25, 0
	s_add_i32 s52, s21, 0x4000
	s_mov_b32 m0, s52
	s_nop 0
	global_load_lds_dwordx4 v2, s[6:7]
	s_add_i32 s53, s21, 0x6000
	s_mov_b32 m0, s53
	s_nop 0
	global_load_lds_dwordx4 v133, s[6:7]
	s_cmp_eq_u32 s17, 1
	s_cselect_b64 s[6:7], -1, 0
	s_cmp_lg_u32 s17, 1
	s_cbranch_scc1 .LBB0_2289
	s_barrier
; #define PG8_STAGE(bufoff, gbase, voff) do { _Pragma("unroll") for (int _i = 0; _i < 2; ++_i) \
;         glds16((const void*)(gbase), (voff)[_i], ldsbase + (unsigned)(bufoff) + ldsw + (unsigned)_i * 8192u); } while (0)
; #define PG8_WAIT_V(n) asm volatile("s_waitcnt vmcnt(" #n ")" ::: "memory")
; #define PG8_BAR __builtin_amdgcn_s_barrier()
;     __device__ __forceinline__ bool next(int i, Unit& u) const { if (!o.idx(i, u.pm, u.pn)) return false; u.tag = 0; u.a = A + (size_t)u.pm * astep; u.b = Bt + (size_t)u.pn * bstep; return true; }
;     ...
;     const unsigned ldsw = (unsigned)wid * 1024u, ldsbase = (unsigned)(size_t)lds;
;     const int aoff = lds_byte(wr * 64 + fr, fq * 8), boff = lds_byte(wc * 32 + fr, fq * 8);
;     ...
;     Unit cur, nxt; int ui = 0;
;     if (!S.next(0, cur)) return;
;     f32x4 acc[2][2][4][2];
; #pragma unroll
;     for (int a = 0; a < 2; ++a)
; #pragma unroll
;         for (int b = 0; b < 2; ++b)
; #pragma unroll
;             for (int m = 0; m < 4; ++m)
; #pragma unroll
;                 for (int n = 0; n < 2; ++n) acc[a][b][m][n] = (f32x4){0.f, 0.f, 0.f, 0.f};
;     bf16x8 At[4][2], B0[2][2], B1[2][2];
;     const char* cA = uniform_ptr(cur.a); const char* cB = uniform_ptr(cur.b);
;     PG8_STAGE(PG8_SB(0, 0), cB, voffB); PG8_STAGE(PG8_SB(0, 1), cB + hstepB, voffB); PG8_STAGE(PG8_SA(0, 0), cA, voffA); PG8_STAGE(PG8_SA(0, 1), cA + hstepA, voffA);
;     if (wr == 1) PG8_BAR;
;     PG8_WAIT_V(2); PG8_BAR;
;     PG8_STAGE(PG8_SB(1, 0), cB + kstep, voffB); PG8_STAGE(PG8_SA(1, 0), cA + kstep, voffA); PG8_STAGE(PG8_SB(1, 1), cB + hstepB + kstep, voffB);
;     PG8_WAIT_V(6); PG8_BAR;
.LBB0_2289:
	s_and_b64 s[2:3], s[2:3], exec
	s_movk_i32 s2, 0x600
	s_cselect_b32 s54, s2, 0x800
	s_mov_b32 s2, 0xe18c000
	v_lshrrev_b32_e32 v4, 1, v0
	s_cselect_b32 s2, s2, 0x1118c000
	v_and_b32_e32 v4, 24, v4
	s_sext_i32_i16 s66, s8
	s_add_u32 s8, s14, s2
	v_and_b32_e32 v1, 15, v0
	v_lshlrev_b32_e32 v5, 1, v4
	v_lshlrev_b32_e32 v0, 2, v0
	s_addc_u32 s9, s15, 0
	v_lshl_or_b32 v135, s17, 6, v1
	v_lshl_or_b32 v1, v1, 6, v5
	s_lshl_b32 s2, s17, 13
	v_and_b32_e32 v0, 32, v0
	v_bitop3_b32 v5, v1, s2, v0 bitop3:0xde
	s_lshl_b32 s2, s16, 5
	s_lshr_b32 s56, s13, 6
	s_and_b32 s13, s2, 0x60
	s_add_i32 s57, s56, -2
	s_lshl_b32 s2, s13, 7
	v_bitop3_b32 v0, v1, s2, v0 bitop3:0xde
	s_add_u32 s2, s22, 0x80
	s_waitcnt vmcnt(2)
	s_barrier
	s_addc_u32 s3, s23, 0
	s_add_i32 s58, s21, 0x18000
	s_mov_b32 m0, s58
	s_nop 0
	global_load_lds_dwordx4 v132, s[2:3]
	s_add_i32 s59, s21, 0x1a000
	s_mov_b32 m0, s59
	s_nop 0
	global_load_lds_dwordx4 v134, s[2:3]
	s_add_u32 s2, s24, 0x80
	s_addc_u32 s3, s25, 0
	s_add_i32 s60, s21, 0x8000
	s_mov_b32 m0, s60
	s_nop 0
	global_load_lds_dwordx4 v2, s[2:3]
	s_add_i32 s61, s21, 0xa000
	s_mov_b32 m0, s61
	s_nop 0
	global_load_lds_dwordx4 v133, s[2:3]
	s_add_u32 s2, s10, 0x80
	s_addc_u32 s3, s11, 0
	s_add_i32 s62, s21, 0x1c000
	s_mov_b32 m0, s62
	s_nop 0
	global_load_lds_dwordx4 v132, s[2:3]
	s_add_i32 s63, s21, 0x1e000
	s_mov_b32 m0, s63
	s_nop 0
	global_load_lds_dwordx4 v134, s[2:3]
	s_waitcnt vmcnt(6)
	s_add_i32 s64, s21, 0xc000
	s_cmpk_lt_u32 s12, 0x100
	s_mov_b32 s55, 0
	s_cselect_b64 s[10:11], -1, 0
	s_add_i32 s65, s21, 0xe000
	v_or_b32_e32 v136, s13, v4
	v_add_u32_e32 v137, 0, v0
	v_add_u32_e32 v138, 0, v5
	s_mov_b64 s[18:19], s[22:23]
	s_mov_b64 s[16:17], s[24:25]
	s_barrier
	s_branch .LBB0_2292

; #define PG8_STAGE(bufoff, gbase, voff) do { _Pragma("unroll") for (int _i = 0; _i < 2; ++_i) \
;         glds16((const void*)(gbase), (voff)[_i], ldsbase + (unsigned)(bufoff) + ldsw + (unsigned)_i * 8192u); } while (0)
; #define PG8_LDA(dst, b, h) do { _Pragma("unroll") for (int m = 0; m < 4; ++m) _Pragma("unroll") for (int k = 0; k < 2; ++k) dst[m][k] = *(const LAS bf16x8*)(lds + PG8_SA(b, h) + aoff + m * 2048 + k * 1024); } while (0)
; #define PG8_LDB(dst, b, h) do { _Pragma("unroll") for (int n = 0; n < 2; ++n) _Pragma("unroll") for (int k = 0; k < 2; ++k) dst[n][k] = *(const LAS bf16x8*)(lds + PG8_SB(b, h) + boff + n * 2048 + k * 1024); } while (0)
; #define PG8_WAIT_V(n) asm volatile("s_waitcnt vmcnt(" #n ")" ::: "memory")
; #define PG8_WAIT_L(n) asm volatile("s_waitcnt lgkmcnt(" #n ")" ::: "memory")
; #define PG8_BAR __builtin_amdgcn_s_barrier()
; #define PG8_SCHED __builtin_amdgcn_sched_barrier(0)
;     ...
;             const char* a1 = cA + (size_t)(t + 1) * kstep;
;             const char* a2 = last ? nA : cA + (size_t)(t + 2) * kstep; const char* b2 = last ? nB : cB + (size_t)(t + 2) * kstep;
;             const char* a3 = a2 + kstep; const char* b3 = b2 + kstep;
;             PG8_LDB(B0, 0, 0); PG8_LDB(B1, 0, 1); PG8_SCHED; PG8_LDA(At, 0, 0); PG8_STAGE(PG8_SA(1, 1), a1 + hstepA, voffA);
;             PG8_WAIT_V(8); PG8_WAIT_L(0); PG8_BAR; PG8_MMA(0, 0, At, B0); PG8_MMA(0, 1, At, B1); PG8_BAR; PG8_SCHED;
;             PG8_LDA(At, 0, 1); PG8_STAGE(PG8_SB(0, 0), b2, voffB); PG8_STAGE(PG8_SB(0, 1), b2 + hstepB, voffB); PG8_STAGE(PG8_SA(0, 0), a2, voffA);
;             PG8_WAIT_V(8); PG8_WAIT_L(0); PG8_BAR; PG8_MMA(1, 0, At, B0); PG8_MMA(1, 1, At, B1); PG8_BAR; PG8_SCHED;
.LBB0_2295:
	v_add_u32_e32 v0, 0x10000, v137
	ds_read_b128 v[140:143], v0
	ds_read_b128 v[144:147], v0 offset:1024
	ds_read_b128 v[148:151], v0 offset:2048
	ds_read_b128 v[152:155], v0 offset:3072
	v_add_u32_e32 v0, 0x14000, v137
	ds_read_b128 v[156:159], v0
	ds_read_b128 v[160:163], v0 offset:1024
	ds_read_b128 v[164:167], v0 offset:2048
	ds_read_b128 v[168:171], v0 offset:3072
	s_add_i32 s69, s22, 2
	s_cmp_eq_u32 s57, s22
	s_cselect_b32 s26, s16, s67
	s_cselect_b32 s27, s17, s68
	s_cselect_b32 s24, s18, s13
	s_cselect_b32 s25, s19, s15
	s_add_u32 s22, s26, 0x80
	s_addc_u32 s23, s27, 0
	ds_read_b128 v[176:179], v138
	ds_read_b128 v[180:183], v138 offset:1024
	ds_read_b128 v[206:209], v138 offset:2048
	ds_read_b128 v[210:213], v138 offset:3072
	ds_read_b128 v[214:217], v138 offset:4096
	ds_read_b128 v[218:221], v138 offset:5120
	ds_read_b128 v[222:225], v138 offset:6144
	ds_read_b128 v[226:229], v138 offset:7168
	s_add_u32 s28, s67, s39
	s_addc_u32 s29, s68, 0
	s_add_u32 s28, s28, 0xffffff80
	s_addc_u32 s29, s29, -1
	s_mov_b32 m0, s64
	s_nop 0
	global_load_lds_dwordx4 v2, s[28:29]
	s_nop 0
	s_mov_b32 m0, s65
	s_nop 0
	global_load_lds_dwordx4 v133, s[28:29]
	s_waitcnt vmcnt(8)
	s_waitcnt lgkmcnt(0)
	s_barrier
	s_setprio 1
	s_waitcnt lgkmcnt(7)
	v_mfma_f32_16x16x32_bf16 v[128:131], v[140:143], v[176:179], v[128:131]
	v_mfma_f32_16x16x32_bf16 v[124:127], v[148:151], v[176:179], v[124:127]
	s_waitcnt lgkmcnt(5)
	v_mfma_f32_16x16x32_bf16 v[120:123], v[140:143], v[206:209], v[120:123]
	v_mfma_f32_16x16x32_bf16 v[112:115], v[148:151], v[206:209], v[112:115]
	s_waitcnt lgkmcnt(3)
	v_mfma_f32_16x16x32_bf16 v[104:107], v[140:143], v[214:217], v[104:107]
	v_mfma_f32_16x16x32_bf16 v[96:99], v[148:151], v[214:217], v[96:99]
	s_waitcnt lgkmcnt(1)
	v_mfma_f32_16x16x32_bf16 v[88:91], v[140:143], v[222:225], v[88:91]
	v_mfma_f32_16x16x32_bf16 v[80:83], v[148:151], v[222:225], v[80:83]
	v_mfma_f32_16x16x32_bf16 v[128:131], v[144:147], v[180:183], v[128:131]
	v_mfma_f32_16x16x32_bf16 v[124:127], v[152:155], v[180:183], v[124:127]
	v_mfma_f32_16x16x32_bf16 v[120:123], v[144:147], v[210:213], v[120:123]
	v_mfma_f32_16x16x32_bf16 v[112:115], v[152:155], v[210:213], v[112:115]
	v_mfma_f32_16x16x32_bf16 v[104:107], v[144:147], v[218:221], v[104:107]
	v_mfma_f32_16x16x32_bf16 v[96:99], v[152:155], v[218:221], v[96:99]
	s_waitcnt lgkmcnt(0)
	v_mfma_f32_16x16x32_bf16 v[88:91], v[144:147], v[226:229], v[88:91]
	v_mfma_f32_16x16x32_bf16 v[80:83], v[152:155], v[226:229], v[80:83]
	s_setprio 0
	s_setprio 1
	v_mfma_f32_16x16x32_bf16 v[116:119], v[156:159], v[176:179], v[116:119]
	v_mfma_f32_16x16x32_bf16 v[108:111], v[164:167], v[176:179], v[108:111]
	v_mfma_f32_16x16x32_bf16 v[100:103], v[156:159], v[206:209], v[100:103]
	v_mfma_f32_16x16x32_bf16 v[92:95], v[164:167], v[206:209], v[92:95]
	v_mfma_f32_16x16x32_bf16 v[84:87], v[156:159], v[214:217], v[84:87]
	v_mfma_f32_16x16x32_bf16 v[76:79], v[164:167], v[214:217], v[76:79]
	v_mfma_f32_16x16x32_bf16 v[72:75], v[156:159], v[222:225], v[72:75]
	v_mfma_f32_16x16x32_bf16 v[68:71], v[164:167], v[222:225], v[68:71]
	v_mfma_f32_16x16x32_bf16 v[116:119], v[160:163], v[180:183], v[116:119]
	v_mfma_f32_16x16x32_bf16 v[108:111], v[168:171], v[180:183], v[108:111]
	v_mfma_f32_16x16x32_bf16 v[100:103], v[160:163], v[210:213], v[100:103]
	v_mfma_f32_16x16x32_bf16 v[92:95], v[168:171], v[210:213], v[92:95]
	v_mfma_f32_16x16x32_bf16 v[84:87], v[160:163], v[218:221], v[84:87]
	v_mfma_f32_16x16x32_bf16 v[76:79], v[168:171], v[218:221], v[76:79]
	v_mfma_f32_16x16x32_bf16 v[72:75], v[160:163], v[226:229], v[72:75]
	v_mfma_f32_16x16x32_bf16 v[68:71], v[168:171], v[226:229], v[68:71]
	s_setprio 0
	s_barrier
	ds_read_b128 v[176:179], v138 offset:16384
	ds_read_b128 v[180:183], v138 offset:17408
	ds_read_b128 v[206:209], v138 offset:18432
	ds_read_b128 v[210:213], v138 offset:19456
	ds_read_b128 v[214:217], v138 offset:20480
	ds_read_b128 v[218:221], v138 offset:21504
	ds_read_b128 v[222:225], v138 offset:22528
	ds_read_b128 v[226:229], v138 offset:23552
	s_mov_b32 m0, s47
	s_nop 0
	global_load_lds_dwordx4 v132, s[24:25]
	s_nop 0
	s_mov_b32 m0, s48
	s_nop 0
	global_load_lds_dwordx4 v134, s[24:25]
	s_add_u32 s28, s24, s39
	s_addc_u32 s29, s25, 0
	s_mov_b32 m0, s49
	s_nop 0
	global_load_lds_dwordx4 v132, s[28:29]
	s_nop 0
	s_mov_b32 m0, s50
	s_nop 0
	global_load_lds_dwordx4 v134, s[28:29]
	s_nop 0
	s_mov_b32 m0, s21
	s_nop 0
	global_load_lds_dwordx4 v2, s[26:27]
	s_nop 0
	s_mov_b32 m0, s51
	s_nop 0
	global_load_lds_dwordx4 v133, s[26:27]
	s_waitcnt vmcnt(8)
	s_waitcnt lgkmcnt(0)
	s_barrier
; #define PG8_STAGE(bufoff, gbase, voff) do { _Pragma("unroll") for (int _i = 0; _i < 2; ++_i) \
;         glds16((const void*)(gbase), (voff)[_i], ldsbase + (unsigned)(bufoff) + ldsw + (unsigned)_i * 8192u); } while (0)
; #define PG8_LDA(dst, b, h) do { _Pragma("unroll") for (int m = 0; m < 4; ++m) _Pragma("unroll") for (int k = 0; k < 2; ++k) dst[m][k] = *(const LAS bf16x8*)(lds + PG8_SA(b, h) + aoff + m * 2048 + k * 1024); } while (0)
; #define PG8_LDB(dst, b, h) do { _Pragma("unroll") for (int n = 0; n < 2; ++n) _Pragma("unroll") for (int k = 0; k < 2; ++k) dst[n][k] = *(const LAS bf16x8*)(lds + PG8_SB(b, h) + boff + n * 2048 + k * 1024); } while (0)
; #define PG8_WAIT_V(n) asm volatile("s_waitcnt vmcnt(" #n ")" ::: "memory")
; #define PG8_WAIT_L(n) asm volatile("s_waitcnt lgkmcnt(" #n ")" ::: "memory")
; #define PG8_BAR __builtin_amdgcn_s_barrier()
; #define PG8_SCHED __builtin_amdgcn_sched_barrier(0)
;     ...
;             PG8_WAIT_V(8); PG8_WAIT_L(0); PG8_BAR; PG8_MMA(1, 0, At, B0); PG8_MMA(1, 1, At, B1); PG8_BAR; PG8_SCHED;
;             PG8_LDB(B0, 1, 0); PG8_LDB(B1, 1, 1); PG8_SCHED; PG8_LDA(At, 1, 0); PG8_STAGE(PG8_SA(0, 1), a2 + hstepA, voffA);
;             PG8_WAIT_V(8); PG8_WAIT_L(0); PG8_BAR; PG8_MMA(0, 0, At, B0); PG8_MMA(0, 1, At, B1); PG8_BAR; PG8_SCHED;
;             PG8_LDA(At, 1, 1); PG8_STAGE(PG8_SB(1, 0), b3, voffB); PG8_STAGE(PG8_SB(1, 1), b3 + hstepB, voffB); PG8_STAGE(PG8_SA(1, 0), a3, voffA);
;             PG8_WAIT_V(8); PG8_WAIT_L(0); PG8_BAR; PG8_MMA(1, 0, At, B0); PG8_MMA(1, 1, At, B1); PG8_BAR; PG8_SCHED;
	s_setprio 1
	s_waitcnt lgkmcnt(7)
	v_mfma_f32_16x16x32_bf16 v[64:67], v[140:143], v[176:179], v[64:67]
	v_mfma_f32_16x16x32_bf16 v[60:63], v[148:151], v[176:179], v[60:63]
	s_waitcnt lgkmcnt(5)
	v_mfma_f32_16x16x32_bf16 v[56:59], v[140:143], v[206:209], v[56:59]
	v_mfma_f32_16x16x32_bf16 v[48:51], v[148:151], v[206:209], v[48:51]
	s_waitcnt lgkmcnt(3)
	v_mfma_f32_16x16x32_bf16 v[40:43], v[140:143], v[214:217], v[40:43]
	v_mfma_f32_16x16x32_bf16 v[32:35], v[148:151], v[214:217], v[32:35]
	s_waitcnt lgkmcnt(1)
	v_mfma_f32_16x16x32_bf16 v[24:27], v[140:143], v[222:225], v[24:27]
	v_mfma_f32_16x16x32_bf16 v[16:19], v[148:151], v[222:225], v[16:19]
	v_mfma_f32_16x16x32_bf16 v[64:67], v[144:147], v[180:183], v[64:67]
	v_mfma_f32_16x16x32_bf16 v[60:63], v[152:155], v[180:183], v[60:63]
	v_mfma_f32_16x16x32_bf16 v[56:59], v[144:147], v[210:213], v[56:59]
	v_mfma_f32_16x16x32_bf16 v[48:51], v[152:155], v[210:213], v[48:51]
	v_mfma_f32_16x16x32_bf16 v[40:43], v[144:147], v[218:221], v[40:43]
	v_mfma_f32_16x16x32_bf16 v[32:35], v[152:155], v[218:221], v[32:35]
	s_waitcnt lgkmcnt(0)
	v_mfma_f32_16x16x32_bf16 v[24:27], v[144:147], v[226:229], v[24:27]
	v_mfma_f32_16x16x32_bf16 v[16:19], v[152:155], v[226:229], v[16:19]
	s_setprio 0
	s_setprio 1
	v_mfma_f32_16x16x32_bf16 v[52:55], v[156:159], v[176:179], v[52:55]
	v_mfma_f32_16x16x32_bf16 v[44:47], v[164:167], v[176:179], v[44:47]
	v_mfma_f32_16x16x32_bf16 v[36:39], v[156:159], v[206:209], v[36:39]
	v_mfma_f32_16x16x32_bf16 v[28:31], v[164:167], v[206:209], v[28:31]
	v_mfma_f32_16x16x32_bf16 v[20:23], v[156:159], v[214:217], v[20:23]
	v_mfma_f32_16x16x32_bf16 v[12:15], v[164:167], v[214:217], v[12:15]
	v_mfma_f32_16x16x32_bf16 v[8:11], v[156:159], v[222:225], v[8:11]
	v_mfma_f32_16x16x32_bf16 v[4:7], v[164:167], v[222:225], v[4:7]
	v_mfma_f32_16x16x32_bf16 v[52:55], v[160:163], v[180:183], v[52:55]
	v_mfma_f32_16x16x32_bf16 v[44:47], v[168:171], v[180:183], v[44:47]
	v_mfma_f32_16x16x32_bf16 v[36:39], v[160:163], v[210:213], v[36:39]
	v_mfma_f32_16x16x32_bf16 v[28:31], v[168:171], v[210:213], v[28:31]
	v_mfma_f32_16x16x32_bf16 v[20:23], v[160:163], v[218:221], v[20:23]
	v_mfma_f32_16x16x32_bf16 v[12:15], v[168:171], v[218:221], v[12:15]
	v_mfma_f32_16x16x32_bf16 v[8:11], v[160:163], v[226:229], v[8:11]
	v_mfma_f32_16x16x32_bf16 v[4:7], v[168:171], v[226:229], v[4:7]
	s_setprio 0
	s_barrier
	v_add_u32_e32 v0, 0x18000, v137
	ds_read_b128 v[140:143], v0
	ds_read_b128 v[144:147], v0 offset:1024
	ds_read_b128 v[148:151], v0 offset:2048
	ds_read_b128 v[152:155], v0 offset:3072
	v_add_u32_e32 v0, 0x1c000, v137
	ds_read_b128 v[156:159], v0
	ds_read_b128 v[160:163], v0 offset:1024
	ds_read_b128 v[164:167], v0 offset:2048
	ds_read_b128 v[168:171], v0 offset:3072
	ds_read_b128 v[176:179], v138 offset:32768
	ds_read_b128 v[180:183], v138 offset:33792
	ds_read_b128 v[206:209], v138 offset:34816
	ds_read_b128 v[210:213], v138 offset:35840
	ds_read_b128 v[214:217], v138 offset:36864
	ds_read_b128 v[218:221], v138 offset:37888
	ds_read_b128 v[222:225], v138 offset:38912
	ds_read_b128 v[226:229], v138 offset:39936
	s_add_u32 s26, s26, s39
	s_addc_u32 s27, s27, 0
	s_mov_b32 m0, s52
	s_nop 0
	global_load_lds_dwordx4 v2, s[26:27]
	s_nop 0
	s_mov_b32 m0, s53
	s_nop 0
	global_load_lds_dwordx4 v133, s[26:27]
	s_waitcnt vmcnt(8)
	s_waitcnt lgkmcnt(0)
	s_barrier
	s_setprio 1
	s_waitcnt lgkmcnt(7)
	v_mfma_f32_16x16x32_bf16 v[128:131], v[140:143], v[176:179], v[128:131]
	v_mfma_f32_16x16x32_bf16 v[124:127], v[148:151], v[176:179], v[124:127]
	s_waitcnt lgkmcnt(5)
	v_mfma_f32_16x16x32_bf16 v[120:123], v[140:143], v[206:209], v[120:123]
	v_mfma_f32_16x16x32_bf16 v[112:115], v[148:151], v[206:209], v[112:115]
	s_waitcnt lgkmcnt(3)
	v_mfma_f32_16x16x32_bf16 v[104:107], v[140:143], v[214:217], v[104:107]
	v_mfma_f32_16x16x32_bf16 v[96:99], v[148:151], v[214:217], v[96:99]
	s_waitcnt lgkmcnt(1)
	v_mfma_f32_16x16x32_bf16 v[88:91], v[140:143], v[222:225], v[88:91]
	v_mfma_f32_16x16x32_bf16 v[80:83], v[148:151], v[222:225], v[80:83]
	v_mfma_f32_16x16x32_bf16 v[128:131], v[144:147], v[180:183], v[128:131]
	v_mfma_f32_16x16x32_bf16 v[124:127], v[152:155], v[180:183], v[124:127]
	v_mfma_f32_16x16x32_bf16 v[120:123], v[144:147], v[210:213], v[120:123]
	v_mfma_f32_16x16x32_bf16 v[112:115], v[152:155], v[210:213], v[112:115]
	v_mfma_f32_16x16x32_bf16 v[104:107], v[144:147], v[218:221], v[104:107]
	v_mfma_f32_16x16x32_bf16 v[96:99], v[152:155], v[218:221], v[96:99]
	s_waitcnt lgkmcnt(0)
	v_mfma_f32_16x16x32_bf16 v[88:91], v[144:147], v[226:229], v[88:91]
	v_mfma_f32_16x16x32_bf16 v[80:83], v[152:155], v[226:229], v[80:83]
	s_setprio 0
	s_setprio 1
	v_mfma_f32_16x16x32_bf16 v[116:119], v[156:159], v[176:179], v[116:119]
	v_mfma_f32_16x16x32_bf16 v[108:111], v[164:167], v[176:179], v[108:111]
	v_mfma_f32_16x16x32_bf16 v[100:103], v[156:159], v[206:209], v[100:103]
	v_mfma_f32_16x16x32_bf16 v[92:95], v[164:167], v[206:209], v[92:95]
	v_mfma_f32_16x16x32_bf16 v[84:87], v[156:159], v[214:217], v[84:87]
	v_mfma_f32_16x16x32_bf16 v[76:79], v[164:167], v[214:217], v[76:79]
	v_mfma_f32_16x16x32_bf16 v[72:75], v[156:159], v[222:225], v[72:75]
	v_mfma_f32_16x16x32_bf16 v[68:71], v[164:167], v[222:225], v[68:71]
	v_mfma_f32_16x16x32_bf16 v[116:119], v[160:163], v[180:183], v[116:119]
	v_mfma_f32_16x16x32_bf16 v[108:111], v[168:171], v[180:183], v[108:111]
	v_mfma_f32_16x16x32_bf16 v[100:103], v[160:163], v[210:213], v[100:103]
	v_mfma_f32_16x16x32_bf16 v[92:95], v[168:171], v[210:213], v[92:95]
	v_mfma_f32_16x16x32_bf16 v[84:87], v[160:163], v[218:221], v[84:87]
	v_mfma_f32_16x16x32_bf16 v[76:79], v[168:171], v[218:221], v[76:79]
	v_mfma_f32_16x16x32_bf16 v[72:75], v[160:163], v[226:229], v[72:75]
	v_mfma_f32_16x16x32_bf16 v[68:71], v[168:171], v[226:229], v[68:71]
	s_setprio 0
	s_barrier
; #define PG8_STAGE(bufoff, gbase, voff) do { _Pragma("unroll") for (int _i = 0; _i < 2; ++_i) \
;         glds16((const void*)(gbase), (voff)[_i], ldsbase + (unsigned)(bufoff) + ldsw + (unsigned)_i * 8192u); } while (0)
; #define PG8_LDA(dst, b, h) do { _Pragma("unroll") for (int m = 0; m < 4; ++m) _Pragma("unroll") for (int k = 0; k < 2; ++k) dst[m][k] = *(const LAS bf16x8*)(lds + PG8_SA(b, h) + aoff + m * 2048 + k * 1024); } while (0)
; #define PG8_WAIT_V(n) asm volatile("s_waitcnt vmcnt(" #n ")" ::: "memory")
; #define PG8_WAIT_L(n) asm volatile("s_waitcnt lgkmcnt(" #n ")" ::: "memory")
; #define PG8_BAR __builtin_amdgcn_s_barrier()
; #define PG8_SCHED __builtin_amdgcn_sched_barrier(0)
;     ...
;             PG8_LDA(At, 1, 1); PG8_STAGE(PG8_SB(1, 0), b3, voffB); PG8_STAGE(PG8_SB(1, 1), b3 + hstepB, voffB); PG8_STAGE(PG8_SA(1, 0), a3, voffA);
;             PG8_WAIT_V(8); PG8_WAIT_L(0); PG8_BAR; PG8_MMA(1, 0, At, B0); PG8_MMA(1, 1, At, B1); PG8_BAR; PG8_SCHED;
;         }
;         if (wr == 0) PG8_BAR;
	ds_read_b128 v[176:179], v138 offset:49152
	ds_read_b128 v[180:183], v138 offset:50176
	ds_read_b128 v[206:209], v138 offset:51200
	ds_read_b128 v[210:213], v138 offset:52224
	ds_read_b128 v[214:217], v138 offset:53248
	ds_read_b128 v[218:221], v138 offset:54272
	ds_read_b128 v[222:225], v138 offset:55296
	ds_read_b128 v[226:229], v138 offset:56320
	s_add_u32 s24, s24, 0x80
	s_addc_u32 s25, s25, 0
	s_mov_b32 m0, s58
	s_nop 0
	global_load_lds_dwordx4 v132, s[24:25]
	s_nop 0
	s_mov_b32 m0, s59
	s_nop 0
	global_load_lds_dwordx4 v134, s[24:25]
	s_add_u32 s24, s28, 0x80
	s_addc_u32 s25, s29, 0
	s_mov_b32 m0, s62
	s_nop 0
	global_load_lds_dwordx4 v132, s[24:25]
	s_nop 0
	s_mov_b32 m0, s63
	s_nop 0
	global_load_lds_dwordx4 v134, s[24:25]
	s_mov_b32 m0, s60
	s_nop 0
	global_load_lds_dwordx4 v2, s[22:23]
	s_nop 0
	s_mov_b32 m0, s61
	s_nop 0
	global_load_lds_dwordx4 v133, s[22:23]
	s_waitcnt vmcnt(8)
	s_waitcnt lgkmcnt(0)
	s_barrier
	s_setprio 1
	s_waitcnt lgkmcnt(7)
	v_mfma_f32_16x16x32_bf16 v[64:67], v[140:143], v[176:179], v[64:67]
	v_mfma_f32_16x16x32_bf16 v[60:63], v[148:151], v[176:179], v[60:63]
	s_waitcnt lgkmcnt(5)
	v_mfma_f32_16x16x32_bf16 v[56:59], v[140:143], v[206:209], v[56:59]
	v_mfma_f32_16x16x32_bf16 v[48:51], v[148:151], v[206:209], v[48:51]
	s_waitcnt lgkmcnt(3)
	v_mfma_f32_16x16x32_bf16 v[40:43], v[140:143], v[214:217], v[40:43]
	v_mfma_f32_16x16x32_bf16 v[32:35], v[148:151], v[214:217], v[32:35]
	s_waitcnt lgkmcnt(1)
	v_mfma_f32_16x16x32_bf16 v[24:27], v[140:143], v[222:225], v[24:27]
	v_mfma_f32_16x16x32_bf16 v[16:19], v[148:151], v[222:225], v[16:19]
	v_mfma_f32_16x16x32_bf16 v[64:67], v[144:147], v[180:183], v[64:67]
	v_mfma_f32_16x16x32_bf16 v[60:63], v[152:155], v[180:183], v[60:63]
	v_mfma_f32_16x16x32_bf16 v[56:59], v[144:147], v[210:213], v[56:59]
	v_mfma_f32_16x16x32_bf16 v[48:51], v[152:155], v[210:213], v[48:51]
	v_mfma_f32_16x16x32_bf16 v[40:43], v[144:147], v[218:221], v[40:43]
	v_mfma_f32_16x16x32_bf16 v[32:35], v[152:155], v[218:221], v[32:35]
	s_waitcnt lgkmcnt(0)
	v_mfma_f32_16x16x32_bf16 v[24:27], v[144:147], v[226:229], v[24:27]
	v_mfma_f32_16x16x32_bf16 v[16:19], v[152:155], v[226:229], v[16:19]
	s_setprio 0
	s_setprio 1
	v_mfma_f32_16x16x32_bf16 v[52:55], v[156:159], v[176:179], v[52:55]
	v_mfma_f32_16x16x32_bf16 v[44:47], v[164:167], v[176:179], v[44:47]
	v_mfma_f32_16x16x32_bf16 v[36:39], v[156:159], v[206:209], v[36:39]
	v_mfma_f32_16x16x32_bf16 v[28:31], v[164:167], v[206:209], v[28:31]
	v_mfma_f32_16x16x32_bf16 v[20:23], v[156:159], v[214:217], v[20:23]
	v_mfma_f32_16x16x32_bf16 v[12:15], v[164:167], v[214:217], v[12:15]
	v_mfma_f32_16x16x32_bf16 v[8:11], v[156:159], v[222:225], v[8:11]
	v_mfma_f32_16x16x32_bf16 v[4:7], v[164:167], v[222:225], v[4:7]
	v_mfma_f32_16x16x32_bf16 v[52:55], v[160:163], v[180:183], v[52:55]
	v_mfma_f32_16x16x32_bf16 v[44:47], v[168:171], v[180:183], v[44:47]
	v_mfma_f32_16x16x32_bf16 v[36:39], v[160:163], v[210:213], v[36:39]
	v_mfma_f32_16x16x32_bf16 v[28:31], v[168:171], v[210:213], v[28:31]
	v_mfma_f32_16x16x32_bf16 v[20:23], v[160:163], v[218:221], v[20:23]
	v_mfma_f32_16x16x32_bf16 v[12:15], v[168:171], v[218:221], v[12:15]
	v_mfma_f32_16x16x32_bf16 v[8:11], v[160:163], v[226:229], v[8:11]
	v_mfma_f32_16x16x32_bf16 v[4:7], v[168:171], v[226:229], v[4:7]
	s_setprio 0
	s_barrier
	s_add_u32 s13, s13, 0x100
	s_addc_u32 s15, s15, 0
	s_add_u32 s67, s67, 0x100
	s_addc_u32 s68, s68, 0
	s_cmp_ge_u32 s69, s56
	s_mov_b32 s22, s69
	s_cbranch_scc0 .LBB0_2295
	s_and_b64 vcc, exec, s[10:11]
	s_cbranch_vccz .LBB0_2298
	s_barrier

; #define LAS __attribute__((address_space(3)))
; __device__ __forceinline__ float bflo(unsigned x) { return __uint_as_float(x << 16); }
; __device__ __forceinline__ float bfhi(unsigned x) { return __uint_as_float(x & 0xffff0000u); }
; __device__ __forceinline__ unsigned cvtpk(float lo, float hi) { unsigned r; asm volatile("v_cvt_pk_bf16_f32 %0, %1, %2" : "=v"(r) : "v"(lo), "v"(hi)); return r; }
; __device__ __forceinline__ int crow(int r, int hi) { return (r & 3) + 8 * (r >> 2) + 4 * hi; }
; __device__ __forceinline__ void branch_accum(const FaState& st, float val, LAS unsigned* ot, bool first, const AttnLane& L) {
;     if (L.hi == 0) L.wsl[32 + L.r32] = val;
;     asm volatile("s_waitcnt lgkmcnt(0)" ::: "memory");
;     float sc16[16];
; #pragma unroll
;     for (int r = 0; r < 16; ++r) sc16[r] = L.wsl[32 + crow(r, L.hi)];
; #pragma unroll
;     for (int d = 0; d < 4; ++d)
; #pragma unroll
;         for (int i = 0; i < 8; ++i) { float a = st.o[d][2 * i] * sc16[2 * i], b = st.o[d][2 * i + 1] * sc16[2 * i + 1];
;             if (!first) { const unsigned w = ot[(d * 8 + i) * 64]; a += bflo(w); b += bfhi(w); }
;             ot[(d * 8 + i) * 64] = cvtpk(a, b); }
; }
; __device__ __forceinline__ void nsa_item(const Bufs& B, int b, int g, int c, LAS char* lds, const AttnLane& L) {
;     ...
;     const unsigned selm = SEL[tk]; const unsigned uni = UNI[0];
;     {
;         const bf16_t* Kg = B.KSL + (size_t)bg * 2048 * 128; const bf16_t* Vg = B.VSL + (size_t)bg * 2048 * 128;
;         fa_reset(st);
;         const DmaOff off = dma_offsets(L.wid, L.lane, 256);
;         const unsigned ldsb = (unsigned)(size_t)lds;
;         unsigned rem = uni; int j = __builtin_ctz(rem); rem &= rem - 1u;
;         __syncthreads();
;         dma_tile(Kg + (size_t)j * 64 * 128, Vg + (size_t)j * 64 * 128, off, ldsb + AT_K0, ldsb + AT_V0, L.wid);
.LBB0_2394:
	s_or_b64 exec, exec, s[16:17]
	s_waitcnt lgkmcnt(0)
	ds_read_b128 v[68:71], v226 offset:128
	ds_read_b128 v[72:75], v226 offset:160
	ds_read_b128 v[76:79], v226 offset:192
	ds_read_b128 v[80:83], v226 offset:224
	v_readlane_b32 s0, v254, 28
	s_waitcnt lgkmcnt(3)
	v_mul_f32_e32 v0, v20, v68
	v_mul_f32_e32 v1, v21, v69
	v_cvt_pk_bf16_f32 v0, v0, v1
	ds_write_b32 v215, v0
	v_mul_f32_e32 v0, v22, v70
	v_mul_f32_e32 v1, v23, v71
	v_cvt_pk_bf16_f32 v0, v0, v1
	ds_write_b32 v215, v0 offset:256
	s_waitcnt lgkmcnt(4)
	v_mul_f32_e32 v0, v24, v72
	v_mul_f32_e32 v1, v25, v73
	v_cvt_pk_bf16_f32 v0, v0, v1
	ds_write_b32 v215, v0 offset:512
	v_mul_f32_e32 v0, v26, v74
	v_mul_f32_e32 v1, v27, v75
	v_cvt_pk_bf16_f32 v0, v0, v1
	ds_write_b32 v215, v0 offset:768
	s_waitcnt lgkmcnt(5)
	v_mul_f32_e32 v0, v28, v76
	v_mul_f32_e32 v1, v29, v77
	v_cvt_pk_bf16_f32 v0, v0, v1
	ds_write_b32 v215, v0 offset:1024
	v_mul_f32_e32 v0, v30, v78
	v_mul_f32_e32 v1, v31, v79
	v_cvt_pk_bf16_f32 v0, v0, v1
	ds_write_b32 v215, v0 offset:1280
	s_waitcnt lgkmcnt(6)
	v_mul_f32_e32 v0, v32, v80
	v_mul_f32_e32 v1, v33, v81
	v_cvt_pk_bf16_f32 v0, v0, v1
	ds_write_b32 v215, v0 offset:1536
	v_mul_f32_e32 v0, v34, v82
	v_mul_f32_e32 v1, v35, v83
	v_cvt_pk_bf16_f32 v0, v0, v1
	ds_write_b32 v215, v0 offset:1792
	v_mul_f32_e32 v0, v36, v68
	v_mul_f32_e32 v1, v37, v69
	v_cvt_pk_bf16_f32 v0, v0, v1
	ds_write_b32 v215, v0 offset:2048
	v_mul_f32_e32 v0, v38, v70
	v_mul_f32_e32 v1, v39, v71
	v_cvt_pk_bf16_f32 v0, v0, v1
	ds_write_b32 v215, v0 offset:2304
	v_mul_f32_e32 v0, v40, v72
	v_mul_f32_e32 v1, v41, v73
	v_cvt_pk_bf16_f32 v0, v0, v1
	ds_write_b32 v215, v0 offset:2560
	v_mul_f32_e32 v0, v42, v74
	v_mul_f32_e32 v1, v43, v75
	v_cvt_pk_bf16_f32 v0, v0, v1
	ds_write_b32 v215, v0 offset:2816
	v_mul_f32_e32 v0, v44, v76
	v_mul_f32_e32 v1, v45, v77
	v_cvt_pk_bf16_f32 v0, v0, v1
	ds_write_b32 v215, v0 offset:3072
	v_mul_f32_e32 v0, v46, v78
	v_mul_f32_e32 v1, v47, v79
	v_cvt_pk_bf16_f32 v0, v0, v1
	ds_write_b32 v215, v0 offset:3328
	v_mul_f32_e32 v0, v48, v80
	v_mul_f32_e32 v1, v49, v81
	v_cvt_pk_bf16_f32 v0, v0, v1
	ds_write_b32 v215, v0 offset:3584
	v_mul_f32_e32 v0, v50, v82
	v_mul_f32_e32 v1, v51, v83
	v_cvt_pk_bf16_f32 v0, v0, v1
	ds_write_b32 v215, v0 offset:3840
	v_mul_f32_e32 v0, v52, v68
	v_mul_f32_e32 v1, v53, v69
	v_cvt_pk_bf16_f32 v0, v0, v1
	ds_write_b32 v215, v0 offset:4096
	v_mul_f32_e32 v0, v54, v70
	v_mul_f32_e32 v1, v55, v71
	v_cvt_pk_bf16_f32 v0, v0, v1
	ds_write_b32 v215, v0 offset:4352
	v_mul_f32_e32 v0, v56, v72
	v_mul_f32_e32 v1, v57, v73
	v_cvt_pk_bf16_f32 v0, v0, v1
	ds_write_b32 v215, v0 offset:4608
	v_mul_f32_e32 v0, v58, v74
	v_mul_f32_e32 v1, v59, v75
	v_cvt_pk_bf16_f32 v0, v0, v1
	ds_write_b32 v215, v0 offset:4864
	v_mul_f32_e32 v0, v60, v76
	v_mul_f32_e32 v1, v61, v77
	v_cvt_pk_bf16_f32 v0, v0, v1
	ds_write_b32 v215, v0 offset:5120
	v_mul_f32_e32 v0, v62, v78
	v_mul_f32_e32 v1, v63, v79
	v_cvt_pk_bf16_f32 v0, v0, v1
	ds_write_b32 v215, v0 offset:5376
	v_mul_f32_e32 v0, v64, v80
	v_mul_f32_e32 v1, v65, v81
	v_cvt_pk_bf16_f32 v0, v0, v1
	ds_write_b32 v215, v0 offset:5632
	v_mul_f32_e32 v0, v66, v82
	v_mul_f32_e32 v1, v67, v83
	v_cvt_pk_bf16_f32 v0, v0, v1
	ds_write_b32 v215, v0 offset:5888
	v_mul_f32_e32 v0, v4, v68
	v_mul_f32_e32 v1, v5, v69
	v_cvt_pk_bf16_f32 v0, v0, v1
	ds_write_b32 v215, v0 offset:6144
	v_mul_f32_e32 v0, v6, v70
	v_mul_f32_e32 v1, v7, v71
	v_cvt_pk_bf16_f32 v0, v0, v1
	ds_write_b32 v215, v0 offset:6400
	v_mul_f32_e32 v0, v8, v72
	v_mul_f32_e32 v1, v9, v73
	v_cvt_pk_bf16_f32 v0, v0, v1
	ds_write_b32 v215, v0 offset:6656
	v_mul_f32_e32 v0, v10, v74
	v_mul_f32_e32 v1, v11, v75
	v_cvt_pk_bf16_f32 v0, v0, v1
	ds_write_b32 v215, v0 offset:6912
	v_mul_f32_e32 v0, v12, v76
	v_mul_f32_e32 v1, v13, v77
	v_cvt_pk_bf16_f32 v0, v0, v1
	ds_write_b32 v215, v0 offset:7168
	v_mul_f32_e32 v0, v14, v78
	v_mul_f32_e32 v1, v15, v79
	v_cvt_pk_bf16_f32 v0, v0, v1
	ds_write_b32 v215, v0 offset:7424
	v_mul_f32_e32 v0, v16, v80
	v_mul_f32_e32 v1, v17, v81
	v_cvt_pk_bf16_f32 v0, v0, v1
	ds_write_b32 v215, v0 offset:7680
	v_mul_f32_e32 v0, v18, v82
	v_mul_f32_e32 v1, v19, v83
	v_cvt_pk_bf16_f32 v0, v0, v1
	ds_write_b32 v215, v0 offset:7936
	v_mov_b32_e32 v0, s0
	ds_read_b32 v0, v0
	ds_read_b32 v155, v227
	s_waitcnt lgkmcnt(0)
	s_barrier
	v_ffbl_b32_e32 v159, v0
	v_add_u32_e32 v1, -1, v0
	v_lshlrev_b32_e32 v2, 14, v159
	v_and_b32_e32 v161, v1, v0
	v_lshl_add_u64 v[0:1], s[34:35], 0, v[2:3]
	v_lshl_add_u64 v[4:5], s[38:39], 0, v[2:3]
	v_readfirstlane_b32 s17, v1
	v_readfirstlane_b32 s16, v0
	s_mov_b32 m0, s40
	s_nop 0
	global_load_lds_dwordx4 v228, s[16:17]
	v_readlane_b32 s20, v250, 61
	s_mov_b32 m0, s20
	s_nop 0
	global_load_lds_dwordx4 v230, s[16:17]
	v_readfirstlane_b32 s19, v5
	v_readfirstlane_b32 s18, v4
	s_mov_b32 m0, s36
	s_nop 0
	global_load_lds_dwordx4 v229, s[18:19]
	v_mov_b32_e32 v14, v3
	v_mov_b32_e32 v15, v3
	s_mov_b32 m0, s37
	s_nop 0
	global_load_lds_dwordx4 v231, s[18:19]
	v_mov_b32_e32 v0, v3
	v_mov_b32_e32 v1, v3
	v_mov_b32_e32 v2, v3
	v_mov_b32_e32 v4, v3
	v_mov_b32_e32 v5, v3
	v_mov_b32_e32 v6, v3
	v_mov_b32_e32 v7, v3
	v_mov_b32_e32 v8, v3
	v_mov_b32_e32 v9, v3
	v_mov_b32_e32 v10, v3
	v_mov_b32_e32 v11, v3
	v_mov_b32_e32 v12, v3
	v_mov_b32_e32 v13, v3
	v_mov_b64_e32 v[66:67], v[14:15]
	v_mov_b64_e32 v[50:51], v[14:15]
	v_mov_b64_e32 v[34:35], v[14:15]
	v_mov_b64_e32 v[64:65], v[12:13]
	v_mov_b64_e32 v[62:63], v[10:11]
	v_mov_b64_e32 v[60:61], v[8:9]
	v_mov_b64_e32 v[58:59], v[6:7]
	v_mov_b64_e32 v[56:57], v[4:5]
	v_mov_b64_e32 v[54:55], v[2:3]
	v_mov_b64_e32 v[52:53], v[0:1]
	v_mov_b64_e32 v[48:49], v[12:13]
	v_mov_b64_e32 v[46:47], v[10:11]
	v_mov_b64_e32 v[44:45], v[8:9]
	v_mov_b64_e32 v[42:43], v[6:7]
	v_mov_b64_e32 v[40:41], v[4:5]
	v_mov_b64_e32 v[38:39], v[2:3]
	v_mov_b64_e32 v[36:37], v[0:1]
	v_mov_b64_e32 v[32:33], v[12:13]
	v_mov_b64_e32 v[30:31], v[10:11]
	v_mov_b64_e32 v[28:29], v[8:9]
	v_mov_b64_e32 v[26:27], v[6:7]
	v_mov_b64_e32 v[24:25], v[4:5]
	v_mov_b64_e32 v[22:23], v[2:3]
	v_mov_b64_e32 v[20:21], v[0:1]
	v_mov_b64_e32 v[18:19], v[14:15]
	v_mov_b32_e32 v240, 0
	v_mov_b32_e32 v238, 0xf149f2ca
	v_mov_b64_e32 v[16:17], v[12:13]
	v_mov_b64_e32 v[14:15], v[10:11]
	v_mov_b64_e32 v[12:13], v[8:9]
	v_mov_b64_e32 v[10:11], v[6:7]
	v_mov_b64_e32 v[8:9], v[4:5]
	v_mov_b64_e32 v[6:7], v[2:3]
	v_mov_b64_e32 v[4:5], v[0:1]
	s_branch .LBB0_2396

.LBB0_2396:
	v_subrev_co_u32_e64 v241, s[16:17], 1, v161
	s_mov_b64 s[18:19], -1
	v_ffbl_b32_e32 v0, v161
	s_and_b64 vcc, exec, s[16:17]
	s_cbranch_vccnz .LBB0_2398
	v_lshlrev_b32_e32 v2, 14, v0
	v_lshl_add_u64 v[68:69], s[34:35], 0, v[2:3]
	v_lshl_add_u64 v[70:71], s[38:39], 0, v[2:3]
	v_readfirstlane_b32 s19, v69
	v_readfirstlane_b32 s18, v68
	s_mov_b32 m0, s42
	s_nop 0
	global_load_lds_dwordx4 v228, s[18:19]
	v_readfirstlane_b32 s21, v71
	s_mov_b32 m0, s45
	s_nop 0
	global_load_lds_dwordx4 v230, s[18:19]
	v_readfirstlane_b32 s20, v70
	s_mov_b32 m0, s44
	s_nop 0
	global_load_lds_dwordx4 v229, s[20:21]
	s_mov_b64 s[18:19], 0
	s_mov_b32 m0, s41
	s_nop 0
	global_load_lds_dwordx4 v231, s[20:21]
	s_waitcnt vmcnt(4)

; #define LGK(n) asm volatile("s_waitcnt lgkmcnt(" #n ")" ::: "memory")
; #define PV_RD(S, d0) do { constexpr int b_ = VOFF + v_rd_off(d0, 0, 0); \
;         TRRD(S##l0, b_); TRRD(S##h0, b_ + 2048); TRRD(S##l1, b_ + 4096); TRRD(S##h1, b_ + 6144); TRRD(S##l2, b_ + 8192); TRRD(S##h2, b_ + 10240); TRRD(S##l3, b_ + 12288); TRRD(S##h3, b_ + 14336); } while (0)
; template <int VOFF>
; __device__ __forceinline__ void pv_tile(f32x16* o, unsigned vb0, bf16x8 pa0, bf16x8 pa1, bf16x8 pa2, bf16x8 pa3) {
;     ...
;     s16x4 Al0, Al1, Al2, Al3, Ah0, Ah1, Ah2, Ah3, Bl0, Bl1, Bl2, Bl3, Bh0, Bh1, Bh2, Bh3;
;     PV_RD(A, 0); PV_RD(B, 1);
;     LGK(8); PV_MM(A, 0); PV_RD(A, 2);
;     LGK(8); PV_MM(B, 1); PV_RD(B, 3);
;     LGK(8); PV_MM(A, 2);
;     LGK(0); PV_MM(B, 3);
; __device__ __forceinline__ void nsa_item(const Bufs& B, int b, int g, int c, LAS char* lds, const AttnLane& L) {
;     ...
;         for (;;) {
;             SLC_STEP(AT_K0, AT_V0, AT_K1, AT_V1); if (j < 0) break;
;             SLC_STEP(AT_K1, AT_V1, AT_K0, AT_V0); if (j < 0) break;
.LBB0_2408:
	v_add_f32_e32 v2, v2, v84
	v_cndmask_b32_e64 v239, v2, 0, s[18:19]
	v_fmac_f32_e32 v239, v240, v85
	s_xor_b64 s[16:17], s[16:17], -1
	ds_read_b64_tr_b16 v[84:85], v205 offset:0x8000
	ds_read_b64_tr_b16 v[86:87], v205 offset:0x8800
	ds_read_b64_tr_b16 v[88:89], v205 offset:0x9000
	ds_read_b64_tr_b16 v[90:91], v205 offset:0x9800
	ds_read_b64_tr_b16 v[92:93], v205 offset:0xa000
	ds_read_b64_tr_b16 v[94:95], v205 offset:0xa800
	ds_read_b64_tr_b16 v[96:97], v205 offset:0xb000
	ds_read_b64_tr_b16 v[98:99], v205 offset:0xb800
	ds_read_b64_tr_b16 v[172:173], v205 offset:0x8200
	ds_read_b64_tr_b16 v[174:175], v205 offset:0x8a00
	ds_read_b64_tr_b16 v[196:197], v205 offset:0x9200
	ds_read_b64_tr_b16 v[198:199], v205 offset:0x9a00
	ds_read_b64_tr_b16 v[242:243], v205 offset:0xa200
	ds_read_b64_tr_b16 v[244:245], v205 offset:0xaa00
	ds_read_b64_tr_b16 v[246:247], v205 offset:0xb200
	ds_read_b64_tr_b16 v[248:249], v205 offset:0xba00
	s_waitcnt lgkmcnt(8)
	s_nop 0
	v_mfma_f32_32x32x16_bf16 v[52:67], v[80:83], v[84:87], v[52:67]
	v_mfma_f32_32x32x16_bf16 v[52:67], v[76:79], v[88:91], v[52:67]
	v_mfma_f32_32x32x16_bf16 v[52:67], v[72:75], v[92:95], v[52:67]
	v_mfma_f32_32x32x16_bf16 v[52:67], v[68:71], v[96:99], v[52:67]
	ds_read_b64_tr_b16 v[84:85], v205 offset:0x8400
	ds_read_b64_tr_b16 v[86:87], v205 offset:0x8c00
	ds_read_b64_tr_b16 v[88:89], v205 offset:0x9400
	ds_read_b64_tr_b16 v[90:91], v205 offset:0x9c00
	ds_read_b64_tr_b16 v[92:93], v205 offset:0xa400
	ds_read_b64_tr_b16 v[94:95], v205 offset:0xac00
	ds_read_b64_tr_b16 v[96:97], v205 offset:0xb400
	ds_read_b64_tr_b16 v[98:99], v205 offset:0xbc00
	s_waitcnt lgkmcnt(8)
	v_mfma_f32_32x32x16_bf16 v[36:51], v[80:83], v[172:175], v[36:51]
	v_mfma_f32_32x32x16_bf16 v[36:51], v[76:79], v[196:199], v[36:51]
	v_mfma_f32_32x32x16_bf16 v[36:51], v[72:75], v[242:245], v[36:51]
	v_mfma_f32_32x32x16_bf16 v[36:51], v[68:71], v[246:249], v[36:51]
	ds_read_b64_tr_b16 v[172:173], v205 offset:0x8600
	ds_read_b64_tr_b16 v[174:175], v205 offset:0x8e00
	ds_read_b64_tr_b16 v[196:197], v205 offset:0x9600
	ds_read_b64_tr_b16 v[198:199], v205 offset:0x9e00
	ds_read_b64_tr_b16 v[242:243], v205 offset:0xa600
	ds_read_b64_tr_b16 v[244:245], v205 offset:0xae00
	ds_read_b64_tr_b16 v[246:247], v205 offset:0xb600
	ds_read_b64_tr_b16 v[248:249], v205 offset:0xbe00
	s_waitcnt lgkmcnt(8)
	v_mfma_f32_32x32x16_bf16 v[20:35], v[80:83], v[84:87], v[20:35]
	v_mfma_f32_32x32x16_bf16 v[20:35], v[76:79], v[88:91], v[20:35]
	v_mfma_f32_32x32x16_bf16 v[20:35], v[72:75], v[92:95], v[20:35]
	v_mfma_f32_32x32x16_bf16 v[20:35], v[68:71], v[96:99], v[20:35]
	s_waitcnt lgkmcnt(0)
	v_mfma_f32_32x32x16_bf16 v[4:19], v[80:83], v[172:175], v[4:19]
	v_mfma_f32_32x32x16_bf16 v[4:19], v[76:79], v[196:199], v[4:19]
	v_mfma_f32_32x32x16_bf16 v[4:19], v[72:75], v[242:245], v[4:19]
	v_mfma_f32_32x32x16_bf16 v[4:19], v[68:71], v[246:249], v[4:19]
	s_andn2_b64 vcc, exec, s[16:17]
	s_barrier
	s_cbranch_vccnz .LBB0_2395
	v_and_b32_e32 v161, v241, v161
	v_subrev_co_u32_e64 v241, s[18:19], 1, v161
	v_ffbl_b32_e32 v159, v161
	s_mov_b64 s[16:17], -1
	s_and_b64 vcc, exec, s[18:19]
	s_cbranch_vccnz .LBB0_2411
	v_lshlrev_b32_e32 v2, 14, v159
	v_lshl_add_u64 v[68:69], s[34:35], 0, v[2:3]
	v_lshl_add_u64 v[70:71], s[38:39], 0, v[2:3]
	v_readfirstlane_b32 s17, v69
	v_readfirstlane_b32 s16, v68
	s_mov_b32 m0, s40
	s_nop 0
	global_load_lds_dwordx4 v228, s[16:17]
	v_readlane_b32 s22, v250, 61
	s_mov_b32 m0, s22
	s_nop 0
	global_load_lds_dwordx4 v230, s[16:17]
	v_readfirstlane_b32 s21, v71
	v_readfirstlane_b32 s20, v70
	s_mov_b32 m0, s36
	s_nop 0
	global_load_lds_dwordx4 v229, s[20:21]
	s_mov_b64 s[16:17], 0
	s_mov_b32 m0, s37
	s_nop 0
	global_load_lds_dwordx4 v231, s[20:21]
	s_waitcnt vmcnt(4)

; #define LAS __attribute__((address_space(3)))
; __device__ __forceinline__ float bflo(unsigned x) { return __uint_as_float(x << 16); }
; __device__ __forceinline__ float bfhi(unsigned x) { return __uint_as_float(x & 0xffff0000u); }
; __device__ __forceinline__ unsigned cvtpk(float lo, float hi) { unsigned r; asm volatile("v_cvt_pk_bf16_f32 %0, %1, %2" : "=v"(r) : "v"(lo), "v"(hi)); return r; }
; __device__ __forceinline__ int crow(int r, int hi) { return (r & 3) + 8 * (r >> 2) + 4 * hi; }
; __device__ __forceinline__ void branch_accum(const FaState& st, float val, LAS unsigned* ot, bool first, const AttnLane& L) {
;     if (L.hi == 0) L.wsl[32 + L.r32] = val;
;     asm volatile("s_waitcnt lgkmcnt(0)" ::: "memory");
;     float sc16[16];
; #pragma unroll
;     for (int r = 0; r < 16; ++r) sc16[r] = L.wsl[32 + crow(r, L.hi)];
; #pragma unroll
;     for (int d = 0; d < 4; ++d)
; #pragma unroll
;         for (int i = 0; i < 8; ++i) { float a = st.o[d][2 * i] * sc16[2 * i], b = st.o[d][2 * i + 1] * sc16[2 * i + 1];
;             if (!first) { const unsigned w = ot[(d * 8 + i) * 64]; a += bflo(w); b += bfhi(w); }
;             ot[(d * 8 + i) * 64] = cvtpk(a, b); }
; }
; __device__ __forceinline__ void nsa_item(const Bufs& B, int b, int g, int c, LAS char* lds, const AttnLane& L) {
;     ...
;         branch_accum(st, gate[1] * (st.l > 0.f ? 1.0f / st.l : 0.f), ot, false, L);
;     }
;     {
;         const bf16_t* Kg = B.KW + (size_t)bg * 2048 * 128; const bf16_t* Vg = B.VW + (size_t)bg * 2048 * 128;
;         fa_reset(st);
;         const DmaOff off = dma_offsets(L.wid, L.lane, 256);
;         const unsigned ldsb = (unsigned)(size_t)lds;
;         int j = c > 8 ? c - 8 : 0;
;         dma_tile(Kg + (size_t)j * 64 * 128, Vg + (size_t)j * 64 * 128, off, ldsb + AT_K0, ldsb + AT_V0, L.wid);
.LBB0_2424:
	s_or_b64 exec, exec, s[16:17]
	s_waitcnt lgkmcnt(0)
	ds_read_b32 v0, v215
	ds_read_b128 v[80:83], v226 offset:128
	ds_read_b128 v[76:79], v226 offset:160
	ds_read_b128 v[72:75], v226 offset:192
	ds_read_b128 v[68:71], v226 offset:224
	s_waitcnt lgkmcnt(4)
	v_lshlrev_b32_e32 v1, 16, v0
	v_and_b32_e32 v0, 0xffff0000, v0
	s_waitcnt lgkmcnt(3)
	v_fmac_f32_e32 v1, v52, v80
	v_fmac_f32_e32 v0, v53, v81
	v_cvt_pk_bf16_f32 v0, v1, v0
	ds_read_b32 v1, v215 offset:256
	ds_write_b32 v215, v0
	s_add_i32 s24, s43, -8
	s_cmp_gt_i32 s43, 8
	s_cselect_b32 s0, s24, 0
	s_waitcnt lgkmcnt(1)
	v_lshlrev_b32_e32 v0, 16, v1
	v_and_b32_e32 v1, 0xffff0000, v1
	v_fmac_f32_e32 v0, v54, v82
	v_fmac_f32_e32 v1, v55, v83
	v_cvt_pk_bf16_f32 v0, v0, v1
	ds_read_b32 v1, v215 offset:512
	ds_write_b32 v215, v0 offset:256
	s_lshl_b64 s[16:17], s[0:1], 14
	v_readlane_b32 s18, v255, 17
	s_add_u32 s18, s18, s16
	s_waitcnt lgkmcnt(1)
	v_lshlrev_b32_e32 v0, 16, v1
	v_and_b32_e32 v1, 0xffff0000, v1
	v_fmac_f32_e32 v0, v56, v76
	v_fmac_f32_e32 v1, v57, v77
	v_cvt_pk_bf16_f32 v0, v0, v1
	ds_read_b32 v1, v215 offset:768
	ds_write_b32 v215, v0 offset:512
	v_readlane_b32 s19, v255, 32
	s_addc_u32 s19, s19, s17
	v_readlane_b32 s20, v255, 27
	s_waitcnt lgkmcnt(1)
	v_lshlrev_b32_e32 v0, 16, v1
	v_and_b32_e32 v1, 0xffff0000, v1
	v_fmac_f32_e32 v0, v58, v78
	v_fmac_f32_e32 v1, v59, v79
	v_cvt_pk_bf16_f32 v0, v0, v1
	ds_read_b32 v1, v215 offset:1024
	ds_write_b32 v215, v0 offset:768
	s_add_u32 s16, s20, s16
	v_readlane_b32 s20, v255, 29
	s_addc_u32 s17, s20, s17
	s_waitcnt lgkmcnt(1)
	v_lshlrev_b32_e32 v0, 16, v1
	v_and_b32_e32 v1, 0xffff0000, v1
	v_fmac_f32_e32 v0, v60, v72
	v_fmac_f32_e32 v1, v61, v73
	v_cvt_pk_bf16_f32 v0, v0, v1
	ds_read_b32 v1, v215 offset:1280
	ds_write_b32 v215, v0 offset:1024
	v_readlane_b32 s21, v250, 61
	v_mov_b32_e32 v2, v3
	v_mov_b32_e32 v159, 0
	s_waitcnt lgkmcnt(1)
	v_lshlrev_b32_e32 v0, 16, v1
	v_and_b32_e32 v1, 0xffff0000, v1
	v_fmac_f32_e32 v0, v62, v74
	v_fmac_f32_e32 v1, v63, v75
	v_cvt_pk_bf16_f32 v0, v0, v1
	ds_read_b32 v1, v215 offset:1536
	ds_write_b32 v215, v0 offset:1280
	v_mov_b32_e32 v161, 0xf149f2ca
	s_waitcnt lgkmcnt(1)
	v_lshlrev_b32_e32 v0, 16, v1
	v_and_b32_e32 v1, 0xffff0000, v1
	v_fmac_f32_e32 v0, v64, v68
	v_fmac_f32_e32 v1, v65, v69
	v_cvt_pk_bf16_f32 v0, v0, v1
	ds_read_b32 v1, v215 offset:1792
	ds_write_b32 v215, v0 offset:1536
	s_waitcnt lgkmcnt(1)
	v_lshlrev_b32_e32 v0, 16, v1
	v_and_b32_e32 v1, 0xffff0000, v1
	v_fmac_f32_e32 v0, v66, v70
	v_fmac_f32_e32 v1, v67, v71
	v_cvt_pk_bf16_f32 v0, v0, v1
	ds_read_b32 v1, v215 offset:2048
	ds_write_b32 v215, v0 offset:1792
	s_waitcnt lgkmcnt(1)
	v_lshlrev_b32_e32 v0, 16, v1
	v_and_b32_e32 v1, 0xffff0000, v1
	v_fmac_f32_e32 v0, v36, v80
	v_fmac_f32_e32 v1, v37, v81
	v_cvt_pk_bf16_f32 v0, v0, v1
	ds_read_b32 v1, v215 offset:2304
	ds_write_b32 v215, v0 offset:2048
	s_waitcnt lgkmcnt(1)
	v_lshlrev_b32_e32 v0, 16, v1
	v_and_b32_e32 v1, 0xffff0000, v1
	v_fmac_f32_e32 v0, v38, v82
	v_fmac_f32_e32 v1, v39, v83
	v_cvt_pk_bf16_f32 v0, v0, v1
	ds_read_b32 v1, v215 offset:2560
	ds_write_b32 v215, v0 offset:2304
	s_waitcnt lgkmcnt(1)
	v_lshlrev_b32_e32 v0, 16, v1
	v_and_b32_e32 v1, 0xffff0000, v1
	v_fmac_f32_e32 v0, v40, v76
	v_fmac_f32_e32 v1, v41, v77
	v_cvt_pk_bf16_f32 v0, v0, v1
	ds_read_b32 v1, v215 offset:2816
	ds_write_b32 v215, v0 offset:2560
	s_waitcnt lgkmcnt(1)
	v_lshlrev_b32_e32 v0, 16, v1
	v_and_b32_e32 v1, 0xffff0000, v1
	v_fmac_f32_e32 v0, v42, v78
	v_fmac_f32_e32 v1, v43, v79
	v_cvt_pk_bf16_f32 v0, v0, v1
	ds_read_b32 v1, v215 offset:3072
	ds_write_b32 v215, v0 offset:2816
	s_waitcnt lgkmcnt(1)
	v_lshlrev_b32_e32 v0, 16, v1
	v_and_b32_e32 v1, 0xffff0000, v1
	v_fmac_f32_e32 v0, v44, v72
	v_fmac_f32_e32 v1, v45, v73
	v_cvt_pk_bf16_f32 v0, v0, v1
	ds_read_b32 v1, v215 offset:3328
	ds_write_b32 v215, v0 offset:3072
	s_waitcnt lgkmcnt(1)
	v_lshlrev_b32_e32 v0, 16, v1
	v_and_b32_e32 v1, 0xffff0000, v1
	v_fmac_f32_e32 v0, v46, v74
	v_fmac_f32_e32 v1, v47, v75
	v_cvt_pk_bf16_f32 v0, v0, v1
	ds_read_b32 v1, v215 offset:3584
	ds_write_b32 v215, v0 offset:3328
	s_waitcnt lgkmcnt(1)
	v_lshlrev_b32_e32 v0, 16, v1
	v_and_b32_e32 v1, 0xffff0000, v1
	v_fmac_f32_e32 v0, v48, v68
	v_fmac_f32_e32 v1, v49, v69
	v_cvt_pk_bf16_f32 v0, v0, v1
	ds_read_b32 v1, v215 offset:3840
	ds_write_b32 v215, v0 offset:3584
	s_waitcnt lgkmcnt(1)
	v_lshlrev_b32_e32 v0, 16, v1
	v_and_b32_e32 v1, 0xffff0000, v1
	v_fmac_f32_e32 v0, v50, v70
	v_fmac_f32_e32 v1, v51, v71
	v_cvt_pk_bf16_f32 v0, v0, v1
	ds_read_b32 v1, v215 offset:4096
	ds_write_b32 v215, v0 offset:3840
	s_waitcnt lgkmcnt(1)
	v_lshlrev_b32_e32 v0, 16, v1
	v_and_b32_e32 v1, 0xffff0000, v1
	v_fmac_f32_e32 v0, v20, v80
	v_fmac_f32_e32 v1, v21, v81
	v_cvt_pk_bf16_f32 v0, v0, v1
	ds_read_b32 v1, v215 offset:4352
	ds_write_b32 v215, v0 offset:4096
	s_waitcnt lgkmcnt(1)
	v_lshlrev_b32_e32 v0, 16, v1
	v_and_b32_e32 v1, 0xffff0000, v1
	v_fmac_f32_e32 v0, v22, v82
	v_fmac_f32_e32 v1, v23, v83
	v_cvt_pk_bf16_f32 v0, v0, v1
	ds_read_b32 v1, v215 offset:4608
	ds_write_b32 v215, v0 offset:4352
	s_waitcnt lgkmcnt(1)
	v_lshlrev_b32_e32 v0, 16, v1
	v_and_b32_e32 v1, 0xffff0000, v1
	v_fmac_f32_e32 v0, v24, v76
	v_fmac_f32_e32 v1, v25, v77
	v_cvt_pk_bf16_f32 v0, v0, v1
	ds_read_b32 v1, v215 offset:4864
	ds_write_b32 v215, v0 offset:4608
	s_waitcnt lgkmcnt(1)
; #define LAS __attribute__((address_space(3)))
; __device__ __forceinline__ float bflo(unsigned x) { return __uint_as_float(x << 16); }
; __device__ __forceinline__ float bfhi(unsigned x) { return __uint_as_float(x & 0xffff0000u); }
; __device__ __forceinline__ unsigned cvtpk(float lo, float hi) { unsigned r; asm volatile("v_cvt_pk_bf16_f32 %0, %1, %2" : "=v"(r) : "v"(lo), "v"(hi)); return r; }
; __device__ __forceinline__ int crow(int r, int hi) { return (r & 3) + 8 * (r >> 2) + 4 * hi; }
; __device__ __forceinline__ void branch_accum(const FaState& st, float val, LAS unsigned* ot, bool first, const AttnLane& L) {
;     if (L.hi == 0) L.wsl[32 + L.r32] = val;
;     asm volatile("s_waitcnt lgkmcnt(0)" ::: "memory");
;     float sc16[16];
; #pragma unroll
;     for (int r = 0; r < 16; ++r) sc16[r] = L.wsl[32 + crow(r, L.hi)];
; #pragma unroll
;     for (int d = 0; d < 4; ++d)
; #pragma unroll
;         for (int i = 0; i < 8; ++i) { float a = st.o[d][2 * i] * sc16[2 * i], b = st.o[d][2 * i + 1] * sc16[2 * i + 1];
;             if (!first) { const unsigned w = ot[(d * 8 + i) * 64]; a += bflo(w); b += bfhi(w); }
;             ot[(d * 8 + i) * 64] = cvtpk(a, b); }
; }
; __device__ __forceinline__ void nsa_item(const Bufs& B, int b, int g, int c, LAS char* lds, const AttnLane& L) {
;     ...
;     {
;         const bf16_t* Kg = B.KW + (size_t)bg * 2048 * 128; const bf16_t* Vg = B.VW + (size_t)bg * 2048 * 128;
;         fa_reset(st);
;         const DmaOff off = dma_offsets(L.wid, L.lane, 256);
;         const unsigned ldsb = (unsigned)(size_t)lds;
;         int j = c > 8 ? c - 8 : 0;
;         dma_tile(Kg + (size_t)j * 64 * 128, Vg + (size_t)j * 64 * 128, off, ldsb + AT_K0, ldsb + AT_V0, L.wid);
	v_lshlrev_b32_e32 v0, 16, v1
	v_and_b32_e32 v1, 0xffff0000, v1
	v_fmac_f32_e32 v0, v26, v78
	v_fmac_f32_e32 v1, v27, v79
	v_cvt_pk_bf16_f32 v0, v0, v1
	ds_read_b32 v1, v215 offset:5120
	ds_write_b32 v215, v0 offset:4864
	s_waitcnt lgkmcnt(1)
	v_lshlrev_b32_e32 v0, 16, v1
	v_and_b32_e32 v1, 0xffff0000, v1
	v_fmac_f32_e32 v0, v28, v72
	v_fmac_f32_e32 v1, v29, v73
	v_cvt_pk_bf16_f32 v0, v0, v1
	ds_read_b32 v1, v215 offset:5376
	ds_write_b32 v215, v0 offset:5120
	s_waitcnt lgkmcnt(1)
	v_lshlrev_b32_e32 v0, 16, v1
	v_and_b32_e32 v1, 0xffff0000, v1
	v_fmac_f32_e32 v0, v30, v74
	v_fmac_f32_e32 v1, v31, v75
	v_cvt_pk_bf16_f32 v0, v0, v1
	ds_read_b32 v1, v215 offset:5632
	ds_write_b32 v215, v0 offset:5376
	s_waitcnt lgkmcnt(1)
	v_lshlrev_b32_e32 v0, 16, v1
	v_and_b32_e32 v1, 0xffff0000, v1
	v_fmac_f32_e32 v0, v32, v68
	v_fmac_f32_e32 v1, v33, v69
	v_cvt_pk_bf16_f32 v0, v0, v1
	ds_read_b32 v1, v215 offset:5888
	ds_write_b32 v215, v0 offset:5632
	s_waitcnt lgkmcnt(1)
	v_lshlrev_b32_e32 v0, 16, v1
	v_and_b32_e32 v1, 0xffff0000, v1
	v_fmac_f32_e32 v0, v34, v70
	v_fmac_f32_e32 v1, v35, v71
	v_cvt_pk_bf16_f32 v0, v0, v1
	ds_read_b32 v1, v215 offset:6144
	ds_write_b32 v215, v0 offset:5888
	s_waitcnt lgkmcnt(1)
	v_lshlrev_b32_e32 v0, 16, v1
	v_and_b32_e32 v1, 0xffff0000, v1
	v_fmac_f32_e32 v0, v4, v80
	v_fmac_f32_e32 v1, v5, v81
	v_cvt_pk_bf16_f32 v0, v0, v1
	ds_read_b32 v1, v215 offset:6400
	ds_write_b32 v215, v0 offset:6144
	v_mov_b32_e32 v4, v3
	v_mov_b32_e32 v5, v3
	s_waitcnt lgkmcnt(1)
	v_lshlrev_b32_e32 v0, 16, v1
	v_and_b32_e32 v1, 0xffff0000, v1
	v_fmac_f32_e32 v0, v6, v82
	v_fmac_f32_e32 v1, v7, v83
	v_cvt_pk_bf16_f32 v0, v0, v1
	ds_read_b32 v1, v215 offset:6656
	ds_write_b32 v215, v0 offset:6400
	v_mov_b32_e32 v6, v3
	v_mov_b32_e32 v7, v3
	s_waitcnt lgkmcnt(1)
	v_lshlrev_b32_e32 v0, 16, v1
	v_and_b32_e32 v1, 0xffff0000, v1
	v_fmac_f32_e32 v0, v8, v76
	v_fmac_f32_e32 v1, v9, v77
	v_cvt_pk_bf16_f32 v0, v0, v1
	ds_read_b32 v1, v215 offset:6912
	ds_write_b32 v215, v0 offset:6656
	v_mov_b32_e32 v8, v3
	v_mov_b32_e32 v9, v3
	s_waitcnt lgkmcnt(1)
	v_lshlrev_b32_e32 v0, 16, v1
	v_and_b32_e32 v1, 0xffff0000, v1
	v_fmac_f32_e32 v0, v10, v78
	v_fmac_f32_e32 v1, v11, v79
	v_cvt_pk_bf16_f32 v0, v0, v1
	ds_read_b32 v1, v215 offset:7168
	ds_write_b32 v215, v0 offset:6912
	v_mov_b32_e32 v10, v3
	v_mov_b32_e32 v11, v3
	s_waitcnt lgkmcnt(1)
	v_lshlrev_b32_e32 v0, 16, v1
	v_and_b32_e32 v1, 0xffff0000, v1
	v_fmac_f32_e32 v0, v12, v72
	v_fmac_f32_e32 v1, v13, v73
	v_cvt_pk_bf16_f32 v0, v0, v1
	ds_read_b32 v1, v215 offset:7424
	ds_write_b32 v215, v0 offset:7168
	v_mov_b32_e32 v12, v3
	v_mov_b32_e32 v13, v3
	s_waitcnt lgkmcnt(1)
	v_lshlrev_b32_e32 v0, 16, v1
	v_and_b32_e32 v1, 0xffff0000, v1
	v_fmac_f32_e32 v0, v14, v74
	v_fmac_f32_e32 v1, v15, v75
	v_cvt_pk_bf16_f32 v0, v0, v1
	ds_read_b32 v1, v215 offset:7680
	ds_write_b32 v215, v0 offset:7424
	v_mov_b32_e32 v14, v3
	v_mov_b32_e32 v15, v3
	s_waitcnt lgkmcnt(1)
	v_lshlrev_b32_e32 v0, 16, v1
	v_and_b32_e32 v1, 0xffff0000, v1
	v_fmac_f32_e32 v0, v16, v68
	v_fmac_f32_e32 v1, v17, v69
	v_cvt_pk_bf16_f32 v0, v0, v1
	ds_read_b32 v1, v215 offset:7936
	ds_write_b32 v215, v0 offset:7680
	s_waitcnt lgkmcnt(1)
	v_lshlrev_b32_e32 v0, 16, v1
	v_fmac_f32_e32 v0, v18, v70
	v_and_b32_e32 v1, 0xffff0000, v1
	v_fmac_f32_e32 v1, v19, v71
	v_cvt_pk_bf16_f32 v0, v0, v1
	ds_write_b32 v215, v0 offset:7936
	s_mov_b32 m0, s40
	s_nop 0
	global_load_lds_dwordx4 v228, s[18:19]
	v_mov_b32_e32 v1, v3
	s_mov_b32 m0, s21
	s_nop 0
	global_load_lds_dwordx4 v230, s[18:19]
	s_mov_b32 m0, s36
	s_nop 0
	global_load_lds_dwordx4 v229, s[16:17]
	s_max_i32 s20, s43, 8
	s_mov_b32 m0, s37
	s_nop 0
	global_load_lds_dwordx4 v231, s[16:17]
	s_mov_b32 s21, s1
	s_lshl_b64 s[18:19], s[20:21], 14
	v_readlane_b32 s16, v255, 28
	s_add_u32 s16, s16, s18
	v_readlane_b32 s17, v255, 30
	s_addc_u32 s17, s17, s19
	v_readlane_b32 s21, v255, 31
	s_add_u32 s18, s21, s18
	v_readlane_b32 s21, v255, 33
	s_addc_u32 s19, s21, s19
	v_readlane_b32 s21, v255, 34
	s_lshl_b32 s20, s20, 6
	s_nop 0
	v_add_u32_e32 v0, s21, v233
	v_subrev_u32_e32 v155, s20, v0
	v_mov_b32_e32 v0, v3
	v_mov_b64_e32 v[66:67], v[14:15]
	v_mov_b64_e32 v[50:51], v[14:15]
	v_mov_b64_e32 v[34:35], v[14:15]
	v_mov_b64_e32 v[64:65], v[12:13]
	v_mov_b64_e32 v[62:63], v[10:11]
	v_mov_b64_e32 v[60:61], v[8:9]
	v_mov_b64_e32 v[58:59], v[6:7]
	v_mov_b64_e32 v[56:57], v[4:5]
	v_mov_b64_e32 v[54:55], v[2:3]
	v_mov_b64_e32 v[52:53], v[0:1]
	v_mov_b64_e32 v[48:49], v[12:13]
	v_mov_b64_e32 v[46:47], v[10:11]
	v_mov_b64_e32 v[44:45], v[8:9]
	v_mov_b64_e32 v[42:43], v[6:7]
	v_mov_b64_e32 v[40:41], v[4:5]
	v_mov_b64_e32 v[38:39], v[2:3]
	v_mov_b64_e32 v[36:37], v[0:1]
	v_mov_b64_e32 v[32:33], v[12:13]
	v_mov_b64_e32 v[30:31], v[10:11]
	v_mov_b64_e32 v[28:29], v[8:9]
	v_mov_b64_e32 v[26:27], v[6:7]
	v_mov_b64_e32 v[24:25], v[4:5]
	v_mov_b64_e32 v[22:23], v[2:3]
	v_mov_b64_e32 v[20:21], v[0:1]
	v_mov_b64_e32 v[18:19], v[14:15]
	v_mov_b64_e32 v[16:17], v[12:13]
	v_mov_b64_e32 v[14:15], v[10:11]
	v_mov_b64_e32 v[12:13], v[8:9]
	v_mov_b64_e32 v[10:11], v[6:7]
	v_mov_b64_e32 v[8:9], v[4:5]
	v_mov_b64_e32 v[6:7], v[2:3]
	v_mov_b64_e32 v[4:5], v[0:1]
	s_branch .LBB0_2426

.LBB0_2428:
	s_andn2_b64 vcc, exec, s[22:23]
	s_cbranch_vccnz .LBB0_2430
	s_mov_b32 m0, s42
	s_nop 0
	global_load_lds_dwordx4 v228, s[18:19]
	s_nop 0
	s_mov_b32 m0, s45
	s_nop 0
	global_load_lds_dwordx4 v230, s[18:19]
	s_nop 0
	s_mov_b32 m0, s44
	s_nop 0
	global_load_lds_dwordx4 v229, s[16:17]
	s_nop 0
	s_mov_b32 m0, s41
	s_nop 0
	global_load_lds_dwordx4 v231, s[16:17]
	s_waitcnt vmcnt(4)

.LBB0_2439:
	s_andn2_b64 vcc, exec, s[20:21]
	s_cbranch_vccnz .LBB0_2441
	s_add_u32 s20, s18, 0x4000
	s_addc_u32 s21, s19, 0
	s_mov_b32 m0, s40
	s_nop 0
	global_load_lds_dwordx4 v228, s[20:21]
	s_add_u32 s22, s16, 0x4000
	v_readlane_b32 s26, v250, 61
	s_mov_b32 m0, s26
	s_nop 0
	global_load_lds_dwordx4 v230, s[20:21]
	s_addc_u32 s23, s17, 0
	s_mov_b32 m0, s36
	s_nop 0
	global_load_lds_dwordx4 v229, s[22:23]
	s_nop 0
	s_mov_b32 m0, s37
	s_nop 0
	global_load_lds_dwordx4 v231, s[22:23]
	s_waitcnt vmcnt(4)

; __device__ __forceinline__ float bflo(unsigned x) { return __uint_as_float(x << 16); }
; __device__ __forceinline__ float bfhi(unsigned x) { return __uint_as_float(x & 0xffff0000u); }
; __device__ __forceinline__ unsigned cvtpk(float lo, float hi) { unsigned r; asm volatile("v_cvt_pk_bf16_f32 %0, %1, %2" : "=v"(r) : "v"(lo), "v"(hi)); return r; }
; __device__ __forceinline__ void mla_item(const Bufs& B, int b, int h, int qb, LAS char* lds, const AttnLane& L) {
;     const int s = qb * 256 + L.wid * 32 + L.r32, t = b * 2048 + s;
;     bf16x8 qr[12];
;     const bf16_t* qp = B.QM + (size_t)t * 1536 + h * 192;
; #pragma unroll
;     for (int d0 = 0; d0 < 8; ++d0) qr[d0] = *(const bf16x8*)(qp + d0 * 16 + L.hi * 8);
; #pragma unroll
;     for (int d0 = 0; d0 < 4; ++d0) {
;         const int i0 = d0 * 16 + L.hi * 8; const bool lo = i0 < 32; const int ib = i0 & 31;
;         const u32x4 xa = *(const u32x4*)(qp + 128 + i0), xb = *(const u32x4*)(qp + 128 + (lo ? i0 + 32 : i0 - 32));
;         const f32x4 c0 = *(const f32x4*)(B.cosM + s * 32 + ib), c1 = *(const f32x4*)(B.cosM + s * 32 + ib + 4), s0 = *(const f32x4*)(B.sinM + s * 32 + ib), s1 = *(const f32x4*)(B.sinM + s * 32 + ib + 4);
;         const float xs[8] = {bflo(xa.x), bfhi(xa.x), bflo(xa.y), bfhi(xa.y), bflo(xa.z), bfhi(xa.z), bflo(xa.w), bfhi(xa.w)};
;         const float xp[8] = {bflo(xb.x), bfhi(xb.x), bflo(xb.y), bfhi(xb.y), bflo(xb.z), bfhi(xb.z), bflo(xb.w), bfhi(xb.w)};
;         const float cs[8] = {c0[0], c0[1], c0[2], c0[3], c1[0], c1[1], c1[2], c1[3]}, sn[8] = {s0[0], s0[1], s0[2], s0[3], s1[0], s1[1], s1[2], s1[3]};
;         float o[8];
; #pragma unroll
;         for (int e = 0; e < 8; ++e) o[e] = lo ? (xs[e] * cs[e] - xp[e] * sn[e]) : (xp[e] * sn[e] + xs[e] * cs[e]);
;         u32x4 w = {cvtpk(o[0], o[1]), cvtpk(o[2], o[3]), cvtpk(o[4], o[5]), cvtpk(o[6], o[7])}; qr[8 + d0] = *reinterpret_cast<bf16x8*>(&w);
;     }
.LBB0_2473:
	s_xor_b64 s[78:79], s[4:5], -1
	s_and_b64 s[4:5], s[4:5], exec
	v_readlane_b32 s0, v250, 61
	v_readlane_b32 s4, v255, 34
	s_cselect_b32 s5, s4, s0
	s_lshl_b32 s4, s5, 8
	v_readlane_b32 s0, v255, 22
	s_add_i32 s0, s4, s0
	s_movk_i32 s6, 0xc00
	v_or_b32_e32 v4, s0, v170
	v_add_u32_e32 v5, s68, v4
	v_mad_i64_i32 v[6:7], s[6:7], v5, s6, v[168:169]
	global_load_dwordx4 v[10:13], v[6:7], off offset:320
	global_load_dwordx4 v[14:17], v[6:7], off offset:256
	v_lshlrev_b32_e32 v4, 5, v4
	v_ashrrev_i32_e32 v5, 31, v4
	v_readlane_b32 s6, v255, 18
	v_lshlrev_b64 v[4:5], 2, v[4:5]
	v_readlane_b32 s7, v255, 19
	v_mov_b32_e32 v165, v3
	v_mov_b32_e32 v167, v3
	v_lshl_add_u64 v[8:9], s[6:7], 0, v[4:5]
	v_readlane_b32 s6, v255, 20
	v_readlane_b32 s7, v255, 21
	v_lshl_add_u64 v[34:35], v[8:9], 0, v[164:165]
	v_lshl_add_u64 v[8:9], v[8:9], 0, v[166:167]
	v_lshl_add_u64 v[4:5], s[6:7], 0, v[4:5]
	v_lshl_add_u64 v[36:37], v[4:5], 0, v[164:165]
	global_load_dwordx4 v[18:21], v[34:35], off
	global_load_dwordx4 v[22:25], v[36:37], off
	global_load_dwordx4 v[26:29], v[34:35], off offset:16
	global_load_dwordx4 v[30:33], v[36:37], off offset:16
	global_load_dwordx4 v[100:103], v[6:7], off
	global_load_dwordx4 v[104:107], v[6:7], off offset:32
	global_load_dwordx4 v[108:111], v[6:7], off offset:64
	global_load_dwordx4 v[112:115], v[6:7], off offset:96
	global_load_dwordx4 v[116:119], v[6:7], off offset:128
	global_load_dwordx4 v[120:123], v[6:7], off offset:160
	global_load_dwordx4 v[124:127], v[6:7], off offset:192
	global_load_dwordx4 v[128:131], v[6:7], off offset:224
	v_lshl_add_u64 v[4:5], v[4:5], 0, v[166:167]
	v_add_u32_e32 v165, s4, v149
	s_lshl_b32 s91, s5, 2
	s_mov_b32 s69, 2
	v_mov_b32_e32 v163, 0xf149f2ca
	v_mov_b32_e32 v167, 0
	s_mov_b64 s[80:81], 0
	s_mov_b32 s34, 63
	s_add_i32 s91, s91, 4
	s_or_b32 s35, s0, 31
	s_mov_b64 s[82:83], s[76:77]
	s_waitcnt vmcnt(13)
	v_lshlrev_b32_e32 v39, 16, v10
	s_waitcnt vmcnt(12)
	v_lshlrev_b32_e32 v38, 16, v14
	v_and_b32_e32 v41, 0xffff0000, v10
	v_and_b32_e32 v40, 0xffff0000, v14
	v_lshlrev_b32_e32 v43, 16, v11
	v_lshlrev_b32_e32 v42, 16, v15
	v_and_b32_e32 v11, 0xffff0000, v11
	v_and_b32_e32 v10, 0xffff0000, v15
	v_lshlrev_b32_e32 v15, 16, v12
	v_lshlrev_b32_e32 v14, 16, v16
	v_and_b32_e32 v45, 0xffff0000, v12
	v_and_b32_e32 v44, 0xffff0000, v16
	v_lshlrev_b32_e32 v47, 16, v13
	v_lshlrev_b32_e32 v46, 16, v17
	v_and_b32_e32 v13, 0xffff0000, v13
	v_and_b32_e32 v12, 0xffff0000, v17
	s_waitcnt vmcnt(11)
	v_mov_b32_e32 v16, v18
	s_waitcnt vmcnt(10)
	v_mov_b32_e32 v17, v22
	v_mov_b32_e32 v22, v19
	v_mov_b32_e32 v18, v20
	v_mov_b32_e32 v19, v24
	v_mov_b32_e32 v24, v21
	s_waitcnt vmcnt(9)
	v_mov_b32_e32 v20, v26
	s_waitcnt vmcnt(8)
	v_mov_b32_e32 v21, v30
	v_mov_b32_e32 v30, v27
	v_mov_b32_e32 v26, v28
	v_mov_b32_e32 v27, v32
	v_mov_b32_e32 v32, v29
	v_pk_mul_f32 v[16:17], v[16:17], v[38:39]
	v_pk_mul_f32 v[22:23], v[22:23], v[40:41]
	v_pk_mul_f32 v[18:19], v[18:19], v[42:43]
	v_pk_mul_f32 v[10:11], v[24:25], v[10:11]
	v_pk_mul_f32 v[14:15], v[20:21], v[14:15]
	v_pk_mul_f32 v[20:21], v[30:31], v[44:45]
	v_pk_mul_f32 v[24:25], v[26:27], v[46:47]
	v_pk_mul_f32 v[12:13], v[32:33], v[12:13]
	v_sub_f32_e32 v16, v16, v17
	v_sub_f32_e32 v17, v22, v23
	v_sub_f32_e32 v18, v18, v19
	v_sub_f32_e32 v10, v10, v11
	v_sub_f32_e32 v11, v14, v15
	v_sub_f32_e32 v14, v20, v21
	v_sub_f32_e32 v15, v24, v25
	v_sub_f32_e32 v12, v12, v13
	v_cvt_pk_bf16_f32 v132, v16, v17
	v_cvt_pk_bf16_f32 v133, v18, v10
	v_cvt_pk_bf16_f32 v134, v11, v14
	v_cvt_pk_bf16_f32 v135, v15, v12
	global_load_dwordx4 v[10:13], v[6:7], off offset:352
	global_load_dwordx4 v[14:17], v[6:7], off offset:288
	global_load_dwordx4 v[18:21], v[34:35], off offset:64
	global_load_dwordx4 v[22:25], v[36:37], off offset:64
	global_load_dwordx4 v[26:29], v[34:35], off offset:80
	global_load_dwordx4 v[30:33], v[36:37], off offset:80
	s_waitcnt vmcnt(5)
	v_lshlrev_b32_e32 v39, 16, v10
	s_waitcnt vmcnt(4)
	v_lshlrev_b32_e32 v38, 16, v14
	s_waitcnt vmcnt(3)
	v_mov_b32_e32 v40, v18
	s_waitcnt vmcnt(2)
	v_mov_b32_e32 v41, v22
	v_and_b32_e32 v43, 0xffff0000, v10
	v_and_b32_e32 v42, 0xffff0000, v14
	v_mov_b32_e32 v22, v19
	v_lshlrev_b32_e32 v19, 16, v11
	v_lshlrev_b32_e32 v18, 16, v15
	v_mov_b32_e32 v44, v20
	v_mov_b32_e32 v45, v24
	v_and_b32_e32 v11, 0xffff0000, v11
	v_and_b32_e32 v10, 0xffff0000, v15
	v_mov_b32_e32 v24, v21
	v_lshlrev_b32_e32 v15, 16, v12
	v_lshlrev_b32_e32 v14, 16, v16
	s_waitcnt vmcnt(1)
	v_mov_b32_e32 v20, v26
	s_waitcnt vmcnt(0)
	v_mov_b32_e32 v21, v30
	v_and_b32_e32 v47, 0xffff0000, v12
	v_and_b32_e32 v46, 0xffff0000, v16
	v_mov_b32_e32 v30, v27
	v_lshlrev_b32_e32 v27, 16, v13
	v_lshlrev_b32_e32 v26, 16, v17
	v_mov_b32_e32 v48, v28
	v_mov_b32_e32 v49, v32
	v_and_b32_e32 v13, 0xffff0000, v13
	v_and_b32_e32 v12, 0xffff0000, v17
	v_mov_b32_e32 v32, v29
	v_pk_mul_f32 v[16:17], v[40:41], v[38:39]
	v_pk_mul_f32 v[22:23], v[22:23], v[42:43]
	v_pk_mul_f32 v[18:19], v[44:45], v[18:19]
	v_pk_mul_f32 v[10:11], v[24:25], v[10:11]
	v_pk_mul_f32 v[14:15], v[20:21], v[14:15]
	v_pk_mul_f32 v[20:21], v[30:31], v[46:47]
	v_pk_mul_f32 v[24:25], v[48:49], v[26:27]
	v_pk_mul_f32 v[12:13], v[32:33], v[12:13]
	v_sub_f32_e32 v16, v16, v17
	v_sub_f32_e32 v17, v22, v23
	v_sub_f32_e32 v18, v18, v19
	v_sub_f32_e32 v10, v10, v11
	v_sub_f32_e32 v11, v14, v15
	v_sub_f32_e32 v14, v20, v21
	v_sub_f32_e32 v15, v24, v25
	v_sub_f32_e32 v12, v12, v13
	v_cvt_pk_bf16_f32 v136, v16, v17
	v_cvt_pk_bf16_f32 v137, v18, v10
	v_cvt_pk_bf16_f32 v138, v11, v14
	v_cvt_pk_bf16_f32 v139, v15, v12
	global_load_dwordx4 v[10:13], v[6:7], off offset:256
	global_load_dwordx4 v[14:17], v[6:7], off offset:320
	global_load_dwordx4 v[18:21], v[34:35], off
	global_load_dwordx4 v[22:25], v[36:37], off
	global_load_dwordx4 v[26:29], v[34:35], off offset:16
	global_load_dwordx4 v[30:33], v[36:37], off offset:16
	s_waitcnt vmcnt(5)
; __device__ __forceinline__ float bflo(unsigned x) { return __uint_as_float(x << 16); }
; __device__ __forceinline__ float bfhi(unsigned x) { return __uint_as_float(x & 0xffff0000u); }
; __device__ __forceinline__ void mla_item(const Bufs& B, int b, int h, int qb, LAS char* lds, const AttnLane& L) {
;     ...
;     for (int d0 = 0; d0 < 4; ++d0) {
;         const int i0 = d0 * 16 + L.hi * 8; const bool lo = i0 < 32; const int ib = i0 & 31;
;         const u32x4 xa = *(const u32x4*)(qp + 128 + i0), xb = *(const u32x4*)(qp + 128 + (lo ? i0 + 32 : i0 - 32));
;         const f32x4 c0 = *(const f32x4*)(B.cosM + s * 32 + ib), c1 = *(const f32x4*)(B.cosM + s * 32 + ib + 4), s0 = *(const f32x4*)(B.sinM + s * 32 + ib), s1 = *(const f32x4*)(B.sinM + s * 32 + ib + 4);
;         const float xs[8] = {bflo(xa.x), bfhi(xa.x), bflo(xa.y), bfhi(xa.y), bflo(xa.z), bfhi(xa.z), bflo(xa.w), bfhi(xa.w)};
;         const float xp[8] = {bflo(xb.x), bfhi(xb.x), bflo(xb.y), bfhi(xb.y), bflo(xb.z), bfhi(xb.z), bflo(xb.w), bfhi(xb.w)};
;         const float cs[8] = {c0[0], c0[1], c0[2], c0[3], c1[0], c1[1], c1[2], c1[3]}, sn[8] = {s0[0], s0[1], s0[2], s0[3], s1[0], s1[1], s1[2], s1[3]};
;         float o[8];
; #pragma unroll
;         for (int e = 0; e < 8; ++e) o[e] = lo ? (xs[e] * cs[e] - xp[e] * sn[e]) : (xp[e] * sn[e] + xs[e] * cs[e]);
;         u32x4 w = {cvtpk(o[0], o[1]), cvtpk(o[2], o[3]), cvtpk(o[4], o[5]), cvtpk(o[6], o[7])}; qr[8 + d0] = *reinterpret_cast<bf16x8*>(&w);
;     }
;     const float c2 = 0.07216878364870322f * LOG2E;
;     const bf16_t* Kg = B.KVM + (size_t)(b * 2048) * 2048 + h * 256; const bf16_t* Vg = Kg + 128; const bf16_t* Rg = B.KR + (size_t)(b * 2048) * 64;
;     FaState st; fa_reset(st);
;     const int nt = 4 * qb + 4, wlast = s | 31;
;     const DmaOff off = dma_offsets(L.wid, L.lane, 4096); const unsigned offr = dma_off_rope(L.wid, L.lane);
;     const unsigned ldsb = (unsigned)(size_t)lds;
;     constexpr int AT_R0 = AT_AC, AT_R1 = AT_AC + 8192;
;     unsigned ka[8], kr0[4], kr1[4]; k_addrs(ka, ldsb, L.r32, L.hi); r_addrs(kr0, ldsb + AT_R0, L.r32, L.hi); r_addrs(kr1, ldsb + AT_R1, L.r32, L.hi);
;     int j = 0;
;     __syncthreads();
;     dma_tile(Kg, Vg, off, ldsb + AT_K0, ldsb + AT_V0, L.wid); pg8::glds16(pg8::uniform_ptr((const char*)Rg), offr, ldsb + AT_R0 + (unsigned)L.wid * 1024u);
	v_lshlrev_b32_e32 v35, 16, v10
	s_waitcnt vmcnt(4)
	v_lshlrev_b32_e32 v34, 16, v14
	s_waitcnt vmcnt(3)
	v_mov_b32_e32 v36, v18
	s_waitcnt vmcnt(2)
	v_mov_b32_e32 v37, v22
	v_and_b32_e32 v39, 0xffff0000, v10
	v_and_b32_e32 v38, 0xffff0000, v14
	v_mov_b32_e32 v22, v19
	v_lshlrev_b32_e32 v19, 16, v11
	v_lshlrev_b32_e32 v18, 16, v15
	v_mov_b32_e32 v40, v20
	v_mov_b32_e32 v41, v24
	v_and_b32_e32 v11, 0xffff0000, v11
	v_and_b32_e32 v10, 0xffff0000, v15
	v_mov_b32_e32 v24, v21
	v_lshlrev_b32_e32 v15, 16, v12
	v_lshlrev_b32_e32 v14, 16, v16
	s_waitcnt vmcnt(1)
	v_mov_b32_e32 v20, v26
	s_waitcnt vmcnt(0)
	v_mov_b32_e32 v21, v30
	v_and_b32_e32 v43, 0xffff0000, v12
	v_and_b32_e32 v42, 0xffff0000, v16
	v_mov_b32_e32 v30, v27
	v_lshlrev_b32_e32 v27, 16, v13
	v_lshlrev_b32_e32 v26, 16, v17
	v_mov_b32_e32 v44, v28
	v_mov_b32_e32 v45, v32
	v_and_b32_e32 v13, 0xffff0000, v13
	v_and_b32_e32 v12, 0xffff0000, v17
	v_mov_b32_e32 v32, v29
	v_pk_mul_f32 v[16:17], v[36:37], v[34:35]
	v_pk_mul_f32 v[22:23], v[22:23], v[38:39]
	v_pk_mul_f32 v[18:19], v[40:41], v[18:19]
	v_pk_mul_f32 v[10:11], v[24:25], v[10:11]
	v_pk_mul_f32 v[14:15], v[20:21], v[14:15]
	v_pk_mul_f32 v[20:21], v[30:31], v[42:43]
	v_pk_mul_f32 v[24:25], v[44:45], v[26:27]
	v_pk_mul_f32 v[12:13], v[32:33], v[12:13]
	v_add_f32_e32 v16, v16, v17
	v_add_f32_e32 v17, v22, v23
	v_add_f32_e32 v18, v18, v19
	v_add_f32_e32 v10, v10, v11
	v_add_f32_e32 v11, v14, v15
	v_add_f32_e32 v14, v20, v21
	v_add_f32_e32 v15, v24, v25
	v_add_f32_e32 v12, v12, v13
	v_cvt_pk_bf16_f32 v140, v16, v17
	v_cvt_pk_bf16_f32 v141, v18, v10
	v_cvt_pk_bf16_f32 v142, v11, v14
	v_cvt_pk_bf16_f32 v143, v15, v12
	global_load_dwordx4 v[20:23], v[6:7], off offset:352
	global_load_dwordx4 v[24:27], v[6:7], off offset:288
	global_load_dwordx4 v[28:31], v[8:9], off
	global_load_dwordx4 v[32:35], v[4:5], off
	global_load_dwordx4 v[36:39], v[8:9], off offset:16
	global_load_dwordx4 v[40:43], v[4:5], off offset:16
	v_mov_b32_e32 v18, v3
	v_mov_b32_e32 v19, v3
	v_mov_b32_e32 v4, v3
	v_mov_b32_e32 v5, v3
	v_mov_b32_e32 v6, v3
	v_mov_b32_e32 v7, v3
	v_mov_b32_e32 v8, v3
	v_mov_b32_e32 v9, v3
	v_mov_b32_e32 v10, v3
	v_mov_b32_e32 v11, v3
	v_mov_b32_e32 v12, v3
	v_mov_b32_e32 v13, v3
	v_mov_b32_e32 v14, v3
	v_mov_b32_e32 v15, v3
	v_mov_b32_e32 v16, v3
	v_mov_b32_e32 v17, v3
	s_waitcnt vmcnt(3)
	v_mov_b32_e32 v46, v28
	v_lshlrev_b32_e32 v44, 16, v20
	v_lshlrev_b32_e32 v45, 16, v24
	s_waitcnt vmcnt(2)
	v_mov_b32_e32 v47, v32
	v_and_b32_e32 v49, 0xffff0000, v24
	v_and_b32_e32 v48, 0xffff0000, v20
	v_mov_b32_e32 v32, v29
	v_lshlrev_b32_e32 v29, 16, v25
	v_lshlrev_b32_e32 v28, 16, v21
	v_mov_b32_e32 v50, v30
	v_mov_b32_e32 v51, v34
	v_and_b32_e32 v25, 0xffff0000, v25
	v_and_b32_e32 v24, 0xffff0000, v21
	v_mov_b32_e32 v34, v31
	v_lshlrev_b32_e32 v21, 16, v26
	v_lshlrev_b32_e32 v20, 16, v22
	s_waitcnt vmcnt(1)
	v_mov_b32_e32 v30, v36
	s_waitcnt vmcnt(0)
	v_mov_b32_e32 v31, v40
	v_and_b32_e32 v53, 0xffff0000, v26
	v_and_b32_e32 v52, 0xffff0000, v22
	v_mov_b32_e32 v40, v37
	v_lshlrev_b32_e32 v37, 16, v27
	v_lshlrev_b32_e32 v36, 16, v23
	v_mov_b32_e32 v54, v38
	v_mov_b32_e32 v55, v42
	v_and_b32_e32 v27, 0xffff0000, v27
	v_and_b32_e32 v26, 0xffff0000, v23
	v_mov_b32_e32 v42, v39
	v_pk_mul_f32 v[22:23], v[46:47], v[44:45]
	v_pk_mul_f32 v[32:33], v[32:33], v[48:49]
	v_pk_mul_f32 v[28:29], v[50:51], v[28:29]
	v_pk_mul_f32 v[24:25], v[34:35], v[24:25]
	v_pk_mul_f32 v[20:21], v[30:31], v[20:21]
	v_pk_mul_f32 v[30:31], v[40:41], v[52:53]
	v_pk_mul_f32 v[34:35], v[54:55], v[36:37]
	v_pk_mul_f32 v[26:27], v[42:43], v[26:27]
	v_add_f32_e32 v22, v22, v23
	v_add_f32_e32 v23, v32, v33
	v_add_f32_e32 v28, v28, v29
	v_add_f32_e32 v24, v24, v25
	v_add_f32_e32 v20, v20, v21
	v_add_f32_e32 v21, v30, v31
	v_add_f32_e32 v25, v34, v35
	v_add_f32_e32 v26, v26, v27
	v_cvt_pk_bf16_f32 v144, v22, v23
	v_cvt_pk_bf16_f32 v145, v28, v24
	v_cvt_pk_bf16_f32 v146, v20, v21
	v_cvt_pk_bf16_f32 v147, v25, v26
	s_barrier
	s_mov_b32 m0, s92
	s_nop 0
	global_load_lds_dwordx4 v176, s[70:71]
	v_mov_b64_e32 v[34:35], v[18:19]
	s_mov_b32 m0, s93
	s_nop 0
	global_load_lds_dwordx4 v178, s[70:71]
	v_mov_b64_e32 v[50:51], v[18:19]
	s_mov_b32 m0, s94
	s_nop 0
	global_load_lds_dwordx4 v177, s[72:73]
	v_mov_b64_e32 v[66:67], v[18:19]
	s_mov_b32 m0, s95
	s_nop 0
	global_load_lds_dwordx4 v179, s[72:73]
	v_mov_b64_e32 v[32:33], v[16:17]
	s_mov_b32 m0, s96
	s_nop 0
	global_load_lds_dwordx4 v180, s[74:75]
	v_mov_b64_e32 v[30:31], v[14:15]
	v_mov_b64_e32 v[28:29], v[12:13]
	v_mov_b64_e32 v[26:27], v[10:11]
	v_mov_b64_e32 v[24:25], v[8:9]
	v_mov_b64_e32 v[22:23], v[6:7]
	v_mov_b64_e32 v[20:21], v[4:5]
	v_mov_b64_e32 v[48:49], v[16:17]
	v_mov_b64_e32 v[46:47], v[14:15]
	v_mov_b64_e32 v[44:45], v[12:13]
	v_mov_b64_e32 v[42:43], v[10:11]
	v_mov_b64_e32 v[40:41], v[8:9]
	v_mov_b64_e32 v[38:39], v[6:7]
	v_mov_b64_e32 v[36:37], v[4:5]
	v_mov_b64_e32 v[64:65], v[16:17]
	v_mov_b64_e32 v[62:63], v[14:15]
	v_mov_b64_e32 v[60:61], v[12:13]
	v_mov_b64_e32 v[58:59], v[10:11]
	v_mov_b64_e32 v[56:57], v[8:9]
	v_mov_b64_e32 v[54:55], v[6:7]
	v_mov_b64_e32 v[52:53], v[4:5]
	s_branch .LBB0_2475

.LBB0_2477:
	s_andn2_b64 vcc, exec, s[4:5]
	s_cbranch_vccnz .LBB0_2479
	s_add_u32 s4, s70, s80
	s_addc_u32 s5, s71, s81
	s_add_u32 s4, s4, 0x40000
	s_addc_u32 s5, s5, 0
	s_add_u32 s6, s72, s80
	s_addc_u32 s7, s73, s81
	s_mov_b32 m0, s97
	s_nop 0
	global_load_lds_dwordx4 v176, s[4:5]
	s_add_u32 s6, s6, 0x40000
	s_mov_b32 m0, s86
	s_nop 0
	global_load_lds_dwordx4 v178, s[4:5]
	s_addc_u32 s7, s7, 0
	s_mov_b32 m0, s87
	s_nop 0
	global_load_lds_dwordx4 v177, s[6:7]
	s_nop 0
	s_mov_b32 m0, s88
	s_nop 0
	global_load_lds_dwordx4 v179, s[6:7]
	s_add_u32 s4, s82, 0xffffe000
	s_addc_u32 s5, s83, -1
	s_mov_b32 m0, s89
	s_nop 0
	global_load_lds_dwordx4 v180, s[4:5]
	s_waitcnt vmcnt(5)

.LBB0_2490:
	s_andn2_b64 vcc, exec, s[4:5]
	s_cbranch_vccnz .LBB0_2492
	s_add_u32 s4, s70, s80
	s_addc_u32 s5, s71, s81
	s_add_u32 s4, s4, 0x80000
	s_addc_u32 s5, s5, 0
	s_add_u32 s6, s72, s80
	s_addc_u32 s7, s73, s81
	s_mov_b32 m0, s92
	s_nop 0
	global_load_lds_dwordx4 v176, s[4:5]
	s_add_u32 s6, s6, 0x80000
	s_mov_b32 m0, s93
	s_nop 0
	global_load_lds_dwordx4 v178, s[4:5]
	s_addc_u32 s7, s7, 0
	s_mov_b32 m0, s94
	s_nop 0
	global_load_lds_dwordx4 v177, s[6:7]
	s_nop 0
	s_mov_b32 m0, s95
	s_nop 0
	global_load_lds_dwordx4 v179, s[6:7]
	s_nop 0
	s_mov_b32 m0, s96
	s_nop 0
	global_load_lds_dwordx4 v180, s[82:83]
	s_waitcnt vmcnt(5)

;     ...
;     int tid = w0_ * 64 + lane_id(); asm volatile("" : "+v"(tid));
;     const int wid = __builtin_amdgcn_readfirstlane(tid >> 6), lane = tid & 63, wr = wid >> 2, wc = wid & 3, fr = lane & 15, fq = lane >> 4;
;     const int nt = nt_ ? nt_ : Kb / 128;
;     unsigned voffA[2], voffB[2];
; #pragma unroll
;     for (int i = 0; i < 2; ++i) { int R, C; stage_rc(tid * 16 + i * 8192, R, C); const int Rb = Epi::PERM ? ((R & ~31) + perm32(R & 31)) : R;
;         voffA[i] = (unsigned)(R * ldab + C * 2); voffB[i] = (unsigned)(Rb * Kb + C * 2); }
;     const size_t kstep = (size_t)(BK * 2);
;     const size_t hstepA = (size_t)HALF * ldab, hstepB = (size_t)HALF * Kb;
;     const unsigned ldsw = (unsigned)wid * 1024u, ldsbase = (unsigned)(size_t)lds;
;     const int aoff = lds_byte(wr * 64 + fr, fq * 8), boff = lds_byte(wc * 32 + fr, fq * 8);
;     ...
;     Unit cur, nxt; int ui = 0;
;     if (!S.next(0, cur)) return;
;     f32x4 acc[2][2][4][2];
; #pragma unroll
;     for (int a = 0; a < 2; ++a)
; #pragma unroll
;         for (int b = 0; b < 2; ++b)
; #pragma unroll
;             for (int m = 0; m < 4; ++m)
; #pragma unroll
;                 for (int n = 0; n < 2; ++n) acc[a][b][m][n] = (f32x4){0.f, 0.f, 0.f, 0.f};
;     bf16x8 At[4][2], B0[2][2], B1[2][2];
;     const char* cA = uniform_ptr(cur.a); const char* cB = uniform_ptr(cur.b);
;     PG8_STAGE(PG8_SB(0, 0), cB, voffB); PG8_STAGE(PG8_SB(0, 1), cB + hstepB, voffB); PG8_STAGE(PG8_SA(0, 0), cA, voffA); PG8_STAGE(PG8_SA(0, 1), cA + hstepA, voffA);
;     if (wr == 1) PG8_BAR;
;     PG8_WAIT_V(2); PG8_BAR;
;     PG8_STAGE(PG8_SB(1, 0), cB + kstep, voffB); PG8_STAGE(PG8_SA(1, 0), cA + kstep, voffA); PG8_STAGE(PG8_SB(1, 1), cB + hstepB + kstep, voffB);
;     PG8_WAIT_V(6); PG8_BAR;
; __global__ void __launch_bounds__(512, 2) fwd(Args args) {
;     ...
;         if (IN(pb + 6)) { PHASE_LOCALS();
;             pg8::SimpleSched S; S.o.init(T / 256, 8, G, bx); S.A = (const char*)(act + A_AO); S.Bt = (const char*)(ws + WS_WOUT + l * SZ_WOUT); S.astep = (size_t)256 * 2048 * 2; S.bstep = (size_t)256 * 2048;
;             if (l == 0) { pg8::EpiResBf16<true> E{(const void*)args.in[I_X], (bf16_t*)(ws + WS_XA), D, (float*)(ws + WS_SS)}; pg8::gemm_phase<true>(lds, 2048, 4096, S, E, w0, 123, 121); }
;             else { pg8::EpiResBf16<false, true> E{(const void*)args.out, (bf16_t*)(ws + WS_XA), D, (float*)nullptr};
.LBB0_2571:
	s_cmp_gt_i32 s82, s0
	s_cselect_b64 s[2:3], -1, 0
	s_cmp_ge_i32 s0, s83
	s_cselect_b64 s[4:5], -1, 0
	s_or_b64 s[2:3], s[2:3], s[4:5]
	s_and_b64 vcc, exec, s[2:3]
	s_cbranch_vccnz .LBB0_2685
	s_mov_b64 s[2:3], 0
	s_add_u32 s0, s80, s2
	s_addc_u32 s26, s81, s3
	v_mbcnt_lo_u32_b32 v0, -1, 0
	v_mbcnt_hi_u32_b32 v0, -1, v0
	v_readlane_b32 s2, v250, 60
	s_add_u32 s30, s0, 0x4fa1e000
	s_addc_u32 s31, s26, 0
	v_add_u32_e32 v0, s2, v0
	s_lshl_b32 s2, s27, 23
	s_add_u32 s2, s0, s2
	s_addc_u32 s3, s26, 0
	s_add_u32 s34, s2, 0x1d00000
	s_addc_u32 s35, s3, 0
	v_readlane_b32 s4, v254, 44
	s_add_u32 s6, s0, 0x32892000
	v_readlane_b32 s5, v254, 45
	s_addc_u32 s7, s26, 0
	s_mov_b64 s[2:3], -1
	s_and_b64 vcc, exec, s[4:5]
	s_cbranch_vccz .LBB0_2594
	v_mbcnt_lo_u32_b32 v0, -1, 0
	v_mbcnt_hi_u32_b32 v0, -1, v0
	v_readlane_b32 s2, v250, 60
	s_nop 1
	v_add_u32_e32 v0, s2, v0
	v_readlane_b32 s2, v252, 42
	v_readlane_b32 s3, v252, 43
	s_andn2_b64 vcc, exec, s[2:3]
	v_readfirstlane_b32 s2, v0
	s_cbranch_vccnz .LBB0_2593
	v_bfe_i32 v4, v0, 27, 1
	s_waitcnt lgkmcnt(0)
	v_lshlrev_b32_e32 v1, 4, v0
	v_lshrrev_b32_e32 v4, 22, v4
	v_add_u32_e32 v4, v1, v4
	v_and_b32_e32 v4, 0xfffffc00, v4
	v_sub_u32_e32 v4, v1, v4
	v_ashrrev_i32_e32 v2, 31, v0
	v_lshrrev_b32_e32 v5, 4, v4
	v_lshrrev_b32_e32 v2, 26, v2
	v_bitop3_b32 v4, v5, v4, 32 bitop3:0x6c
	v_add_u32_e32 v2, v0, v2
	v_ashrrev_i32_e32 v6, 31, v4
	v_ashrrev_i32_e32 v2, 6, v2
	v_lshrrev_b32_e32 v6, 26, v6
	v_lshlrev_b32_e32 v5, 3, v2
	v_add_u32_e32 v6, v4, v6
	v_and_b32_e32 v5, -16, v5
	v_ashrrev_i32_e32 v7, 6, v6
	v_and_b32_e32 v6, 0xc0, v6
	v_add_u32_e32 v5, v7, v5
	v_sub_u32_e32 v4, v4, v6
	v_lshlrev_b32_e32 v2, 5, v2
	v_ashrrev_i16_sdwa v4, v188, sext(v4) dst_sel:DWORD dst_unused:UNUSED_PAD src0_sel:DWORD src1_sel:BYTE_0
	v_lshlrev_b32_e32 v6, 1, v5
	v_lshrrev_b32_e32 v8, 2, v5
	v_and_b32_e32 v7, 3, v7
	s_mov_b32 s4, 0x1fffe0
	v_and_b32_e32 v2, 32, v2
	v_bfe_i32 v4, v4, 0, 16
	v_and_b32_e32 v6, 24, v6
	v_and_b32_e32 v8, 4, v8
	v_and_or_b32 v7, v5, s4, v7
	v_or3_b32 v6, v7, v8, v6
	v_add_lshl_u32 v4, v2, v4, 1
	v_add_u32_e32 v1, 0x2000, v1
	v_lshl_add_u32 v2, v5, 12, v4
	v_lshl_add_u32 v164, v6, 11, v4
	v_ashrrev_i32_e32 v4, 31, v1
	v_lshrrev_b32_e32 v4, 22, v4
	v_add_u32_e32 v4, v1, v4
	v_ashrrev_i32_e32 v4, 10, v4
	v_mul_i32_i24_e32 v5, 0x400, v4
	v_sub_u32_e32 v1, v1, v5
	v_lshrrev_b32_e32 v5, 4, v1
	v_bitop3_b32 v1, v5, v1, 32 bitop3:0x6c
	v_ashrrev_i32_e32 v6, 31, v1
	v_lshrrev_b32_e32 v6, 26, v6
	v_lshlrev_b32_e32 v5, 3, v4
	v_add_u32_e32 v6, v1, v6
	v_and_b32_e32 v5, -16, v5
	v_ashrrev_i32_e32 v7, 6, v6
	v_add_u32_e32 v5, v7, v5
	v_and_b32_e32 v7, 3, v7
	s_ashr_i32 s8, s2, 6
	s_ashr_i32 s3, s2, 8
	v_and_or_b32 v7, v5, s4, v7
	s_lshl_b32 s27, s8, 10
	v_readlane_b32 s4, v253, 21
	v_and_b32_e32 v6, 0xc0, v6
	v_readlane_b32 s5, v253, 22
	s_add_u32 s20, s34, s4
	v_sub_u32_e32 v1, v1, v6
	s_addc_u32 s21, s35, s5
	v_readlane_b32 s4, v253, 28
	v_lshlrev_b32_e32 v4, 5, v4
	v_ashrrev_i16_sdwa v1, v188, sext(v1) dst_sel:DWORD dst_unused:UNUSED_PAD src0_sel:DWORD src1_sel:BYTE_0
	v_lshlrev_b32_e32 v6, 1, v5
	v_lshrrev_b32_e32 v8, 2, v5
	v_readlane_b32 s5, v253, 29
	s_add_u32 s18, s30, s4
	v_and_b32_e32 v4, 32, v4
	v_bfe_i32 v1, v1, 0, 16
	v_and_b32_e32 v6, 24, v6
	v_and_b32_e32 v8, 4, v8
	s_addc_u32 s19, s31, s5
	s_add_i32 s27, s27, 0
	v_or3_b32 v6, v7, v8, v6
	v_add_lshl_u32 v1, v4, v1, 1
	s_add_i32 s28, s27, 0x10000
	s_mov_b32 m0, s28
	s_nop 0
	global_load_lds_dwordx4 v164, s[20:21]
	v_lshl_add_u32 v166, v6, 11, v1
	s_add_i32 s29, s27, 0x12000
	s_mov_b32 m0, s29
	s_nop 0
	global_load_lds_dwordx4 v166, s[20:21]
	s_add_u32 s4, s20, 0x40000
	s_addc_u32 s5, s21, 0
	s_add_i32 s36, s27, 0x14000
	s_mov_b32 m0, s36
	s_nop 0
	global_load_lds_dwordx4 v164, s[4:5]
	s_add_i32 s37, s27, 0x16000
	s_mov_b32 m0, s37
	s_nop 0
	global_load_lds_dwordx4 v166, s[4:5]
	s_mov_b32 m0, s27
	s_nop 0
	global_load_lds_dwordx4 v2, s[18:19]
	v_lshl_add_u32 v165, v5, 12, v1
	s_add_i32 s38, s27, 0x2000
	s_mov_b32 m0, s38
	s_nop 0
	global_load_lds_dwordx4 v165, s[18:19]
	s_add_u32 s4, s18, 0x80000
	s_addc_u32 s5, s19, 0
	s_add_i32 s39, s27, 0x4000
	s_mov_b32 m0, s39
	s_nop 0
	global_load_lds_dwordx4 v2, s[4:5]
	s_add_i32 s40, s27, 0x6000
	s_mov_b32 m0, s40
	s_nop 0
	global_load_lds_dwordx4 v165, s[4:5]
	s_cmp_eq_u32 s3, 1
	s_cselect_b64 s[4:5], -1, 0
	s_cmp_lg_u32 s3, 1
	s_cbranch_scc1 .LBB0_2576
	s_barrier
.LBB0_2576:
	v_lshrrev_b32_e32 v4, 1, v0
	v_and_b32_e32 v4, 24, v4
	v_and_b32_e32 v1, 15, v0
	v_lshlrev_b32_e32 v5, 1, v4
	v_lshlrev_b32_e32 v0, 2, v0
	v_lshl_or_b32 v167, s3, 6, v1
	v_lshl_or_b32 v1, v1, 6, v5
	s_lshl_b32 s3, s3, 13
	v_and_b32_e32 v0, 32, v0
	v_bitop3_b32 v5, v1, s3, v0 bitop3:0xde
	s_lshl_b32 s3, s8, 5
	s_and_b32 s3, s3, 0x60
	s_lshl_b32 s8, s3, 7
	v_bitop3_b32 v0, v1, s8, v0 bitop3:0xde
	s_add_u32 s8, s20, 0x80
	s_waitcnt vmcnt(2)
	s_barrier
	s_addc_u32 s9, s21, 0
	s_add_i32 s41, s27, 0x18000
	s_mov_b32 m0, s41
	s_nop 0
	global_load_lds_dwordx4 v164, s[8:9]
	s_add_i32 s42, s27, 0x1a000
	s_mov_b32 m0, s42
	s_nop 0
	global_load_lds_dwordx4 v166, s[8:9]
	s_add_u32 s8, s18, 0x80
	s_addc_u32 s9, s19, 0
	s_add_i32 s43, s27, 0x8000
	s_mov_b32 m0, s43
	s_nop 0
	global_load_lds_dwordx4 v2, s[8:9]
	s_add_i32 s44, s27, 0xa000
	s_mov_b32 m0, s44
	s_nop 0
	global_load_lds_dwordx4 v165, s[8:9]
	s_add_u32 s8, s20, 0x40080
	s_addc_u32 s9, s21, 0
	s_add_i32 s45, s27, 0x1c000
	s_mov_b32 m0, s45
	s_nop 0
	global_load_lds_dwordx4 v164, s[8:9]
	s_add_i32 s46, s27, 0x1e000
	s_mov_b32 m0, s46
	s_nop 0
	global_load_lds_dwordx4 v166, s[8:9]
	s_waitcnt vmcnt(6)
	s_add_i32 s47, s27, 0xc000
	s_cmpk_lt_u32 s2, 0x100
	v_or_b32_e32 v168, s3, v4
	v_readlane_b32 s2, v253, 26
	s_cselect_b64 s[8:9], -1, 0
	s_add_i32 s48, s27, 0xe000
	s_mov_b32 s49, 0
	v_add_u32_e32 v169, 0, v0
	v_add_u32_e32 v170, 0, v5
	v_readlane_b32 s50, v253, 20
	s_mov_b32 s51, s2
	s_mov_b64 s[14:15], s[18:19]
	s_mov_b64 s[16:17], s[20:21]
	s_barrier
	v_readlane_b32 s3, v253, 27
	s_branch .LBB0_2579

; #define PG8_STAGE(bufoff, gbase, voff) do { _Pragma("unroll") for (int _i = 0; _i < 2; ++_i) \
;         glds16((const void*)(gbase), (voff)[_i], ldsbase + (unsigned)(bufoff) + ldsw + (unsigned)_i * 8192u); } while (0)
; #define PG8_LDA(dst, b, h) do { _Pragma("unroll") for (int m = 0; m < 4; ++m) _Pragma("unroll") for (int k = 0; k < 2; ++k) dst[m][k] = *(const LAS bf16x8*)(lds + PG8_SA(b, h) + aoff + m * 2048 + k * 1024); } while (0)
; #define PG8_LDB(dst, b, h) do { _Pragma("unroll") for (int n = 0; n < 2; ++n) _Pragma("unroll") for (int k = 0; k < 2; ++k) dst[n][k] = *(const LAS bf16x8*)(lds + PG8_SB(b, h) + boff + n * 2048 + k * 1024); } while (0)
; #define PG8_WAIT_V(n) asm volatile("s_waitcnt vmcnt(" #n ")" ::: "memory")
; #define PG8_WAIT_L(n) asm volatile("s_waitcnt lgkmcnt(" #n ")" ::: "memory")
; #define PG8_BAR __builtin_amdgcn_s_barrier()
; #define PG8_SCHED __builtin_amdgcn_sched_barrier(0)
;     ...
;             const char* a1 = cA + (size_t)(t + 1) * kstep;
;             const char* a2 = last ? nA : cA + (size_t)(t + 2) * kstep; const char* b2 = last ? nB : cB + (size_t)(t + 2) * kstep;
;             const char* a3 = a2 + kstep; const char* b3 = b2 + kstep;
;             PG8_LDB(B0, 0, 0); PG8_LDB(B1, 0, 1); PG8_SCHED; PG8_LDA(At, 0, 0); PG8_STAGE(PG8_SA(1, 1), a1 + hstepA, voffA);
;             PG8_WAIT_V(8); PG8_WAIT_L(0); PG8_BAR; PG8_MMA(0, 0, At, B0); PG8_MMA(0, 1, At, B1); PG8_BAR; PG8_SCHED;
;             PG8_LDA(At, 0, 1); PG8_STAGE(PG8_SB(0, 0), b2, voffB); PG8_STAGE(PG8_SB(0, 1), b2 + hstepB, voffB); PG8_STAGE(PG8_SA(0, 0), a2, voffA);
;             PG8_WAIT_V(8); PG8_WAIT_L(0); PG8_BAR; PG8_MMA(1, 0, At, B0); PG8_MMA(1, 1, At, B1); PG8_BAR; PG8_SCHED;
.LBB0_2586:
	v_add_u32_e32 v0, 0x10000, v169
	ds_read_b128 v[28:31], v0
	ds_read_b128 v[32:35], v0 offset:1024
	ds_read_b128 v[20:23], v0 offset:2048
	ds_read_b128 v[24:27], v0 offset:3072
	v_add_u32_e32 v0, 0x14000, v169
	s_waitcnt lgkmcnt(4)
	ds_read_b128 v[12:15], v0
	ds_read_b128 v[16:19], v0 offset:1024
	ds_read_b128 v[4:7], v0 offset:2048
	ds_read_b128 v[8:11], v0 offset:3072
	s_add_u32 s20, s18, 0xfff80080
	s_addc_u32 s21, s19, -1
	s_cmp_eq_u32 s52, 12
	s_cselect_b32 s24, s14, s20
	s_cselect_b32 s25, s15, s21
	s_cselect_b32 s22, s16, s11
	s_cselect_b32 s23, s17, s13
	s_add_u32 s20, s24, 0x80
	s_addc_u32 s21, s25, 0
	ds_read_b128 v[176:179], v170
	ds_read_b128 v[180:183], v170 offset:1024
	ds_read_b128 v[206:209], v170 offset:2048
	ds_read_b128 v[210:213], v170 offset:3072
	ds_read_b128 v[214:217], v170 offset:4096
	ds_read_b128 v[218:221], v170 offset:5120
	ds_read_b128 v[222:225], v170 offset:6144
	ds_read_b128 v[226:229], v170 offset:7168
	s_mov_b32 m0, s47
	s_nop 0
	global_load_lds_dwordx4 v2, s[18:19]
	s_nop 0
	s_mov_b32 m0, s48
	s_nop 0
	global_load_lds_dwordx4 v165, s[18:19]
	s_waitcnt vmcnt(8)
	s_waitcnt lgkmcnt(0)
	s_barrier
	s_setprio 1
	s_waitcnt lgkmcnt(6)
	v_mfma_scale_f32_16x16x128_f8f6f4 v[160:163], v[28:35], v[176:183], v[160:163], v189, v190 op_sel_hi:[0,0,0]
	v_mfma_scale_f32_16x16x128_f8f6f4 v[156:159], v[20:27], v[176:183], v[156:159], v189, v190 op_sel_hi:[0,0,0]
	s_waitcnt lgkmcnt(4)
	v_mfma_scale_f32_16x16x128_f8f6f4 v[144:147], v[28:35], v[206:213], v[144:147], v189, v190 op_sel_hi:[0,0,0]
	v_mfma_scale_f32_16x16x128_f8f6f4 v[140:143], v[20:27], v[206:213], v[140:143], v189, v190 op_sel_hi:[0,0,0]
	s_waitcnt lgkmcnt(2)
	v_mfma_scale_f32_16x16x128_f8f6f4 v[128:131], v[28:35], v[214:221], v[128:131], v189, v190 op_sel_hi:[0,0,0]
	v_mfma_scale_f32_16x16x128_f8f6f4 v[124:127], v[20:27], v[214:221], v[124:127], v189, v190 op_sel_hi:[0,0,0]
	s_waitcnt lgkmcnt(0)
	v_mfma_scale_f32_16x16x128_f8f6f4 v[112:115], v[28:35], v[222:229], v[112:115], v189, v190 op_sel_hi:[0,0,0]
	v_mfma_scale_f32_16x16x128_f8f6f4 v[108:111], v[20:27], v[222:229], v[108:111], v189, v190 op_sel_hi:[0,0,0]
	s_setprio 0
	s_setprio 1
	v_mfma_scale_f32_16x16x128_f8f6f4 v[152:155], v[12:19], v[176:183], v[152:155], v189, v190 op_sel_hi:[0,0,0]
	v_mfma_scale_f32_16x16x128_f8f6f4 v[148:151], v[4:11], v[176:183], v[148:151], v189, v190 op_sel_hi:[0,0,0]
	v_mfma_scale_f32_16x16x128_f8f6f4 v[136:139], v[12:19], v[206:213], v[136:139], v189, v190 op_sel_hi:[0,0,0]
	v_mfma_scale_f32_16x16x128_f8f6f4 v[132:135], v[4:11], v[206:213], v[132:135], v189, v190 op_sel_hi:[0,0,0]
	v_mfma_scale_f32_16x16x128_f8f6f4 v[120:123], v[12:19], v[214:221], v[120:123], v189, v190 op_sel_hi:[0,0,0]
	v_mfma_scale_f32_16x16x128_f8f6f4 v[116:119], v[4:11], v[214:221], v[116:119], v189, v190 op_sel_hi:[0,0,0]
	v_mfma_scale_f32_16x16x128_f8f6f4 v[104:107], v[12:19], v[222:229], v[104:107], v189, v190 op_sel_hi:[0,0,0]
	v_mfma_scale_f32_16x16x128_f8f6f4 v[100:103], v[4:11], v[222:229], v[100:103], v189, v190 op_sel_hi:[0,0,0]
	s_setprio 0
	s_barrier
	ds_read_b128 v[176:179], v170 offset:16384
	ds_read_b128 v[180:183], v170 offset:17408
	ds_read_b128 v[206:209], v170 offset:18432
	ds_read_b128 v[210:213], v170 offset:19456
	ds_read_b128 v[214:217], v170 offset:20480
	ds_read_b128 v[218:221], v170 offset:21504
	ds_read_b128 v[222:225], v170 offset:22528
	ds_read_b128 v[226:229], v170 offset:23552
	s_mov_b32 m0, s28
	s_nop 0
	global_load_lds_dwordx4 v164, s[22:23]
	s_add_u32 s54, s22, 0x40000
	s_mov_b32 m0, s29
	s_nop 0
	global_load_lds_dwordx4 v166, s[22:23]
	s_addc_u32 s55, s23, 0
	s_mov_b32 m0, s36
	s_nop 0
	global_load_lds_dwordx4 v164, s[54:55]
	s_nop 0
	s_mov_b32 m0, s37
	s_nop 0
	global_load_lds_dwordx4 v166, s[54:55]
	s_nop 0
	s_mov_b32 m0, s27
	s_nop 0
	global_load_lds_dwordx4 v2, s[24:25]
	s_nop 0
	s_mov_b32 m0, s38
	s_nop 0
	global_load_lds_dwordx4 v165, s[24:25]
	s_waitcnt vmcnt(8)
	s_waitcnt lgkmcnt(0)
	s_barrier
	s_setprio 1
	s_waitcnt lgkmcnt(6)
	v_mfma_scale_f32_16x16x128_f8f6f4 v[96:99], v[28:35], v[176:183], v[96:99], v189, v190 op_sel_hi:[0,0,0]
	v_mfma_scale_f32_16x16x128_f8f6f4 v[92:95], v[20:27], v[176:183], v[92:95], v189, v190 op_sel_hi:[0,0,0]
	s_waitcnt lgkmcnt(4)
	v_mfma_scale_f32_16x16x128_f8f6f4 v[80:83], v[28:35], v[206:213], v[80:83], v189, v190 op_sel_hi:[0,0,0]
	v_mfma_scale_f32_16x16x128_f8f6f4 v[76:79], v[20:27], v[206:213], v[76:79], v189, v190 op_sel_hi:[0,0,0]
	s_waitcnt lgkmcnt(2)
	v_mfma_scale_f32_16x16x128_f8f6f4 v[64:67], v[28:35], v[214:221], v[64:67], v189, v190 op_sel_hi:[0,0,0]
	v_mfma_scale_f32_16x16x128_f8f6f4 v[60:63], v[20:27], v[214:221], v[60:63], v189, v190 op_sel_hi:[0,0,0]
	s_waitcnt lgkmcnt(0)
	v_mfma_scale_f32_16x16x128_f8f6f4 v[48:51], v[28:35], v[222:229], v[48:51], v189, v190 op_sel_hi:[0,0,0]
	v_mfma_scale_f32_16x16x128_f8f6f4 v[44:47], v[20:27], v[222:229], v[44:47], v189, v190 op_sel_hi:[0,0,0]
	s_setprio 0
	s_setprio 1
	v_mfma_scale_f32_16x16x128_f8f6f4 v[88:91], v[12:19], v[176:183], v[88:91], v189, v190 op_sel_hi:[0,0,0]
	v_mfma_scale_f32_16x16x128_f8f6f4 v[84:87], v[4:11], v[176:183], v[84:87], v189, v190 op_sel_hi:[0,0,0]
	v_mfma_scale_f32_16x16x128_f8f6f4 v[72:75], v[12:19], v[206:213], v[72:75], v189, v190 op_sel_hi:[0,0,0]
	v_mfma_scale_f32_16x16x128_f8f6f4 v[68:71], v[4:11], v[206:213], v[68:71], v189, v190 op_sel_hi:[0,0,0]
	v_mfma_scale_f32_16x16x128_f8f6f4 v[56:59], v[12:19], v[214:221], v[56:59], v189, v190 op_sel_hi:[0,0,0]
	v_mfma_scale_f32_16x16x128_f8f6f4 v[52:55], v[4:11], v[214:221], v[52:55], v189, v190 op_sel_hi:[0,0,0]
	v_mfma_scale_f32_16x16x128_f8f6f4 v[40:43], v[12:19], v[222:229], v[40:43], v189, v190 op_sel_hi:[0,0,0]
	v_mfma_scale_f32_16x16x128_f8f6f4 v[36:39], v[4:11], v[222:229], v[36:39], v189, v190 op_sel_hi:[0,0,0]
	s_setprio 0
	s_barrier
; #define PG8_STAGE(bufoff, gbase, voff) do { _Pragma("unroll") for (int _i = 0; _i < 2; ++_i) \
;         glds16((const void*)(gbase), (voff)[_i], ldsbase + (unsigned)(bufoff) + ldsw + (unsigned)_i * 8192u); } while (0)
; #define PG8_LDA(dst, b, h) do { _Pragma("unroll") for (int m = 0; m < 4; ++m) _Pragma("unroll") for (int k = 0; k < 2; ++k) dst[m][k] = *(const LAS bf16x8*)(lds + PG8_SA(b, h) + aoff + m * 2048 + k * 1024); } while (0)
; #define PG8_LDB(dst, b, h) do { _Pragma("unroll") for (int n = 0; n < 2; ++n) _Pragma("unroll") for (int k = 0; k < 2; ++k) dst[n][k] = *(const LAS bf16x8*)(lds + PG8_SB(b, h) + boff + n * 2048 + k * 1024); } while (0)
; #define PG8_WAIT_V(n) asm volatile("s_waitcnt vmcnt(" #n ")" ::: "memory")
; #define PG8_WAIT_L(n) asm volatile("s_waitcnt lgkmcnt(" #n ")" ::: "memory")
; #define PG8_BAR __builtin_amdgcn_s_barrier()
; #define PG8_SCHED __builtin_amdgcn_sched_barrier(0)
;     ...
;             PG8_WAIT_V(8); PG8_WAIT_L(0); PG8_BAR; PG8_MMA(1, 0, At, B0); PG8_MMA(1, 1, At, B1); PG8_BAR; PG8_SCHED;
;             PG8_LDB(B0, 1, 0); PG8_LDB(B1, 1, 1); PG8_SCHED; PG8_LDA(At, 1, 0); PG8_STAGE(PG8_SA(0, 1), a2 + hstepA, voffA);
;             PG8_WAIT_V(8); PG8_WAIT_L(0); PG8_BAR; PG8_MMA(0, 0, At, B0); PG8_MMA(0, 1, At, B1); PG8_BAR; PG8_SCHED;
;             PG8_LDA(At, 1, 1); PG8_STAGE(PG8_SB(1, 0), b3, voffB); PG8_STAGE(PG8_SB(1, 1), b3 + hstepB, voffB); PG8_STAGE(PG8_SA(1, 0), a3, voffA);
;             PG8_WAIT_V(8); PG8_WAIT_L(0); PG8_BAR; PG8_MMA(1, 0, At, B0); PG8_MMA(1, 1, At, B1); PG8_BAR; PG8_SCHED;
;         }
;         if (wr == 0) PG8_BAR;
	v_add_u32_e32 v0, 0x18000, v169
	ds_read_b128 v[20:23], v0
	ds_read_b128 v[24:27], v0 offset:1024
	ds_read_b128 v[28:31], v0 offset:2048
	ds_read_b128 v[32:35], v0 offset:3072
	v_add_u32_e32 v0, 0x1c000, v169
	ds_read_b128 v[12:15], v0
	ds_read_b128 v[16:19], v0 offset:1024
	ds_read_b128 v[4:7], v0 offset:2048
	ds_read_b128 v[8:11], v0 offset:3072
	ds_read_b128 v[176:179], v170 offset:32768
	ds_read_b128 v[180:183], v170 offset:33792
	ds_read_b128 v[206:209], v170 offset:34816
	ds_read_b128 v[210:213], v170 offset:35840
	ds_read_b128 v[214:217], v170 offset:36864
	ds_read_b128 v[218:221], v170 offset:37888
	ds_read_b128 v[222:225], v170 offset:38912
	ds_read_b128 v[226:229], v170 offset:39936
	s_add_u32 s24, s24, 0x80000
	s_addc_u32 s25, s25, 0
	s_mov_b32 m0, s39
	s_nop 0
	global_load_lds_dwordx4 v2, s[24:25]
	s_nop 0
	s_mov_b32 m0, s40
	s_nop 0
	global_load_lds_dwordx4 v165, s[24:25]
	s_waitcnt vmcnt(8)
	s_waitcnt lgkmcnt(0)
	s_barrier
	s_setprio 1
	s_waitcnt lgkmcnt(6)
	v_mfma_scale_f32_16x16x128_f8f6f4 v[160:163], v[20:27], v[176:183], v[160:163], v189, v190 op_sel_hi:[0,0,0]
	v_mfma_scale_f32_16x16x128_f8f6f4 v[156:159], v[28:35], v[176:183], v[156:159], v189, v190 op_sel_hi:[0,0,0]
	s_waitcnt lgkmcnt(4)
	v_mfma_scale_f32_16x16x128_f8f6f4 v[144:147], v[20:27], v[206:213], v[144:147], v189, v190 op_sel_hi:[0,0,0]
	v_mfma_scale_f32_16x16x128_f8f6f4 v[140:143], v[28:35], v[206:213], v[140:143], v189, v190 op_sel_hi:[0,0,0]
	s_waitcnt lgkmcnt(2)
	v_mfma_scale_f32_16x16x128_f8f6f4 v[128:131], v[20:27], v[214:221], v[128:131], v189, v190 op_sel_hi:[0,0,0]
	v_mfma_scale_f32_16x16x128_f8f6f4 v[124:127], v[28:35], v[214:221], v[124:127], v189, v190 op_sel_hi:[0,0,0]
	s_waitcnt lgkmcnt(0)
	v_mfma_scale_f32_16x16x128_f8f6f4 v[112:115], v[20:27], v[222:229], v[112:115], v189, v190 op_sel_hi:[0,0,0]
	v_mfma_scale_f32_16x16x128_f8f6f4 v[108:111], v[28:35], v[222:229], v[108:111], v189, v190 op_sel_hi:[0,0,0]
	s_setprio 0
	s_setprio 1
	v_mfma_scale_f32_16x16x128_f8f6f4 v[152:155], v[12:19], v[176:183], v[152:155], v189, v190 op_sel_hi:[0,0,0]
	v_mfma_scale_f32_16x16x128_f8f6f4 v[148:151], v[4:11], v[176:183], v[148:151], v189, v190 op_sel_hi:[0,0,0]
	v_mfma_scale_f32_16x16x128_f8f6f4 v[136:139], v[12:19], v[206:213], v[136:139], v189, v190 op_sel_hi:[0,0,0]
	v_mfma_scale_f32_16x16x128_f8f6f4 v[132:135], v[4:11], v[206:213], v[132:135], v189, v190 op_sel_hi:[0,0,0]
	v_mfma_scale_f32_16x16x128_f8f6f4 v[120:123], v[12:19], v[214:221], v[120:123], v189, v190 op_sel_hi:[0,0,0]
	v_mfma_scale_f32_16x16x128_f8f6f4 v[116:119], v[4:11], v[214:221], v[116:119], v189, v190 op_sel_hi:[0,0,0]
	v_mfma_scale_f32_16x16x128_f8f6f4 v[104:107], v[12:19], v[222:229], v[104:107], v189, v190 op_sel_hi:[0,0,0]
	v_mfma_scale_f32_16x16x128_f8f6f4 v[100:103], v[4:11], v[222:229], v[100:103], v189, v190 op_sel_hi:[0,0,0]
	s_setprio 0
	s_barrier
	ds_read_b128 v[176:179], v170 offset:49152
	ds_read_b128 v[180:183], v170 offset:50176
	ds_read_b128 v[206:209], v170 offset:51200
	ds_read_b128 v[210:213], v170 offset:52224
	ds_read_b128 v[214:217], v170 offset:53248
	ds_read_b128 v[218:221], v170 offset:54272
	ds_read_b128 v[222:225], v170 offset:55296
	ds_read_b128 v[226:229], v170 offset:56320
	s_add_u32 s24, s22, 0x80
	s_addc_u32 s25, s23, 0
	s_mov_b32 m0, s41
	s_nop 0
	global_load_lds_dwordx4 v164, s[24:25]
	s_add_u32 s22, s22, 0x40080
	s_mov_b32 m0, s42
	s_nop 0
	global_load_lds_dwordx4 v166, s[24:25]
	s_addc_u32 s23, s23, 0
	s_mov_b32 m0, s45
	s_nop 0
	global_load_lds_dwordx4 v164, s[22:23]
	s_nop 0
	s_mov_b32 m0, s46
	s_nop 0
	global_load_lds_dwordx4 v166, s[22:23]
	s_mov_b32 m0, s43
	s_nop 0
	global_load_lds_dwordx4 v2, s[20:21]
	s_nop 0
	s_mov_b32 m0, s44
	s_nop 0
	global_load_lds_dwordx4 v165, s[20:21]
	s_waitcnt vmcnt(8)
	s_waitcnt lgkmcnt(0)
	s_barrier
	s_setprio 1
	s_waitcnt lgkmcnt(6)
	v_mfma_scale_f32_16x16x128_f8f6f4 v[96:99], v[20:27], v[176:183], v[96:99], v189, v190 op_sel_hi:[0,0,0]
	v_mfma_scale_f32_16x16x128_f8f6f4 v[92:95], v[28:35], v[176:183], v[92:95], v189, v190 op_sel_hi:[0,0,0]
	s_waitcnt lgkmcnt(4)
	v_mfma_scale_f32_16x16x128_f8f6f4 v[80:83], v[20:27], v[206:213], v[80:83], v189, v190 op_sel_hi:[0,0,0]
	v_mfma_scale_f32_16x16x128_f8f6f4 v[76:79], v[28:35], v[206:213], v[76:79], v189, v190 op_sel_hi:[0,0,0]
	s_waitcnt lgkmcnt(2)
	v_mfma_scale_f32_16x16x128_f8f6f4 v[64:67], v[20:27], v[214:221], v[64:67], v189, v190 op_sel_hi:[0,0,0]
	v_mfma_scale_f32_16x16x128_f8f6f4 v[60:63], v[28:35], v[214:221], v[60:63], v189, v190 op_sel_hi:[0,0,0]
	s_waitcnt lgkmcnt(0)
	v_mfma_scale_f32_16x16x128_f8f6f4 v[48:51], v[20:27], v[222:229], v[48:51], v189, v190 op_sel_hi:[0,0,0]
	v_mfma_scale_f32_16x16x128_f8f6f4 v[44:47], v[28:35], v[222:229], v[44:47], v189, v190 op_sel_hi:[0,0,0]
	s_setprio 0
	s_setprio 1
	v_mfma_scale_f32_16x16x128_f8f6f4 v[88:91], v[12:19], v[176:183], v[88:91], v189, v190 op_sel_hi:[0,0,0]
	v_mfma_scale_f32_16x16x128_f8f6f4 v[84:87], v[4:11], v[176:183], v[84:87], v189, v190 op_sel_hi:[0,0,0]
	v_mfma_scale_f32_16x16x128_f8f6f4 v[72:75], v[12:19], v[206:213], v[72:75], v189, v190 op_sel_hi:[0,0,0]
	v_mfma_scale_f32_16x16x128_f8f6f4 v[68:71], v[4:11], v[206:213], v[68:71], v189, v190 op_sel_hi:[0,0,0]
	v_mfma_scale_f32_16x16x128_f8f6f4 v[56:59], v[12:19], v[214:221], v[56:59], v189, v190 op_sel_hi:[0,0,0]
	v_mfma_scale_f32_16x16x128_f8f6f4 v[52:55], v[4:11], v[214:221], v[52:55], v189, v190 op_sel_hi:[0,0,0]
	v_mfma_scale_f32_16x16x128_f8f6f4 v[40:43], v[12:19], v[222:229], v[40:43], v189, v190 op_sel_hi:[0,0,0]
	v_mfma_scale_f32_16x16x128_f8f6f4 v[36:39], v[4:11], v[222:229], v[36:39], v189, v190 op_sel_hi:[0,0,0]
	s_setprio 0
	s_barrier
	s_add_i32 s52, s52, 2
	s_add_u32 s11, s11, 0x100
	s_addc_u32 s13, s13, 0
	s_add_u32 s18, s18, 0x100
	s_addc_u32 s19, s19, 0
	s_cmp_gt_u32 s52, 13
	s_cbranch_scc0 .LBB0_2586
	s_and_b64 vcc, exec, s[8:9]
	s_cbranch_vccz .LBB0_2589
	s_barrier
; __device__ __forceinline__ float bflo(unsigned x) { return __uint_as_float(x << 16); }
; __device__ __forceinline__ float bfhi(unsigned x) { return __uint_as_float(x & 0xffff0000u); }
; __device__ __forceinline__ unsigned cvtpk(float lo, float hi) { unsigned r; asm volatile("v_cvt_pk_bf16_f32 %0, %1, %2" : "=v"(r) : "v"(lo), "v"(hi)); return r; }
;     ...
;         if constexpr (FMT != 0) {
;             asm volatile("s_nop 7\n\ts_nop 7\n\ts_nop 3" ::: "memory");
; #pragma unroll
;             for (int a = 0; a < 2; ++a)
; #pragma unroll
;                 for (int b = 0; b < 2; ++b)
; #pragma unroll
;                     for (int m = 0; m < 4; ++m)
; #pragma unroll
;                         for (int n = 0; n < 2; ++n) asm volatile("" : "+v"(acc[a][b][m][n]));
;         }
;     __device__ __forceinline__ void operator()(const f32x4 (&acc)[2][2][4][2], const Unit& u, int wr, int wc, int fr, int fq) const {
;     ...
;         if constexpr (PLAIN) {
; #pragma unroll
;             for (int ai = 0; ai < 2; ++ai)
; #pragma unroll
;                 for (int m = 0; m < 4; ++m) { const size_t off = (size_t)(row0 + ai * HALF + m * 16) * ldc + col0;
;                     const u32x4 ra = *(const u32x4*)((const bf16_t*)res + off), rb = *(const u32x4*)((const bf16_t*)res + off + HALF);
; #pragma unroll
;                     for (int bj = 0; bj < 2; ++bj) { const u32x4 w_ = bj ? rb : ra; const f32x4 v0 = (f32x4){bflo(w_.x), bfhi(w_.x), bflo(w_.y), bfhi(w_.y)} + acc[ai][bj][m][0], v1 = (f32x4){bflo(w_.z), bfhi(w_.z), bflo(w_.w), bfhi(w_.w)} + acc[ai][bj][m][1];
;                         u32x4 w; w.x = cvtpk(v0[0], v0[1]); w.y = cvtpk(v0[2], v0[3]); w.z = cvtpk(v1[0], v1[1]); w.w = cvtpk(v1[2], v1[3]);
;                         *(u32x4*)(out + off + bj * HALF) = w; }
;                     asm volatile("" ::: "memory"); }
;             return; }
.LBB0_2589:
	v_lshl_add_u32 v6, s51, 8, v167
	v_lshl_or_b32 v4, s50, 8, v168
	v_ashrrev_i32_e32 v7, 31, v6
	v_readlane_b32 s52, v250, 34
	v_ashrrev_i32_e32 v5, 31, v4
	v_lshlrev_b64 v[0:1], 11, v[6:7]
	v_readlane_b32 s53, v250, 35
	v_readlane_b32 s54, v250, 36
	v_readlane_b32 s55, v250, 37
	v_readlane_b32 s56, v250, 38
	v_readlane_b32 s57, v250, 39
	v_readlane_b32 s58, v250, 40
	v_readlane_b32 s59, v250, 41
	v_readlane_b32 s60, v250, 42
	v_readlane_b32 s61, v250, 43
	v_readlane_b32 s62, v250, 44
	v_readlane_b32 s63, v250, 45
	v_lshl_add_u64 v[0:1], v[0:1], 0, v[4:5]
	v_readlane_b32 s64, v250, 46
	v_readlane_b32 s65, v250, 47
	v_readlane_b32 s66, v250, 48
	v_readlane_b32 s67, v250, 49
	s_mov_b64 s[52:53], s[56:57]
	v_lshlrev_b64 v[0:1], 1, v[0:1]
	s_mov_b64 s[54:55], s[58:59]
	s_mov_b64 s[56:57], s[60:61]
	s_mov_b64 s[58:59], s[62:63]
	s_mov_b64 s[60:61], s[64:65]
	s_mov_b64 s[62:63], s[66:67]
	v_lshl_add_u64 v[12:13], s[62:63], 0, v[0:1]
	s_nop 7
	s_nop 7
	s_nop 3
	s_mov_b64 s[66:67], 0x10000
	v_lshl_add_u64 v[248:249], s[66:67], 0, v[12:13]
	global_load_dwordx4 v[208:211], v[248:249], off
	global_load_dwordx4 v[212:215], v[248:249], off offset:256
	s_mov_b64 s[66:67], 0x20000
	v_lshl_add_u64 v[248:249], s[66:67], 0, v[12:13]
	global_load_dwordx4 v[216:219], v[248:249], off
	global_load_dwordx4 v[220:223], v[248:249], off offset:256
	s_mov_b64 s[66:67], 0x30000
	v_lshl_add_u64 v[248:249], s[66:67], 0, v[12:13]
	global_load_dwordx4 v[224:227], v[248:249], off
	global_load_dwordx4 v[228:231], v[248:249], off offset:256
	s_mov_b64 s[66:67], 0x80000
	v_lshl_add_u64 v[248:249], s[66:67], 0, v[12:13]
	global_load_dwordx4 v[232:235], v[248:249], off
	global_load_dwordx4 v[236:239], v[248:249], off offset:256
	s_mov_b64 s[66:67], 0x90000
	v_lshl_add_u64 v[248:249], s[66:67], 0, v[12:13]
	global_load_dwordx4 v[240:243], v[248:249], off
	global_load_dwordx4 v[244:247], v[248:249], off offset:256
	s_mov_b64 s[66:67], 0xa0000
	v_lshl_add_u64 v[248:249], s[66:67], 0, v[12:13]
	global_load_dwordx4 v[24:27], v[248:249], off
	global_load_dwordx4 v[28:31], v[248:249], off offset:256
	s_mov_b64 s[66:67], 0xb0000
	v_lshl_add_u64 v[248:249], s[66:67], 0, v[12:13]
	global_load_dwordx4 v[196:199], v[248:249], off
	global_load_dwordx4 v[180:183], v[248:249], off offset:256
	global_load_dwordx4 v[8:11], v[12:13], off
	s_nop 0
	global_load_dwordx4 v[12:15], v[12:13], off offset:256
	s_mov_b64 s[18:19], 0x80000
	s_andn2_b64 vcc, exec, s[2:3]
	s_waitcnt vmcnt(1)
	v_lshlrev_b32_e32 v16, 16, v8
	v_and_b32_e32 v17, 0xffff0000, v8
	v_lshlrev_b32_e32 v8, 16, v9
	v_and_b32_e32 v9, 0xffff0000, v9
	v_pk_add_f32 v[18:19], v[162:163], v[8:9]
	v_pk_add_f32 v[8:9], v[160:161], v[16:17]
	v_lshlrev_b32_e32 v16, 16, v10
	v_and_b32_e32 v17, 0xffff0000, v10
	v_lshlrev_b32_e32 v10, 16, v11
	v_and_b32_e32 v11, 0xffff0000, v11
	v_pk_add_f32 v[20:21], v[158:159], v[10:11]
	v_pk_add_f32 v[10:11], v[156:157], v[16:17]
	v_cvt_pk_bf16_f32 v8, v8, v9
	v_cvt_pk_bf16_f32 v9, v18, v19
	v_lshl_add_u64 v[16:17], s[6:7], 0, v[0:1]
	v_cvt_pk_bf16_f32 v10, v10, v11
	v_cvt_pk_bf16_f32 v11, v20, v21
	global_store_dwordx4 v[16:17], v[8:11], off
	s_waitcnt vmcnt(1)
	s_nop 0
	v_lshlrev_b32_e32 v8, 16, v12
	v_and_b32_e32 v9, 0xffff0000, v12
	v_lshlrev_b32_e32 v10, 16, v13
	v_and_b32_e32 v11, 0xffff0000, v13
	v_pk_add_f32 v[8:9], v[152:153], v[8:9]
	v_pk_add_f32 v[10:11], v[154:155], v[10:11]
	v_lshlrev_b32_e32 v12, 16, v14
	v_and_b32_e32 v13, 0xffff0000, v14
	v_lshlrev_b32_e32 v14, 16, v15
	v_and_b32_e32 v15, 0xffff0000, v15
	v_cvt_pk_bf16_f32 v8, v8, v9
	v_pk_add_f32 v[14:15], v[150:151], v[14:15]
	v_pk_add_f32 v[12:13], v[148:149], v[12:13]
	v_cvt_pk_bf16_f32 v9, v10, v11
	s_nop 0
	v_cvt_pk_bf16_f32 v10, v12, v13
	v_cvt_pk_bf16_f32 v11, v14, v15
	global_store_dwordx4 v[16:17], v[8:11], off offset:256
	s_nop 1
	v_or_b32_e32 v8, 16, v6
	v_ashrrev_i32_e32 v9, 31, v8
	v_lshlrev_b64 v[8:9], 11, v[8:9]
	v_lshl_add_u64 v[8:9], v[8:9], 0, v[4:5]
	v_lshlrev_b64 v[16:17], 1, v[8:9]
	v_lshl_add_u64 v[12:13], s[62:63], 0, v[16:17]
	s_nop 0
	v_lshl_add_u64 v[16:17], s[6:7], 0, v[16:17]
	s_nop 0
	v_lshlrev_b32_e32 v18, 16, v208
	v_and_b32_e32 v19, 0xffff0000, v208
	v_lshlrev_b32_e32 v208, 16, v209
	v_and_b32_e32 v209, 0xffff0000, v209
	v_pk_add_f32 v[20:21], v[146:147], v[208:209]
	v_pk_add_f32 v[208:209], v[144:145], v[18:19]
	v_lshlrev_b32_e32 v18, 16, v210
	v_and_b32_e32 v19, 0xffff0000, v210
	v_lshlrev_b32_e32 v210, 16, v211
	v_and_b32_e32 v211, 0xffff0000, v211
	v_pk_add_f32 v[22:23], v[142:143], v[210:211]
	v_pk_add_f32 v[210:211], v[140:141], v[18:19]
	v_cvt_pk_bf16_f32 v208, v208, v209
	v_cvt_pk_bf16_f32 v209, v20, v21
	s_nop 0
	v_cvt_pk_bf16_f32 v210, v210, v211
	v_cvt_pk_bf16_f32 v211, v22, v23
	global_store_dwordx4 v[16:17], v[208:211], off
	s_nop 0
	s_nop 0
	v_lshlrev_b32_e32 v208, 16, v212
	v_and_b32_e32 v209, 0xffff0000, v212
	v_lshlrev_b32_e32 v210, 16, v213
	v_and_b32_e32 v211, 0xffff0000, v213
	v_pk_add_f32 v[208:209], v[136:137], v[208:209]
	v_pk_add_f32 v[210:211], v[138:139], v[210:211]
	v_lshlrev_b32_e32 v212, 16, v214
	v_and_b32_e32 v213, 0xffff0000, v214
	v_lshlrev_b32_e32 v214, 16, v215
	v_and_b32_e32 v215, 0xffff0000, v215
	v_cvt_pk_bf16_f32 v208, v208, v209
	v_pk_add_f32 v[214:215], v[134:135], v[214:215]
	v_pk_add_f32 v[212:213], v[132:133], v[212:213]
	v_cvt_pk_bf16_f32 v209, v210, v211
	s_nop 0
	v_cvt_pk_bf16_f32 v210, v212, v213
	v_cvt_pk_bf16_f32 v211, v214, v215
	global_store_dwordx4 v[16:17], v[208:211], off offset:256
	s_nop 1
	v_or_b32_e32 v8, 32, v6
	v_ashrrev_i32_e32 v9, 31, v8
	v_lshlrev_b64 v[8:9], 11, v[8:9]
	v_lshl_add_u64 v[8:9], v[8:9], 0, v[4:5]
	v_lshlrev_b64 v[16:17], 1, v[8:9]
; __device__ __forceinline__ float bflo(unsigned x) { return __uint_as_float(x << 16); }
; __device__ __forceinline__ float bfhi(unsigned x) { return __uint_as_float(x & 0xffff0000u); }
; __device__ __forceinline__ unsigned cvtpk(float lo, float hi) { unsigned r; asm volatile("v_cvt_pk_bf16_f32 %0, %1, %2" : "=v"(r) : "v"(lo), "v"(hi)); return r; }
;     __device__ __forceinline__ void operator()(const f32x4 (&acc)[2][2][4][2], const Unit& u, int wr, int wc, int fr, int fq) const {
;     ...
;         if constexpr (PLAIN) {
; #pragma unroll
;             for (int ai = 0; ai < 2; ++ai)
; #pragma unroll
;                 for (int m = 0; m < 4; ++m) { const size_t off = (size_t)(row0 + ai * HALF + m * 16) * ldc + col0;
;                     const u32x4 ra = *(const u32x4*)((const bf16_t*)res + off), rb = *(const u32x4*)((const bf16_t*)res + off + HALF);
; #pragma unroll
;                     for (int bj = 0; bj < 2; ++bj) { const u32x4 w_ = bj ? rb : ra; const f32x4 v0 = (f32x4){bflo(w_.x), bfhi(w_.x), bflo(w_.y), bfhi(w_.y)} + acc[ai][bj][m][0], v1 = (f32x4){bflo(w_.z), bfhi(w_.z), bflo(w_.w), bfhi(w_.w)} + acc[ai][bj][m][1];
;                         u32x4 w; w.x = cvtpk(v0[0], v0[1]); w.y = cvtpk(v0[2], v0[3]); w.z = cvtpk(v1[0], v1[1]); w.w = cvtpk(v1[2], v1[3]);
;                         *(u32x4*)(out + off + bj * HALF) = w; }
;                     asm volatile("" ::: "memory"); }
;             return; }
	v_lshl_add_u64 v[12:13], s[62:63], 0, v[16:17]
	s_nop 0
	v_or_b32_e32 v6, 48, v6
	v_lshl_add_u64 v[16:17], s[6:7], 0, v[16:17]
	v_ashrrev_i32_e32 v7, 31, v6
	v_lshlrev_b64 v[6:7], 11, v[6:7]
	v_lshl_add_u64 v[4:5], v[6:7], 0, v[4:5]
	s_nop 0
	v_lshlrev_b32_e32 v18, 16, v216
	v_and_b32_e32 v19, 0xffff0000, v216
	v_lshlrev_b32_e32 v216, 16, v217
	v_and_b32_e32 v217, 0xffff0000, v217
	v_pk_add_f32 v[20:21], v[130:131], v[216:217]
	v_pk_add_f32 v[216:217], v[128:129], v[18:19]
	v_lshlrev_b32_e32 v18, 16, v218
	v_and_b32_e32 v19, 0xffff0000, v218
	v_lshlrev_b32_e32 v218, 16, v219
	v_and_b32_e32 v219, 0xffff0000, v219
	v_pk_add_f32 v[22:23], v[126:127], v[218:219]
	v_pk_add_f32 v[218:219], v[124:125], v[18:19]
	v_cvt_pk_bf16_f32 v216, v216, v217
	v_cvt_pk_bf16_f32 v217, v20, v21
	s_nop 0
	v_cvt_pk_bf16_f32 v218, v218, v219
	v_cvt_pk_bf16_f32 v219, v22, v23
	global_store_dwordx4 v[16:17], v[216:219], off
	s_nop 0
	s_nop 0
	v_lshlrev_b32_e32 v216, 16, v220
	v_and_b32_e32 v217, 0xffff0000, v220
	v_lshlrev_b32_e32 v218, 16, v221
	v_and_b32_e32 v219, 0xffff0000, v221
	v_lshlrev_b32_e32 v220, 16, v222
	v_and_b32_e32 v221, 0xffff0000, v222
	v_pk_add_f32 v[218:219], v[122:123], v[218:219]
	v_pk_add_f32 v[216:217], v[120:121], v[216:217]
	v_lshlrev_b32_e32 v222, 16, v223
	v_and_b32_e32 v223, 0xffff0000, v223
	v_pk_add_f32 v[220:221], v[116:117], v[220:221]
	v_pk_add_f32 v[222:223], v[118:119], v[222:223]
	v_cvt_pk_bf16_f32 v216, v216, v217
	v_cvt_pk_bf16_f32 v217, v218, v219
	v_cvt_pk_bf16_f32 v218, v220, v221
	v_lshlrev_b64 v[12:13], 1, v[4:5]
	v_cvt_pk_bf16_f32 v219, v222, v223
	global_store_dwordx4 v[16:17], v[216:219], off offset:256
	s_nop 1
	v_lshl_add_u64 v[8:9], s[62:63], 0, v[12:13]
	s_nop 0
	v_lshl_add_u64 v[12:13], s[6:7], 0, v[12:13]
	s_nop 0
	v_lshlrev_b32_e32 v14, 16, v224
	v_and_b32_e32 v15, 0xffff0000, v224
	v_lshlrev_b32_e32 v224, 16, v225
	v_and_b32_e32 v225, 0xffff0000, v225
	v_pk_add_f32 v[16:17], v[114:115], v[224:225]
	v_pk_add_f32 v[224:225], v[112:113], v[14:15]
	v_lshlrev_b32_e32 v14, 16, v226
	v_and_b32_e32 v15, 0xffff0000, v226
	v_lshlrev_b32_e32 v226, 16, v227
	v_and_b32_e32 v227, 0xffff0000, v227
	v_pk_add_f32 v[18:19], v[110:111], v[226:227]
	v_pk_add_f32 v[226:227], v[108:109], v[14:15]
	v_cvt_pk_bf16_f32 v224, v224, v225
	v_cvt_pk_bf16_f32 v225, v16, v17
	s_nop 0
	v_cvt_pk_bf16_f32 v226, v226, v227
	v_cvt_pk_bf16_f32 v227, v18, v19
	global_store_dwordx4 v[12:13], v[224:227], off
	s_nop 0
	s_nop 0
	v_lshlrev_b32_e32 v224, 16, v228
	v_and_b32_e32 v225, 0xffff0000, v228
	v_lshlrev_b32_e32 v226, 16, v229
	v_and_b32_e32 v227, 0xffff0000, v229
	v_pk_add_f32 v[226:227], v[106:107], v[226:227]
	v_pk_add_f32 v[224:225], v[104:105], v[224:225]
	v_lshlrev_b32_e32 v228, 16, v230
	v_and_b32_e32 v229, 0xffff0000, v230
	v_lshlrev_b32_e32 v230, 16, v231
	v_and_b32_e32 v231, 0xffff0000, v231
	v_pk_add_f32 v[230:231], v[102:103], v[230:231]
	v_pk_add_f32 v[228:229], v[100:101], v[228:229]
	v_cvt_pk_bf16_f32 v224, v224, v225
	v_cvt_pk_bf16_f32 v225, v226, v227
	s_nop 0
	v_cvt_pk_bf16_f32 v226, v228, v229
	v_cvt_pk_bf16_f32 v227, v230, v231
	global_store_dwordx4 v[12:13], v[224:227], off offset:256
	v_lshl_add_u64 v[12:13], v[0:1], 0, s[18:19]
	v_lshl_add_u64 v[8:9], s[62:63], 0, v[12:13]
	s_nop 0
	v_lshl_add_u64 v[12:13], s[6:7], 0, v[12:13]
	s_mov_b64 s[18:19], 0x90000
	s_nop 0
	v_lshlrev_b32_e32 v14, 16, v232
	v_and_b32_e32 v15, 0xffff0000, v232
	v_lshlrev_b32_e32 v232, 16, v233
	v_and_b32_e32 v233, 0xffff0000, v233
	v_pk_add_f32 v[16:17], v[98:99], v[232:233]
	v_pk_add_f32 v[232:233], v[96:97], v[14:15]
	v_lshlrev_b32_e32 v14, 16, v234
	v_and_b32_e32 v15, 0xffff0000, v234
	v_lshlrev_b32_e32 v234, 16, v235
	v_and_b32_e32 v235, 0xffff0000, v235
	v_pk_add_f32 v[18:19], v[94:95], v[234:235]
	v_pk_add_f32 v[234:235], v[92:93], v[14:15]
	v_cvt_pk_bf16_f32 v232, v232, v233
	v_cvt_pk_bf16_f32 v233, v16, v17
	s_nop 0
	v_cvt_pk_bf16_f32 v234, v234, v235
	v_cvt_pk_bf16_f32 v235, v18, v19
	global_store_dwordx4 v[12:13], v[232:235], off
	s_nop 0
	s_nop 0
	v_lshlrev_b32_e32 v232, 16, v236
	v_and_b32_e32 v233, 0xffff0000, v236
	v_lshlrev_b32_e32 v234, 16, v237
	v_and_b32_e32 v235, 0xffff0000, v237
	v_pk_add_f32 v[234:235], v[90:91], v[234:235]
	v_pk_add_f32 v[232:233], v[88:89], v[232:233]
	v_lshlrev_b32_e32 v236, 16, v238
	v_and_b32_e32 v237, 0xffff0000, v238
	v_lshlrev_b32_e32 v238, 16, v239
	v_and_b32_e32 v239, 0xffff0000, v239
	v_pk_add_f32 v[238:239], v[86:87], v[238:239]
	v_pk_add_f32 v[236:237], v[84:85], v[236:237]
	v_cvt_pk_bf16_f32 v232, v232, v233
	v_cvt_pk_bf16_f32 v233, v234, v235
	s_nop 0
	v_cvt_pk_bf16_f32 v234, v236, v237
	v_cvt_pk_bf16_f32 v235, v238, v239
	global_store_dwordx4 v[12:13], v[232:235], off offset:256
; __device__ __forceinline__ float bflo(unsigned x) { return __uint_as_float(x << 16); }
; __device__ __forceinline__ float bfhi(unsigned x) { return __uint_as_float(x & 0xffff0000u); }
; __device__ __forceinline__ unsigned cvtpk(float lo, float hi) { unsigned r; asm volatile("v_cvt_pk_bf16_f32 %0, %1, %2" : "=v"(r) : "v"(lo), "v"(hi)); return r; }
;     __device__ __forceinline__ void operator()(const f32x4 (&acc)[2][2][4][2], const Unit& u, int wr, int wc, int fr, int fq) const {
;     ...
;         if constexpr (PLAIN) {
; #pragma unroll
;             for (int ai = 0; ai < 2; ++ai)
; #pragma unroll
;                 for (int m = 0; m < 4; ++m) { const size_t off = (size_t)(row0 + ai * HALF + m * 16) * ldc + col0;
;                     const u32x4 ra = *(const u32x4*)((const bf16_t*)res + off), rb = *(const u32x4*)((const bf16_t*)res + off + HALF);
; #pragma unroll
;                     for (int bj = 0; bj < 2; ++bj) { const u32x4 w_ = bj ? rb : ra; const f32x4 v0 = (f32x4){bflo(w_.x), bfhi(w_.x), bflo(w_.y), bfhi(w_.y)} + acc[ai][bj][m][0], v1 = (f32x4){bflo(w_.z), bfhi(w_.z), bflo(w_.w), bfhi(w_.w)} + acc[ai][bj][m][1];
;                         u32x4 w; w.x = cvtpk(v0[0], v0[1]); w.y = cvtpk(v0[2], v0[3]); w.z = cvtpk(v1[0], v1[1]); w.w = cvtpk(v1[2], v1[3]);
;                         *(u32x4*)(out + off + bj * HALF) = w; }
;                     asm volatile("" ::: "memory"); }
;             return; }
	v_lshl_add_u64 v[12:13], v[0:1], 0, s[18:19]
	v_lshl_add_u64 v[8:9], s[62:63], 0, v[12:13]
	s_nop 0
	v_lshl_add_u64 v[12:13], s[6:7], 0, v[12:13]
	s_mov_b64 s[18:19], 0xa0000
	s_nop 0
	v_lshlrev_b32_e32 v14, 16, v240
	v_and_b32_e32 v15, 0xffff0000, v240
	v_lshlrev_b32_e32 v240, 16, v241
	v_and_b32_e32 v241, 0xffff0000, v241
	v_pk_add_f32 v[16:17], v[82:83], v[240:241]
	v_pk_add_f32 v[240:241], v[80:81], v[14:15]
	v_lshlrev_b32_e32 v14, 16, v242
	v_and_b32_e32 v15, 0xffff0000, v242
	v_lshlrev_b32_e32 v242, 16, v243
	v_and_b32_e32 v243, 0xffff0000, v243
	v_pk_add_f32 v[18:19], v[78:79], v[242:243]
	v_pk_add_f32 v[242:243], v[76:77], v[14:15]
	v_cvt_pk_bf16_f32 v240, v240, v241
	v_cvt_pk_bf16_f32 v241, v16, v17
	s_nop 0
	v_cvt_pk_bf16_f32 v242, v242, v243
	v_cvt_pk_bf16_f32 v243, v18, v19
	global_store_dwordx4 v[12:13], v[240:243], off
	s_nop 0
	s_nop 0
	v_lshlrev_b32_e32 v240, 16, v244
	v_and_b32_e32 v241, 0xffff0000, v244
	v_lshlrev_b32_e32 v242, 16, v245
	v_and_b32_e32 v243, 0xffff0000, v245
	v_pk_add_f32 v[242:243], v[74:75], v[242:243]
	v_pk_add_f32 v[240:241], v[72:73], v[240:241]
	v_lshlrev_b32_e32 v244, 16, v246
	v_and_b32_e32 v245, 0xffff0000, v246
	v_lshlrev_b32_e32 v246, 16, v247
	v_and_b32_e32 v247, 0xffff0000, v247
	v_pk_add_f32 v[246:247], v[70:71], v[246:247]
	v_pk_add_f32 v[244:245], v[68:69], v[244:245]
	v_cvt_pk_bf16_f32 v240, v240, v241
	v_cvt_pk_bf16_f32 v241, v242, v243
	s_nop 0
	v_cvt_pk_bf16_f32 v242, v244, v245
	v_cvt_pk_bf16_f32 v243, v246, v247
	global_store_dwordx4 v[12:13], v[240:243], off offset:256
	v_lshl_add_u64 v[12:13], v[0:1], 0, s[18:19]
	v_lshl_add_u64 v[8:9], s[62:63], 0, v[12:13]
	s_nop 0
	v_lshl_add_u64 v[12:13], s[6:7], 0, v[12:13]
	s_mov_b64 s[18:19], 0xb0000
	v_lshl_add_u64 v[0:1], v[0:1], 0, s[18:19]
	s_mov_b64 s[18:19], -1
	s_nop 0
	v_lshlrev_b32_e32 v14, 16, v24
	v_and_b32_e32 v15, 0xffff0000, v24
	v_lshlrev_b32_e32 v24, 16, v25
	v_and_b32_e32 v25, 0xffff0000, v25
	v_pk_add_f32 v[16:17], v[66:67], v[24:25]
	v_pk_add_f32 v[24:25], v[64:65], v[14:15]
	v_lshlrev_b32_e32 v14, 16, v26
	v_and_b32_e32 v15, 0xffff0000, v26
	v_lshlrev_b32_e32 v26, 16, v27
	v_and_b32_e32 v27, 0xffff0000, v27
	v_pk_add_f32 v[18:19], v[62:63], v[26:27]
	v_pk_add_f32 v[26:27], v[60:61], v[14:15]
	v_cvt_pk_bf16_f32 v24, v24, v25
	v_cvt_pk_bf16_f32 v25, v16, v17
	s_nop 0
	v_cvt_pk_bf16_f32 v26, v26, v27
	v_cvt_pk_bf16_f32 v27, v18, v19
	global_store_dwordx4 v[12:13], v[24:27], off
	s_nop 0
	s_nop 0
	v_lshlrev_b32_e32 v24, 16, v28
	v_and_b32_e32 v25, 0xffff0000, v28
	v_lshlrev_b32_e32 v26, 16, v29
	v_and_b32_e32 v27, 0xffff0000, v29
	v_pk_add_f32 v[26:27], v[58:59], v[26:27]
	v_pk_add_f32 v[24:25], v[56:57], v[24:25]
	v_lshlrev_b32_e32 v28, 16, v30
	v_and_b32_e32 v29, 0xffff0000, v30
	v_lshlrev_b32_e32 v30, 16, v31
	v_and_b32_e32 v31, 0xffff0000, v31
	v_pk_add_f32 v[30:31], v[54:55], v[30:31]
	v_pk_add_f32 v[28:29], v[52:53], v[28:29]
	v_cvt_pk_bf16_f32 v24, v24, v25
	v_cvt_pk_bf16_f32 v25, v26, v27
	s_nop 0
	v_cvt_pk_bf16_f32 v26, v28, v29
	v_cvt_pk_bf16_f32 v27, v30, v31
	global_store_dwordx4 v[12:13], v[24:27], off offset:256
	v_lshl_add_u64 v[8:9], s[62:63], 0, v[0:1]
	s_nop 0
	v_lshl_add_u64 v[0:1], s[6:7], 0, v[0:1]
	s_nop 0
	v_lshlrev_b32_e32 v12, 16, v196
	v_and_b32_e32 v13, 0xffff0000, v196
	v_lshlrev_b32_e32 v196, 16, v197
	v_and_b32_e32 v197, 0xffff0000, v197
	v_pk_add_f32 v[14:15], v[50:51], v[196:197]
	v_pk_add_f32 v[196:197], v[48:49], v[12:13]
	v_lshlrev_b32_e32 v12, 16, v198
	v_and_b32_e32 v13, 0xffff0000, v198
	v_lshlrev_b32_e32 v198, 16, v199
	v_and_b32_e32 v199, 0xffff0000, v199
	v_pk_add_f32 v[16:17], v[46:47], v[198:199]
	v_pk_add_f32 v[198:199], v[44:45], v[12:13]
	v_cvt_pk_bf16_f32 v196, v196, v197
	v_cvt_pk_bf16_f32 v197, v14, v15
	s_nop 0
	v_cvt_pk_bf16_f32 v198, v198, v199
	v_cvt_pk_bf16_f32 v199, v16, v17
	global_store_dwordx4 v[0:1], v[196:199], off
	s_nop 0
	s_nop 0
	v_lshlrev_b32_e32 v196, 16, v180
	v_and_b32_e32 v197, 0xffff0000, v180
	v_lshlrev_b32_e32 v198, 16, v181
	v_and_b32_e32 v199, 0xffff0000, v181
	v_pk_add_f32 v[198:199], v[42:43], v[198:199]
	v_pk_add_f32 v[196:197], v[40:41], v[196:197]
	v_lshlrev_b32_e32 v180, 16, v182
	v_and_b32_e32 v181, 0xffff0000, v182
	v_lshlrev_b32_e32 v182, 16, v183
	v_and_b32_e32 v183, 0xffff0000, v183
	v_pk_add_f32 v[182:183], v[38:39], v[182:183]
	v_pk_add_f32 v[180:181], v[36:37], v[180:181]
	v_cvt_pk_bf16_f32 v196, v196, v197
	v_cvt_pk_bf16_f32 v197, v198, v199
	s_nop 0
	v_cvt_pk_bf16_f32 v198, v180, v181
	v_cvt_pk_bf16_f32 v199, v182, v183
	global_store_dwordx4 v[0:1], v[196:199], off offset:256
	s_cbranch_vccnz .LBB0_2578
	s_andn2_b64 vcc, exec, s[4:5]
	s_cbranch_vccnz .LBB0_2577
	s_barrier
	s_branch .LBB0_2577

; __device__ __forceinline__ int lane_id() { int l_; asm volatile("v_mbcnt_lo_u32_b32 %0, -1, 0\n\tv_mbcnt_hi_u32_b32 %0, -1, %0" : "=v"(l_)); return l_; }
;     ...
;     int tid = w0_ * 64 + lane_id(); asm volatile("" : "+v"(tid));
;     const int wid = __builtin_amdgcn_readfirstlane(tid >> 6), lane = tid & 63, wr = wid >> 2, wc = wid & 3, fr = lane & 15, fq = lane >> 4;
;     const int nt = nt_ ? nt_ : Kb / 128;
;     unsigned voffA[2], voffB[2];
; #pragma unroll
;     for (int i = 0; i < 2; ++i) { int R, C; stage_rc(tid * 16 + i * 8192, R, C); const int Rb = Epi::PERM ? ((R & ~31) + perm32(R & 31)) : R;
;         voffA[i] = (unsigned)(R * ldab + C * 2); voffB[i] = (unsigned)(Rb * Kb + C * 2); }
;     const size_t kstep = (size_t)(BK * 2);
;     const size_t hstepA = (size_t)HALF * ldab, hstepB = (size_t)HALF * Kb;
;     const unsigned ldsw = (unsigned)wid * 1024u, ldsbase = (unsigned)(size_t)lds;
;     const int aoff = lds_byte(wr * 64 + fr, fq * 8), boff = lds_byte(wc * 32 + fr, fq * 8);
;     ...
;     Unit cur, nxt; int ui = 0;
;     if (!S.next(0, cur)) return;
;     f32x4 acc[2][2][4][2];
; #pragma unroll
;     for (int a = 0; a < 2; ++a)
; #pragma unroll
;         for (int b = 0; b < 2; ++b)
; #pragma unroll
;             for (int m = 0; m < 4; ++m)
; #pragma unroll
;                 for (int n = 0; n < 2; ++n) acc[a][b][m][n] = (f32x4){0.f, 0.f, 0.f, 0.f};
;     bf16x8 At[4][2], B0[2][2], B1[2][2];
;     const char* cA = uniform_ptr(cur.a); const char* cB = uniform_ptr(cur.b);
;     PG8_STAGE(PG8_SB(0, 0), cB, voffB); PG8_STAGE(PG8_SB(0, 1), cB + hstepB, voffB); PG8_STAGE(PG8_SA(0, 0), cA, voffA); PG8_STAGE(PG8_SA(0, 1), cA + hstepA, voffA);
;     if (wr == 1) PG8_BAR;
;     PG8_WAIT_V(2); PG8_BAR;
;     PG8_STAGE(PG8_SB(1, 0), cB + kstep, voffB); PG8_STAGE(PG8_SA(1, 0), cA + kstep, voffA); PG8_STAGE(PG8_SB(1, 1), cB + hstepB + kstep, voffB);
;     PG8_WAIT_V(6); PG8_BAR;
; __global__ void __launch_bounds__(512, 2) fwd(Args args) {
;     ...
;             pg8::SimpleSched S; S.o.init(T / 256, 8, G, bx); S.A = (const char*)(act + A_AO); S.Bt = (const char*)(ws + WS_WOUT + l * SZ_WOUT); S.astep = (size_t)256 * 2048 * 2; S.bstep = (size_t)256 * 2048;
;             if (l == 0) { pg8::EpiResBf16<true> E{(const void*)args.in[I_X], (bf16_t*)(ws + WS_XA), D, (float*)(ws + WS_SS)}; pg8::gemm_phase<true>(lds, 2048, 4096, S, E, w0, 123, 121); }
.LBB0_2597:
	s_and_b64 vcc, exec, s[2:3]
	s_cbranch_vccnz .LBB0_2633
	v_bfe_i32 v4, v0, 27, 1
	v_lshlrev_b32_e32 v1, 4, v0
	v_lshrrev_b32_e32 v4, 22, v4
	v_add_u32_e32 v4, v1, v4
	v_and_b32_e32 v4, 0xfffffc00, v4
	v_sub_u32_e32 v4, v1, v4
	v_ashrrev_i32_e32 v2, 31, v0
	v_lshrrev_b32_e32 v5, 4, v4
	v_lshrrev_b32_e32 v2, 26, v2
	v_bitop3_b32 v4, v5, v4, 32 bitop3:0x6c
	v_add_u32_e32 v2, v0, v2
	v_ashrrev_i32_e32 v6, 31, v4
	v_ashrrev_i32_e32 v2, 6, v2
	v_lshrrev_b32_e32 v6, 26, v6
	v_lshlrev_b32_e32 v5, 3, v2
	v_add_u32_e32 v6, v4, v6
	v_and_b32_e32 v5, -16, v5
	v_ashrrev_i32_e32 v7, 6, v6
	v_and_b32_e32 v6, 0xc0, v6
	v_add_u32_e32 v5, v7, v5
	v_sub_u32_e32 v4, v4, v6
	v_lshlrev_b32_e32 v2, 5, v2
	v_ashrrev_i16_sdwa v4, v188, sext(v4) dst_sel:DWORD dst_unused:UNUSED_PAD src0_sel:DWORD src1_sel:BYTE_0
	v_lshlrev_b32_e32 v6, 1, v5
	v_lshrrev_b32_e32 v8, 2, v5
	v_and_b32_e32 v7, 3, v7
	s_mov_b32 s3, 0x1fffe0
	v_and_b32_e32 v2, 32, v2
	v_bfe_i32 v4, v4, 0, 16
	v_and_b32_e32 v6, 24, v6
	v_and_b32_e32 v8, 4, v8
	v_and_or_b32 v7, v5, s3, v7
	v_or3_b32 v6, v7, v8, v6
	v_add_lshl_u32 v4, v2, v4, 1
	v_add_u32_e32 v1, 0x2000, v1
	v_lshl_add_u32 v2, v5, 12, v4
	v_lshl_add_u32 v164, v6, 11, v4
	v_ashrrev_i32_e32 v4, 31, v1
	v_lshrrev_b32_e32 v4, 22, v4
	v_add_u32_e32 v4, v1, v4
	v_ashrrev_i32_e32 v4, 10, v4
	v_mul_i32_i24_e32 v5, 0x400, v4
	v_sub_u32_e32 v1, v1, v5
	v_lshrrev_b32_e32 v5, 4, v1
	v_bitop3_b32 v1, v5, v1, 32 bitop3:0x6c
	v_ashrrev_i32_e32 v6, 31, v1
	v_lshrrev_b32_e32 v6, 26, v6
	v_lshlrev_b32_e32 v5, 3, v4
	v_add_u32_e32 v6, v1, v6
	v_and_b32_e32 v5, -16, v5
	v_ashrrev_i32_e32 v7, 6, v6
	v_and_b32_e32 v6, 0xc0, v6
	s_ashr_i32 s2, s4, 6
	v_add_u32_e32 v5, v7, v5
	v_sub_u32_e32 v1, v1, v6
	v_lshlrev_b32_e32 v4, 5, v4
	v_ashrrev_i16_sdwa v1, v188, sext(v1) dst_sel:DWORD dst_unused:UNUSED_PAD src0_sel:DWORD src1_sel:BYTE_0
	v_lshlrev_b32_e32 v6, 1, v5
	v_lshrrev_b32_e32 v8, 2, v5
	v_and_b32_e32 v7, 3, v7
	s_lshl_b32 s5, s2, 10
	v_and_b32_e32 v4, 32, v4
	v_bfe_i32 v1, v1, 0, 16
	v_and_b32_e32 v6, 24, v6
	v_and_b32_e32 v8, 4, v8
	v_and_or_b32 v7, v5, s3, v7
	s_add_i32 s36, s5, 0
	v_or3_b32 v6, v7, v8, v6
	v_add_lshl_u32 v1, v4, v1, 1
	s_ashr_i32 s3, s4, 8
	s_add_i32 s37, s36, 0x10000
	s_mov_b32 m0, s37
	s_nop 0
	global_load_lds_dwordx4 v164, s[24:25]
	s_add_i32 s38, s36, 0x12000
	v_lshl_add_u32 v166, v6, 11, v1
	s_mov_b32 m0, s38
	s_nop 0
	global_load_lds_dwordx4 v166, s[24:25]
	s_add_u32 s8, s24, 0x40000
	s_addc_u32 s9, s25, 0
	s_add_i32 s39, s36, 0x14000
	s_mov_b32 m0, s39
	s_nop 0
	global_load_lds_dwordx4 v164, s[8:9]
	s_add_i32 s40, s36, 0x16000
	s_mov_b32 m0, s40
	s_nop 0
	global_load_lds_dwordx4 v166, s[8:9]
	s_add_i32 s41, s36, 0x2000
	s_mov_b32 m0, s36
	s_nop 0
	global_load_lds_dwordx4 v2, s[22:23]
	v_lshl_add_u32 v165, v5, 12, v1
	s_mov_b32 m0, s41
	s_nop 0
	global_load_lds_dwordx4 v165, s[22:23]
	s_add_u32 s8, s22, 0x80000
	s_addc_u32 s9, s23, 0
	s_add_i32 s42, s36, 0x4000
	s_mov_b32 m0, s42
	s_nop 0
	global_load_lds_dwordx4 v2, s[8:9]
	s_add_i32 s43, s36, 0x6000
	s_mov_b32 m0, s43
	s_nop 0
	global_load_lds_dwordx4 v165, s[8:9]
	s_cmp_eq_u32 s3, 1
	s_cselect_b64 s[8:9], -1, 0
	s_cmp_lg_u32 s3, 1
	s_cbranch_scc1 .LBB0_2600
	s_barrier
.LBB0_2600:
	v_bfe_u32 v4, v0, 4, 2
	s_add_u32 s10, s0, 0x32682000
	v_and_b32_e32 v1, 15, v0
	v_lshlrev_b32_e32 v6, 4, v4
	v_lshlrev_b32_e32 v0, 2, v0
	s_addc_u32 s11, s26, 0
	s_and_b32 s44, s2, 3
	v_lshl_or_b32 v167, s3, 6, v1
	v_lshl_or_b32 v1, v1, 6, v6
	s_lshl_b32 s0, s3, 13
	v_and_b32_e32 v0, 32, v0
	v_bitop3_b32 v6, v1, s0, v0 bitop3:0xde
	s_lshl_b32 s0, s44, 12
	s_add_u32 s2, s24, 0x80
	v_bitop3_b32 v0, v1, s0, v0 bitop3:0xde
	s_waitcnt vmcnt(2)
	s_barrier
	s_addc_u32 s3, s25, 0
	s_add_i32 s45, s36, 0x18000
	s_mov_b32 m0, s45
	s_nop 0
	global_load_lds_dwordx4 v164, s[2:3]
	s_add_i32 s46, s36, 0x1a000
	s_mov_b32 m0, s46
	s_nop 0
	global_load_lds_dwordx4 v166, s[2:3]
	s_add_u32 s2, s22, 0x80
	s_addc_u32 s3, s23, 0
	s_add_i32 s47, s36, 0x8000
	s_mov_b32 m0, s47
	s_nop 0
	global_load_lds_dwordx4 v2, s[2:3]
	s_add_i32 s48, s36, 0xa000
	s_mov_b32 m0, s48
	s_nop 0
	global_load_lds_dwordx4 v165, s[2:3]
	s_add_u32 s2, s24, 0x40080
	s_addc_u32 s3, s25, 0
	s_add_i32 s49, s36, 0x1c000
	s_mov_b32 m0, s49
	s_nop 0
	global_load_lds_dwordx4 v164, s[2:3]
	s_add_i32 s50, s36, 0x1e000
	s_mov_b32 m0, s50
	s_nop 0
	global_load_lds_dwordx4 v166, s[2:3]
	s_waitcnt vmcnt(6)
	s_add_i32 s51, s36, 0xc000
	v_lshlrev_b32_e32 v5, 3, v4
	s_cmpk_lt_u32 s4, 0x100
	v_lshl_or_b32 v168, s44, 5, v5
	s_cselect_b64 s[12:13], -1, 0
	s_mov_b32 s52, 0
	v_cmp_eq_u32_e64 s[2:3], 0, v4
	s_add_i32 s53, s36, 0xe000
	v_add_u32_e32 v169, 0, v0
	v_add_u32_e32 v170, 0, v6
	s_mov_b64 s[18:19], s[22:23]
	s_mov_b64 s[20:21], s[24:25]
	s_barrier
	s_branch .LBB0_2603

; #define PG8_STAGE(bufoff, gbase, voff) do { _Pragma("unroll") for (int _i = 0; _i < 2; ++_i) \
;         glds16((const void*)(gbase), (voff)[_i], ldsbase + (unsigned)(bufoff) + ldsw + (unsigned)_i * 8192u); } while (0)
; #define PG8_LDA(dst, b, h) do { _Pragma("unroll") for (int m = 0; m < 4; ++m) _Pragma("unroll") for (int k = 0; k < 2; ++k) dst[m][k] = *(const LAS bf16x8*)(lds + PG8_SA(b, h) + aoff + m * 2048 + k * 1024); } while (0)
; #define PG8_LDB(dst, b, h) do { _Pragma("unroll") for (int n = 0; n < 2; ++n) _Pragma("unroll") for (int k = 0; k < 2; ++k) dst[n][k] = *(const LAS bf16x8*)(lds + PG8_SB(b, h) + boff + n * 2048 + k * 1024); } while (0)
; #define PG8_WAIT_V(n) asm volatile("s_waitcnt vmcnt(" #n ")" ::: "memory")
; #define PG8_WAIT_L(n) asm volatile("s_waitcnt lgkmcnt(" #n ")" ::: "memory")
; #define PG8_BAR __builtin_amdgcn_s_barrier()
; #define PG8_SCHED __builtin_amdgcn_sched_barrier(0)
;     ...
;             PG8_LDB(B0, 0, 0); PG8_LDB(B1, 0, 1); PG8_SCHED; PG8_LDA(At, 0, 0); PG8_STAGE(PG8_SA(1, 1), a1 + hstepA, voffA);
;             PG8_WAIT_V(8); PG8_WAIT_L(0); PG8_BAR; PG8_MMA(0, 0, At, B0); PG8_MMA(0, 1, At, B1); PG8_BAR; PG8_SCHED;
;             PG8_LDA(At, 0, 1); PG8_STAGE(PG8_SB(0, 0), b2, voffB); PG8_STAGE(PG8_SB(0, 1), b2 + hstepB, voffB); PG8_STAGE(PG8_SA(0, 0), a2, voffA);
;             PG8_WAIT_V(8); PG8_WAIT_L(0); PG8_BAR; PG8_MMA(1, 0, At, B0); PG8_MMA(1, 1, At, B1); PG8_BAR; PG8_SCHED;
.LBB0_2610:
	v_add_u32_e32 v0, 0x10000, v169
	ds_read_b128 v[28:31], v0
	ds_read_b128 v[32:35], v0 offset:1024
	ds_read_b128 v[20:23], v0 offset:2048
	ds_read_b128 v[24:27], v0 offset:3072
	v_add_u32_e32 v0, 0x14000, v169
	s_waitcnt lgkmcnt(4)
	ds_read_b128 v[12:15], v0
	ds_read_b128 v[16:19], v0 offset:1024
	ds_read_b128 v[4:7], v0 offset:2048
	ds_read_b128 v[8:11], v0 offset:3072
	s_add_u32 s24, s22, 0xfff80080
	s_addc_u32 s25, s23, -1
	s_cmp_eq_u32 s17, 12
	s_cselect_b32 s28, s18, s24
	s_cselect_b32 s29, s19, s25
	s_cselect_b32 s26, s20, s0
	s_cselect_b32 s27, s21, s15
	s_add_u32 s24, s28, 0x80
	s_addc_u32 s25, s29, 0
	ds_read_b128 v[176:179], v170
	ds_read_b128 v[180:183], v170 offset:1024
	ds_read_b128 v[206:209], v170 offset:2048
	ds_read_b128 v[210:213], v170 offset:3072
	ds_read_b128 v[214:217], v170 offset:4096
	ds_read_b128 v[218:221], v170 offset:5120
	ds_read_b128 v[222:225], v170 offset:6144
	ds_read_b128 v[226:229], v170 offset:7168
	s_mov_b32 m0, s51
	s_nop 0
	global_load_lds_dwordx4 v2, s[22:23]
	s_nop 0
	s_mov_b32 m0, s53
	s_nop 0
	global_load_lds_dwordx4 v165, s[22:23]
	s_waitcnt vmcnt(8)
	s_waitcnt lgkmcnt(0)
	s_barrier
	s_setprio 1
	s_waitcnt lgkmcnt(6)
	v_mfma_scale_f32_16x16x128_f8f6f4 v[160:163], v[28:35], v[176:183], v[160:163], v189, v190 op_sel_hi:[0,0,0]
	v_mfma_scale_f32_16x16x128_f8f6f4 v[156:159], v[20:27], v[176:183], v[156:159], v189, v190 op_sel_hi:[0,0,0]
	s_waitcnt lgkmcnt(4)
	v_mfma_scale_f32_16x16x128_f8f6f4 v[144:147], v[28:35], v[206:213], v[144:147], v189, v190 op_sel_hi:[0,0,0]
	v_mfma_scale_f32_16x16x128_f8f6f4 v[140:143], v[20:27], v[206:213], v[140:143], v189, v190 op_sel_hi:[0,0,0]
	s_waitcnt lgkmcnt(2)
	v_mfma_scale_f32_16x16x128_f8f6f4 v[128:131], v[28:35], v[214:221], v[128:131], v189, v190 op_sel_hi:[0,0,0]
	v_mfma_scale_f32_16x16x128_f8f6f4 v[124:127], v[20:27], v[214:221], v[124:127], v189, v190 op_sel_hi:[0,0,0]
	s_waitcnt lgkmcnt(0)
	v_mfma_scale_f32_16x16x128_f8f6f4 v[112:115], v[28:35], v[222:229], v[112:115], v189, v190 op_sel_hi:[0,0,0]
	v_mfma_scale_f32_16x16x128_f8f6f4 v[108:111], v[20:27], v[222:229], v[108:111], v189, v190 op_sel_hi:[0,0,0]
	s_setprio 0
	s_setprio 1
	v_mfma_scale_f32_16x16x128_f8f6f4 v[152:155], v[12:19], v[176:183], v[152:155], v189, v190 op_sel_hi:[0,0,0]
	v_mfma_scale_f32_16x16x128_f8f6f4 v[148:151], v[4:11], v[176:183], v[148:151], v189, v190 op_sel_hi:[0,0,0]
	v_mfma_scale_f32_16x16x128_f8f6f4 v[136:139], v[12:19], v[206:213], v[136:139], v189, v190 op_sel_hi:[0,0,0]
	v_mfma_scale_f32_16x16x128_f8f6f4 v[132:135], v[4:11], v[206:213], v[132:135], v189, v190 op_sel_hi:[0,0,0]
	v_mfma_scale_f32_16x16x128_f8f6f4 v[120:123], v[12:19], v[214:221], v[120:123], v189, v190 op_sel_hi:[0,0,0]
	v_mfma_scale_f32_16x16x128_f8f6f4 v[116:119], v[4:11], v[214:221], v[116:119], v189, v190 op_sel_hi:[0,0,0]
	v_mfma_scale_f32_16x16x128_f8f6f4 v[104:107], v[12:19], v[222:229], v[104:107], v189, v190 op_sel_hi:[0,0,0]
	v_mfma_scale_f32_16x16x128_f8f6f4 v[100:103], v[4:11], v[222:229], v[100:103], v189, v190 op_sel_hi:[0,0,0]
	s_setprio 0
	s_barrier
	ds_read_b128 v[176:179], v170 offset:16384
	ds_read_b128 v[180:183], v170 offset:17408
	ds_read_b128 v[206:209], v170 offset:18432
	ds_read_b128 v[210:213], v170 offset:19456
	ds_read_b128 v[214:217], v170 offset:20480
	ds_read_b128 v[218:221], v170 offset:21504
	ds_read_b128 v[222:225], v170 offset:22528
	ds_read_b128 v[226:229], v170 offset:23552
	s_mov_b32 m0, s37
	s_nop 0
	global_load_lds_dwordx4 v164, s[26:27]
	s_nop 0
	s_mov_b32 m0, s38
	s_nop 0
	global_load_lds_dwordx4 v166, s[26:27]
	s_add_u32 s56, s26, 0x40000
	s_addc_u32 s57, s27, 0
	s_mov_b32 m0, s39
	s_nop 0
	global_load_lds_dwordx4 v164, s[56:57]
	s_nop 0
	s_mov_b32 m0, s40
	s_nop 0
	global_load_lds_dwordx4 v166, s[56:57]
	s_mov_b32 m0, s36
	s_nop 0
	global_load_lds_dwordx4 v2, s[28:29]
	s_nop 0
	s_mov_b32 m0, s41
	s_nop 0
	global_load_lds_dwordx4 v165, s[28:29]
	s_waitcnt vmcnt(8)
	s_waitcnt lgkmcnt(0)
	s_barrier
	s_setprio 1
	s_waitcnt lgkmcnt(6)
	v_mfma_scale_f32_16x16x128_f8f6f4 v[96:99], v[28:35], v[176:183], v[96:99], v189, v190 op_sel_hi:[0,0,0]
	v_mfma_scale_f32_16x16x128_f8f6f4 v[92:95], v[20:27], v[176:183], v[92:95], v189, v190 op_sel_hi:[0,0,0]
	s_waitcnt lgkmcnt(4)
	v_mfma_scale_f32_16x16x128_f8f6f4 v[80:83], v[28:35], v[206:213], v[80:83], v189, v190 op_sel_hi:[0,0,0]
	v_mfma_scale_f32_16x16x128_f8f6f4 v[76:79], v[20:27], v[206:213], v[76:79], v189, v190 op_sel_hi:[0,0,0]
	s_waitcnt lgkmcnt(2)
	v_mfma_scale_f32_16x16x128_f8f6f4 v[64:67], v[28:35], v[214:221], v[64:67], v189, v190 op_sel_hi:[0,0,0]
	v_mfma_scale_f32_16x16x128_f8f6f4 v[60:63], v[20:27], v[214:221], v[60:63], v189, v190 op_sel_hi:[0,0,0]
	s_waitcnt lgkmcnt(0)
	v_mfma_scale_f32_16x16x128_f8f6f4 v[48:51], v[28:35], v[222:229], v[48:51], v189, v190 op_sel_hi:[0,0,0]
	v_mfma_scale_f32_16x16x128_f8f6f4 v[44:47], v[20:27], v[222:229], v[44:47], v189, v190 op_sel_hi:[0,0,0]
	s_setprio 0
	s_setprio 1
	v_mfma_scale_f32_16x16x128_f8f6f4 v[88:91], v[12:19], v[176:183], v[88:91], v189, v190 op_sel_hi:[0,0,0]
	v_mfma_scale_f32_16x16x128_f8f6f4 v[84:87], v[4:11], v[176:183], v[84:87], v189, v190 op_sel_hi:[0,0,0]
	v_mfma_scale_f32_16x16x128_f8f6f4 v[72:75], v[12:19], v[206:213], v[72:75], v189, v190 op_sel_hi:[0,0,0]
	v_mfma_scale_f32_16x16x128_f8f6f4 v[68:71], v[4:11], v[206:213], v[68:71], v189, v190 op_sel_hi:[0,0,0]
	v_mfma_scale_f32_16x16x128_f8f6f4 v[56:59], v[12:19], v[214:221], v[56:59], v189, v190 op_sel_hi:[0,0,0]
	v_mfma_scale_f32_16x16x128_f8f6f4 v[52:55], v[4:11], v[214:221], v[52:55], v189, v190 op_sel_hi:[0,0,0]
	v_mfma_scale_f32_16x16x128_f8f6f4 v[40:43], v[12:19], v[222:229], v[40:43], v189, v190 op_sel_hi:[0,0,0]
	v_mfma_scale_f32_16x16x128_f8f6f4 v[36:39], v[4:11], v[222:229], v[36:39], v189, v190 op_sel_hi:[0,0,0]
	s_setprio 0
	s_barrier
; #define PG8_STAGE(bufoff, gbase, voff) do { _Pragma("unroll") for (int _i = 0; _i < 2; ++_i) \
;         glds16((const void*)(gbase), (voff)[_i], ldsbase + (unsigned)(bufoff) + ldsw + (unsigned)_i * 8192u); } while (0)
; #define PG8_LDA(dst, b, h) do { _Pragma("unroll") for (int m = 0; m < 4; ++m) _Pragma("unroll") for (int k = 0; k < 2; ++k) dst[m][k] = *(const LAS bf16x8*)(lds + PG8_SA(b, h) + aoff + m * 2048 + k * 1024); } while (0)
; #define PG8_LDB(dst, b, h) do { _Pragma("unroll") for (int n = 0; n < 2; ++n) _Pragma("unroll") for (int k = 0; k < 2; ++k) dst[n][k] = *(const LAS bf16x8*)(lds + PG8_SB(b, h) + boff + n * 2048 + k * 1024); } while (0)
; #define PG8_WAIT_V(n) asm volatile("s_waitcnt vmcnt(" #n ")" ::: "memory")
; #define PG8_WAIT_L(n) asm volatile("s_waitcnt lgkmcnt(" #n ")" ::: "memory")
; #define PG8_BAR __builtin_amdgcn_s_barrier()
; #define PG8_SCHED __builtin_amdgcn_sched_barrier(0)
;     ...
;             PG8_LDB(B0, 1, 0); PG8_LDB(B1, 1, 1); PG8_SCHED; PG8_LDA(At, 1, 0); PG8_STAGE(PG8_SA(0, 1), a2 + hstepA, voffA);
;             PG8_WAIT_V(8); PG8_WAIT_L(0); PG8_BAR; PG8_MMA(0, 0, At, B0); PG8_MMA(0, 1, At, B1); PG8_BAR; PG8_SCHED;
;             PG8_LDA(At, 1, 1); PG8_STAGE(PG8_SB(1, 0), b3, voffB); PG8_STAGE(PG8_SB(1, 1), b3 + hstepB, voffB); PG8_STAGE(PG8_SA(1, 0), a3, voffA);
;             PG8_WAIT_V(8); PG8_WAIT_L(0); PG8_BAR; PG8_MMA(1, 0, At, B0); PG8_MMA(1, 1, At, B1); PG8_BAR; PG8_SCHED;
;         }
	v_add_u32_e32 v0, 0x18000, v169
	ds_read_b128 v[20:23], v0
	ds_read_b128 v[24:27], v0 offset:1024
	ds_read_b128 v[28:31], v0 offset:2048
	ds_read_b128 v[32:35], v0 offset:3072
	v_add_u32_e32 v0, 0x1c000, v169
	ds_read_b128 v[12:15], v0
	ds_read_b128 v[16:19], v0 offset:1024
	ds_read_b128 v[4:7], v0 offset:2048
	ds_read_b128 v[8:11], v0 offset:3072
	ds_read_b128 v[176:179], v170 offset:32768
	ds_read_b128 v[180:183], v170 offset:33792
	ds_read_b128 v[206:209], v170 offset:34816
	ds_read_b128 v[210:213], v170 offset:35840
	ds_read_b128 v[214:217], v170 offset:36864
	ds_read_b128 v[218:221], v170 offset:37888
	ds_read_b128 v[222:225], v170 offset:38912
	ds_read_b128 v[226:229], v170 offset:39936
	s_add_u32 s28, s28, 0x80000
	s_addc_u32 s29, s29, 0
	s_mov_b32 m0, s42
	s_nop 0
	global_load_lds_dwordx4 v2, s[28:29]
	s_nop 0
	s_mov_b32 m0, s43
	s_nop 0
	global_load_lds_dwordx4 v165, s[28:29]
	s_waitcnt vmcnt(8)
	s_waitcnt lgkmcnt(0)
	s_barrier
	s_setprio 1
	s_waitcnt lgkmcnt(6)
	v_mfma_scale_f32_16x16x128_f8f6f4 v[160:163], v[20:27], v[176:183], v[160:163], v189, v190 op_sel_hi:[0,0,0]
	v_mfma_scale_f32_16x16x128_f8f6f4 v[156:159], v[28:35], v[176:183], v[156:159], v189, v190 op_sel_hi:[0,0,0]
	s_waitcnt lgkmcnt(4)
	v_mfma_scale_f32_16x16x128_f8f6f4 v[144:147], v[20:27], v[206:213], v[144:147], v189, v190 op_sel_hi:[0,0,0]
	v_mfma_scale_f32_16x16x128_f8f6f4 v[140:143], v[28:35], v[206:213], v[140:143], v189, v190 op_sel_hi:[0,0,0]
	s_waitcnt lgkmcnt(2)
	v_mfma_scale_f32_16x16x128_f8f6f4 v[128:131], v[20:27], v[214:221], v[128:131], v189, v190 op_sel_hi:[0,0,0]
	v_mfma_scale_f32_16x16x128_f8f6f4 v[124:127], v[28:35], v[214:221], v[124:127], v189, v190 op_sel_hi:[0,0,0]
	s_waitcnt lgkmcnt(0)
	v_mfma_scale_f32_16x16x128_f8f6f4 v[112:115], v[20:27], v[222:229], v[112:115], v189, v190 op_sel_hi:[0,0,0]
	v_mfma_scale_f32_16x16x128_f8f6f4 v[108:111], v[28:35], v[222:229], v[108:111], v189, v190 op_sel_hi:[0,0,0]
	s_setprio 0
	s_setprio 1
	v_mfma_scale_f32_16x16x128_f8f6f4 v[152:155], v[12:19], v[176:183], v[152:155], v189, v190 op_sel_hi:[0,0,0]
	v_mfma_scale_f32_16x16x128_f8f6f4 v[148:151], v[4:11], v[176:183], v[148:151], v189, v190 op_sel_hi:[0,0,0]
	v_mfma_scale_f32_16x16x128_f8f6f4 v[136:139], v[12:19], v[206:213], v[136:139], v189, v190 op_sel_hi:[0,0,0]
	v_mfma_scale_f32_16x16x128_f8f6f4 v[132:135], v[4:11], v[206:213], v[132:135], v189, v190 op_sel_hi:[0,0,0]
	v_mfma_scale_f32_16x16x128_f8f6f4 v[120:123], v[12:19], v[214:221], v[120:123], v189, v190 op_sel_hi:[0,0,0]
	v_mfma_scale_f32_16x16x128_f8f6f4 v[116:119], v[4:11], v[214:221], v[116:119], v189, v190 op_sel_hi:[0,0,0]
	v_mfma_scale_f32_16x16x128_f8f6f4 v[104:107], v[12:19], v[222:229], v[104:107], v189, v190 op_sel_hi:[0,0,0]
	v_mfma_scale_f32_16x16x128_f8f6f4 v[100:103], v[4:11], v[222:229], v[100:103], v189, v190 op_sel_hi:[0,0,0]
	s_setprio 0
	s_barrier
	ds_read_b128 v[176:179], v170 offset:49152
	ds_read_b128 v[180:183], v170 offset:50176
	ds_read_b128 v[206:209], v170 offset:51200
	ds_read_b128 v[210:213], v170 offset:52224
	ds_read_b128 v[214:217], v170 offset:53248
	ds_read_b128 v[218:221], v170 offset:54272
	ds_read_b128 v[222:225], v170 offset:55296
	ds_read_b128 v[226:229], v170 offset:56320
	s_add_u32 s28, s26, 0x80
	s_addc_u32 s29, s27, 0
	s_mov_b32 m0, s45
	s_nop 0
	global_load_lds_dwordx4 v164, s[28:29]
	s_add_u32 s26, s26, 0x40080
	s_mov_b32 m0, s46
	s_nop 0
	global_load_lds_dwordx4 v166, s[28:29]
	s_addc_u32 s27, s27, 0
	s_mov_b32 m0, s49
	s_nop 0
	global_load_lds_dwordx4 v164, s[26:27]
	s_nop 0
	s_mov_b32 m0, s50
	s_nop 0
	global_load_lds_dwordx4 v166, s[26:27]
	s_mov_b32 m0, s47
	s_nop 0
	global_load_lds_dwordx4 v2, s[24:25]
	s_nop 0
	s_mov_b32 m0, s48
	s_nop 0
	global_load_lds_dwordx4 v165, s[24:25]
	s_waitcnt vmcnt(8)
	s_waitcnt lgkmcnt(0)
	s_barrier
	s_setprio 1
	s_waitcnt lgkmcnt(6)
	v_mfma_scale_f32_16x16x128_f8f6f4 v[96:99], v[20:27], v[176:183], v[96:99], v189, v190 op_sel_hi:[0,0,0]
	v_mfma_scale_f32_16x16x128_f8f6f4 v[92:95], v[28:35], v[176:183], v[92:95], v189, v190 op_sel_hi:[0,0,0]
	s_waitcnt lgkmcnt(4)
	v_mfma_scale_f32_16x16x128_f8f6f4 v[80:83], v[20:27], v[206:213], v[80:83], v189, v190 op_sel_hi:[0,0,0]
	v_mfma_scale_f32_16x16x128_f8f6f4 v[76:79], v[28:35], v[206:213], v[76:79], v189, v190 op_sel_hi:[0,0,0]
	s_waitcnt lgkmcnt(2)
	v_mfma_scale_f32_16x16x128_f8f6f4 v[64:67], v[20:27], v[214:221], v[64:67], v189, v190 op_sel_hi:[0,0,0]
	v_mfma_scale_f32_16x16x128_f8f6f4 v[60:63], v[28:35], v[214:221], v[60:63], v189, v190 op_sel_hi:[0,0,0]
	s_waitcnt lgkmcnt(0)
	v_mfma_scale_f32_16x16x128_f8f6f4 v[48:51], v[20:27], v[222:229], v[48:51], v189, v190 op_sel_hi:[0,0,0]
	v_mfma_scale_f32_16x16x128_f8f6f4 v[44:47], v[28:35], v[222:229], v[44:47], v189, v190 op_sel_hi:[0,0,0]
	s_setprio 0
	s_setprio 1
	v_mfma_scale_f32_16x16x128_f8f6f4 v[88:91], v[12:19], v[176:183], v[88:91], v189, v190 op_sel_hi:[0,0,0]
	v_mfma_scale_f32_16x16x128_f8f6f4 v[84:87], v[4:11], v[176:183], v[84:87], v189, v190 op_sel_hi:[0,0,0]
	v_mfma_scale_f32_16x16x128_f8f6f4 v[72:75], v[12:19], v[206:213], v[72:75], v189, v190 op_sel_hi:[0,0,0]
	v_mfma_scale_f32_16x16x128_f8f6f4 v[68:71], v[4:11], v[206:213], v[68:71], v189, v190 op_sel_hi:[0,0,0]
	v_mfma_scale_f32_16x16x128_f8f6f4 v[56:59], v[12:19], v[214:221], v[56:59], v189, v190 op_sel_hi:[0,0,0]
	v_mfma_scale_f32_16x16x128_f8f6f4 v[52:55], v[4:11], v[214:221], v[52:55], v189, v190 op_sel_hi:[0,0,0]
	v_mfma_scale_f32_16x16x128_f8f6f4 v[40:43], v[12:19], v[222:229], v[40:43], v189, v190 op_sel_hi:[0,0,0]
	v_mfma_scale_f32_16x16x128_f8f6f4 v[36:39], v[4:11], v[222:229], v[36:39], v189, v190 op_sel_hi:[0,0,0]
	s_setprio 0
	s_barrier
	s_add_i32 s17, s17, 2
	s_add_u32 s0, s0, 0x100
	s_addc_u32 s15, s15, 0
	s_add_u32 s22, s22, 0x100
	s_addc_u32 s23, s23, 0
	s_cmp_gt_u32 s17, 13
	s_cbranch_scc0 .LBB0_2610
	s_and_b64 vcc, exec, s[12:13]
	s_cbranch_vccz .LBB0_2613
	s_barrier

; __device__ __forceinline__ int lane_id() { int l_; asm volatile("v_mbcnt_lo_u32_b32 %0, -1, 0\n\tv_mbcnt_hi_u32_b32 %0, -1, %0" : "=v"(l_)); return l_; }
; #define PG8_STAGE(bufoff, gbase, voff) do { _Pragma("unroll") for (int _i = 0; _i < 2; ++_i) \
;         glds16((const void*)(gbase), (voff)[_i], ldsbase + (unsigned)(bufoff) + ldsw + (unsigned)_i * 8192u); } while (0)
; #define PG8_WAIT_V(n) asm volatile("s_waitcnt vmcnt(" #n ")" ::: "memory")
; #define PG8_BAR __builtin_amdgcn_s_barrier()
;     ...
;     int tid = w0_ * 64 + lane_id(); asm volatile("" : "+v"(tid));
;     const int wid = __builtin_amdgcn_readfirstlane(tid >> 6), lane = tid & 63, wr = wid >> 2, wc = wid & 3, fr = lane & 15, fq = lane >> 4;
;     const int nt = nt_ ? nt_ : Kb / 128;
;     unsigned voffA[2], voffB[2];
; #pragma unroll
;     for (int i = 0; i < 2; ++i) { int R, C; stage_rc(tid * 16 + i * 8192, R, C); const int Rb = Epi::PERM ? ((R & ~31) + perm32(R & 31)) : R;
;         voffA[i] = (unsigned)(R * ldab + C * 2); voffB[i] = (unsigned)(Rb * Kb + C * 2); }
;     const size_t kstep = (size_t)(BK * 2);
;     const size_t hstepA = (size_t)HALF * ldab, hstepB = (size_t)HALF * Kb;
;     const unsigned ldsw = (unsigned)wid * 1024u, ldsbase = (unsigned)(size_t)lds;
;     const int aoff = lds_byte(wr * 64 + fr, fq * 8), boff = lds_byte(wc * 32 + fr, fq * 8);
;     ...
;     Unit cur, nxt; int ui = 0;
;     if (!S.next(0, cur)) return;
;     f32x4 acc[2][2][4][2];
; #pragma unroll
;     for (int a = 0; a < 2; ++a)
; #pragma unroll
;         for (int b = 0; b < 2; ++b)
; #pragma unroll
;             for (int m = 0; m < 4; ++m)
; #pragma unroll
;                 for (int n = 0; n < 2; ++n) acc[a][b][m][n] = (f32x4){0.f, 0.f, 0.f, 0.f};
;     bf16x8 At[4][2], B0[2][2], B1[2][2];
;     const char* cA = uniform_ptr(cur.a); const char* cB = uniform_ptr(cur.b);
;     PG8_STAGE(PG8_SB(0, 0), cB, voffB); PG8_STAGE(PG8_SB(0, 1), cB + hstepB, voffB); PG8_STAGE(PG8_SA(0, 0), cA, voffA); PG8_STAGE(PG8_SA(0, 1), cA + hstepA, voffA);
;     if (wr == 1) PG8_BAR;
;     PG8_WAIT_V(2); PG8_BAR;
;     PG8_STAGE(PG8_SB(1, 0), cB + kstep, voffB); PG8_STAGE(PG8_SA(1, 0), cA + kstep, voffA); PG8_STAGE(PG8_SB(1, 1), cB + hstepB + kstep, voffB);
;     PG8_WAIT_V(6); PG8_BAR;
.LBB0_2837:
	s_or_b64 exec, exec, s[4:5]
	s_waitcnt lgkmcnt(0)
	s_barrier
	v_mbcnt_lo_u32_b32 v0, -1, 0
	v_mbcnt_hi_u32_b32 v0, -1, v0
	v_readlane_b32 s5, v250, 60
	s_mul_i32 s4, s0, 56
	s_cmp_ge_i32 s78, s4
	v_add_u32_e32 v0, s5, v0
	s_nop 0
	v_readfirstlane_b32 s12, v0
	s_cbranch_scc1 .LBB0_2853
	v_bfe_i32 v4, v0, 27, 1
	v_lshlrev_b32_e32 v1, 4, v0
	v_lshrrev_b32_e32 v4, 22, v4
	v_add_u32_e32 v4, v1, v4
	v_and_b32_e32 v4, 0xfffffc00, v4
	v_sub_u32_e32 v4, v1, v4
	v_ashrrev_i32_e32 v2, 31, v0
	v_lshrrev_b32_e32 v5, 4, v4
	v_lshrrev_b32_e32 v2, 26, v2
	v_bitop3_b32 v4, v5, v4, 32 bitop3:0x6c
	v_add_u32_e32 v2, v0, v2
	v_ashrrev_i32_e32 v6, 31, v4
	v_ashrrev_i32_e32 v2, 6, v2
	v_lshrrev_b32_e32 v6, 26, v6
	v_lshlrev_b32_e32 v5, 3, v2
	v_add_u32_e32 v6, v4, v6
	v_and_b32_e32 v5, -16, v5
	v_ashrrev_i32_e32 v7, 6, v6
	v_and_b32_e32 v6, 0xc0, v6
	v_add_u32_e32 v5, v7, v5
	v_sub_u32_e32 v4, v4, v6
	v_lshlrev_b32_e32 v2, 5, v2
	v_ashrrev_i16_sdwa v4, v188, sext(v4) dst_sel:DWORD dst_unused:UNUSED_PAD src0_sel:DWORD src1_sel:BYTE_0
	v_lshlrev_b32_e32 v6, 1, v5
	v_lshrrev_b32_e32 v8, 2, v5
	v_and_b32_e32 v7, 3, v7
	s_mov_b32 s5, 0x1fffe0
	v_and_b32_e32 v2, 32, v2
	v_bfe_i32 v4, v4, 0, 16
	v_and_b32_e32 v6, 24, v6
	v_and_b32_e32 v8, 4, v8
	v_and_or_b32 v7, v5, s5, v7
	v_or3_b32 v6, v7, v8, v6
	v_add_lshl_u32 v2, v2, v4, 1
	v_add_u32_e32 v1, 0x2000, v1
	v_lshl_add_u32 v176, v5, 11, v2
	v_lshl_add_u32 v177, v6, 11, v2
	v_ashrrev_i32_e32 v2, 31, v1
	v_lshrrev_b32_e32 v2, 22, v2
	v_add_u32_e32 v2, v1, v2
	v_ashrrev_i32_e32 v2, 10, v2
	v_mul_i32_i24_e32 v4, 0x400, v2
	v_sub_u32_e32 v1, v1, v4
	v_lshrrev_b32_e32 v4, 4, v1
	v_bitop3_b32 v1, v4, v1, 32 bitop3:0x6c
	v_ashrrev_i32_e32 v5, 31, v1
	s_add_u32 s36, s2, 0x58492000
	v_lshrrev_b32_e32 v5, 26, v5
	s_addc_u32 s37, s3, 0
	v_lshlrev_b32_e32 v4, 3, v2
	v_add_u32_e32 v5, v1, v5
	s_add_u32 s6, s2, 0x8500000
	v_and_b32_e32 v4, -16, v4
	v_ashrrev_i32_e32 v6, 6, v5
	s_addc_u32 s7, s3, 0
	s_mul_i32 s38, s0, 7
	v_add_u32_e32 v4, v6, v4
	v_and_b32_e32 v6, 3, v6
	s_ashr_i32 s11, s12, 6
	v_readlane_b32 s8, v252, 62
	s_add_i32 s39, s38, 1
	s_ashr_i32 s10, s12, 8
	v_and_or_b32 v6, v4, s5, v6
	s_lshl_b32 s5, s11, 10
	v_readlane_b32 s9, v252, 63
	s_and_b64 s[8:9], s[8:9], exec
	s_cselect_b32 s8, s39, s38
	v_readlane_b32 s9, v253, 16
	s_mul_i32 s8, s8, s9
	v_readlane_b32 s9, v253, 17
	s_add_i32 s8, s8, s9
	s_mul_hi_i32 s9, s8, 0x92492493
	s_add_i32 s9, s9, s8
	s_lshr_b32 s13, s9, 31
	s_ashr_i32 s9, s9, 8
	v_and_b32_e32 v5, 0xc0, v5
	s_add_i32 s9, s9, s13
	v_sub_u32_e32 v1, v1, v5
	s_lshl_b32 s13, s9, 3
	v_lshlrev_b32_e32 v2, 5, v2
	v_ashrrev_i16_sdwa v1, v188, sext(v1) dst_sel:DWORD dst_unused:UNUSED_PAD src0_sel:DWORD src1_sel:BYTE_0
	v_lshlrev_b32_e32 v5, 1, v4
	v_lshrrev_b32_e32 v7, 2, v4
	s_sub_i32 s14, s0, s13
	v_and_b32_e32 v2, 32, v2
	v_bfe_i32 v1, v1, 0, 16
	v_and_b32_e32 v5, 24, v5
	v_and_b32_e32 v7, 4, v7
	s_min_i32 s14, s14, 8
	v_or3_b32 v5, v6, v7, v5
	v_add_lshl_u32 v1, v2, v1, 1
	s_abs_i32 s16, s14
	v_lshl_add_u32 v178, v4, 11, v1
	v_lshl_add_u32 v179, v5, 11, v1
	v_cvt_f32_u32_e32 v1, s16
	s_sub_i32 s17, 0, s16
	s_mulk_i32 s9, 0x1c0
	s_sub_i32 s8, s8, s9
	v_rcp_iflag_f32_e32 v1, v1
	s_abs_i32 s15, s8
	s_xor_b32 s9, s8, s14
	s_ashr_i32 s9, s9, 31
	v_mul_f32_e32 v1, 0x4f7ffffe, v1
	v_cvt_u32_f32_e32 v1, v1
	v_mov_b32_e32 v7, s1
	v_readfirstlane_b32 s18, v1
	s_mul_i32 s17, s17, s18
	s_mul_hi_u32 s17, s18, s17
	s_add_i32 s18, s18, s17
	s_mul_hi_u32 s17, s15, s18
	s_mul_i32 s18, s17, s16
	s_sub_i32 s15, s15, s18
	s_add_i32 s18, s17, 1
	s_sub_i32 s19, s15, s16
	s_cmp_ge_u32 s15, s16
	s_cselect_b32 s17, s18, s17
	s_cselect_b32 s15, s19, s15
	s_add_i32 s18, s17, 1
	s_cmp_ge_u32 s15, s16
	s_cselect_b32 s15, s18, s17
	s_xor_b32 s15, s15, s9
	s_sub_i32 s20, s15, s9
	s_mul_i32 s9, s20, s14
	s_sub_i32 s8, s8, s9
	s_add_i32 s22, s13, s8
	v_readlane_b32 s8, v254, 29
	v_readlane_b32 s9, v254, 30
	s_nop 0
	v_mov_b32_e32 v1, s8
	ds_read2_b32 v[4:5], v1 offset1:1
	v_mov_b32_e32 v1, s9
	v_readlane_b32 s9, v254, 31
	s_waitcnt lgkmcnt(0)
	v_readfirstlane_b32 s13, v4
	v_readfirstlane_b32 s8, v5
	ds_read2_b32 v[4:5], v1 offset1:1
	v_mov_b32_e32 v1, s9
	v_readlane_b32 s9, v254, 32
	s_cmp_ge_i32 s22, s8
	s_waitcnt lgkmcnt(0)
	v_readfirstlane_b32 s16, v4
	v_readfirstlane_b32 s17, v5
	ds_read2_b32 v[4:5], v1 offset1:1
	v_mov_b32_e32 v1, s9
	ds_read_b32 v1, v1
	s_cselect_b64 s[8:9], -1, 0
	s_cmp_ge_i32 s22, s13
	s_cselect_b64 s[14:15], -1, 0
	s_cmp_ge_i32 s22, s16
	s_waitcnt lgkmcnt(1)
	v_readfirstlane_b32 s18, v4
	s_cselect_b64 vcc, -1, 0
	s_cmp_ge_i32 s22, s17
	v_readfirstlane_b32 s19, v5
	s_waitcnt lgkmcnt(0)
	v_readfirstlane_b32 s21, v1
	v_cndmask_b32_e64 v1, 0, 1, s[8:9]
	v_cndmask_b32_e64 v2, 0, 1, s[14:15]
	s_cselect_b64 s[8:9], -1, 0
	s_cmp_ge_i32 s22, s18
	v_addc_co_u32_e32 v2, vcc, v1, v2, vcc
	v_cndmask_b32_e64 v4, 0, 1, s[8:9]
	v_mov_b32_e32 v5, s1
	s_cselect_b64 s[8:9], -1, 0
	s_cmp_ge_i32 s22, s19
	v_lshl_add_u64 v[4:5], v[2:3], 0, v[4:5]
	v_cndmask_b32_e64 v6, 0, 1, s[8:9]
	s_cselect_b64 s[8:9], -1, 0
	s_cmp_ge_i32 s22, s21
	v_lshl_add_u64 v[4:5], v[4:5], 0, v[6:7]
	v_cndmask_b32_e64 v6, 0, 1, s[8:9]
	s_cselect_b64 s[8:9], -1, 0
	v_lshl_add_u64 v[4:5], v[4:5], 0, v[6:7]
	v_cndmask_b32_e64 v6, 0, 1, s[8:9]
	v_lshl_add_u64 v[4:5], v[4:5], 0, v[6:7]
	s_mov_b32 s8, 0x3800000
	v_mul_lo_u32 v1, v5, s8
	v_mul_hi_u32 v2, v4, s8
	v_add_u32_e32 v5, v2, v1
	v_mul_lo_u32 v4, v4, s8
	s_ashr_i32 s21, s20, 31
	v_lshl_add_u64 v[4:5], s[6:7], 0, v[4:5]
	s_lshl_b64 s[8:9], s[20:21], 19
	s_ashr_i32 s23, s22, 31
	v_lshl_add_u64 v[4:5], v[4:5], 0, s[8:9]
	s_lshl_b64 s[8:9], s[22:23], 19
	s_add_u32 s26, s36, s8
	s_addc_u32 s27, s37, s9
	s_add_i32 s21, s5, 0
	v_readfirstlane_b32 s29, v5
	v_readfirstlane_b32 s28, v4
	s_add_i32 s23, s21, 0x10000
	s_mov_b32 m0, s23
	s_nop 0
	global_load_lds_dwordx4 v177, s[28:29]
	s_add_i32 s40, s21, 0x12000
	s_mov_b32 m0, s40
	s_nop 0
	global_load_lds_dwordx4 v179, s[28:29]
	s_add_u32 s8, s28, 0x40000
	s_addc_u32 s9, s29, 0
	s_add_i32 s41, s21, 0x14000
	s_mov_b32 m0, s41
	s_nop 0
	global_load_lds_dwordx4 v177, s[8:9]
	s_add_i32 s42, s21, 0x16000
	s_mov_b32 m0, s42
	s_nop 0
	global_load_lds_dwordx4 v179, s[8:9]
	s_add_i32 s43, s21, 0x2000
	s_mov_b32 m0, s21
	s_nop 0
	global_load_lds_dwordx4 v176, s[26:27]
	s_add_u32 s8, s26, 0x40000
	s_mov_b32 m0, s43
	s_nop 0
	global_load_lds_dwordx4 v178, s[26:27]
	s_addc_u32 s9, s27, 0
	s_add_i32 s44, s21, 0x4000
	s_mov_b32 m0, s44
	s_nop 0
	global_load_lds_dwordx4 v176, s[8:9]
	s_add_i32 s45, s21, 0x6000
	s_mov_b32 m0, s45
	s_nop 0
	global_load_lds_dwordx4 v178, s[8:9]
	s_cmp_eq_u32 s10, 1
	s_cselect_b64 s[8:9], -1, 0
	s_cmp_lg_u32 s10, 1
	s_cbranch_scc1 .LBB0_2840
	s_barrier
; #define PG8_STAGE(bufoff, gbase, voff) do { _Pragma("unroll") for (int _i = 0; _i < 2; ++_i) \
;         glds16((const void*)(gbase), (voff)[_i], ldsbase + (unsigned)(bufoff) + ldsw + (unsigned)_i * 8192u); } while (0)
; #define PG8_WAIT_V(n) asm volatile("s_waitcnt vmcnt(" #n ")" ::: "memory")
; #define PG8_BAR __builtin_amdgcn_s_barrier()
;     __device__ __forceinline__ bool next(int i, Unit& u) const { if (!o.idx(i, u.pm, u.pn)) return false; u.tag = 0; u.a = A + (size_t)u.pm * astep; u.b = Bt + (size_t)u.pn * bstep; return true; }
;     ...
;     const unsigned ldsw = (unsigned)wid * 1024u, ldsbase = (unsigned)(size_t)lds;
;     const int aoff = lds_byte(wr * 64 + fr, fq * 8), boff = lds_byte(wc * 32 + fr, fq * 8);
;     ...
;     if (wr == 1) PG8_BAR;
;     PG8_WAIT_V(2); PG8_BAR;
;     PG8_STAGE(PG8_SB(1, 0), cB + kstep, voffB); PG8_STAGE(PG8_SA(1, 0), cA + kstep, voffA); PG8_STAGE(PG8_SB(1, 1), cB + hstepB + kstep, voffB);
;     PG8_WAIT_V(6); PG8_BAR;
;     for (;;) {
;         const bool has_next = S.next(ui + 1, nxt);
;         const char* nA = uniform_ptr(has_next ? nxt.a : cA); const char* nB = uniform_ptr(has_next ? nxt.b : cB);
.LBB0_2840:
	v_lshrrev_b32_e32 v2, 1, v0
	v_and_b32_e32 v2, 24, v2
	v_and_b32_e32 v1, 15, v0
	v_lshlrev_b32_e32 v4, 1, v2
	v_lshlrev_b32_e32 v0, 2, v0
	v_lshl_or_b32 v180, s10, 6, v1
	v_lshl_or_b32 v1, v1, 6, v4
	s_lshl_b32 s10, s10, 13
	v_and_b32_e32 v0, 32, v0
	v_bitop3_b32 v4, v1, s10, v0 bitop3:0xde
	s_lshl_b32 s10, s11, 5
	s_and_b32 s14, s10, 0x60
	s_ashr_i32 s5, s4, 31
	s_lshl_b32 s10, s14, 7
	v_bitop3_b32 v0, v1, s10, v0 bitop3:0xde
	s_add_u32 s10, s2, 0x3a892000
	s_addc_u32 s11, s3, 0
	s_add_u32 s2, s28, 0x80
	s_waitcnt vmcnt(2)
	s_barrier
	s_addc_u32 s3, s29, 0
	s_add_i32 s46, s21, 0x18000
	s_mov_b32 m0, s46
	s_nop 0
	global_load_lds_dwordx4 v177, s[2:3]
	s_add_i32 s47, s21, 0x1a000
	s_mov_b32 m0, s47
	s_nop 0
	global_load_lds_dwordx4 v179, s[2:3]
	s_add_u32 s2, s26, 0x80
	s_addc_u32 s3, s27, 0
	s_add_i32 s48, s21, 0x8000
	s_mov_b32 m0, s48
	s_nop 0
	global_load_lds_dwordx4 v176, s[2:3]
	s_add_i32 s49, s21, 0xa000
	s_mov_b32 m0, s49
	s_nop 0
	global_load_lds_dwordx4 v178, s[2:3]
	s_add_u32 s2, s28, 0x40080
	s_addc_u32 s3, s29, 0
	s_add_i32 s50, s21, 0x1c000
	s_mov_b32 m0, s50
	s_nop 0
	global_load_lds_dwordx4 v177, s[2:3]
	s_add_i32 s51, s21, 0x1e000
	s_mov_b32 m0, s51
	s_nop 0
	global_load_lds_dwordx4 v179, s[2:3]
	s_waitcnt vmcnt(6)
	s_add_i32 s52, s21, 0xc000
	s_cmpk_lt_u32 s12, 0x100
	s_cselect_b64 s[12:13], -1, 0
	s_add_i32 s53, s21, 0xe000
	v_or_b32_e32 v181, s14, v2
	s_mov_b32 s54, 0
	v_add_u32_e32 v182, 0, v0
	v_add_u32_e32 v183, 0, v4
	s_mov_b64 s[18:19], s[26:27]
	s_barrier
	s_branch .LBB0_2843

; #define PG8_STAGE(bufoff, gbase, voff) do { _Pragma("unroll") for (int _i = 0; _i < 2; ++_i) \
;         glds16((const void*)(gbase), (voff)[_i], ldsbase + (unsigned)(bufoff) + ldsw + (unsigned)_i * 8192u); } while (0)
; #define PG8_LDA(dst, b, h) do { _Pragma("unroll") for (int m = 0; m < 4; ++m) _Pragma("unroll") for (int k = 0; k < 2; ++k) dst[m][k] = *(const LAS bf16x8*)(lds + PG8_SA(b, h) + aoff + m * 2048 + k * 1024); } while (0)
; #define PG8_LDB(dst, b, h) do { _Pragma("unroll") for (int n = 0; n < 2; ++n) _Pragma("unroll") for (int k = 0; k < 2; ++k) dst[n][k] = *(const LAS bf16x8*)(lds + PG8_SB(b, h) + boff + n * 2048 + k * 1024); } while (0)
; #define PG8_WAIT_V(n) asm volatile("s_waitcnt vmcnt(" #n ")" ::: "memory")
; #define PG8_WAIT_L(n) asm volatile("s_waitcnt lgkmcnt(" #n ")" ::: "memory")
; #define PG8_BAR __builtin_amdgcn_s_barrier()
; #define PG8_SCHED __builtin_amdgcn_sched_barrier(0)
;     ...
;             PG8_LDB(B0, 0, 0); PG8_LDB(B1, 0, 1); PG8_SCHED; PG8_LDA(At, 0, 0); PG8_STAGE(PG8_SA(1, 1), a1 + hstepA, voffA);
;             PG8_WAIT_V(8); PG8_WAIT_L(0); PG8_BAR; PG8_MMA(0, 0, At, B0); PG8_MMA(0, 1, At, B1); PG8_BAR; PG8_SCHED;
;             PG8_LDA(At, 0, 1); PG8_STAGE(PG8_SB(0, 0), b2, voffB); PG8_STAGE(PG8_SB(0, 1), b2 + hstepB, voffB); PG8_STAGE(PG8_SA(0, 0), a2, voffA);
;             PG8_WAIT_V(8); PG8_WAIT_L(0); PG8_BAR; PG8_MMA(1, 0, At, B0); PG8_MMA(1, 1, At, B1); PG8_BAR; PG8_SCHED;
.LBB0_2846:
	v_add_u32_e32 v0, 0x10000, v182
	ds_read_b128 v[22:25], v0
	ds_read_b128 v[168:171], v0 offset:1024
	ds_read_b128 v[16:19], v0 offset:2048
	ds_read_b128 v[164:167], v0 offset:3072
	v_add_u32_e32 v0, 0x14000, v182
	ds_read_b128 v[10:13], v0
	ds_read_b128 v[160:163], v0 offset:1024
	ds_read_b128 v[4:7], v0 offset:2048
	ds_read_b128 v[156:159], v0 offset:3072
	s_add_u32 s28, s26, 0xfffc0080
	s_addc_u32 s29, s27, -1
	s_cmp_eq_u32 s55, 12
	s_cselect_b32 s34, s18, s28
	s_cselect_b32 s35, s19, s29
	s_cselect_b32 s30, s24, s15
	s_cselect_b32 s31, s25, s17
	s_add_u32 s28, s34, 0x80
	s_addc_u32 s29, s35, 0
	ds_read_b128 v[206:209], v183
	ds_read_b128 v[172:175], v183 offset:1024
	ds_read_b128 v[212:215], v183 offset:2048
	ds_read_b128 v[184:187], v183 offset:3072
	ds_read_b128 v[218:221], v183 offset:4096
	ds_read_b128 v[196:199], v183 offset:5120
	ds_read_b128 v[224:227], v183 offset:6144
	ds_read_b128 v[228:231], v183 offset:7168
	s_mov_b32 m0, s52
	s_nop 0
	global_load_lds_dwordx4 v176, s[26:27]
	s_nop 0
	s_mov_b32 m0, s53
	s_nop 0
	global_load_lds_dwordx4 v178, s[26:27]
	s_waitcnt vmcnt(8)
	s_waitcnt lgkmcnt(0)
	s_barrier
	s_setprio 0
	s_waitcnt lgkmcnt(6)
	v_mov_b32_e32 v210, v172
	v_mov_b32_e32 v211, v173
	v_mov_b32_e32 v26, v168
	v_mov_b32_e32 v27, v169
	s_nop 1
	v_mfma_scale_f32_16x16x128_f8f6f4 v[152:155], v[22:27], v[206:211], v[152:155], v170, v174 op_sel_hi:[0,0,0] cbsz:2 blgp:2
	v_mov_b32_e32 v20, v164
	v_mov_b32_e32 v21, v165
	s_nop 1
	v_mfma_scale_f32_16x16x128_f8f6f4 v[144:147], v[16:21], v[206:211], v[144:147], v166, v174 op_sel_hi:[0,0,0] cbsz:2 blgp:2
	s_waitcnt lgkmcnt(4)
	v_mov_b32_e32 v216, v184
	v_mov_b32_e32 v217, v185
	s_nop 1
	v_mfma_scale_f32_16x16x128_f8f6f4 v[136:139], v[22:27], v[212:217], v[136:139], v170, v186 op_sel_hi:[0,0,0] cbsz:2 blgp:2
	s_nop 1
	v_mfma_scale_f32_16x16x128_f8f6f4 v[128:131], v[16:21], v[212:217], v[128:131], v166, v186 op_sel_hi:[0,0,0] cbsz:2 blgp:2
	s_waitcnt lgkmcnt(2)
	v_mov_b32_e32 v222, v196
	v_mov_b32_e32 v223, v197
	s_nop 1
	v_mfma_scale_f32_16x16x128_f8f6f4 v[120:123], v[22:27], v[218:223], v[120:123], v170, v198 op_sel_hi:[0,0,0] cbsz:2 blgp:2
	s_nop 1
	v_mfma_scale_f32_16x16x128_f8f6f4 v[112:115], v[16:21], v[218:223], v[112:115], v166, v198 op_sel_hi:[0,0,0] cbsz:2 blgp:2
	s_waitcnt lgkmcnt(0)
	s_nop 1
	v_mfma_scale_f32_16x16x128_f8f6f4 v[104:107], v[22:27], v[224:229], v[104:107], v170, v230 op_sel_hi:[0,0,0] cbsz:2 blgp:2
	s_nop 1
	v_mfma_scale_f32_16x16x128_f8f6f4 v[96:99], v[16:21], v[224:229], v[96:99], v166, v230 op_sel_hi:[0,0,0] cbsz:2 blgp:2
	s_setprio 0
	s_setprio 0
	v_mov_b32_e32 v14, v160
	v_mov_b32_e32 v15, v161
	s_nop 1
	v_mfma_scale_f32_16x16x128_f8f6f4 v[148:151], v[10:15], v[206:211], v[148:151], v162, v174 op_sel_hi:[0,0,0] cbsz:2 blgp:2
	v_mov_b32_e32 v8, v156
	v_mov_b32_e32 v9, v157
	s_nop 1
	v_mfma_scale_f32_16x16x128_f8f6f4 v[140:143], v[4:9], v[206:211], v[140:143], v158, v174 op_sel_hi:[0,0,0] cbsz:2 blgp:2
	s_nop 1
	v_mfma_scale_f32_16x16x128_f8f6f4 v[132:135], v[10:15], v[212:217], v[132:135], v162, v186 op_sel_hi:[0,0,0] cbsz:2 blgp:2
	s_nop 1
	v_mfma_scale_f32_16x16x128_f8f6f4 v[124:127], v[4:9], v[212:217], v[124:127], v158, v186 op_sel_hi:[0,0,0] cbsz:2 blgp:2
	s_nop 1
	v_mfma_scale_f32_16x16x128_f8f6f4 v[116:119], v[10:15], v[218:223], v[116:119], v162, v198 op_sel_hi:[0,0,0] cbsz:2 blgp:2
	s_nop 1
	v_mfma_scale_f32_16x16x128_f8f6f4 v[108:111], v[4:9], v[218:223], v[108:111], v158, v198 op_sel_hi:[0,0,0] cbsz:2 blgp:2
	s_nop 1
	v_mfma_scale_f32_16x16x128_f8f6f4 v[100:103], v[10:15], v[224:229], v[100:103], v162, v230 op_sel_hi:[0,0,0] cbsz:2 blgp:2
	s_nop 1
	v_mfma_scale_f32_16x16x128_f8f6f4 v[92:95], v[4:9], v[224:229], v[92:95], v158, v230 op_sel_hi:[0,0,0] cbsz:2 blgp:2
	s_setprio 0
	s_barrier
	ds_read_b128 v[206:209], v183 offset:16384
	ds_read_b128 v[172:175], v183 offset:17408
	ds_read_b128 v[212:215], v183 offset:18432
	ds_read_b128 v[184:187], v183 offset:19456
	ds_read_b128 v[218:221], v183 offset:20480
	ds_read_b128 v[196:199], v183 offset:21504
	ds_read_b128 v[224:227], v183 offset:22528
	ds_read_b128 v[228:231], v183 offset:23552
	s_mov_b32 m0, s23
	s_nop 0
	global_load_lds_dwordx4 v177, s[30:31]
	s_nop 0
	s_mov_b32 m0, s40
	s_nop 0
	global_load_lds_dwordx4 v179, s[30:31]
	s_add_u32 s56, s30, 0x40000
	s_addc_u32 s57, s31, 0
	s_mov_b32 m0, s41
	s_nop 0
	global_load_lds_dwordx4 v177, s[56:57]
	s_nop 0
	s_mov_b32 m0, s42
	s_nop 0
	global_load_lds_dwordx4 v179, s[56:57]
	s_mov_b32 m0, s21
	s_nop 0
	global_load_lds_dwordx4 v176, s[34:35]
	s_nop 0
	s_mov_b32 m0, s43
	s_nop 0
	global_load_lds_dwordx4 v178, s[34:35]
	s_waitcnt vmcnt(8)
	s_waitcnt lgkmcnt(0)
	s_barrier
; #define PG8_STAGE(bufoff, gbase, voff) do { _Pragma("unroll") for (int _i = 0; _i < 2; ++_i) \
;         glds16((const void*)(gbase), (voff)[_i], ldsbase + (unsigned)(bufoff) + ldsw + (unsigned)_i * 8192u); } while (0)
; #define PG8_LDA(dst, b, h) do { _Pragma("unroll") for (int m = 0; m < 4; ++m) _Pragma("unroll") for (int k = 0; k < 2; ++k) dst[m][k] = *(const LAS bf16x8*)(lds + PG8_SA(b, h) + aoff + m * 2048 + k * 1024); } while (0)
; #define PG8_LDB(dst, b, h) do { _Pragma("unroll") for (int n = 0; n < 2; ++n) _Pragma("unroll") for (int k = 0; k < 2; ++k) dst[n][k] = *(const LAS bf16x8*)(lds + PG8_SB(b, h) + boff + n * 2048 + k * 1024); } while (0)
; #define PG8_WAIT_V(n) asm volatile("s_waitcnt vmcnt(" #n ")" ::: "memory")
; #define PG8_WAIT_L(n) asm volatile("s_waitcnt lgkmcnt(" #n ")" ::: "memory")
; #define PG8_BAR __builtin_amdgcn_s_barrier()
; #define PG8_SCHED __builtin_amdgcn_sched_barrier(0)
;     ...
;             PG8_WAIT_V(8); PG8_WAIT_L(0); PG8_BAR; PG8_MMA(1, 0, At, B0); PG8_MMA(1, 1, At, B1); PG8_BAR; PG8_SCHED;
;             PG8_LDB(B0, 1, 0); PG8_LDB(B1, 1, 1); PG8_SCHED; PG8_LDA(At, 1, 0); PG8_STAGE(PG8_SA(0, 1), a2 + hstepA, voffA);
;             PG8_WAIT_V(8); PG8_WAIT_L(0); PG8_BAR; PG8_MMA(0, 0, At, B0); PG8_MMA(0, 1, At, B1); PG8_BAR; PG8_SCHED;
;             PG8_LDA(At, 1, 1); PG8_STAGE(PG8_SB(1, 0), b3, voffB); PG8_STAGE(PG8_SB(1, 1), b3 + hstepB, voffB); PG8_STAGE(PG8_SA(1, 0), a3, voffA);
;             PG8_WAIT_V(8); PG8_WAIT_L(0); PG8_BAR; PG8_MMA(1, 0, At, B0); PG8_MMA(1, 1, At, B1); PG8_BAR; PG8_SCHED;
	s_setprio 0
	s_waitcnt lgkmcnt(6)
	v_mov_b32_e32 v210, v172
	v_mov_b32_e32 v211, v173
	s_nop 1
	v_mfma_scale_f32_16x16x128_f8f6f4 v[88:91], v[22:27], v[206:211], v[88:91], v170, v174 op_sel_hi:[0,0,0] cbsz:2 blgp:2
	s_nop 1
	v_mfma_scale_f32_16x16x128_f8f6f4 v[80:83], v[16:21], v[206:211], v[80:83], v166, v174 op_sel_hi:[0,0,0] cbsz:2 blgp:2
	s_waitcnt lgkmcnt(4)
	v_mov_b32_e32 v216, v184
	v_mov_b32_e32 v217, v185
	s_nop 1
	v_mfma_scale_f32_16x16x128_f8f6f4 v[72:75], v[22:27], v[212:217], v[72:75], v170, v186 op_sel_hi:[0,0,0] cbsz:2 blgp:2
	s_nop 1
	v_mfma_scale_f32_16x16x128_f8f6f4 v[64:67], v[16:21], v[212:217], v[64:67], v166, v186 op_sel_hi:[0,0,0] cbsz:2 blgp:2
	s_waitcnt lgkmcnt(2)
	v_mov_b32_e32 v222, v196
	v_mov_b32_e32 v223, v197
	s_nop 1
	v_mfma_scale_f32_16x16x128_f8f6f4 v[56:59], v[22:27], v[218:223], v[56:59], v170, v198 op_sel_hi:[0,0,0] cbsz:2 blgp:2
	s_nop 1
	v_mfma_scale_f32_16x16x128_f8f6f4 v[48:51], v[16:21], v[218:223], v[48:51], v166, v198 op_sel_hi:[0,0,0] cbsz:2 blgp:2
	s_waitcnt lgkmcnt(0)
	s_nop 1
	v_mfma_scale_f32_16x16x128_f8f6f4 v[40:43], v[22:27], v[224:229], v[40:43], v170, v230 op_sel_hi:[0,0,0] cbsz:2 blgp:2
	s_nop 1
	v_mfma_scale_f32_16x16x128_f8f6f4 v[32:35], v[16:21], v[224:229], v[32:35], v166, v230 op_sel_hi:[0,0,0] cbsz:2 blgp:2
	s_setprio 0
	s_setprio 0
	s_nop 1
	v_mfma_scale_f32_16x16x128_f8f6f4 v[84:87], v[10:15], v[206:211], v[84:87], v162, v174 op_sel_hi:[0,0,0] cbsz:2 blgp:2
	s_nop 1
	v_mfma_scale_f32_16x16x128_f8f6f4 v[76:79], v[4:9], v[206:211], v[76:79], v158, v174 op_sel_hi:[0,0,0] cbsz:2 blgp:2
	s_nop 1
	v_mfma_scale_f32_16x16x128_f8f6f4 v[68:71], v[10:15], v[212:217], v[68:71], v162, v186 op_sel_hi:[0,0,0] cbsz:2 blgp:2
	s_nop 1
	v_mfma_scale_f32_16x16x128_f8f6f4 v[60:63], v[4:9], v[212:217], v[60:63], v158, v186 op_sel_hi:[0,0,0] cbsz:2 blgp:2
	s_nop 1
	v_mfma_scale_f32_16x16x128_f8f6f4 v[52:55], v[10:15], v[218:223], v[52:55], v162, v198 op_sel_hi:[0,0,0] cbsz:2 blgp:2
	s_nop 1
	v_mfma_scale_f32_16x16x128_f8f6f4 v[44:47], v[4:9], v[218:223], v[44:47], v158, v198 op_sel_hi:[0,0,0] cbsz:2 blgp:2
	s_nop 1
	v_mfma_scale_f32_16x16x128_f8f6f4 v[36:39], v[10:15], v[224:229], v[36:39], v162, v230 op_sel_hi:[0,0,0] cbsz:2 blgp:2
	s_nop 1
	v_mfma_scale_f32_16x16x128_f8f6f4 v[28:31], v[4:9], v[224:229], v[28:31], v158, v230 op_sel_hi:[0,0,0] cbsz:2 blgp:2
	s_setprio 0
	s_barrier
	v_add_u32_e32 v0, 0x18000, v182
	ds_read_b128 v[22:25], v0
	ds_read_b128 v[168:171], v0 offset:1024
	ds_read_b128 v[16:19], v0 offset:2048
	ds_read_b128 v[164:167], v0 offset:3072
	v_add_u32_e32 v0, 0x1c000, v182
	ds_read_b128 v[10:13], v0
	ds_read_b128 v[156:159], v0 offset:1024
	ds_read_b128 v[4:7], v0 offset:2048
	ds_read_b128 v[160:163], v0 offset:3072
	ds_read_b128 v[206:209], v183 offset:32768
	ds_read_b128 v[172:175], v183 offset:33792
	ds_read_b128 v[212:215], v183 offset:34816
	ds_read_b128 v[184:187], v183 offset:35840
	ds_read_b128 v[218:221], v183 offset:36864
	ds_read_b128 v[196:199], v183 offset:37888
	ds_read_b128 v[224:227], v183 offset:38912
	ds_read_b128 v[228:231], v183 offset:39936
	s_add_u32 s34, s34, 0x40000
	s_addc_u32 s35, s35, 0
	s_mov_b32 m0, s44
	s_nop 0
	global_load_lds_dwordx4 v176, s[34:35]
	s_nop 0
	s_mov_b32 m0, s45
	s_nop 0
	global_load_lds_dwordx4 v178, s[34:35]
	s_waitcnt vmcnt(8)
	s_waitcnt lgkmcnt(0)
	s_barrier
	s_setprio 0
	s_waitcnt lgkmcnt(6)
	v_mov_b32_e32 v210, v172
	v_mov_b32_e32 v211, v173
	v_mov_b32_e32 v26, v168
	v_mov_b32_e32 v27, v169
	s_nop 1
	v_mfma_scale_f32_16x16x128_f8f6f4 v[152:155], v[22:27], v[206:211], v[152:155], v170, v174 op_sel_hi:[0,0,0] cbsz:2 blgp:2
	v_mov_b32_e32 v20, v164
	v_mov_b32_e32 v21, v165
	s_nop 1
	v_mfma_scale_f32_16x16x128_f8f6f4 v[144:147], v[16:21], v[206:211], v[144:147], v166, v174 op_sel_hi:[0,0,0] cbsz:2 blgp:2
	s_waitcnt lgkmcnt(4)
	v_mov_b32_e32 v216, v184
	v_mov_b32_e32 v217, v185
	s_nop 1
	v_mfma_scale_f32_16x16x128_f8f6f4 v[136:139], v[22:27], v[212:217], v[136:139], v170, v186 op_sel_hi:[0,0,0] cbsz:2 blgp:2
	s_nop 1
	v_mfma_scale_f32_16x16x128_f8f6f4 v[128:131], v[16:21], v[212:217], v[128:131], v166, v186 op_sel_hi:[0,0,0] cbsz:2 blgp:2
	s_waitcnt lgkmcnt(2)
	v_mov_b32_e32 v222, v196
	v_mov_b32_e32 v223, v197
	s_nop 1
	v_mfma_scale_f32_16x16x128_f8f6f4 v[120:123], v[22:27], v[218:223], v[120:123], v170, v198 op_sel_hi:[0,0,0] cbsz:2 blgp:2
	s_nop 1
	v_mfma_scale_f32_16x16x128_f8f6f4 v[112:115], v[16:21], v[218:223], v[112:115], v166, v198 op_sel_hi:[0,0,0] cbsz:2 blgp:2
	s_waitcnt lgkmcnt(0)
	s_nop 1
	v_mfma_scale_f32_16x16x128_f8f6f4 v[104:107], v[22:27], v[224:229], v[104:107], v170, v230 op_sel_hi:[0,0,0] cbsz:2 blgp:2
	s_nop 1
	v_mfma_scale_f32_16x16x128_f8f6f4 v[96:99], v[16:21], v[224:229], v[96:99], v166, v230 op_sel_hi:[0,0,0] cbsz:2 blgp:2
	s_setprio 0
	s_setprio 0
	v_mov_b32_e32 v14, v156
	v_mov_b32_e32 v15, v157
	s_nop 1
	v_mfma_scale_f32_16x16x128_f8f6f4 v[148:151], v[10:15], v[206:211], v[148:151], v158, v174 op_sel_hi:[0,0,0] cbsz:2 blgp:2
	v_mov_b32_e32 v8, v160
	v_mov_b32_e32 v9, v161
	s_nop 1
	v_mfma_scale_f32_16x16x128_f8f6f4 v[140:143], v[4:9], v[206:211], v[140:143], v162, v174 op_sel_hi:[0,0,0] cbsz:2 blgp:2
	s_nop 1
	v_mfma_scale_f32_16x16x128_f8f6f4 v[132:135], v[10:15], v[212:217], v[132:135], v158, v186 op_sel_hi:[0,0,0] cbsz:2 blgp:2
	s_nop 1
	v_mfma_scale_f32_16x16x128_f8f6f4 v[124:127], v[4:9], v[212:217], v[124:127], v162, v186 op_sel_hi:[0,0,0] cbsz:2 blgp:2
	s_nop 1
	v_mfma_scale_f32_16x16x128_f8f6f4 v[116:119], v[10:15], v[218:223], v[116:119], v158, v198 op_sel_hi:[0,0,0] cbsz:2 blgp:2
	s_nop 1
	v_mfma_scale_f32_16x16x128_f8f6f4 v[108:111], v[4:9], v[218:223], v[108:111], v162, v198 op_sel_hi:[0,0,0] cbsz:2 blgp:2
	s_nop 1
	v_mfma_scale_f32_16x16x128_f8f6f4 v[100:103], v[10:15], v[224:229], v[100:103], v158, v230 op_sel_hi:[0,0,0] cbsz:2 blgp:2
	s_nop 1
	v_mfma_scale_f32_16x16x128_f8f6f4 v[92:95], v[4:9], v[224:229], v[92:95], v162, v230 op_sel_hi:[0,0,0] cbsz:2 blgp:2
	s_setprio 0
	s_barrier
; #define PG8_STAGE(bufoff, gbase, voff) do { _Pragma("unroll") for (int _i = 0; _i < 2; ++_i) \
;         glds16((const void*)(gbase), (voff)[_i], ldsbase + (unsigned)(bufoff) + ldsw + (unsigned)_i * 8192u); } while (0)
; #define PG8_LDA(dst, b, h) do { _Pragma("unroll") for (int m = 0; m < 4; ++m) _Pragma("unroll") for (int k = 0; k < 2; ++k) dst[m][k] = *(const LAS bf16x8*)(lds + PG8_SA(b, h) + aoff + m * 2048 + k * 1024); } while (0)
; #define PG8_WAIT_V(n) asm volatile("s_waitcnt vmcnt(" #n ")" ::: "memory")
; #define PG8_WAIT_L(n) asm volatile("s_waitcnt lgkmcnt(" #n ")" ::: "memory")
; #define PG8_BAR __builtin_amdgcn_s_barrier()
; #define PG8_SCHED __builtin_amdgcn_sched_barrier(0)
;     ...
;             PG8_LDA(At, 1, 1); PG8_STAGE(PG8_SB(1, 0), b3, voffB); PG8_STAGE(PG8_SB(1, 1), b3 + hstepB, voffB); PG8_STAGE(PG8_SA(1, 0), a3, voffA);
;             PG8_WAIT_V(8); PG8_WAIT_L(0); PG8_BAR; PG8_MMA(1, 0, At, B0); PG8_MMA(1, 1, At, B1); PG8_BAR; PG8_SCHED;
;         }
	ds_read_b128 v[206:209], v183 offset:49152
	ds_read_b128 v[172:175], v183 offset:50176
	ds_read_b128 v[212:215], v183 offset:51200
	ds_read_b128 v[184:187], v183 offset:52224
	ds_read_b128 v[218:221], v183 offset:53248
	ds_read_b128 v[196:199], v183 offset:54272
	ds_read_b128 v[224:227], v183 offset:55296
	ds_read_b128 v[228:231], v183 offset:56320
	s_add_u32 s34, s30, 0x80
	s_addc_u32 s35, s31, 0
	s_mov_b32 m0, s46
	s_nop 0
	global_load_lds_dwordx4 v177, s[34:35]
	s_add_u32 s30, s30, 0x40080
	s_mov_b32 m0, s47
	s_nop 0
	global_load_lds_dwordx4 v179, s[34:35]
	s_addc_u32 s31, s31, 0
	s_mov_b32 m0, s50
	s_nop 0
	global_load_lds_dwordx4 v177, s[30:31]
	s_nop 0
	s_mov_b32 m0, s51
	s_nop 0
	global_load_lds_dwordx4 v179, s[30:31]
	s_mov_b32 m0, s48
	s_nop 0
	global_load_lds_dwordx4 v176, s[28:29]
	s_nop 0
	s_mov_b32 m0, s49
	s_nop 0
	global_load_lds_dwordx4 v178, s[28:29]
	s_waitcnt vmcnt(8)
	s_waitcnt lgkmcnt(0)
	s_barrier
	s_setprio 0
	s_waitcnt lgkmcnt(6)
	v_mov_b32_e32 v210, v172
	v_mov_b32_e32 v211, v173
	s_nop 1
	v_mfma_scale_f32_16x16x128_f8f6f4 v[88:91], v[22:27], v[206:211], v[88:91], v170, v174 op_sel_hi:[0,0,0] cbsz:2 blgp:2
	s_nop 1
	v_mfma_scale_f32_16x16x128_f8f6f4 v[80:83], v[16:21], v[206:211], v[80:83], v166, v174 op_sel_hi:[0,0,0] cbsz:2 blgp:2
	s_waitcnt lgkmcnt(4)
	v_mov_b32_e32 v216, v184
	v_mov_b32_e32 v217, v185
	s_nop 1
	v_mfma_scale_f32_16x16x128_f8f6f4 v[72:75], v[22:27], v[212:217], v[72:75], v170, v186 op_sel_hi:[0,0,0] cbsz:2 blgp:2
	s_nop 1
	v_mfma_scale_f32_16x16x128_f8f6f4 v[64:67], v[16:21], v[212:217], v[64:67], v166, v186 op_sel_hi:[0,0,0] cbsz:2 blgp:2
	s_waitcnt lgkmcnt(2)
	v_mov_b32_e32 v222, v196
	v_mov_b32_e32 v223, v197
	s_nop 1
	v_mfma_scale_f32_16x16x128_f8f6f4 v[56:59], v[22:27], v[218:223], v[56:59], v170, v198 op_sel_hi:[0,0,0] cbsz:2 blgp:2
	s_nop 1
	v_mfma_scale_f32_16x16x128_f8f6f4 v[48:51], v[16:21], v[218:223], v[48:51], v166, v198 op_sel_hi:[0,0,0] cbsz:2 blgp:2
	s_waitcnt lgkmcnt(0)
	s_nop 1
	v_mfma_scale_f32_16x16x128_f8f6f4 v[40:43], v[22:27], v[224:229], v[40:43], v170, v230 op_sel_hi:[0,0,0] cbsz:2 blgp:2
	s_nop 1
	v_mfma_scale_f32_16x16x128_f8f6f4 v[32:35], v[16:21], v[224:229], v[32:35], v166, v230 op_sel_hi:[0,0,0] cbsz:2 blgp:2
	s_setprio 0
	s_setprio 0
	s_nop 1
	v_mfma_scale_f32_16x16x128_f8f6f4 v[84:87], v[10:15], v[206:211], v[84:87], v158, v174 op_sel_hi:[0,0,0] cbsz:2 blgp:2
	s_nop 1
	v_mfma_scale_f32_16x16x128_f8f6f4 v[76:79], v[4:9], v[206:211], v[76:79], v162, v174 op_sel_hi:[0,0,0] cbsz:2 blgp:2
	s_nop 1
	v_mfma_scale_f32_16x16x128_f8f6f4 v[68:71], v[10:15], v[212:217], v[68:71], v158, v186 op_sel_hi:[0,0,0] cbsz:2 blgp:2
	s_nop 1
	v_mfma_scale_f32_16x16x128_f8f6f4 v[60:63], v[4:9], v[212:217], v[60:63], v162, v186 op_sel_hi:[0,0,0] cbsz:2 blgp:2
	s_nop 1
	v_mfma_scale_f32_16x16x128_f8f6f4 v[52:55], v[10:15], v[218:223], v[52:55], v158, v198 op_sel_hi:[0,0,0] cbsz:2 blgp:2
	s_nop 1
	v_mfma_scale_f32_16x16x128_f8f6f4 v[44:47], v[4:9], v[218:223], v[44:47], v162, v198 op_sel_hi:[0,0,0] cbsz:2 blgp:2
	s_nop 1
	v_mfma_scale_f32_16x16x128_f8f6f4 v[36:39], v[10:15], v[224:229], v[36:39], v158, v230 op_sel_hi:[0,0,0] cbsz:2 blgp:2
	s_nop 1
	v_mfma_scale_f32_16x16x128_f8f6f4 v[28:31], v[4:9], v[224:229], v[28:31], v162, v230 op_sel_hi:[0,0,0] cbsz:2 blgp:2
	s_setprio 0
	s_barrier
	s_add_i32 s55, s55, 2
	s_add_u32 s15, s15, 0x100
	s_addc_u32 s17, s17, 0
	s_add_u32 s26, s26, 0x100
	s_addc_u32 s27, s27, 0
	s_cmp_gt_u32 s55, 13
	s_cbranch_scc0 .LBB0_2846
	s_and_b64 vcc, exec, s[12:13]
	s_cbranch_vccz .LBB0_2849
	s_barrier

; __device__ __forceinline__ int lane_id() { int l_; asm volatile("v_mbcnt_lo_u32_b32 %0, -1, 0\n\tv_mbcnt_hi_u32_b32 %0, -1, %0" : "=v"(l_)); return l_; }
; #define PG8_STAGE(bufoff, gbase, voff) do { _Pragma("unroll") for (int _i = 0; _i < 2; ++_i) \
;         glds16((const void*)(gbase), (voff)[_i], ldsbase + (unsigned)(bufoff) + ldsw + (unsigned)_i * 8192u); } while (0)
; #define PG8_WAIT_V(n) asm volatile("s_waitcnt vmcnt(" #n ")" ::: "memory")
; #define PG8_BAR __builtin_amdgcn_s_barrier()
;     ...
;     int tid = w0_ * 64 + lane_id(); asm volatile("" : "+v"(tid));
;     const int wid = __builtin_amdgcn_readfirstlane(tid >> 6), lane = tid & 63, wr = wid >> 2, wc = wid & 3, fr = lane & 15, fq = lane >> 4;
;     const int nt = nt_ ? nt_ : Kb / 128;
;     unsigned voffA[2], voffB[2];
; #pragma unroll
;     for (int i = 0; i < 2; ++i) { int R, C; stage_rc(tid * 16 + i * 8192, R, C); const int Rb = Epi::PERM ? ((R & ~31) + perm32(R & 31)) : R;
;         voffA[i] = (unsigned)(R * ldab + C * 2); voffB[i] = (unsigned)(Rb * Kb + C * 2); }
;     const size_t kstep = (size_t)(BK * 2);
;     const size_t hstepA = (size_t)HALF * ldab, hstepB = (size_t)HALF * Kb;
;     const unsigned ldsw = (unsigned)wid * 1024u, ldsbase = (unsigned)(size_t)lds;
;     const int aoff = lds_byte(wr * 64 + fr, fq * 8), boff = lds_byte(wc * 32 + fr, fq * 8);
;     ...
;     Unit cur, nxt; int ui = 0;
;     if (!S.next(0, cur)) return;
;     f32x4 acc[2][2][4][2];
; #pragma unroll
;     for (int a = 0; a < 2; ++a)
; #pragma unroll
;         for (int b = 0; b < 2; ++b)
; #pragma unroll
;             for (int m = 0; m < 4; ++m)
; #pragma unroll
;                 for (int n = 0; n < 2; ++n) acc[a][b][m][n] = (f32x4){0.f, 0.f, 0.f, 0.f};
;     bf16x8 At[4][2], B0[2][2], B1[2][2];
;     const char* cA = uniform_ptr(cur.a); const char* cB = uniform_ptr(cur.b);
;     PG8_STAGE(PG8_SB(0, 0), cB, voffB); PG8_STAGE(PG8_SB(0, 1), cB + hstepB, voffB); PG8_STAGE(PG8_SA(0, 0), cA, voffA); PG8_STAGE(PG8_SA(0, 1), cA + hstepA, voffA);
;     if (wr == 1) PG8_BAR;
;     PG8_WAIT_V(2); PG8_BAR;
;     PG8_STAGE(PG8_SB(1, 0), cB + kstep, voffB); PG8_STAGE(PG8_SA(1, 0), cA + kstep, voffA); PG8_STAGE(PG8_SB(1, 1), cB + hstepB + kstep, voffB);
;     PG8_WAIT_V(6); PG8_BAR;
.LBB0_2910:
	s_or_b64 exec, exec, s[4:5]
	v_readlane_b32 s5, v250, 60
	s_waitcnt lgkmcnt(0)
	s_barrier
	s_lshl_b32 s4, s0, 3
	v_mbcnt_lo_u32_b32 v0, -1, 0
	v_mbcnt_hi_u32_b32 v0, -1, v0
	s_cmp_ge_i32 s78, s4
	v_add_u32_e32 v4, s5, v0
	s_nop 0
	v_readfirstlane_b32 s14, v4
	s_cbranch_scc1 .LBB0_2926
	v_bfe_i32 v1, v4, 27, 1
	v_lshlrev_b32_e32 v5, 4, v4
	v_lshrrev_b32_e32 v1, 22, v1
	v_add_u32_e32 v1, v5, v1
	v_and_b32_e32 v1, 0xfffffc00, v1
	v_sub_u32_e32 v1, v5, v1
	v_ashrrev_i32_e32 v0, 31, v4
	v_lshrrev_b32_e32 v2, 4, v1
	v_lshrrev_b32_e32 v0, 26, v0
	v_bitop3_b32 v1, v2, v1, 32 bitop3:0x6c
	v_add_u32_e32 v0, v4, v0
	v_ashrrev_i32_e32 v6, 31, v1
	v_ashrrev_i32_e32 v0, 6, v0
	v_lshrrev_b32_e32 v6, 26, v6
	v_lshlrev_b32_e32 v2, 3, v0
	v_add_u32_e32 v6, v1, v6
	v_and_b32_e32 v2, -16, v2
	v_ashrrev_i32_e32 v7, 6, v6
	v_add_u32_e32 v8, v7, v2
	v_and_b32_e32 v2, 0xc0, v6
	v_sub_u32_e32 v1, v1, v2
	v_lshlrev_b32_e32 v0, 5, v0
	v_ashrrev_i16_sdwa v1, v188, sext(v1) dst_sel:DWORD dst_unused:UNUSED_PAD src0_sel:DWORD src1_sel:BYTE_0
	v_lshlrev_b32_e32 v2, 1, v8
	v_lshrrev_b32_e32 v6, 2, v8
	v_and_b32_e32 v7, 3, v7
	s_mov_b32 s10, 0x3fffe0
	v_and_b32_e32 v0, 32, v0
	v_bfe_i32 v1, v1, 0, 16
	v_and_b32_e32 v2, 24, v2
	v_and_b32_e32 v6, 4, v6
	v_and_or_b32 v7, v8, s10, v7
	v_or3_b32 v6, v7, v6, v2
	v_add_lshl_u32 v2, v0, v1, 1
	s_movk_i32 s5, 0x1c00
	v_mad_u64_u32 v[0:1], s[8:9], v8, s5, v[2:3]
	v_mad_u32_u24 v1, v6, s5, v2
	v_add_u32_e32 v2, 0x2000, v5
	v_ashrrev_i32_e32 v5, 31, v2
	v_lshrrev_b32_e32 v5, 22, v5
	v_add_u32_e32 v5, v2, v5
	v_ashrrev_i32_e32 v5, 10, v5
	v_mul_i32_i24_e32 v6, 0x400, v5
	v_sub_u32_e32 v2, v2, v6
	v_lshrrev_b32_e32 v6, 4, v2
	v_bitop3_b32 v2, v6, v2, 32 bitop3:0x6c
	v_ashrrev_i32_e32 v7, 31, v2
	v_lshrrev_b32_e32 v7, 26, v7
	v_add_u32_e32 v7, v2, v7
	v_lshlrev_b32_e32 v6, 3, v5
	v_ashrrev_i32_e32 v8, 6, v7
	v_and_b32_e32 v7, 0xc0, v7
	v_and_b32_e32 v6, -16, v6
	v_sub_u32_e32 v2, v2, v7
	v_add_u32_e32 v6, v8, v6
	v_lshlrev_b32_e32 v5, 5, v5
	v_ashrrev_i16_sdwa v2, v188, sext(v2) dst_sel:DWORD dst_unused:UNUSED_PAD src0_sel:DWORD src1_sel:BYTE_0
	v_and_b32_e32 v5, 32, v5
	v_bfe_i32 v2, v2, 0, 16
	v_lshlrev_b32_e32 v7, 1, v6
	v_lshrrev_b32_e32 v9, 2, v6
	v_and_b32_e32 v8, 3, v8
	s_add_u32 s6, s2, 0x24500000
	v_and_b32_e32 v7, 24, v7
	v_and_b32_e32 v9, 4, v9
	v_and_or_b32 v8, v6, s10, v8
	v_add_lshl_u32 v2, v5, v2, 1
	s_addc_u32 s7, s3, 0
	v_or3_b32 v7, v8, v9, v7
	v_mad_u64_u32 v[164:165], s[8:9], v6, s5, v[2:3]
	s_ashr_i32 s16, s14, 6
	s_add_i32 s28, s0, 1
	s_ashr_i32 s15, s14, 8
	v_mad_u32_u24 v165, v7, s5, v2
	s_lshl_b32 s5, s16, 10
	s_add_u32 s29, s2, 0x3a892000
	v_readlane_b32 s8, v252, 62
	s_addc_u32 s30, s3, 0
	v_readlane_b32 s9, v252, 63
	s_and_b64 s[8:9], s[8:9], exec
	s_cselect_b32 s8, s28, s0
	v_readlane_b32 s9, v253, 16
	s_mul_i32 s8, s8, s9
	v_readlane_b32 s9, v253, 17
	s_add_i32 s8, s8, s9
	s_ashr_i32 s9, s8, 31
	s_lshr_b32 s9, s9, 26
	s_add_i32 s9, s8, s9
	s_ashr_i32 s10, s9, 6
	s_lshl_b32 s10, s10, 3
	s_sub_i32 s11, s0, s10
	s_min_i32 s11, s11, 8
	s_abs_i32 s13, s11
	v_cvt_f32_u32_e32 v2, s13
	s_sub_i32 s17, 0, s13
	s_andn2_b32 s9, s9, 63
	s_sub_i32 s8, s8, s9
	v_rcp_iflag_f32_e32 v2, v2
	s_abs_i32 s12, s8
	s_xor_b32 s9, s8, s11
	s_ashr_i32 s9, s9, 31
	v_mul_f32_e32 v2, 0x4f7ffffe, v2
	v_cvt_u32_f32_e32 v2, v2
	v_mov_b32_e32 v9, s1
	v_readfirstlane_b32 s18, v2
	s_mul_i32 s17, s17, s18
	s_mul_hi_u32 s17, s18, s17
	s_add_i32 s18, s18, s17
	s_mul_hi_u32 s17, s12, s18
	s_mul_i32 s18, s17, s13
	s_sub_i32 s12, s12, s18
	s_add_i32 s18, s17, 1
	s_sub_i32 s19, s12, s13
	s_cmp_ge_u32 s12, s13
	s_cselect_b32 s17, s18, s17
	s_cselect_b32 s12, s19, s12
	s_add_i32 s18, s17, 1
	s_cmp_ge_u32 s12, s13
	s_cselect_b32 s12, s18, s17
	s_xor_b32 s12, s12, s9
	s_sub_i32 s52, s12, s9
	s_mul_i32 s9, s52, s11
	s_sub_i32 s8, s8, s9
	s_add_i32 s53, s10, s8
	v_readlane_b32 s8, v254, 29
	v_readlane_b32 s9, v254, 30
	s_nop 0
	v_mov_b32_e32 v2, s8
	ds_read2_b32 v[6:7], v2 offset1:1
	v_mov_b32_e32 v2, s9
	v_readlane_b32 s9, v254, 31
	s_waitcnt lgkmcnt(0)
	v_readfirstlane_b32 s10, v6
	v_readfirstlane_b32 s8, v7
	ds_read2_b32 v[6:7], v2 offset1:1
	v_mov_b32_e32 v2, s9
	v_readlane_b32 s9, v254, 32
	s_cmp_ge_i32 s53, s8
	s_waitcnt lgkmcnt(0)
	v_readfirstlane_b32 s12, v6
	v_readfirstlane_b32 s13, v7
	ds_read2_b32 v[6:7], v2 offset1:1
	v_mov_b32_e32 v2, s9
	ds_read_b32 v2, v2
	s_cselect_b64 s[8:9], -1, 0
	s_cmp_ge_i32 s53, s10
	s_cselect_b64 s[10:11], -1, 0
	s_cmp_ge_i32 s53, s12
	s_waitcnt lgkmcnt(1)
	v_readfirstlane_b32 s17, v6
	s_cselect_b64 vcc, -1, 0
	s_cmp_ge_i32 s53, s13
	v_readfirstlane_b32 s18, v7
	s_waitcnt lgkmcnt(0)
	v_readfirstlane_b32 s19, v2
	v_cndmask_b32_e64 v2, 0, 1, s[8:9]
	v_cndmask_b32_e64 v5, 0, 1, s[10:11]
	s_cselect_b64 s[8:9], -1, 0
	s_cmp_ge_i32 s53, s17
	v_addc_co_u32_e32 v2, vcc, v2, v5, vcc
	v_cndmask_b32_e64 v6, 0, 1, s[8:9]
	v_mov_b32_e32 v7, s1
	s_cselect_b64 s[8:9], -1, 0
	s_cmp_ge_i32 s53, s18
	v_lshl_add_u64 v[6:7], v[2:3], 0, v[6:7]
	v_cndmask_b32_e64 v8, 0, 1, s[8:9]
	s_cselect_b64 s[8:9], -1, 0
	s_cmp_ge_i32 s53, s19
	v_lshl_add_u64 v[6:7], v[6:7], 0, v[8:9]
	v_cndmask_b32_e64 v8, 0, 1, s[8:9]
	s_cselect_b64 s[8:9], -1, 0
	v_lshl_add_u64 v[6:7], v[6:7], 0, v[8:9]
	v_cndmask_b32_e64 v8, 0, 1, s[8:9]
	v_lshl_add_u64 v[6:7], v[6:7], 0, v[8:9]
	s_mov_b32 s8, 0x1c00000
	v_mul_lo_u32 v2, v7, s8
	v_mul_hi_u32 v5, v6, s8
	v_add_u32_e32 v7, v5, v2
	v_mul_lo_u32 v6, v6, s8
	v_lshl_add_u64 v[6:7], s[6:7], 0, v[6:7]
	s_mul_hi_i32 s9, s52, 0x1c0000
	s_mul_i32 s8, s52, 0x1c0000
	v_lshl_add_u64 v[6:7], v[6:7], 0, s[8:9]
	s_mul_i32 s9, s53, 0x1c0000
	s_mul_hi_i32 s8, s53, 0x1c0000
	s_add_u32 s20, s29, s9
	s_addc_u32 s21, s30, s8
	s_add_i32 s31, s5, 0
	v_readfirstlane_b32 s23, v7
	v_readfirstlane_b32 s22, v6
	s_add_i32 s34, s31, 0x10000
	s_mov_b32 m0, s34
	s_nop 0
	global_load_lds_dwordx4 v1, s[22:23]
	s_add_i32 s35, s31, 0x12000
	s_mov_b32 m0, s35
	s_nop 0
	global_load_lds_dwordx4 v165, s[22:23]
	s_add_u32 s8, s22, 0xe0000
	s_addc_u32 s9, s23, 0
	s_add_i32 s36, s31, 0x14000
	s_mov_b32 m0, s36
	s_nop 0
	global_load_lds_dwordx4 v1, s[8:9]
	s_add_i32 s37, s31, 0x16000
	s_mov_b32 m0, s37
	s_nop 0
	global_load_lds_dwordx4 v165, s[8:9]
	s_add_i32 s38, s31, 0x2000
	s_mov_b32 m0, s31
	s_nop 0
	global_load_lds_dwordx4 v0, s[20:21]
	s_add_u32 s8, s20, 0xe0000
	s_mov_b32 m0, s38
	s_nop 0
	global_load_lds_dwordx4 v164, s[20:21]
	s_addc_u32 s9, s21, 0
	s_add_i32 s39, s31, 0x4000
	s_mov_b32 m0, s39
	s_nop 0
	global_load_lds_dwordx4 v0, s[8:9]
	s_add_i32 s40, s31, 0x6000
	s_mov_b32 m0, s40
	s_nop 0
	global_load_lds_dwordx4 v164, s[8:9]
	s_cmp_eq_u32 s15, 1
	s_cselect_b64 s[8:9], -1, 0
	s_cmp_lg_u32 s15, 1
	s_cbranch_scc1 .LBB0_2913
	s_barrier
; #define PG8_STAGE(bufoff, gbase, voff) do { _Pragma("unroll") for (int _i = 0; _i < 2; ++_i) \
;         glds16((const void*)(gbase), (voff)[_i], ldsbase + (unsigned)(bufoff) + ldsw + (unsigned)_i * 8192u); } while (0)
; #define PG8_WAIT_V(n) asm volatile("s_waitcnt vmcnt(" #n ")" ::: "memory")
; #define PG8_BAR __builtin_amdgcn_s_barrier()
;     __device__ __forceinline__ bool next(int i, Unit& u) const { if (!o.idx(i, u.pm, u.pn)) return false; u.tag = 0; u.a = A + (size_t)u.pm * astep; u.b = Bt + (size_t)u.pn * bstep; return true; }
;     ...
;     const unsigned ldsw = (unsigned)wid * 1024u, ldsbase = (unsigned)(size_t)lds;
;     const int aoff = lds_byte(wr * 64 + fr, fq * 8), boff = lds_byte(wc * 32 + fr, fq * 8);
;     ...
;     if (wr == 1) PG8_BAR;
;     PG8_WAIT_V(2); PG8_BAR;
;     PG8_STAGE(PG8_SB(1, 0), cB + kstep, voffB); PG8_STAGE(PG8_SA(1, 0), cA + kstep, voffA); PG8_STAGE(PG8_SB(1, 1), cB + hstepB + kstep, voffB);
;     PG8_WAIT_V(6); PG8_BAR;
;     for (;;) {
;         const bool has_next = S.next(ui + 1, nxt);
;         const char* nA = uniform_ptr(has_next ? nxt.a : cA); const char* nB = uniform_ptr(has_next ? nxt.b : cB);
.LBB0_2913:
	s_add_u32 s10, s2, 0x60c92000
	v_lshrrev_b32_e32 v5, 1, v4
	s_addc_u32 s11, s3, 0
	v_and_b32_e32 v5, 24, v5
	s_add_u32 s12, s2, 0x69512000
	v_and_b32_e32 v2, 15, v4
	v_lshlrev_b32_e32 v6, 1, v5
	v_lshlrev_b32_e32 v4, 2, v4
	s_addc_u32 s13, s3, 0
	v_lshl_or_b32 v166, s15, 6, v2
	v_lshl_or_b32 v2, v2, 6, v6
	s_lshl_b32 s2, s15, 13
	v_and_b32_e32 v4, 32, v4
	v_bitop3_b32 v6, v2, s2, v4 bitop3:0xde
	s_lshl_b32 s2, s16, 5
	s_and_b32 s16, s2, 0x60
	s_ashr_i32 s5, s4, 31
	s_lshl_b32 s2, s16, 7
	v_bitop3_b32 v2, v2, s2, v4 bitop3:0xde
	s_add_u32 s2, s22, 0x80
	s_waitcnt vmcnt(2)
	s_barrier
	s_addc_u32 s3, s23, 0
	s_add_i32 s41, s31, 0x18000
	s_mov_b32 m0, s41
	s_nop 0
	global_load_lds_dwordx4 v1, s[2:3]
	s_add_i32 s42, s31, 0x1a000
	s_mov_b32 m0, s42
	s_nop 0
	global_load_lds_dwordx4 v165, s[2:3]
	s_add_u32 s2, s20, 0x80
	s_addc_u32 s3, s21, 0
	s_add_i32 s43, s31, 0x8000
	s_mov_b32 m0, s43
	s_nop 0
	global_load_lds_dwordx4 v0, s[2:3]
	s_add_i32 s44, s31, 0xa000
	s_mov_b32 m0, s44
	s_nop 0
	global_load_lds_dwordx4 v164, s[2:3]
	s_add_u32 s2, s22, 0xe0080
	s_addc_u32 s3, s23, 0
	s_add_i32 s45, s31, 0x1c000
	s_mov_b32 m0, s45
	s_nop 0
	global_load_lds_dwordx4 v1, s[2:3]
	s_add_i32 s46, s31, 0x1e000
	s_mov_b32 m0, s46
	s_nop 0
	global_load_lds_dwordx4 v165, s[2:3]
	s_waitcnt vmcnt(6)
	s_add_i32 s47, s31, 0xc000
	s_cmpk_lt_u32 s14, 0x100
	s_cselect_b64 s[14:15], -1, 0
	s_add_i32 s48, s31, 0xe000
	v_or_b32_e32 v167, s16, v5
	s_mov_b32 s49, 0
	v_add_u32_e32 v168, 0, v2
	v_add_u32_e32 v169, 0, v6
	s_mov_b64 s[16:17], s[20:21]
	s_barrier
	s_branch .LBB0_2916

; #define PG8_STAGE(bufoff, gbase, voff) do { _Pragma("unroll") for (int _i = 0; _i < 2; ++_i) \
;         glds16((const void*)(gbase), (voff)[_i], ldsbase + (unsigned)(bufoff) + ldsw + (unsigned)_i * 8192u); } while (0)
; #define PG8_LDA(dst, b, h) do { _Pragma("unroll") for (int m = 0; m < 4; ++m) _Pragma("unroll") for (int k = 0; k < 2; ++k) dst[m][k] = *(const LAS bf16x8*)(lds + PG8_SA(b, h) + aoff + m * 2048 + k * 1024); } while (0)
; #define PG8_LDB(dst, b, h) do { _Pragma("unroll") for (int n = 0; n < 2; ++n) _Pragma("unroll") for (int k = 0; k < 2; ++k) dst[n][k] = *(const LAS bf16x8*)(lds + PG8_SB(b, h) + boff + n * 2048 + k * 1024); } while (0)
; #define PG8_WAIT_V(n) asm volatile("s_waitcnt vmcnt(" #n ")" ::: "memory")
; #define PG8_WAIT_L(n) asm volatile("s_waitcnt lgkmcnt(" #n ")" ::: "memory")
; #define PG8_BAR __builtin_amdgcn_s_barrier()
; #define PG8_SCHED __builtin_amdgcn_sched_barrier(0)
;     ...
;             PG8_LDB(B0, 0, 0); PG8_LDB(B1, 0, 1); PG8_SCHED; PG8_LDA(At, 0, 0); PG8_STAGE(PG8_SA(1, 1), a1 + hstepA, voffA);
;             PG8_WAIT_V(8); PG8_WAIT_L(0); PG8_BAR; PG8_MMA(0, 0, At, B0); PG8_MMA(0, 1, At, B1); PG8_BAR; PG8_SCHED;
;             PG8_LDA(At, 0, 1); PG8_STAGE(PG8_SB(0, 0), b2, voffB); PG8_STAGE(PG8_SB(0, 1), b2 + hstepB, voffB); PG8_STAGE(PG8_SA(0, 0), a2, voffA);
;             PG8_WAIT_V(8); PG8_WAIT_L(0); PG8_BAR; PG8_MMA(1, 0, At, B0); PG8_MMA(1, 1, At, B1); PG8_BAR; PG8_SCHED;
.LBB0_2919:
	v_add_u32_e32 v2, 0x10000, v168
	ds_read_b128 v[28:31], v2
	ds_read_b128 v[32:35], v2 offset:1024
	ds_read_b128 v[20:23], v2 offset:2048
	ds_read_b128 v[24:27], v2 offset:3072
	v_add_u32_e32 v2, 0x14000, v168
	ds_read_b128 v[12:15], v2
	ds_read_b128 v[16:19], v2 offset:1024
	ds_read_b128 v[4:7], v2 offset:2048
	ds_read_b128 v[8:11], v2 offset:3072
	s_add_u32 s22, s20, 0xfff20080
	s_addc_u32 s23, s21, -1
	s_cmp_eq_u32 s56, 52
	s_cselect_b32 s26, s16, s22
	s_cselect_b32 s27, s17, s23
	s_cselect_b32 s24, s18, s54
	s_cselect_b32 s25, s19, s55
	s_add_u32 s22, s26, 0x80
	s_addc_u32 s23, s27, 0
	ds_read_b128 v[176:179], v169
	ds_read_b128 v[180:183], v169 offset:1024
	ds_read_b128 v[206:209], v169 offset:2048
	ds_read_b128 v[210:213], v169 offset:3072
	ds_read_b128 v[214:217], v169 offset:4096
	ds_read_b128 v[218:221], v169 offset:5120
	ds_read_b128 v[222:225], v169 offset:6144
	ds_read_b128 v[226:229], v169 offset:7168
	s_mov_b32 m0, s47
	s_nop 0
	global_load_lds_dwordx4 v0, s[20:21]
	s_nop 0
	s_mov_b32 m0, s48
	s_nop 0
	global_load_lds_dwordx4 v164, s[20:21]
	s_waitcnt vmcnt(8)
	s_waitcnt lgkmcnt(0)
	s_barrier
	s_setprio 1
	s_waitcnt lgkmcnt(6)
	v_mfma_scale_f32_16x16x128_f8f6f4 v[160:163], v[28:35], v[176:183], v[160:163], v189, v193 op_sel_hi:[0,0,0]
	v_mfma_scale_f32_16x16x128_f8f6f4 v[156:159], v[20:27], v[176:183], v[156:159], v189, v193 op_sel_hi:[0,0,0]
	s_waitcnt lgkmcnt(4)
	v_mfma_scale_f32_16x16x128_f8f6f4 v[152:155], v[28:35], v[206:213], v[152:155], v189, v193 op_sel_hi:[0,0,0]
	v_mfma_scale_f32_16x16x128_f8f6f4 v[148:151], v[20:27], v[206:213], v[148:151], v189, v193 op_sel_hi:[0,0,0]
	s_waitcnt lgkmcnt(2)
	v_mfma_scale_f32_16x16x128_f8f6f4 v[132:135], v[28:35], v[214:221], v[132:135], v189, v193 op_sel_hi:[0,0,0]
	v_mfma_scale_f32_16x16x128_f8f6f4 v[124:127], v[20:27], v[214:221], v[124:127], v189, v193 op_sel_hi:[0,0,0]
	s_waitcnt lgkmcnt(0)
	v_mfma_scale_f32_16x16x128_f8f6f4 v[116:119], v[28:35], v[222:229], v[116:119], v189, v193 op_sel_hi:[0,0,0]
	v_mfma_scale_f32_16x16x128_f8f6f4 v[108:111], v[20:27], v[222:229], v[108:111], v189, v193 op_sel_hi:[0,0,0]
	s_setprio 0
	s_setprio 1
	v_mfma_scale_f32_16x16x128_f8f6f4 v[144:147], v[12:19], v[176:183], v[144:147], v189, v193 op_sel_hi:[0,0,0]
	v_mfma_scale_f32_16x16x128_f8f6f4 v[140:143], v[4:11], v[176:183], v[140:143], v189, v193 op_sel_hi:[0,0,0]
	v_mfma_scale_f32_16x16x128_f8f6f4 v[136:139], v[12:19], v[206:213], v[136:139], v189, v193 op_sel_hi:[0,0,0]
	v_mfma_scale_f32_16x16x128_f8f6f4 v[128:131], v[4:11], v[206:213], v[128:131], v189, v193 op_sel_hi:[0,0,0]
	v_mfma_scale_f32_16x16x128_f8f6f4 v[120:123], v[12:19], v[214:221], v[120:123], v189, v193 op_sel_hi:[0,0,0]
	v_mfma_scale_f32_16x16x128_f8f6f4 v[112:115], v[4:11], v[214:221], v[112:115], v189, v193 op_sel_hi:[0,0,0]
	v_mfma_scale_f32_16x16x128_f8f6f4 v[104:107], v[12:19], v[222:229], v[104:107], v189, v193 op_sel_hi:[0,0,0]
	v_mfma_scale_f32_16x16x128_f8f6f4 v[100:103], v[4:11], v[222:229], v[100:103], v189, v193 op_sel_hi:[0,0,0]
	s_setprio 0
	s_barrier
	ds_read_b128 v[176:179], v169 offset:16384
	ds_read_b128 v[180:183], v169 offset:17408
	ds_read_b128 v[206:209], v169 offset:18432
	ds_read_b128 v[210:213], v169 offset:19456
	ds_read_b128 v[214:217], v169 offset:20480
	ds_read_b128 v[218:221], v169 offset:21504
	ds_read_b128 v[222:225], v169 offset:22528
	ds_read_b128 v[226:229], v169 offset:23552
	s_mov_b32 m0, s34
	s_nop 0
	global_load_lds_dwordx4 v1, s[24:25]
	s_add_u32 s58, s24, 0xe0000
	s_mov_b32 m0, s35
	s_nop 0
	global_load_lds_dwordx4 v165, s[24:25]
	s_addc_u32 s59, s25, 0
	s_mov_b32 m0, s36
	s_nop 0
	global_load_lds_dwordx4 v1, s[58:59]
	s_nop 0
	s_mov_b32 m0, s37
	s_nop 0
	global_load_lds_dwordx4 v165, s[58:59]
	s_nop 0
	s_mov_b32 m0, s31
	s_nop 0
	global_load_lds_dwordx4 v0, s[26:27]
	s_nop 0
	s_mov_b32 m0, s38
	s_nop 0
	global_load_lds_dwordx4 v164, s[26:27]
	s_waitcnt vmcnt(8)
	s_waitcnt lgkmcnt(0)
	s_barrier
	s_setprio 1
	s_waitcnt lgkmcnt(6)
	v_mfma_scale_f32_16x16x128_f8f6f4 v[96:99], v[28:35], v[176:183], v[96:99], v189, v193 op_sel_hi:[0,0,0]
	v_mfma_scale_f32_16x16x128_f8f6f4 v[92:95], v[20:27], v[176:183], v[92:95], v189, v193 op_sel_hi:[0,0,0]
	s_waitcnt lgkmcnt(4)
	v_mfma_scale_f32_16x16x128_f8f6f4 v[84:87], v[28:35], v[206:213], v[84:87], v189, v193 op_sel_hi:[0,0,0]
	v_mfma_scale_f32_16x16x128_f8f6f4 v[76:79], v[20:27], v[206:213], v[76:79], v189, v193 op_sel_hi:[0,0,0]
	s_waitcnt lgkmcnt(2)
	v_mfma_scale_f32_16x16x128_f8f6f4 v[68:71], v[28:35], v[214:221], v[68:71], v189, v193 op_sel_hi:[0,0,0]
	v_mfma_scale_f32_16x16x128_f8f6f4 v[60:63], v[20:27], v[214:221], v[60:63], v189, v193 op_sel_hi:[0,0,0]
	s_waitcnt lgkmcnt(0)
	v_mfma_scale_f32_16x16x128_f8f6f4 v[52:55], v[28:35], v[222:229], v[52:55], v189, v193 op_sel_hi:[0,0,0]
	v_mfma_scale_f32_16x16x128_f8f6f4 v[44:47], v[20:27], v[222:229], v[44:47], v189, v193 op_sel_hi:[0,0,0]
	s_setprio 0
	s_setprio 1
	v_mfma_scale_f32_16x16x128_f8f6f4 v[88:91], v[12:19], v[176:183], v[88:91], v189, v193 op_sel_hi:[0,0,0]
	v_mfma_scale_f32_16x16x128_f8f6f4 v[80:83], v[4:11], v[176:183], v[80:83], v189, v193 op_sel_hi:[0,0,0]
	v_mfma_scale_f32_16x16x128_f8f6f4 v[72:75], v[12:19], v[206:213], v[72:75], v189, v193 op_sel_hi:[0,0,0]
	v_mfma_scale_f32_16x16x128_f8f6f4 v[64:67], v[4:11], v[206:213], v[64:67], v189, v193 op_sel_hi:[0,0,0]
	v_mfma_scale_f32_16x16x128_f8f6f4 v[56:59], v[12:19], v[214:221], v[56:59], v189, v193 op_sel_hi:[0,0,0]
	v_mfma_scale_f32_16x16x128_f8f6f4 v[48:51], v[4:11], v[214:221], v[48:51], v189, v193 op_sel_hi:[0,0,0]
	v_mfma_scale_f32_16x16x128_f8f6f4 v[40:43], v[12:19], v[222:229], v[40:43], v189, v193 op_sel_hi:[0,0,0]
	v_mfma_scale_f32_16x16x128_f8f6f4 v[36:39], v[4:11], v[222:229], v[36:39], v189, v193 op_sel_hi:[0,0,0]
	s_setprio 0
	s_barrier
; #define PG8_STAGE(bufoff, gbase, voff) do { _Pragma("unroll") for (int _i = 0; _i < 2; ++_i) \
;         glds16((const void*)(gbase), (voff)[_i], ldsbase + (unsigned)(bufoff) + ldsw + (unsigned)_i * 8192u); } while (0)
; #define PG8_LDA(dst, b, h) do { _Pragma("unroll") for (int m = 0; m < 4; ++m) _Pragma("unroll") for (int k = 0; k < 2; ++k) dst[m][k] = *(const LAS bf16x8*)(lds + PG8_SA(b, h) + aoff + m * 2048 + k * 1024); } while (0)
; #define PG8_LDB(dst, b, h) do { _Pragma("unroll") for (int n = 0; n < 2; ++n) _Pragma("unroll") for (int k = 0; k < 2; ++k) dst[n][k] = *(const LAS bf16x8*)(lds + PG8_SB(b, h) + boff + n * 2048 + k * 1024); } while (0)
; #define PG8_WAIT_V(n) asm volatile("s_waitcnt vmcnt(" #n ")" ::: "memory")
; #define PG8_WAIT_L(n) asm volatile("s_waitcnt lgkmcnt(" #n ")" ::: "memory")
; #define PG8_BAR __builtin_amdgcn_s_barrier()
; #define PG8_SCHED __builtin_amdgcn_sched_barrier(0)
;     ...
;             PG8_LDB(B0, 1, 0); PG8_LDB(B1, 1, 1); PG8_SCHED; PG8_LDA(At, 1, 0); PG8_STAGE(PG8_SA(0, 1), a2 + hstepA, voffA);
;             PG8_WAIT_V(8); PG8_WAIT_L(0); PG8_BAR; PG8_MMA(0, 0, At, B0); PG8_MMA(0, 1, At, B1); PG8_BAR; PG8_SCHED;
;             PG8_LDA(At, 1, 1); PG8_STAGE(PG8_SB(1, 0), b3, voffB); PG8_STAGE(PG8_SB(1, 1), b3 + hstepB, voffB); PG8_STAGE(PG8_SA(1, 0), a3, voffA);
;             PG8_WAIT_V(8); PG8_WAIT_L(0); PG8_BAR; PG8_MMA(1, 0, At, B0); PG8_MMA(1, 1, At, B1); PG8_BAR; PG8_SCHED;
;         }
	v_add_u32_e32 v2, 0x18000, v168
	ds_read_b128 v[20:23], v2
	ds_read_b128 v[24:27], v2 offset:1024
	ds_read_b128 v[28:31], v2 offset:2048
	ds_read_b128 v[32:35], v2 offset:3072
	v_add_u32_e32 v2, 0x1c000, v168
	ds_read_b128 v[12:15], v2
	ds_read_b128 v[16:19], v2 offset:1024
	ds_read_b128 v[4:7], v2 offset:2048
	ds_read_b128 v[8:11], v2 offset:3072
	ds_read_b128 v[176:179], v169 offset:32768
	ds_read_b128 v[180:183], v169 offset:33792
	ds_read_b128 v[206:209], v169 offset:34816
	ds_read_b128 v[210:213], v169 offset:35840
	ds_read_b128 v[214:217], v169 offset:36864
	ds_read_b128 v[218:221], v169 offset:37888
	ds_read_b128 v[222:225], v169 offset:38912
	ds_read_b128 v[226:229], v169 offset:39936
	s_add_u32 s26, s26, 0xe0000
	s_addc_u32 s27, s27, 0
	s_mov_b32 m0, s39
	s_nop 0
	global_load_lds_dwordx4 v0, s[26:27]
	s_nop 0
	s_mov_b32 m0, s40
	s_nop 0
	global_load_lds_dwordx4 v164, s[26:27]
	s_waitcnt vmcnt(8)
	s_waitcnt lgkmcnt(0)
	s_barrier
	s_setprio 1
	s_waitcnt lgkmcnt(6)
	v_mfma_scale_f32_16x16x128_f8f6f4 v[160:163], v[20:27], v[176:183], v[160:163], v189, v193 op_sel_hi:[0,0,0]
	v_mfma_scale_f32_16x16x128_f8f6f4 v[156:159], v[28:35], v[176:183], v[156:159], v189, v193 op_sel_hi:[0,0,0]
	s_waitcnt lgkmcnt(4)
	v_mfma_scale_f32_16x16x128_f8f6f4 v[152:155], v[20:27], v[206:213], v[152:155], v189, v193 op_sel_hi:[0,0,0]
	v_mfma_scale_f32_16x16x128_f8f6f4 v[148:151], v[28:35], v[206:213], v[148:151], v189, v193 op_sel_hi:[0,0,0]
	s_waitcnt lgkmcnt(2)
	v_mfma_scale_f32_16x16x128_f8f6f4 v[132:135], v[20:27], v[214:221], v[132:135], v189, v193 op_sel_hi:[0,0,0]
	v_mfma_scale_f32_16x16x128_f8f6f4 v[124:127], v[28:35], v[214:221], v[124:127], v189, v193 op_sel_hi:[0,0,0]
	s_waitcnt lgkmcnt(0)
	v_mfma_scale_f32_16x16x128_f8f6f4 v[116:119], v[20:27], v[222:229], v[116:119], v189, v193 op_sel_hi:[0,0,0]
	v_mfma_scale_f32_16x16x128_f8f6f4 v[108:111], v[28:35], v[222:229], v[108:111], v189, v193 op_sel_hi:[0,0,0]
	s_setprio 0
	s_setprio 1
	v_mfma_scale_f32_16x16x128_f8f6f4 v[144:147], v[12:19], v[176:183], v[144:147], v189, v193 op_sel_hi:[0,0,0]
	v_mfma_scale_f32_16x16x128_f8f6f4 v[140:143], v[4:11], v[176:183], v[140:143], v189, v193 op_sel_hi:[0,0,0]
	v_mfma_scale_f32_16x16x128_f8f6f4 v[136:139], v[12:19], v[206:213], v[136:139], v189, v193 op_sel_hi:[0,0,0]
	v_mfma_scale_f32_16x16x128_f8f6f4 v[128:131], v[4:11], v[206:213], v[128:131], v189, v193 op_sel_hi:[0,0,0]
	v_mfma_scale_f32_16x16x128_f8f6f4 v[120:123], v[12:19], v[214:221], v[120:123], v189, v193 op_sel_hi:[0,0,0]
	v_mfma_scale_f32_16x16x128_f8f6f4 v[112:115], v[4:11], v[214:221], v[112:115], v189, v193 op_sel_hi:[0,0,0]
	v_mfma_scale_f32_16x16x128_f8f6f4 v[104:107], v[12:19], v[222:229], v[104:107], v189, v193 op_sel_hi:[0,0,0]
	v_mfma_scale_f32_16x16x128_f8f6f4 v[100:103], v[4:11], v[222:229], v[100:103], v189, v193 op_sel_hi:[0,0,0]
	s_setprio 0
	s_barrier
	ds_read_b128 v[176:179], v169 offset:49152
	ds_read_b128 v[180:183], v169 offset:50176
	ds_read_b128 v[206:209], v169 offset:51200
	ds_read_b128 v[210:213], v169 offset:52224
	ds_read_b128 v[214:217], v169 offset:53248
	ds_read_b128 v[218:221], v169 offset:54272
	ds_read_b128 v[222:225], v169 offset:55296
	ds_read_b128 v[226:229], v169 offset:56320
	s_add_u32 s26, s24, 0x80
	s_addc_u32 s27, s25, 0
	s_mov_b32 m0, s41
	s_nop 0
	global_load_lds_dwordx4 v1, s[26:27]
	s_add_u32 s24, s24, 0xe0080
	s_mov_b32 m0, s42
	s_nop 0
	global_load_lds_dwordx4 v165, s[26:27]
	s_addc_u32 s25, s25, 0
	s_mov_b32 m0, s45
	s_nop 0
	global_load_lds_dwordx4 v1, s[24:25]
	s_nop 0
	s_mov_b32 m0, s46
	s_nop 0
	global_load_lds_dwordx4 v165, s[24:25]
	s_mov_b32 m0, s43
	s_nop 0
	global_load_lds_dwordx4 v0, s[22:23]
	s_nop 0
	s_mov_b32 m0, s44
	s_nop 0
	global_load_lds_dwordx4 v164, s[22:23]
	s_waitcnt vmcnt(8)
	s_waitcnt lgkmcnt(0)
	s_barrier
	s_setprio 1
	s_waitcnt lgkmcnt(6)
	v_mfma_scale_f32_16x16x128_f8f6f4 v[96:99], v[20:27], v[176:183], v[96:99], v189, v193 op_sel_hi:[0,0,0]
	v_mfma_scale_f32_16x16x128_f8f6f4 v[92:95], v[28:35], v[176:183], v[92:95], v189, v193 op_sel_hi:[0,0,0]
	s_waitcnt lgkmcnt(4)
	v_mfma_scale_f32_16x16x128_f8f6f4 v[84:87], v[20:27], v[206:213], v[84:87], v189, v193 op_sel_hi:[0,0,0]
	v_mfma_scale_f32_16x16x128_f8f6f4 v[76:79], v[28:35], v[206:213], v[76:79], v189, v193 op_sel_hi:[0,0,0]
	s_waitcnt lgkmcnt(2)
	v_mfma_scale_f32_16x16x128_f8f6f4 v[68:71], v[20:27], v[214:221], v[68:71], v189, v193 op_sel_hi:[0,0,0]
	v_mfma_scale_f32_16x16x128_f8f6f4 v[60:63], v[28:35], v[214:221], v[60:63], v189, v193 op_sel_hi:[0,0,0]
	s_waitcnt lgkmcnt(0)
	v_mfma_scale_f32_16x16x128_f8f6f4 v[52:55], v[20:27], v[222:229], v[52:55], v189, v193 op_sel_hi:[0,0,0]
	v_mfma_scale_f32_16x16x128_f8f6f4 v[44:47], v[28:35], v[222:229], v[44:47], v189, v193 op_sel_hi:[0,0,0]
	s_setprio 0
	s_setprio 1
	v_mfma_scale_f32_16x16x128_f8f6f4 v[88:91], v[12:19], v[176:183], v[88:91], v189, v193 op_sel_hi:[0,0,0]
	v_mfma_scale_f32_16x16x128_f8f6f4 v[80:83], v[4:11], v[176:183], v[80:83], v189, v193 op_sel_hi:[0,0,0]
	v_mfma_scale_f32_16x16x128_f8f6f4 v[72:75], v[12:19], v[206:213], v[72:75], v189, v193 op_sel_hi:[0,0,0]
	v_mfma_scale_f32_16x16x128_f8f6f4 v[64:67], v[4:11], v[206:213], v[64:67], v189, v193 op_sel_hi:[0,0,0]
	v_mfma_scale_f32_16x16x128_f8f6f4 v[56:59], v[12:19], v[214:221], v[56:59], v189, v193 op_sel_hi:[0,0,0]
	v_mfma_scale_f32_16x16x128_f8f6f4 v[48:51], v[4:11], v[214:221], v[48:51], v189, v193 op_sel_hi:[0,0,0]
	v_mfma_scale_f32_16x16x128_f8f6f4 v[40:43], v[12:19], v[222:229], v[40:43], v189, v193 op_sel_hi:[0,0,0]
	v_mfma_scale_f32_16x16x128_f8f6f4 v[36:39], v[4:11], v[222:229], v[36:39], v189, v193 op_sel_hi:[0,0,0]
	s_setprio 0
	s_barrier
	s_add_i32 s56, s56, 2
	s_add_u32 s54, s54, 0x100
	s_addc_u32 s55, s55, 0
	s_add_u32 s20, s20, 0x100
	s_addc_u32 s21, s21, 0
	s_cmp_gt_u32 s56, 53
	s_cbranch_scc0 .LBB0_2919
	s_and_b64 vcc, exec, s[14:15]
	s_cbranch_vccz .LBB0_2922
	s_barrier

; __device__ __forceinline__ int lane_id() { int l_; asm volatile("v_mbcnt_lo_u32_b32 %0, -1, 0\n\tv_mbcnt_hi_u32_b32 %0, -1, %0" : "=v"(l_)); return l_; }
; #define PG8_STAGE(bufoff, gbase, voff) do { _Pragma("unroll") for (int _i = 0; _i < 2; ++_i) \
;         glds16((const void*)(gbase), (voff)[_i], ldsbase + (unsigned)(bufoff) + ldsw + (unsigned)_i * 8192u); } while (0)
; #define PG8_WAIT_V(n) asm volatile("s_waitcnt vmcnt(" #n ")" ::: "memory")
; #define PG8_BAR __builtin_amdgcn_s_barrier()
;     ...
;     int tid = w0_ * 64 + lane_id(); asm volatile("" : "+v"(tid));
;     const int wid = __builtin_amdgcn_readfirstlane(tid >> 6), lane = tid & 63, wr = wid >> 2, wc = wid & 3, fr = lane & 15, fq = lane >> 4;
;     const int nt = nt_ ? nt_ : Kb / 128;
;     unsigned voffA[2], voffB[2];
; #pragma unroll
;     for (int i = 0; i < 2; ++i) { int R, C; stage_rc(tid * 16 + i * 8192, R, C); const int Rb = Epi::PERM ? ((R & ~31) + perm32(R & 31)) : R;
;         voffA[i] = (unsigned)(R * ldab + C * 2); voffB[i] = (unsigned)(Rb * Kb + C * 2); }
;     const size_t kstep = (size_t)(BK * 2);
;     const size_t hstepA = (size_t)HALF * ldab, hstepB = (size_t)HALF * Kb;
;     const unsigned ldsw = (unsigned)wid * 1024u, ldsbase = (unsigned)(size_t)lds;
;     const int aoff = lds_byte(wr * 64 + fr, fq * 8), boff = lds_byte(wc * 32 + fr, fq * 8);
;     ...
;     Unit cur, nxt; int ui = 0;
;     if (!S.next(0, cur)) return;
;     f32x4 acc[2][2][4][2];
; #pragma unroll
;     for (int a = 0; a < 2; ++a)
; #pragma unroll
;         for (int b = 0; b < 2; ++b)
; #pragma unroll
;             for (int m = 0; m < 4; ++m)
; #pragma unroll
;                 for (int n = 0; n < 2; ++n) acc[a][b][m][n] = (f32x4){0.f, 0.f, 0.f, 0.f};
;     bf16x8 At[4][2], B0[2][2], B1[2][2];
;     const char* cA = uniform_ptr(cur.a); const char* cB = uniform_ptr(cur.b);
;     PG8_STAGE(PG8_SB(0, 0), cB, voffB); PG8_STAGE(PG8_SB(0, 1), cB + hstepB, voffB); PG8_STAGE(PG8_SA(0, 0), cA, voffA); PG8_STAGE(PG8_SA(0, 1), cA + hstepA, voffA);
;     if (wr == 1) PG8_BAR;
;     PG8_WAIT_V(2); PG8_BAR;
;     PG8_STAGE(PG8_SB(1, 0), cB + kstep, voffB); PG8_STAGE(PG8_SA(1, 0), cA + kstep, voffA); PG8_STAGE(PG8_SB(1, 1), cB + hstepB + kstep, voffB);
;     PG8_WAIT_V(6); PG8_BAR;
.LBB0_3046:
	v_readlane_b32 s2, v252, 50
	v_readlane_b32 s3, v252, 51
	s_andn2_b64 vcc, exec, s[2:3]
	s_cbranch_vccnz .LBB0_3115
	s_mov_b64 s[2:3], 0
	v_mbcnt_lo_u32_b32 v0, -1, 0
	v_mbcnt_hi_u32_b32 v0, -1, v0
	v_readlane_b32 s0, v250, 60
	v_readlane_b32 s4, v252, 52
	v_readlane_b32 s5, v252, 53
	v_add_u32_e32 v0, s0, v0
	s_andn2_b64 vcc, exec, s[4:5]
	v_mbcnt_lo_u32_b32 v0, -1, 0
	v_mbcnt_hi_u32_b32 v0, -1, v0
	s_nop 0
	v_add_u32_e32 v0, s0, v0
	s_nop 0
	v_readfirstlane_b32 s10, v0
	s_cbranch_vccnz .LBB0_3063
	v_bfe_i32 v4, v0, 27, 1
	v_lshlrev_b32_e32 v2, 4, v0
	v_lshrrev_b32_e32 v4, 22, v4
	v_add_u32_e32 v4, v2, v4
	v_and_b32_e32 v4, 0xfffffc00, v4
	v_sub_u32_e32 v4, v2, v4
	s_waitcnt lgkmcnt(0)
	v_ashrrev_i32_e32 v1, 31, v0
	v_lshrrev_b32_e32 v5, 4, v4
	v_lshrrev_b32_e32 v1, 26, v1
	v_bitop3_b32 v4, v5, v4, 32 bitop3:0x6c
	v_add_u32_e32 v1, v0, v1
	v_ashrrev_i32_e32 v6, 31, v4
	v_ashrrev_i32_e32 v1, 6, v1
	v_lshrrev_b32_e32 v6, 26, v6
	v_lshlrev_b32_e32 v5, 3, v1
	v_add_u32_e32 v6, v4, v6
	v_and_b32_e32 v5, -16, v5
	v_ashrrev_i32_e32 v7, 6, v6
	v_and_b32_e32 v6, 0xc0, v6
	v_add_u32_e32 v5, v7, v5
	v_sub_u32_e32 v4, v4, v6
	v_lshlrev_b32_e32 v1, 5, v1
	v_ashrrev_i16_sdwa v4, v188, sext(v4) dst_sel:DWORD dst_unused:UNUSED_PAD src0_sel:DWORD src1_sel:BYTE_0
	v_lshlrev_b32_e32 v6, 1, v5
	v_lshrrev_b32_e32 v8, 2, v5
	v_and_b32_e32 v7, 3, v7
	s_mov_b32 s4, 0xfffe0
	v_and_b32_e32 v1, 32, v1
	v_bfe_i32 v4, v4, 0, 16
	v_and_b32_e32 v6, 24, v6
	v_and_b32_e32 v8, 4, v8
	v_and_or_b32 v7, v5, s4, v7
	v_or3_b32 v6, v7, v8, v6
	v_add_lshl_u32 v4, v1, v4, 1
	v_add_u32_e32 v2, 0x2000, v2
	v_lshl_add_u32 v1, v5, 12, v4
	s_waitcnt vmcnt(0)
	v_lshl_add_u32 v137, v6, 12, v4
	v_ashrrev_i32_e32 v4, 31, v2
	v_lshrrev_b32_e32 v4, 22, v4
	v_add_u32_e32 v4, v2, v4
	v_ashrrev_i32_e32 v4, 10, v4
	v_mul_i32_i24_e32 v5, 0x400, v4
	v_sub_u32_e32 v2, v2, v5
	v_lshrrev_b32_e32 v5, 4, v2
	s_add_u32 s8, s80, s2
	v_bitop3_b32 v2, v5, v2, 32 bitop3:0x6c
	s_addc_u32 s3, s81, s3
	v_ashrrev_i32_e32 v6, 31, v2
	s_add_u32 s0, s8, 0x32892000
	v_lshrrev_b32_e32 v6, 26, v6
	s_addc_u32 s28, s3, 0
	v_lshlrev_b32_e32 v5, 3, v4
	v_add_u32_e32 v6, v2, v6
	s_add_u32 s29, s8, 0x4300000
	v_and_b32_e32 v5, -16, v5
	v_ashrrev_i32_e32 v7, 6, v6
	s_addc_u32 s30, s3, 0
	v_add_u32_e32 v5, v7, v5
	v_and_b32_e32 v7, 3, v7
	s_ashr_i32 s11, s10, 6
	s_ashr_i32 s2, s10, 8
	v_and_or_b32 v7, v5, s4, v7
	s_lshl_b32 s4, s11, 10
	v_readlane_b32 s6, v253, 24
	v_and_b32_e32 v6, 0xc0, v6
	v_readlane_b32 s7, v253, 25
	s_add_u32 s22, s29, s6
	v_sub_u32_e32 v2, v2, v6
	s_addc_u32 s23, s30, s7
	v_readlane_b32 s6, v253, 32
	v_lshlrev_b32_e32 v4, 5, v4
	v_ashrrev_i16_sdwa v2, v188, sext(v2) dst_sel:DWORD dst_unused:UNUSED_PAD src0_sel:DWORD src1_sel:BYTE_0
	v_lshlrev_b32_e32 v6, 1, v5
	v_lshrrev_b32_e32 v8, 2, v5
	v_readlane_b32 s7, v253, 33
	s_add_u32 s20, s0, s6
	v_and_b32_e32 v4, 32, v4
	v_bfe_i32 v2, v2, 0, 16
	v_and_b32_e32 v6, 24, v6
	v_and_b32_e32 v8, 4, v8
	s_addc_u32 s21, s28, s7
	s_add_i32 s31, s4, 0
	v_or3_b32 v6, v7, v8, v6
	v_add_lshl_u32 v2, v4, v2, 1
	s_add_i32 s34, s31, 0x10000
	s_mov_b32 m0, s34
	s_nop 0
	global_load_lds_dwordx4 v137, s[22:23]
	v_lshl_add_u32 v141, v6, 12, v2
	s_add_i32 s35, s31, 0x12000
	s_mov_b32 m0, s35
	s_nop 0
	global_load_lds_dwordx4 v141, s[22:23]
	s_add_u32 s4, s22, 0x80000
	s_addc_u32 s5, s23, 0
	s_add_i32 s36, s31, 0x14000
	s_mov_b32 m0, s36
	s_nop 0
	global_load_lds_dwordx4 v137, s[4:5]
	s_add_i32 s37, s31, 0x16000
	s_mov_b32 m0, s37
	s_nop 0
	global_load_lds_dwordx4 v141, s[4:5]
	s_mov_b32 m0, s31
	s_nop 0
	global_load_lds_dwordx4 v1, s[20:21]
	v_lshl_add_u32 v139, v5, 12, v2
	s_add_i32 s38, s31, 0x2000
	s_mov_b32 m0, s38
	s_nop 0
	global_load_lds_dwordx4 v139, s[20:21]
	s_add_u32 s4, s20, 0x80000
	s_addc_u32 s5, s21, 0
	s_add_i32 s39, s31, 0x4000
	s_mov_b32 m0, s39
	s_nop 0
	global_load_lds_dwordx4 v1, s[4:5]
	s_add_i32 s40, s31, 0x6000
	s_mov_b32 m0, s40
	s_nop 0
	global_load_lds_dwordx4 v139, s[4:5]
	s_cmp_eq_u32 s2, 1
	s_cselect_b64 s[4:5], -1, 0
	s_cmp_lg_u32 s2, 1
	s_cbranch_scc1 .LBB0_3050
	s_barrier
.LBB0_3050:
	s_add_u32 s6, s8, 0x3a892000
	v_lshrrev_b32_e32 v4, 1, v0
	s_addc_u32 s7, s3, 0
	v_and_b32_e32 v4, 24, v4
	s_add_u32 s8, s8, 0x32882000
	v_and_b32_e32 v2, 15, v0
	v_lshlrev_b32_e32 v5, 1, v4
	v_lshlrev_b32_e32 v0, 2, v0
	s_addc_u32 s9, s3, 0
	v_lshl_or_b32 v145, s2, 6, v2
	v_lshl_or_b32 v2, v2, 6, v5
	s_lshl_b32 s2, s2, 13
	v_and_b32_e32 v0, 32, v0
	v_bitop3_b32 v5, v2, s2, v0 bitop3:0xde
	s_lshl_b32 s2, s11, 5
	s_and_b32 s12, s2, 0x60
	s_lshl_b32 s2, s12, 7
	v_bitop3_b32 v0, v2, s2, v0 bitop3:0xde
	s_add_u32 s2, s22, 0x80
	s_waitcnt vmcnt(2)
	s_barrier
	s_addc_u32 s3, s23, 0
	s_add_i32 s41, s31, 0x18000
	s_mov_b32 m0, s41
	s_nop 0
	global_load_lds_dwordx4 v137, s[2:3]
	s_add_i32 s42, s31, 0x1a000
	s_mov_b32 m0, s42
	s_nop 0
	global_load_lds_dwordx4 v141, s[2:3]
	s_add_u32 s2, s20, 0x80
	s_addc_u32 s3, s21, 0
	s_add_i32 s43, s31, 0x8000
	s_mov_b32 m0, s43
	s_nop 0
	global_load_lds_dwordx4 v1, s[2:3]
	s_add_i32 s44, s31, 0xa000
	s_mov_b32 m0, s44
	s_nop 0
	global_load_lds_dwordx4 v139, s[2:3]
	s_add_u32 s2, s22, 0x80080
	s_addc_u32 s3, s23, 0
	s_add_i32 s45, s31, 0x1c000
	s_mov_b32 m0, s45
	s_nop 0
	global_load_lds_dwordx4 v137, s[2:3]
	s_add_i32 s46, s31, 0x1e000
	s_mov_b32 m0, s46
	s_nop 0
	global_load_lds_dwordx4 v141, s[2:3]
	s_waitcnt vmcnt(6)
	s_add_i32 s47, s31, 0xc000
	s_cmpk_lt_u32 s10, 0x100
	v_readlane_b32 s2, v253, 30
	s_cselect_b64 s[10:11], -1, 0
	s_add_i32 s48, s31, 0xe000
	v_or_b32_e32 v149, s12, v4
	s_mov_b32 s49, 0
	v_add_u32_e32 v152, 0, v0
	v_add_u32_e32 v153, 0, v5
	v_readlane_b32 s50, v253, 23
	s_mov_b32 s51, s2
	s_mov_b64 s[18:19], s[22:23]
	s_mov_b64 s[16:17], s[20:21]
	s_barrier
	v_readlane_b32 s3, v253, 31
	s_branch .LBB0_3053

; #define PG8_STAGE(bufoff, gbase, voff) do { _Pragma("unroll") for (int _i = 0; _i < 2; ++_i) \
;         glds16((const void*)(gbase), (voff)[_i], ldsbase + (unsigned)(bufoff) + ldsw + (unsigned)_i * 8192u); } while (0)
; #define PG8_LDA(dst, b, h) do { _Pragma("unroll") for (int m = 0; m < 4; ++m) _Pragma("unroll") for (int k = 0; k < 2; ++k) dst[m][k] = *(const LAS bf16x8*)(lds + PG8_SA(b, h) + aoff + m * 2048 + k * 1024); } while (0)
; #define PG8_LDB(dst, b, h) do { _Pragma("unroll") for (int n = 0; n < 2; ++n) _Pragma("unroll") for (int k = 0; k < 2; ++k) dst[n][k] = *(const LAS bf16x8*)(lds + PG8_SB(b, h) + boff + n * 2048 + k * 1024); } while (0)
; #define PG8_WAIT_V(n) asm volatile("s_waitcnt vmcnt(" #n ")" ::: "memory")
; #define PG8_WAIT_L(n) asm volatile("s_waitcnt lgkmcnt(" #n ")" ::: "memory")
; #define PG8_BAR __builtin_amdgcn_s_barrier()
; #define PG8_SCHED __builtin_amdgcn_sched_barrier(0)
;     ...
;             PG8_LDB(B0, 0, 0); PG8_LDB(B1, 0, 1); PG8_SCHED; PG8_LDA(At, 0, 0); PG8_STAGE(PG8_SA(1, 1), a1 + hstepA, voffA);
;             PG8_WAIT_V(8); PG8_WAIT_L(0); PG8_BAR; PG8_MMA(0, 0, At, B0); PG8_MMA(0, 1, At, B1); PG8_BAR; PG8_SCHED;
;             PG8_LDA(At, 0, 1); PG8_STAGE(PG8_SB(0, 0), b2, voffB); PG8_STAGE(PG8_SB(0, 1), b2 + hstepB, voffB); PG8_STAGE(PG8_SA(0, 0), a2, voffA);
;             PG8_WAIT_V(8); PG8_WAIT_L(0); PG8_BAR; PG8_MMA(1, 0, At, B0); PG8_MMA(1, 1, At, B1); PG8_BAR; PG8_SCHED;
.LBB0_3056:
	v_add_u32_e32 v0, 0x10000, v152
	ds_read_b128 v[132:135], v0
	ds_read_b128 v[154:157], v0 offset:1024
	ds_read_b128 v[158:161], v0 offset:2048
	ds_read_b128 v[162:165], v0 offset:3072
	v_add_u32_e32 v0, 0x14000, v152
	ds_read_b128 v[166:169], v0
	ds_read_b128 v[170:173], v0 offset:1024
	ds_read_b128 v[174:177], v0 offset:2048
	ds_read_b128 v[178:181], v0 offset:3072
	s_add_u32 s22, s20, 0xfff80080
	s_addc_u32 s23, s21, -1
	s_cmp_eq_u32 s52, 28
	s_cselect_b32 s26, s16, s22
	s_cselect_b32 s27, s17, s23
	s_cselect_b32 s24, s18, s13
	s_cselect_b32 s25, s19, s15
	s_add_u32 s22, s26, 0x80
	s_addc_u32 s23, s27, 0
	ds_read_b128 v[182:185], v153
	ds_read_b128 v[196:199], v153 offset:1024
	ds_read_b128 v[206:209], v153 offset:2048
	ds_read_b128 v[210:213], v153 offset:3072
	ds_read_b128 v[214:217], v153 offset:4096
	ds_read_b128 v[218:221], v153 offset:5120
	ds_read_b128 v[222:225], v153 offset:6144
	ds_read_b128 v[226:229], v153 offset:7168
	s_mov_b32 m0, s47
	s_nop 0
	global_load_lds_dwordx4 v1, s[20:21]
	s_nop 0
	s_mov_b32 m0, s48
	s_nop 0
	global_load_lds_dwordx4 v139, s[20:21]
	s_waitcnt vmcnt(8)
	s_waitcnt lgkmcnt(0)
	s_barrier
	s_setprio 1
	s_waitcnt lgkmcnt(7)
	v_mfma_f32_16x16x32_bf16 v[128:131], v[132:135], v[182:185], v[128:131]
	v_mfma_f32_16x16x32_bf16 v[124:127], v[158:161], v[182:185], v[124:127]
	s_waitcnt lgkmcnt(5)
	v_mfma_f32_16x16x32_bf16 v[112:115], v[132:135], v[206:209], v[112:115]
	v_mfma_f32_16x16x32_bf16 v[108:111], v[158:161], v[206:209], v[108:111]
	s_waitcnt lgkmcnt(3)
	v_mfma_f32_16x16x32_bf16 v[96:99], v[132:135], v[214:217], v[96:99]
	v_mfma_f32_16x16x32_bf16 v[92:95], v[158:161], v[214:217], v[92:95]
	s_waitcnt lgkmcnt(1)
	v_mfma_f32_16x16x32_bf16 v[80:83], v[132:135], v[222:225], v[80:83]
	v_mfma_f32_16x16x32_bf16 v[76:79], v[158:161], v[222:225], v[76:79]
	v_mfma_f32_16x16x32_bf16 v[128:131], v[154:157], v[196:199], v[128:131]
	v_mfma_f32_16x16x32_bf16 v[124:127], v[162:165], v[196:199], v[124:127]
	v_mfma_f32_16x16x32_bf16 v[112:115], v[154:157], v[210:213], v[112:115]
	v_mfma_f32_16x16x32_bf16 v[108:111], v[162:165], v[210:213], v[108:111]
	v_mfma_f32_16x16x32_bf16 v[96:99], v[154:157], v[218:221], v[96:99]
	v_mfma_f32_16x16x32_bf16 v[92:95], v[162:165], v[218:221], v[92:95]
	s_waitcnt lgkmcnt(0)
	v_mfma_f32_16x16x32_bf16 v[80:83], v[154:157], v[226:229], v[80:83]
	v_mfma_f32_16x16x32_bf16 v[76:79], v[162:165], v[226:229], v[76:79]
	s_setprio 0
	s_setprio 1
	v_mfma_f32_16x16x32_bf16 v[120:123], v[166:169], v[182:185], v[120:123]
	v_mfma_f32_16x16x32_bf16 v[116:119], v[174:177], v[182:185], v[116:119]
	v_mfma_f32_16x16x32_bf16 v[104:107], v[166:169], v[206:209], v[104:107]
	v_mfma_f32_16x16x32_bf16 v[100:103], v[174:177], v[206:209], v[100:103]
	v_mfma_f32_16x16x32_bf16 v[88:91], v[166:169], v[214:217], v[88:91]
	v_mfma_f32_16x16x32_bf16 v[84:87], v[174:177], v[214:217], v[84:87]
	v_mfma_f32_16x16x32_bf16 v[72:75], v[166:169], v[222:225], v[72:75]
	v_mfma_f32_16x16x32_bf16 v[68:71], v[174:177], v[222:225], v[68:71]
	v_mfma_f32_16x16x32_bf16 v[120:123], v[170:173], v[196:199], v[120:123]
	v_mfma_f32_16x16x32_bf16 v[116:119], v[178:181], v[196:199], v[116:119]
	v_mfma_f32_16x16x32_bf16 v[104:107], v[170:173], v[210:213], v[104:107]
	v_mfma_f32_16x16x32_bf16 v[100:103], v[178:181], v[210:213], v[100:103]
	v_mfma_f32_16x16x32_bf16 v[88:91], v[170:173], v[218:221], v[88:91]
	v_mfma_f32_16x16x32_bf16 v[84:87], v[178:181], v[218:221], v[84:87]
	v_mfma_f32_16x16x32_bf16 v[72:75], v[170:173], v[226:229], v[72:75]
	v_mfma_f32_16x16x32_bf16 v[68:71], v[178:181], v[226:229], v[68:71]
	s_setprio 0
	s_barrier
	ds_read_b128 v[182:185], v153 offset:16384
	ds_read_b128 v[196:199], v153 offset:17408
	ds_read_b128 v[206:209], v153 offset:18432
	ds_read_b128 v[210:213], v153 offset:19456
	ds_read_b128 v[214:217], v153 offset:20480
	ds_read_b128 v[218:221], v153 offset:21504
	ds_read_b128 v[222:225], v153 offset:22528
	ds_read_b128 v[226:229], v153 offset:23552
	s_mov_b32 m0, s34
	s_nop 0
	global_load_lds_dwordx4 v137, s[24:25]
	s_add_u32 s54, s24, 0x80000
	s_mov_b32 m0, s35
	s_nop 0
	global_load_lds_dwordx4 v141, s[24:25]
	s_addc_u32 s55, s25, 0
	s_mov_b32 m0, s36
	s_nop 0
	global_load_lds_dwordx4 v137, s[54:55]
	s_nop 0
	s_mov_b32 m0, s37
	s_nop 0
	global_load_lds_dwordx4 v141, s[54:55]
	s_nop 0
	s_mov_b32 m0, s31
	s_nop 0
	global_load_lds_dwordx4 v1, s[26:27]
	s_nop 0
	s_mov_b32 m0, s38
	s_nop 0
	global_load_lds_dwordx4 v139, s[26:27]
	s_waitcnt vmcnt(8)
	s_waitcnt lgkmcnt(0)
	s_barrier
; #define PG8_STAGE(bufoff, gbase, voff) do { _Pragma("unroll") for (int _i = 0; _i < 2; ++_i) \
;         glds16((const void*)(gbase), (voff)[_i], ldsbase + (unsigned)(bufoff) + ldsw + (unsigned)_i * 8192u); } while (0)
; #define PG8_LDA(dst, b, h) do { _Pragma("unroll") for (int m = 0; m < 4; ++m) _Pragma("unroll") for (int k = 0; k < 2; ++k) dst[m][k] = *(const LAS bf16x8*)(lds + PG8_SA(b, h) + aoff + m * 2048 + k * 1024); } while (0)
; #define PG8_LDB(dst, b, h) do { _Pragma("unroll") for (int n = 0; n < 2; ++n) _Pragma("unroll") for (int k = 0; k < 2; ++k) dst[n][k] = *(const LAS bf16x8*)(lds + PG8_SB(b, h) + boff + n * 2048 + k * 1024); } while (0)
; #define PG8_WAIT_V(n) asm volatile("s_waitcnt vmcnt(" #n ")" ::: "memory")
; #define PG8_WAIT_L(n) asm volatile("s_waitcnt lgkmcnt(" #n ")" ::: "memory")
; #define PG8_BAR __builtin_amdgcn_s_barrier()
; #define PG8_SCHED __builtin_amdgcn_sched_barrier(0)
;     ...
;             PG8_LDB(B0, 1, 0); PG8_LDB(B1, 1, 1); PG8_SCHED; PG8_LDA(At, 1, 0); PG8_STAGE(PG8_SA(0, 1), a2 + hstepA, voffA);
;             PG8_WAIT_V(8); PG8_WAIT_L(0); PG8_BAR; PG8_MMA(0, 0, At, B0); PG8_MMA(0, 1, At, B1); PG8_BAR; PG8_SCHED;
;             PG8_LDA(At, 1, 1); PG8_STAGE(PG8_SB(1, 0), b3, voffB); PG8_STAGE(PG8_SB(1, 1), b3 + hstepB, voffB); PG8_STAGE(PG8_SA(1, 0), a3, voffA);
;             PG8_WAIT_V(8); PG8_WAIT_L(0); PG8_BAR; PG8_MMA(1, 0, At, B0); PG8_MMA(1, 1, At, B1); PG8_BAR; PG8_SCHED;
	s_setprio 1
	s_waitcnt lgkmcnt(7)
	v_mfma_f32_16x16x32_bf16 v[64:67], v[132:135], v[182:185], v[64:67]
	v_mfma_f32_16x16x32_bf16 v[60:63], v[158:161], v[182:185], v[60:63]
	s_waitcnt lgkmcnt(5)
	v_mfma_f32_16x16x32_bf16 v[48:51], v[132:135], v[206:209], v[48:51]
	v_mfma_f32_16x16x32_bf16 v[44:47], v[158:161], v[206:209], v[44:47]
	s_waitcnt lgkmcnt(3)
	v_mfma_f32_16x16x32_bf16 v[32:35], v[132:135], v[214:217], v[32:35]
	v_mfma_f32_16x16x32_bf16 v[28:31], v[158:161], v[214:217], v[28:31]
	s_waitcnt lgkmcnt(1)
	v_mfma_f32_16x16x32_bf16 v[16:19], v[132:135], v[222:225], v[16:19]
	v_mfma_f32_16x16x32_bf16 v[12:15], v[158:161], v[222:225], v[12:15]
	v_mfma_f32_16x16x32_bf16 v[64:67], v[154:157], v[196:199], v[64:67]
	v_mfma_f32_16x16x32_bf16 v[60:63], v[162:165], v[196:199], v[60:63]
	v_mfma_f32_16x16x32_bf16 v[48:51], v[154:157], v[210:213], v[48:51]
	v_mfma_f32_16x16x32_bf16 v[44:47], v[162:165], v[210:213], v[44:47]
	v_mfma_f32_16x16x32_bf16 v[32:35], v[154:157], v[218:221], v[32:35]
	v_mfma_f32_16x16x32_bf16 v[28:31], v[162:165], v[218:221], v[28:31]
	s_waitcnt lgkmcnt(0)
	v_mfma_f32_16x16x32_bf16 v[16:19], v[154:157], v[226:229], v[16:19]
	v_mfma_f32_16x16x32_bf16 v[12:15], v[162:165], v[226:229], v[12:15]
	s_setprio 0
	s_setprio 1
	v_mfma_f32_16x16x32_bf16 v[56:59], v[166:169], v[182:185], v[56:59]
	v_mfma_f32_16x16x32_bf16 v[52:55], v[174:177], v[182:185], v[52:55]
	v_mfma_f32_16x16x32_bf16 v[40:43], v[166:169], v[206:209], v[40:43]
	v_mfma_f32_16x16x32_bf16 v[36:39], v[174:177], v[206:209], v[36:39]
	v_mfma_f32_16x16x32_bf16 v[24:27], v[166:169], v[214:217], v[24:27]
	v_mfma_f32_16x16x32_bf16 v[20:23], v[174:177], v[214:217], v[20:23]
	v_mfma_f32_16x16x32_bf16 v[8:11], v[166:169], v[222:225], v[8:11]
	v_mfma_f32_16x16x32_bf16 v[4:7], v[174:177], v[222:225], v[4:7]
	v_mfma_f32_16x16x32_bf16 v[56:59], v[170:173], v[196:199], v[56:59]
	v_mfma_f32_16x16x32_bf16 v[52:55], v[178:181], v[196:199], v[52:55]
	v_mfma_f32_16x16x32_bf16 v[40:43], v[170:173], v[210:213], v[40:43]
	v_mfma_f32_16x16x32_bf16 v[36:39], v[178:181], v[210:213], v[36:39]
	v_mfma_f32_16x16x32_bf16 v[24:27], v[170:173], v[218:221], v[24:27]
	v_mfma_f32_16x16x32_bf16 v[20:23], v[178:181], v[218:221], v[20:23]
	v_mfma_f32_16x16x32_bf16 v[8:11], v[170:173], v[226:229], v[8:11]
	v_mfma_f32_16x16x32_bf16 v[4:7], v[178:181], v[226:229], v[4:7]
	s_setprio 0
	s_barrier
	v_add_u32_e32 v0, 0x18000, v152
	ds_read_b128 v[132:135], v0
	ds_read_b128 v[154:157], v0 offset:1024
	ds_read_b128 v[158:161], v0 offset:2048
	ds_read_b128 v[162:165], v0 offset:3072
	v_add_u32_e32 v0, 0x1c000, v152
	ds_read_b128 v[166:169], v0
	ds_read_b128 v[170:173], v0 offset:1024
	ds_read_b128 v[174:177], v0 offset:2048
	ds_read_b128 v[178:181], v0 offset:3072
	ds_read_b128 v[182:185], v153 offset:32768
	ds_read_b128 v[196:199], v153 offset:33792
	ds_read_b128 v[206:209], v153 offset:34816
	ds_read_b128 v[210:213], v153 offset:35840
	ds_read_b128 v[214:217], v153 offset:36864
	ds_read_b128 v[218:221], v153 offset:37888
	ds_read_b128 v[222:225], v153 offset:38912
	ds_read_b128 v[226:229], v153 offset:39936
	s_add_u32 s26, s26, 0x80000
	s_addc_u32 s27, s27, 0
	s_mov_b32 m0, s39
	s_nop 0
	global_load_lds_dwordx4 v1, s[26:27]
	s_nop 0
	s_mov_b32 m0, s40
	s_nop 0
	global_load_lds_dwordx4 v139, s[26:27]
	s_waitcnt vmcnt(8)
	s_waitcnt lgkmcnt(0)
	s_barrier
	s_setprio 1
	s_waitcnt lgkmcnt(7)
	v_mfma_f32_16x16x32_bf16 v[128:131], v[132:135], v[182:185], v[128:131]
	v_mfma_f32_16x16x32_bf16 v[124:127], v[158:161], v[182:185], v[124:127]
	s_waitcnt lgkmcnt(5)
	v_mfma_f32_16x16x32_bf16 v[112:115], v[132:135], v[206:209], v[112:115]
	v_mfma_f32_16x16x32_bf16 v[108:111], v[158:161], v[206:209], v[108:111]
	s_waitcnt lgkmcnt(3)
	v_mfma_f32_16x16x32_bf16 v[96:99], v[132:135], v[214:217], v[96:99]
	v_mfma_f32_16x16x32_bf16 v[92:95], v[158:161], v[214:217], v[92:95]
	s_waitcnt lgkmcnt(1)
	v_mfma_f32_16x16x32_bf16 v[80:83], v[132:135], v[222:225], v[80:83]
	v_mfma_f32_16x16x32_bf16 v[76:79], v[158:161], v[222:225], v[76:79]
	v_mfma_f32_16x16x32_bf16 v[128:131], v[154:157], v[196:199], v[128:131]
	v_mfma_f32_16x16x32_bf16 v[124:127], v[162:165], v[196:199], v[124:127]
	v_mfma_f32_16x16x32_bf16 v[112:115], v[154:157], v[210:213], v[112:115]
	v_mfma_f32_16x16x32_bf16 v[108:111], v[162:165], v[210:213], v[108:111]
	v_mfma_f32_16x16x32_bf16 v[96:99], v[154:157], v[218:221], v[96:99]
	v_mfma_f32_16x16x32_bf16 v[92:95], v[162:165], v[218:221], v[92:95]
	s_waitcnt lgkmcnt(0)
	v_mfma_f32_16x16x32_bf16 v[80:83], v[154:157], v[226:229], v[80:83]
	v_mfma_f32_16x16x32_bf16 v[76:79], v[162:165], v[226:229], v[76:79]
	s_setprio 0
	s_setprio 1
	v_mfma_f32_16x16x32_bf16 v[120:123], v[166:169], v[182:185], v[120:123]
	v_mfma_f32_16x16x32_bf16 v[116:119], v[174:177], v[182:185], v[116:119]
	v_mfma_f32_16x16x32_bf16 v[104:107], v[166:169], v[206:209], v[104:107]
	v_mfma_f32_16x16x32_bf16 v[100:103], v[174:177], v[206:209], v[100:103]
	v_mfma_f32_16x16x32_bf16 v[88:91], v[166:169], v[214:217], v[88:91]
	v_mfma_f32_16x16x32_bf16 v[84:87], v[174:177], v[214:217], v[84:87]
	v_mfma_f32_16x16x32_bf16 v[72:75], v[166:169], v[222:225], v[72:75]
	v_mfma_f32_16x16x32_bf16 v[68:71], v[174:177], v[222:225], v[68:71]
	v_mfma_f32_16x16x32_bf16 v[120:123], v[170:173], v[196:199], v[120:123]
	v_mfma_f32_16x16x32_bf16 v[116:119], v[178:181], v[196:199], v[116:119]
	v_mfma_f32_16x16x32_bf16 v[104:107], v[170:173], v[210:213], v[104:107]
	v_mfma_f32_16x16x32_bf16 v[100:103], v[178:181], v[210:213], v[100:103]
	v_mfma_f32_16x16x32_bf16 v[88:91], v[170:173], v[218:221], v[88:91]
	v_mfma_f32_16x16x32_bf16 v[84:87], v[178:181], v[218:221], v[84:87]
	v_mfma_f32_16x16x32_bf16 v[72:75], v[170:173], v[226:229], v[72:75]
	v_mfma_f32_16x16x32_bf16 v[68:71], v[178:181], v[226:229], v[68:71]
	s_setprio 0
	s_barrier
; #define PG8_STAGE(bufoff, gbase, voff) do { _Pragma("unroll") for (int _i = 0; _i < 2; ++_i) \
;         glds16((const void*)(gbase), (voff)[_i], ldsbase + (unsigned)(bufoff) + ldsw + (unsigned)_i * 8192u); } while (0)
; #define PG8_LDA(dst, b, h) do { _Pragma("unroll") for (int m = 0; m < 4; ++m) _Pragma("unroll") for (int k = 0; k < 2; ++k) dst[m][k] = *(const LAS bf16x8*)(lds + PG8_SA(b, h) + aoff + m * 2048 + k * 1024); } while (0)
; #define PG8_WAIT_V(n) asm volatile("s_waitcnt vmcnt(" #n ")" ::: "memory")
; #define PG8_WAIT_L(n) asm volatile("s_waitcnt lgkmcnt(" #n ")" ::: "memory")
; #define PG8_BAR __builtin_amdgcn_s_barrier()
; #define PG8_SCHED __builtin_amdgcn_sched_barrier(0)
;     ...
;             PG8_LDA(At, 1, 1); PG8_STAGE(PG8_SB(1, 0), b3, voffB); PG8_STAGE(PG8_SB(1, 1), b3 + hstepB, voffB); PG8_STAGE(PG8_SA(1, 0), a3, voffA);
;             PG8_WAIT_V(8); PG8_WAIT_L(0); PG8_BAR; PG8_MMA(1, 0, At, B0); PG8_MMA(1, 1, At, B1); PG8_BAR; PG8_SCHED;
;         }
	ds_read_b128 v[182:185], v153 offset:49152
	ds_read_b128 v[196:199], v153 offset:50176
	ds_read_b128 v[206:209], v153 offset:51200
	ds_read_b128 v[210:213], v153 offset:52224
	ds_read_b128 v[214:217], v153 offset:53248
	ds_read_b128 v[218:221], v153 offset:54272
	ds_read_b128 v[222:225], v153 offset:55296
	ds_read_b128 v[226:229], v153 offset:56320
	s_add_u32 s26, s24, 0x80
	s_addc_u32 s27, s25, 0
	s_mov_b32 m0, s41
	s_nop 0
	global_load_lds_dwordx4 v137, s[26:27]
	s_add_u32 s24, s24, 0x80080
	s_mov_b32 m0, s42
	s_nop 0
	global_load_lds_dwordx4 v141, s[26:27]
	s_addc_u32 s25, s25, 0
	s_mov_b32 m0, s45
	s_nop 0
	global_load_lds_dwordx4 v137, s[24:25]
	s_nop 0
	s_mov_b32 m0, s46
	s_nop 0
	global_load_lds_dwordx4 v141, s[24:25]
	s_mov_b32 m0, s43
	s_nop 0
	global_load_lds_dwordx4 v1, s[22:23]
	s_nop 0
	s_mov_b32 m0, s44
	s_nop 0
	global_load_lds_dwordx4 v139, s[22:23]
	s_waitcnt vmcnt(8)
	s_waitcnt lgkmcnt(0)
	s_barrier
	s_setprio 1
	s_waitcnt lgkmcnt(7)
	v_mfma_f32_16x16x32_bf16 v[64:67], v[132:135], v[182:185], v[64:67]
	v_mfma_f32_16x16x32_bf16 v[60:63], v[158:161], v[182:185], v[60:63]
	s_waitcnt lgkmcnt(5)
	v_mfma_f32_16x16x32_bf16 v[48:51], v[132:135], v[206:209], v[48:51]
	v_mfma_f32_16x16x32_bf16 v[44:47], v[158:161], v[206:209], v[44:47]
	s_waitcnt lgkmcnt(3)
	v_mfma_f32_16x16x32_bf16 v[32:35], v[132:135], v[214:217], v[32:35]
	v_mfma_f32_16x16x32_bf16 v[28:31], v[158:161], v[214:217], v[28:31]
	s_waitcnt lgkmcnt(1)
	v_mfma_f32_16x16x32_bf16 v[16:19], v[132:135], v[222:225], v[16:19]
	v_mfma_f32_16x16x32_bf16 v[12:15], v[158:161], v[222:225], v[12:15]
	v_mfma_f32_16x16x32_bf16 v[64:67], v[154:157], v[196:199], v[64:67]
	v_mfma_f32_16x16x32_bf16 v[60:63], v[162:165], v[196:199], v[60:63]
	v_mfma_f32_16x16x32_bf16 v[48:51], v[154:157], v[210:213], v[48:51]
	v_mfma_f32_16x16x32_bf16 v[44:47], v[162:165], v[210:213], v[44:47]
	v_mfma_f32_16x16x32_bf16 v[32:35], v[154:157], v[218:221], v[32:35]
	v_mfma_f32_16x16x32_bf16 v[28:31], v[162:165], v[218:221], v[28:31]
	s_waitcnt lgkmcnt(0)
	v_mfma_f32_16x16x32_bf16 v[16:19], v[154:157], v[226:229], v[16:19]
	v_mfma_f32_16x16x32_bf16 v[12:15], v[162:165], v[226:229], v[12:15]
	s_setprio 0
	s_setprio 1
	v_mfma_f32_16x16x32_bf16 v[56:59], v[166:169], v[182:185], v[56:59]
	v_mfma_f32_16x16x32_bf16 v[52:55], v[174:177], v[182:185], v[52:55]
	v_mfma_f32_16x16x32_bf16 v[40:43], v[166:169], v[206:209], v[40:43]
	v_mfma_f32_16x16x32_bf16 v[36:39], v[174:177], v[206:209], v[36:39]
	v_mfma_f32_16x16x32_bf16 v[24:27], v[166:169], v[214:217], v[24:27]
	v_mfma_f32_16x16x32_bf16 v[20:23], v[174:177], v[214:217], v[20:23]
	v_mfma_f32_16x16x32_bf16 v[8:11], v[166:169], v[222:225], v[8:11]
	v_mfma_f32_16x16x32_bf16 v[4:7], v[174:177], v[222:225], v[4:7]
	v_mfma_f32_16x16x32_bf16 v[56:59], v[170:173], v[196:199], v[56:59]
	v_mfma_f32_16x16x32_bf16 v[52:55], v[178:181], v[196:199], v[52:55]
	v_mfma_f32_16x16x32_bf16 v[40:43], v[170:173], v[210:213], v[40:43]
	v_mfma_f32_16x16x32_bf16 v[36:39], v[178:181], v[210:213], v[36:39]
	v_mfma_f32_16x16x32_bf16 v[24:27], v[170:173], v[218:221], v[24:27]
	v_mfma_f32_16x16x32_bf16 v[20:23], v[178:181], v[218:221], v[20:23]
	v_mfma_f32_16x16x32_bf16 v[8:11], v[170:173], v[226:229], v[8:11]
	v_mfma_f32_16x16x32_bf16 v[4:7], v[178:181], v[226:229], v[4:7]
	s_setprio 0
	s_barrier
	s_add_i32 s52, s52, 2
	s_add_u32 s13, s13, 0x100
	s_addc_u32 s15, s15, 0
	s_add_u32 s20, s20, 0x100
	s_addc_u32 s21, s21, 0
	s_cmp_gt_u32 s52, 29
	s_cbranch_scc0 .LBB0_3056
	s_and_b64 vcc, exec, s[10:11]
	s_cbranch_vccz .LBB0_3059
	s_barrier

; __device__ __forceinline__ int lane_id() { int l_; asm volatile("v_mbcnt_lo_u32_b32 %0, -1, 0\n\tv_mbcnt_hi_u32_b32 %0, -1, %0" : "=v"(l_)); return l_; }
; #define PG8_STAGE(bufoff, gbase, voff) do { _Pragma("unroll") for (int _i = 0; _i < 2; ++_i) \
;         glds16((const void*)(gbase), (voff)[_i], ldsbase + (unsigned)(bufoff) + ldsw + (unsigned)_i * 8192u); } while (0)
; #define PG8_WAIT_V(n) asm volatile("s_waitcnt vmcnt(" #n ")" ::: "memory")
; #define PG8_BAR __builtin_amdgcn_s_barrier()
;     ...
;     int tid = w0_ * 64 + lane_id(); asm volatile("" : "+v"(tid));
;     const int wid = __builtin_amdgcn_readfirstlane(tid >> 6), lane = tid & 63, wr = wid >> 2, wc = wid & 3, fr = lane & 15, fq = lane >> 4;
;     const int nt = nt_ ? nt_ : Kb / 128;
;     unsigned voffA[2], voffB[2];
; #pragma unroll
;     for (int i = 0; i < 2; ++i) { int R, C; stage_rc(tid * 16 + i * 8192, R, C); const int Rb = Epi::PERM ? ((R & ~31) + perm32(R & 31)) : R;
;         voffA[i] = (unsigned)(R * ldab + C * 2); voffB[i] = (unsigned)(Rb * Kb + C * 2); }
;     const size_t kstep = (size_t)(BK * 2);
;     const size_t hstepA = (size_t)HALF * ldab, hstepB = (size_t)HALF * Kb;
;     const unsigned ldsw = (unsigned)wid * 1024u, ldsbase = (unsigned)(size_t)lds;
;     const int aoff = lds_byte(wr * 64 + fr, fq * 8), boff = lds_byte(wc * 32 + fr, fq * 8);
;     ...
;     Unit cur, nxt; int ui = 0;
;     if (!S.next(0, cur)) return;
;     f32x4 acc[2][2][4][2];
; #pragma unroll
;     for (int a = 0; a < 2; ++a)
; #pragma unroll
;         for (int b = 0; b < 2; ++b)
; #pragma unroll
;             for (int m = 0; m < 4; ++m)
; #pragma unroll
;                 for (int n = 0; n < 2; ++n) acc[a][b][m][n] = (f32x4){0.f, 0.f, 0.f, 0.f};
;     bf16x8 At[4][2], B0[2][2], B1[2][2];
;     const char* cA = uniform_ptr(cur.a); const char* cB = uniform_ptr(cur.b);
;     PG8_STAGE(PG8_SB(0, 0), cB, voffB); PG8_STAGE(PG8_SB(0, 1), cB + hstepB, voffB); PG8_STAGE(PG8_SA(0, 0), cA, voffA); PG8_STAGE(PG8_SA(0, 1), cA + hstepA, voffA);
;     if (wr == 1) PG8_BAR;
;     PG8_WAIT_V(2); PG8_BAR;
;     PG8_STAGE(PG8_SB(1, 0), cB + kstep, voffB); PG8_STAGE(PG8_SA(1, 0), cA + kstep, voffA); PG8_STAGE(PG8_SB(1, 1), cB + hstepB + kstep, voffB);
;     PG8_WAIT_V(6); PG8_BAR;
.LBB0_3118:
	s_and_b64 vcc, exec, s[2:3]
	s_cbranch_vccnz .LBB0_3154
	s_waitcnt lgkmcnt(0)
	v_bfe_i32 v1, v4, 27, 1
	v_lshlrev_b32_e32 v5, 4, v4
	v_lshrrev_b32_e32 v1, 22, v1
	v_add_u32_e32 v1, v5, v1
	v_and_b32_e32 v1, 0xfffffc00, v1
	v_sub_u32_e32 v1, v5, v1
	v_ashrrev_i32_e32 v0, 31, v4
	v_lshrrev_b32_e32 v2, 4, v1
	v_lshrrev_b32_e32 v0, 26, v0
	v_bitop3_b32 v1, v2, v1, 32 bitop3:0x6c
	v_add_u32_e32 v0, v4, v0
	v_ashrrev_i32_e32 v6, 31, v1
	v_ashrrev_i32_e32 v0, 6, v0
	v_lshrrev_b32_e32 v6, 26, v6
	v_lshlrev_b32_e32 v2, 3, v0
	v_add_u32_e32 v6, v1, v6
	v_and_b32_e32 v2, -16, v2
	v_ashrrev_i32_e32 v7, 6, v6
	v_add_u32_e32 v8, v7, v2
	v_and_b32_e32 v2, 0xc0, v6
	v_sub_u32_e32 v1, v1, v2
	v_lshlrev_b32_e32 v0, 5, v0
	v_ashrrev_i16_sdwa v1, v188, sext(v1) dst_sel:DWORD dst_unused:UNUSED_PAD src0_sel:DWORD src1_sel:BYTE_0
	v_lshlrev_b32_e32 v2, 1, v8
	v_lshrrev_b32_e32 v6, 2, v8
	v_and_b32_e32 v7, 3, v7
	s_mov_b32 s3, 0x3fffe0
	v_and_b32_e32 v0, 32, v0
	v_bfe_i32 v1, v1, 0, 16
	v_and_b32_e32 v2, 24, v2
	v_and_b32_e32 v6, 4, v6
	v_and_or_b32 v7, v8, s3, v7
	v_or3_b32 v6, v7, v6, v2
	v_add_lshl_u32 v2, v0, v1, 1
	s_movk_i32 s8, 0x2c00
	v_mad_u64_u32 v[0:1], s[6:7], v8, s8, v[2:3]
	v_mad_u32_u24 v1, v6, s8, v2
	v_add_u32_e32 v2, 0x2000, v5
	v_ashrrev_i32_e32 v5, 31, v2
	v_lshrrev_b32_e32 v5, 22, v5
	v_add_u32_e32 v5, v2, v5
	v_ashrrev_i32_e32 v5, 10, v5
	v_mul_i32_i24_e32 v6, 0x400, v5
	v_sub_u32_e32 v2, v2, v6
	v_lshrrev_b32_e32 v6, 4, v2
	v_bitop3_b32 v2, v6, v2, 32 bitop3:0x6c
	v_ashrrev_i32_e32 v7, 31, v2
	v_lshrrev_b32_e32 v7, 26, v7
	v_add_u32_e32 v7, v2, v7
	v_ashrrev_i32_e32 v8, 6, v7
	v_and_b32_e32 v7, 0xc0, v7
	v_sub_u32_e32 v2, v2, v7
	v_lshlrev_b32_e32 v6, 3, v5
	v_lshlrev_b32_e32 v5, 5, v5
	v_ashrrev_i16_sdwa v2, v188, sext(v2) dst_sel:DWORD dst_unused:UNUSED_PAD src0_sel:DWORD src1_sel:BYTE_0
	v_and_b32_e32 v6, -16, v6
	v_and_b32_e32 v5, 32, v5
	v_bfe_i32 v2, v2, 0, 16
	v_add_u32_e32 v6, v8, v6
	v_add_lshl_u32 v2, v5, v2, 1
	s_ashr_i32 s2, s4, 6
	s_waitcnt vmcnt(0)
	v_mad_u64_u32 v[140:141], s[6:7], v6, s8, v[2:3]
	v_lshlrev_b32_e32 v7, 1, v6
	v_lshrrev_b32_e32 v9, 2, v6
	v_and_b32_e32 v8, 3, v8
	s_lshl_b32 s6, s2, 10
	v_and_b32_e32 v7, 24, v7
	v_and_b32_e32 v9, 4, v9
	v_and_or_b32 v8, v6, s3, v8
	s_add_i32 s34, s6, 0
	v_or3_b32 v7, v8, v9, v7
	s_add_i32 s35, s34, 0x10000
	s_mov_b32 m0, s35
	s_nop 0
	global_load_lds_dwordx4 v1, s[22:23]
	v_mad_u32_u24 v2, v7, s8, v2
	s_ashr_i32 s3, s4, 8
	s_add_i32 s36, s34, 0x12000
	s_mov_b32 m0, s36
	s_nop 0
	global_load_lds_dwordx4 v2, s[22:23]
	s_add_u32 s6, s22, 0x160000
	s_addc_u32 s7, s23, 0
	s_add_i32 s37, s34, 0x14000
	s_mov_b32 m0, s37
	s_nop 0
	global_load_lds_dwordx4 v1, s[6:7]
	s_add_i32 s38, s34, 0x16000
	s_mov_b32 m0, s38
	s_nop 0
	global_load_lds_dwordx4 v2, s[6:7]
	s_mov_b32 m0, s34
	s_nop 0
	global_load_lds_dwordx4 v0, s[20:21]
	s_add_i32 s39, s34, 0x2000
	s_mov_b32 m0, s39
	s_nop 0
	global_load_lds_dwordx4 v140, s[20:21]
	s_add_u32 s6, s20, 0x160000
	s_addc_u32 s7, s21, 0
	s_add_i32 s40, s34, 0x4000
	s_mov_b32 m0, s40
	s_nop 0
	global_load_lds_dwordx4 v0, s[6:7]
	s_add_i32 s41, s34, 0x6000
	s_mov_b32 m0, s41
	s_nop 0
	global_load_lds_dwordx4 v140, s[6:7]
	s_cmp_eq_u32 s3, 1
	s_cselect_b64 s[6:7], -1, 0
	s_cmp_lg_u32 s3, 1
	s_cbranch_scc1 .LBB0_3121
	s_barrier
.LBB0_3121:
	s_add_u32 s8, s5, 0x32892000
	s_addc_u32 s9, s13, 0
	s_add_u32 s10, s5, 0x32682000
	s_addc_u32 s11, s13, 0
	v_bfe_u32 v6, v4, 4, 2
	s_add_u32 s12, s5, 0x36892000
	v_and_b32_e32 v5, 15, v4
	v_lshlrev_b32_e32 v8, 4, v6
	v_lshlrev_b32_e32 v4, 2, v4
	s_addc_u32 s13, s13, 0
	s_and_b32 s42, s2, 3
	v_lshl_or_b32 v141, s3, 6, v5
	v_lshl_or_b32 v5, v5, 6, v8
	s_lshl_b32 s2, s3, 13
	v_and_b32_e32 v4, 32, v4
	v_bitop3_b32 v8, v5, s2, v4 bitop3:0xde
	s_lshl_b32 s2, s42, 12
	v_bitop3_b32 v4, v5, s2, v4 bitop3:0xde
	s_add_u32 s2, s22, 0x80
	s_waitcnt vmcnt(2)
	s_barrier
	s_addc_u32 s3, s23, 0
	s_add_i32 s43, s34, 0x18000
	s_mov_b32 m0, s43
	s_nop 0
	global_load_lds_dwordx4 v1, s[2:3]
	s_add_i32 s44, s34, 0x1a000
	s_mov_b32 m0, s44
	s_nop 0
	global_load_lds_dwordx4 v2, s[2:3]
	s_add_u32 s2, s20, 0x80
	s_addc_u32 s3, s21, 0
	s_add_i32 s45, s34, 0x8000
	s_mov_b32 m0, s45
	s_nop 0
	global_load_lds_dwordx4 v0, s[2:3]
	s_add_i32 s46, s34, 0xa000
	s_mov_b32 m0, s46
	s_nop 0
	global_load_lds_dwordx4 v140, s[2:3]
	s_add_u32 s2, s22, 0x160080
	s_addc_u32 s3, s23, 0
	s_add_i32 s47, s34, 0x1c000
	s_mov_b32 m0, s47
	s_nop 0
	global_load_lds_dwordx4 v1, s[2:3]
	s_add_i32 s48, s34, 0x1e000
	s_mov_b32 m0, s48
	s_nop 0
	global_load_lds_dwordx4 v2, s[2:3]
	s_waitcnt vmcnt(6)
	s_add_i32 s49, s34, 0xc000
	v_lshlrev_b32_e32 v7, 3, v6
	s_cmpk_lt_u32 s4, 0x100
	v_lshl_or_b32 v150, s42, 5, v7
	s_cselect_b64 s[14:15], -1, 0
	s_mov_b32 s50, 0
	v_cmp_eq_u32_e64 s[2:3], 0, v6
	s_add_i32 s51, s34, 0xe000
	v_add_u32_e32 v151, 0, v4
	v_add_u32_e32 v152, 0, v8
	s_mov_b64 s[16:17], s[20:21]
	s_mov_b64 s[18:19], s[22:23]
	s_barrier
	s_branch .LBB0_3124

; #define PG8_STAGE(bufoff, gbase, voff) do { _Pragma("unroll") for (int _i = 0; _i < 2; ++_i) \
;         glds16((const void*)(gbase), (voff)[_i], ldsbase + (unsigned)(bufoff) + ldsw + (unsigned)_i * 8192u); } while (0)
; #define PG8_LDA(dst, b, h) do { _Pragma("unroll") for (int m = 0; m < 4; ++m) _Pragma("unroll") for (int k = 0; k < 2; ++k) dst[m][k] = *(const LAS bf16x8*)(lds + PG8_SA(b, h) + aoff + m * 2048 + k * 1024); } while (0)
; #define PG8_LDB(dst, b, h) do { _Pragma("unroll") for (int n = 0; n < 2; ++n) _Pragma("unroll") for (int k = 0; k < 2; ++k) dst[n][k] = *(const LAS bf16x8*)(lds + PG8_SB(b, h) + boff + n * 2048 + k * 1024); } while (0)
; #define PG8_WAIT_V(n) asm volatile("s_waitcnt vmcnt(" #n ")" ::: "memory")
; #define PG8_WAIT_L(n) asm volatile("s_waitcnt lgkmcnt(" #n ")" ::: "memory")
; #define PG8_BAR __builtin_amdgcn_s_barrier()
; #define PG8_SCHED __builtin_amdgcn_sched_barrier(0)
;     ...
;             PG8_LDB(B0, 0, 0); PG8_LDB(B1, 0, 1); PG8_SCHED; PG8_LDA(At, 0, 0); PG8_STAGE(PG8_SA(1, 1), a1 + hstepA, voffA);
;             PG8_WAIT_V(8); PG8_WAIT_L(0); PG8_BAR; PG8_MMA(0, 0, At, B0); PG8_MMA(0, 1, At, B1); PG8_BAR; PG8_SCHED;
;             PG8_LDA(At, 0, 1); PG8_STAGE(PG8_SB(0, 0), b2, voffB); PG8_STAGE(PG8_SB(0, 1), b2 + hstepB, voffB); PG8_STAGE(PG8_SA(0, 0), a2, voffA);
;             PG8_WAIT_V(8); PG8_WAIT_L(0); PG8_BAR; PG8_MMA(1, 0, At, B0); PG8_MMA(1, 1, At, B1); PG8_BAR; PG8_SCHED;
.LBB0_3131:
	v_add_u32_e32 v146, 0x10000, v151
	v_add_u32_e32 v153, 0x14000, v151
	ds_read_b128 v[132:135], v146
	ds_read_b128 v[136:139], v146 offset:1024
	ds_read_b128 v[142:145], v146 offset:2048
	ds_read_b128 v[146:149], v146 offset:3072
	ds_read_b128 v[154:157], v153
	ds_read_b128 v[158:161], v153 offset:1024
	ds_read_b128 v[162:165], v153 offset:2048
	ds_read_b128 v[166:169], v153 offset:3072
	s_add_u32 s22, s20, 0xffea0080
	s_addc_u32 s23, s21, -1
	s_cmpk_eq_i32 s57, 0x54
	s_cselect_b32 s26, s16, s22
	s_cselect_b32 s27, s17, s23
	s_cselect_b32 s24, s18, s55
	s_cselect_b32 s25, s19, s56
	s_add_u32 s22, s26, 0x80
	s_addc_u32 s23, s27, 0
	ds_read_b128 v[170:173], v152
	ds_read_b128 v[174:177], v152 offset:1024
	ds_read_b128 v[178:181], v152 offset:2048
	ds_read_b128 v[182:185], v152 offset:3072
	ds_read_b128 v[196:199], v152 offset:4096
	ds_read_b128 v[206:209], v152 offset:5120
	ds_read_b128 v[210:213], v152 offset:6144
	ds_read_b128 v[214:217], v152 offset:7168
	s_mov_b32 m0, s49
	s_nop 0
	global_load_lds_dwordx4 v0, s[20:21]
	s_nop 0
	s_mov_b32 m0, s51
	s_nop 0
	global_load_lds_dwordx4 v140, s[20:21]
	s_waitcnt vmcnt(8)
	s_waitcnt lgkmcnt(0)
	s_barrier
	s_setprio 1
	s_waitcnt lgkmcnt(7)
	v_mfma_f32_16x16x32_bf16 v[128:131], v[132:135], v[170:173], v[128:131]
	v_mfma_f32_16x16x32_bf16 v[124:127], v[142:145], v[170:173], v[124:127]
	s_waitcnt lgkmcnt(5)
	v_mfma_f32_16x16x32_bf16 v[112:115], v[132:135], v[178:181], v[112:115]
	v_mfma_f32_16x16x32_bf16 v[108:111], v[142:145], v[178:181], v[108:111]
	s_waitcnt lgkmcnt(3)
	v_mfma_f32_16x16x32_bf16 v[96:99], v[132:135], v[196:199], v[96:99]
	v_mfma_f32_16x16x32_bf16 v[92:95], v[142:145], v[196:199], v[92:95]
	s_waitcnt lgkmcnt(1)
	v_mfma_f32_16x16x32_bf16 v[80:83], v[132:135], v[210:213], v[80:83]
	v_mfma_f32_16x16x32_bf16 v[76:79], v[142:145], v[210:213], v[76:79]
	v_mfma_f32_16x16x32_bf16 v[128:131], v[136:139], v[174:177], v[128:131]
	v_mfma_f32_16x16x32_bf16 v[124:127], v[146:149], v[174:177], v[124:127]
	v_mfma_f32_16x16x32_bf16 v[112:115], v[136:139], v[182:185], v[112:115]
	v_mfma_f32_16x16x32_bf16 v[108:111], v[146:149], v[182:185], v[108:111]
	v_mfma_f32_16x16x32_bf16 v[96:99], v[136:139], v[206:209], v[96:99]
	v_mfma_f32_16x16x32_bf16 v[92:95], v[146:149], v[206:209], v[92:95]
	s_waitcnt lgkmcnt(0)
	v_mfma_f32_16x16x32_bf16 v[80:83], v[136:139], v[214:217], v[80:83]
	v_mfma_f32_16x16x32_bf16 v[76:79], v[146:149], v[214:217], v[76:79]
	s_setprio 0
	s_setprio 1
	v_mfma_f32_16x16x32_bf16 v[120:123], v[154:157], v[170:173], v[120:123]
	v_mfma_f32_16x16x32_bf16 v[116:119], v[162:165], v[170:173], v[116:119]
	v_mfma_f32_16x16x32_bf16 v[104:107], v[154:157], v[178:181], v[104:107]
	v_mfma_f32_16x16x32_bf16 v[100:103], v[162:165], v[178:181], v[100:103]
	v_mfma_f32_16x16x32_bf16 v[88:91], v[154:157], v[196:199], v[88:91]
	v_mfma_f32_16x16x32_bf16 v[84:87], v[162:165], v[196:199], v[84:87]
	v_mfma_f32_16x16x32_bf16 v[72:75], v[154:157], v[210:213], v[72:75]
	v_mfma_f32_16x16x32_bf16 v[68:71], v[162:165], v[210:213], v[68:71]
	v_mfma_f32_16x16x32_bf16 v[120:123], v[158:161], v[174:177], v[120:123]
	v_mfma_f32_16x16x32_bf16 v[116:119], v[166:169], v[174:177], v[116:119]
	v_mfma_f32_16x16x32_bf16 v[104:107], v[158:161], v[182:185], v[104:107]
	v_mfma_f32_16x16x32_bf16 v[100:103], v[166:169], v[182:185], v[100:103]
	v_mfma_f32_16x16x32_bf16 v[88:91], v[158:161], v[206:209], v[88:91]
	v_mfma_f32_16x16x32_bf16 v[84:87], v[166:169], v[206:209], v[84:87]
	v_mfma_f32_16x16x32_bf16 v[72:75], v[158:161], v[214:217], v[72:75]
	v_mfma_f32_16x16x32_bf16 v[68:71], v[166:169], v[214:217], v[68:71]
	s_setprio 0
	s_barrier
	ds_read_b128 v[170:173], v152 offset:16384
	ds_read_b128 v[174:177], v152 offset:17408
	ds_read_b128 v[178:181], v152 offset:18432
	ds_read_b128 v[182:185], v152 offset:19456
	ds_read_b128 v[196:199], v152 offset:20480
	ds_read_b128 v[206:209], v152 offset:21504
	ds_read_b128 v[210:213], v152 offset:22528
	ds_read_b128 v[214:217], v152 offset:23552
	s_mov_b32 m0, s35
	s_nop 0
	global_load_lds_dwordx4 v1, s[24:25]
	s_nop 0
	s_mov_b32 m0, s36
	s_nop 0
	global_load_lds_dwordx4 v2, s[24:25]
	s_add_u32 s58, s24, 0x160000
	s_addc_u32 s59, s25, 0
	s_mov_b32 m0, s37
	s_nop 0
	global_load_lds_dwordx4 v1, s[58:59]
	s_nop 0
	s_mov_b32 m0, s38
	s_nop 0
	global_load_lds_dwordx4 v2, s[58:59]
	s_mov_b32 m0, s34
	s_nop 0
	global_load_lds_dwordx4 v0, s[26:27]
	s_nop 0
	s_mov_b32 m0, s39
	s_nop 0
	global_load_lds_dwordx4 v140, s[26:27]
	s_waitcnt vmcnt(8)
	s_waitcnt lgkmcnt(0)
	s_barrier
; #define PG8_STAGE(bufoff, gbase, voff) do { _Pragma("unroll") for (int _i = 0; _i < 2; ++_i) \
;         glds16((const void*)(gbase), (voff)[_i], ldsbase + (unsigned)(bufoff) + ldsw + (unsigned)_i * 8192u); } while (0)
; #define PG8_LDA(dst, b, h) do { _Pragma("unroll") for (int m = 0; m < 4; ++m) _Pragma("unroll") for (int k = 0; k < 2; ++k) dst[m][k] = *(const LAS bf16x8*)(lds + PG8_SA(b, h) + aoff + m * 2048 + k * 1024); } while (0)
; #define PG8_LDB(dst, b, h) do { _Pragma("unroll") for (int n = 0; n < 2; ++n) _Pragma("unroll") for (int k = 0; k < 2; ++k) dst[n][k] = *(const LAS bf16x8*)(lds + PG8_SB(b, h) + boff + n * 2048 + k * 1024); } while (0)
; #define PG8_WAIT_V(n) asm volatile("s_waitcnt vmcnt(" #n ")" ::: "memory")
; #define PG8_WAIT_L(n) asm volatile("s_waitcnt lgkmcnt(" #n ")" ::: "memory")
; #define PG8_BAR __builtin_amdgcn_s_barrier()
; #define PG8_SCHED __builtin_amdgcn_sched_barrier(0)
;     ...
;             PG8_WAIT_V(8); PG8_WAIT_L(0); PG8_BAR; PG8_MMA(1, 0, At, B0); PG8_MMA(1, 1, At, B1); PG8_BAR; PG8_SCHED;
;             PG8_LDB(B0, 1, 0); PG8_LDB(B1, 1, 1); PG8_SCHED; PG8_LDA(At, 1, 0); PG8_STAGE(PG8_SA(0, 1), a2 + hstepA, voffA);
;             PG8_WAIT_V(8); PG8_WAIT_L(0); PG8_BAR; PG8_MMA(0, 0, At, B0); PG8_MMA(0, 1, At, B1); PG8_BAR; PG8_SCHED;
;             PG8_LDA(At, 1, 1); PG8_STAGE(PG8_SB(1, 0), b3, voffB); PG8_STAGE(PG8_SB(1, 1), b3 + hstepB, voffB); PG8_STAGE(PG8_SA(1, 0), a3, voffA);
;             PG8_WAIT_V(8); PG8_WAIT_L(0); PG8_BAR; PG8_MMA(1, 0, At, B0); PG8_MMA(1, 1, At, B1); PG8_BAR; PG8_SCHED;
	s_setprio 1
	s_waitcnt lgkmcnt(7)
	v_mfma_f32_16x16x32_bf16 v[64:67], v[132:135], v[170:173], v[64:67]
	v_mfma_f32_16x16x32_bf16 v[60:63], v[142:145], v[170:173], v[60:63]
	s_waitcnt lgkmcnt(5)
	v_mfma_f32_16x16x32_bf16 v[48:51], v[132:135], v[178:181], v[48:51]
	v_mfma_f32_16x16x32_bf16 v[44:47], v[142:145], v[178:181], v[44:47]
	s_waitcnt lgkmcnt(3)
	v_mfma_f32_16x16x32_bf16 v[32:35], v[132:135], v[196:199], v[32:35]
	v_mfma_f32_16x16x32_bf16 v[28:31], v[142:145], v[196:199], v[28:31]
	s_waitcnt lgkmcnt(1)
	v_mfma_f32_16x16x32_bf16 v[16:19], v[132:135], v[210:213], v[16:19]
	v_mfma_f32_16x16x32_bf16 v[12:15], v[142:145], v[210:213], v[12:15]
	v_mfma_f32_16x16x32_bf16 v[64:67], v[136:139], v[174:177], v[64:67]
	v_mfma_f32_16x16x32_bf16 v[60:63], v[146:149], v[174:177], v[60:63]
	v_mfma_f32_16x16x32_bf16 v[48:51], v[136:139], v[182:185], v[48:51]
	v_mfma_f32_16x16x32_bf16 v[44:47], v[146:149], v[182:185], v[44:47]
	v_mfma_f32_16x16x32_bf16 v[32:35], v[136:139], v[206:209], v[32:35]
	v_mfma_f32_16x16x32_bf16 v[28:31], v[146:149], v[206:209], v[28:31]
	s_waitcnt lgkmcnt(0)
	v_mfma_f32_16x16x32_bf16 v[16:19], v[136:139], v[214:217], v[16:19]
	v_mfma_f32_16x16x32_bf16 v[12:15], v[146:149], v[214:217], v[12:15]
	s_setprio 0
	s_setprio 1
	v_mfma_f32_16x16x32_bf16 v[56:59], v[154:157], v[170:173], v[56:59]
	v_mfma_f32_16x16x32_bf16 v[52:55], v[162:165], v[170:173], v[52:55]
	v_mfma_f32_16x16x32_bf16 v[40:43], v[154:157], v[178:181], v[40:43]
	v_mfma_f32_16x16x32_bf16 v[36:39], v[162:165], v[178:181], v[36:39]
	v_mfma_f32_16x16x32_bf16 v[24:27], v[154:157], v[196:199], v[24:27]
	v_mfma_f32_16x16x32_bf16 v[20:23], v[162:165], v[196:199], v[20:23]
	v_mfma_f32_16x16x32_bf16 v[8:11], v[154:157], v[210:213], v[8:11]
	v_mfma_f32_16x16x32_bf16 v[4:7], v[162:165], v[210:213], v[4:7]
	v_mfma_f32_16x16x32_bf16 v[56:59], v[158:161], v[174:177], v[56:59]
	v_mfma_f32_16x16x32_bf16 v[52:55], v[166:169], v[174:177], v[52:55]
	v_mfma_f32_16x16x32_bf16 v[40:43], v[158:161], v[182:185], v[40:43]
	v_mfma_f32_16x16x32_bf16 v[36:39], v[166:169], v[182:185], v[36:39]
	v_mfma_f32_16x16x32_bf16 v[24:27], v[158:161], v[206:209], v[24:27]
	v_mfma_f32_16x16x32_bf16 v[20:23], v[166:169], v[206:209], v[20:23]
	v_mfma_f32_16x16x32_bf16 v[8:11], v[158:161], v[214:217], v[8:11]
	v_mfma_f32_16x16x32_bf16 v[4:7], v[166:169], v[214:217], v[4:7]
	s_setprio 0
	s_barrier
	v_add_u32_e32 v146, 0x18000, v151
	v_add_u32_e32 v153, 0x1c000, v151
	ds_read_b128 v[132:135], v146
	ds_read_b128 v[136:139], v146 offset:1024
	ds_read_b128 v[142:145], v146 offset:2048
	ds_read_b128 v[146:149], v146 offset:3072
	ds_read_b128 v[154:157], v153
	ds_read_b128 v[158:161], v153 offset:1024
	ds_read_b128 v[162:165], v153 offset:2048
	ds_read_b128 v[166:169], v153 offset:3072
	ds_read_b128 v[170:173], v152 offset:32768
	ds_read_b128 v[174:177], v152 offset:33792
	ds_read_b128 v[178:181], v152 offset:34816
	ds_read_b128 v[182:185], v152 offset:35840
	ds_read_b128 v[196:199], v152 offset:36864
	ds_read_b128 v[206:209], v152 offset:37888
	ds_read_b128 v[210:213], v152 offset:38912
	ds_read_b128 v[214:217], v152 offset:39936
	s_add_u32 s26, s26, 0x160000
	s_addc_u32 s27, s27, 0
	s_mov_b32 m0, s40
	s_nop 0
	global_load_lds_dwordx4 v0, s[26:27]
	s_nop 0
	s_mov_b32 m0, s41
	s_nop 0
	global_load_lds_dwordx4 v140, s[26:27]
	s_waitcnt vmcnt(8)
	s_waitcnt lgkmcnt(0)
	s_barrier
	s_setprio 1
	s_waitcnt lgkmcnt(7)
	v_mfma_f32_16x16x32_bf16 v[128:131], v[132:135], v[170:173], v[128:131]
	v_mfma_f32_16x16x32_bf16 v[124:127], v[142:145], v[170:173], v[124:127]
	s_waitcnt lgkmcnt(5)
	v_mfma_f32_16x16x32_bf16 v[112:115], v[132:135], v[178:181], v[112:115]
	v_mfma_f32_16x16x32_bf16 v[108:111], v[142:145], v[178:181], v[108:111]
	s_waitcnt lgkmcnt(3)
	v_mfma_f32_16x16x32_bf16 v[96:99], v[132:135], v[196:199], v[96:99]
	v_mfma_f32_16x16x32_bf16 v[92:95], v[142:145], v[196:199], v[92:95]
	s_waitcnt lgkmcnt(1)
	v_mfma_f32_16x16x32_bf16 v[80:83], v[132:135], v[210:213], v[80:83]
	v_mfma_f32_16x16x32_bf16 v[76:79], v[142:145], v[210:213], v[76:79]
	v_mfma_f32_16x16x32_bf16 v[128:131], v[136:139], v[174:177], v[128:131]
	v_mfma_f32_16x16x32_bf16 v[124:127], v[146:149], v[174:177], v[124:127]
	v_mfma_f32_16x16x32_bf16 v[112:115], v[136:139], v[182:185], v[112:115]
	v_mfma_f32_16x16x32_bf16 v[108:111], v[146:149], v[182:185], v[108:111]
	v_mfma_f32_16x16x32_bf16 v[96:99], v[136:139], v[206:209], v[96:99]
	v_mfma_f32_16x16x32_bf16 v[92:95], v[146:149], v[206:209], v[92:95]
	s_waitcnt lgkmcnt(0)
	v_mfma_f32_16x16x32_bf16 v[80:83], v[136:139], v[214:217], v[80:83]
	v_mfma_f32_16x16x32_bf16 v[76:79], v[146:149], v[214:217], v[76:79]
	s_setprio 0
	s_setprio 1
	v_mfma_f32_16x16x32_bf16 v[120:123], v[154:157], v[170:173], v[120:123]
	v_mfma_f32_16x16x32_bf16 v[116:119], v[162:165], v[170:173], v[116:119]
	v_mfma_f32_16x16x32_bf16 v[104:107], v[154:157], v[178:181], v[104:107]
	v_mfma_f32_16x16x32_bf16 v[100:103], v[162:165], v[178:181], v[100:103]
	v_mfma_f32_16x16x32_bf16 v[88:91], v[154:157], v[196:199], v[88:91]
	v_mfma_f32_16x16x32_bf16 v[84:87], v[162:165], v[196:199], v[84:87]
	v_mfma_f32_16x16x32_bf16 v[72:75], v[154:157], v[210:213], v[72:75]
	v_mfma_f32_16x16x32_bf16 v[68:71], v[162:165], v[210:213], v[68:71]
	v_mfma_f32_16x16x32_bf16 v[120:123], v[158:161], v[174:177], v[120:123]
	v_mfma_f32_16x16x32_bf16 v[116:119], v[166:169], v[174:177], v[116:119]
	v_mfma_f32_16x16x32_bf16 v[104:107], v[158:161], v[182:185], v[104:107]
	v_mfma_f32_16x16x32_bf16 v[100:103], v[166:169], v[182:185], v[100:103]
	v_mfma_f32_16x16x32_bf16 v[88:91], v[158:161], v[206:209], v[88:91]
	v_mfma_f32_16x16x32_bf16 v[84:87], v[166:169], v[206:209], v[84:87]
	v_mfma_f32_16x16x32_bf16 v[72:75], v[158:161], v[214:217], v[72:75]
	v_mfma_f32_16x16x32_bf16 v[68:71], v[166:169], v[214:217], v[68:71]
	s_setprio 0
	s_barrier
; #define PG8_STAGE(bufoff, gbase, voff) do { _Pragma("unroll") for (int _i = 0; _i < 2; ++_i) \
;         glds16((const void*)(gbase), (voff)[_i], ldsbase + (unsigned)(bufoff) + ldsw + (unsigned)_i * 8192u); } while (0)
; #define PG8_LDA(dst, b, h) do { _Pragma("unroll") for (int m = 0; m < 4; ++m) _Pragma("unroll") for (int k = 0; k < 2; ++k) dst[m][k] = *(const LAS bf16x8*)(lds + PG8_SA(b, h) + aoff + m * 2048 + k * 1024); } while (0)
; #define PG8_WAIT_V(n) asm volatile("s_waitcnt vmcnt(" #n ")" ::: "memory")
; #define PG8_WAIT_L(n) asm volatile("s_waitcnt lgkmcnt(" #n ")" ::: "memory")
; #define PG8_BAR __builtin_amdgcn_s_barrier()
; #define PG8_SCHED __builtin_amdgcn_sched_barrier(0)
;     ...
;             PG8_LDA(At, 1, 1); PG8_STAGE(PG8_SB(1, 0), b3, voffB); PG8_STAGE(PG8_SB(1, 1), b3 + hstepB, voffB); PG8_STAGE(PG8_SA(1, 0), a3, voffA);
;             PG8_WAIT_V(8); PG8_WAIT_L(0); PG8_BAR; PG8_MMA(1, 0, At, B0); PG8_MMA(1, 1, At, B1); PG8_BAR; PG8_SCHED;
;         }
	ds_read_b128 v[170:173], v152 offset:49152
	ds_read_b128 v[174:177], v152 offset:50176
	ds_read_b128 v[178:181], v152 offset:51200
	ds_read_b128 v[182:185], v152 offset:52224
	ds_read_b128 v[196:199], v152 offset:53248
	ds_read_b128 v[206:209], v152 offset:54272
	ds_read_b128 v[210:213], v152 offset:55296
	ds_read_b128 v[214:217], v152 offset:56320
	s_add_u32 s26, s24, 0x80
	s_addc_u32 s27, s25, 0
	s_mov_b32 m0, s43
	s_nop 0
	global_load_lds_dwordx4 v1, s[26:27]
	s_add_u32 s24, s24, 0x160080
	s_mov_b32 m0, s44
	s_nop 0
	global_load_lds_dwordx4 v2, s[26:27]
	s_addc_u32 s25, s25, 0
	s_mov_b32 m0, s47
	s_nop 0
	global_load_lds_dwordx4 v1, s[24:25]
	s_nop 0
	s_mov_b32 m0, s48
	s_nop 0
	global_load_lds_dwordx4 v2, s[24:25]
	s_mov_b32 m0, s45
	s_nop 0
	global_load_lds_dwordx4 v0, s[22:23]
	s_nop 0
	s_mov_b32 m0, s46
	s_nop 0
	global_load_lds_dwordx4 v140, s[22:23]
	s_waitcnt vmcnt(8)
	s_waitcnt lgkmcnt(0)
	s_barrier
	s_setprio 1
	s_waitcnt lgkmcnt(7)
	v_mfma_f32_16x16x32_bf16 v[64:67], v[132:135], v[170:173], v[64:67]
	v_mfma_f32_16x16x32_bf16 v[60:63], v[142:145], v[170:173], v[60:63]
	s_waitcnt lgkmcnt(5)
	v_mfma_f32_16x16x32_bf16 v[48:51], v[132:135], v[178:181], v[48:51]
	v_mfma_f32_16x16x32_bf16 v[44:47], v[142:145], v[178:181], v[44:47]
	s_waitcnt lgkmcnt(3)
	v_mfma_f32_16x16x32_bf16 v[32:35], v[132:135], v[196:199], v[32:35]
	v_mfma_f32_16x16x32_bf16 v[28:31], v[142:145], v[196:199], v[28:31]
	s_waitcnt lgkmcnt(1)
	v_mfma_f32_16x16x32_bf16 v[16:19], v[132:135], v[210:213], v[16:19]
	v_mfma_f32_16x16x32_bf16 v[12:15], v[142:145], v[210:213], v[12:15]
	v_mfma_f32_16x16x32_bf16 v[64:67], v[136:139], v[174:177], v[64:67]
	v_mfma_f32_16x16x32_bf16 v[60:63], v[146:149], v[174:177], v[60:63]
	v_mfma_f32_16x16x32_bf16 v[48:51], v[136:139], v[182:185], v[48:51]
	v_mfma_f32_16x16x32_bf16 v[44:47], v[146:149], v[182:185], v[44:47]
	v_mfma_f32_16x16x32_bf16 v[32:35], v[136:139], v[206:209], v[32:35]
	v_mfma_f32_16x16x32_bf16 v[28:31], v[146:149], v[206:209], v[28:31]
	s_waitcnt lgkmcnt(0)
	v_mfma_f32_16x16x32_bf16 v[16:19], v[136:139], v[214:217], v[16:19]
	v_mfma_f32_16x16x32_bf16 v[12:15], v[146:149], v[214:217], v[12:15]
	s_setprio 0
	s_setprio 1
	v_mfma_f32_16x16x32_bf16 v[56:59], v[154:157], v[170:173], v[56:59]
	v_mfma_f32_16x16x32_bf16 v[52:55], v[162:165], v[170:173], v[52:55]
	v_mfma_f32_16x16x32_bf16 v[40:43], v[154:157], v[178:181], v[40:43]
	v_mfma_f32_16x16x32_bf16 v[36:39], v[162:165], v[178:181], v[36:39]
	v_mfma_f32_16x16x32_bf16 v[24:27], v[154:157], v[196:199], v[24:27]
	v_mfma_f32_16x16x32_bf16 v[20:23], v[162:165], v[196:199], v[20:23]
	v_mfma_f32_16x16x32_bf16 v[8:11], v[154:157], v[210:213], v[8:11]
	v_mfma_f32_16x16x32_bf16 v[4:7], v[162:165], v[210:213], v[4:7]
	v_mfma_f32_16x16x32_bf16 v[56:59], v[158:161], v[174:177], v[56:59]
	v_mfma_f32_16x16x32_bf16 v[52:55], v[166:169], v[174:177], v[52:55]
	v_mfma_f32_16x16x32_bf16 v[40:43], v[158:161], v[182:185], v[40:43]
	v_mfma_f32_16x16x32_bf16 v[36:39], v[166:169], v[182:185], v[36:39]
	v_mfma_f32_16x16x32_bf16 v[24:27], v[158:161], v[206:209], v[24:27]
	v_mfma_f32_16x16x32_bf16 v[20:23], v[166:169], v[206:209], v[20:23]
	v_mfma_f32_16x16x32_bf16 v[8:11], v[158:161], v[214:217], v[8:11]
	v_mfma_f32_16x16x32_bf16 v[4:7], v[166:169], v[214:217], v[4:7]
	s_setprio 0
	s_barrier
	s_add_i32 s57, s57, 2
	s_add_u32 s55, s55, 0x100
	s_addc_u32 s56, s56, 0
	s_add_u32 s20, s20, 0x100
	s_addc_u32 s21, s21, 0
	s_cmpk_gt_u32 s57, 0x55
	s_cbranch_scc0 .LBB0_3131
	s_and_b64 vcc, exec, s[14:15]
	s_cbranch_vccz .LBB0_3134
	s_barrier
